# LDS-DMA blocks: s_nop 4 -> s_nop 0 before buffer_load..lds where no VALU-written SGPR operand (1 wait state for M0 suffices)
# speedup vs baseline: 1.0020x; 1.0020x over previous
; #define OPAQUE_TID(P) (((P).wid0 << 6) | lane_id_now())
; #define G_WAIT_V(n) asm volatile("s_waitcnt vmcnt(" #n ")" ::: "memory")
; #define G_BAR() __builtin_amdgcn_s_barrier()
; #define D_STAGE_A(slot, half, kt) D_STAGE(rsA, voffA, slot, half, kt)
; #define D_STAGE_B(slot, half, kt) D_STAGE(rsB, voffB, slot, half, kt)
; #define D_STAGE_A(slot, half, kt) D_STAGE(rsA, voffA, slot, half, kt)
;   DI unsigned bt_rowoff(int h, int R) const { return (unsigned)(pn * 256 + 128 * h + (pn < 15 ? tcol_adj(R) : tcol_p64(R))) * 4096u; }
;   DI unsigned a_bytes() const { return (unsigned)NTOK * 4096u; }
; template <class Cfg>
; DI void gemm256dma_unit(LDS_AS unsigned char* lds, const Cfg& cfg) {
;   const int tid = OPAQUE_TID(cfg.p), wid = __builtin_amdgcn_readfirstlane(tid >> 6), lane = tid & 63, wr = wid >> 2, wc = wid & 3, fr = lane & 15, fq = lane >> 4;
;   const int nt = cfg.nkt();
;   unsigned voffA[2][2], voffB[2][2];
; #pragma unroll
;   for (int i = 0; i < 2; ++i) {
;     int R, C; stage_rc(tid * 16 + i * 8192, R, C);
;     voffA[0][i] = cfg.a_rowoff(R) + (unsigned)C * 2u;
;     voffA[1][i] = cfg.a_rowoff(128 + R) + (unsigned)C * 2u;
;     voffB[0][i] = cfg.bt_rowoff(0, R) + (unsigned)C * 2u;
;     voffB[1][i] = cfg.bt_rowoff(1, R) + (unsigned)C * 2u;
;   }
;   const __amdgpu_buffer_rsrc_t rsA = __builtin_amdgcn_make_buffer_rsrc((void*)cfg.a_base(), 0, cfg.a_bytes(), 0x00020000);
;   const __amdgpu_buffer_rsrc_t rsB = __builtin_amdgcn_make_buffer_rsrc((void*)cfg.bt_base(), 0, cfg.bt_bytes(), 0x00020000);
;   const unsigned ldsw = (unsigned)__builtin_amdgcn_readfirstlane((int)(unsigned)(size_t)lds) + (unsigned)wid * 1024u;
;     ...
;   const int aoff = lds_byte(wr * 64 + fr, fq * 8), boff = lds_byte(wc * 32 + fr, fq * 8);
;     ...
;   f32x4 acc[2][2][4][2];
; #pragma unroll
;   for (int a = 0; a < 2; ++a)
; #pragma unroll
;     for (int b = 0; b < 2; ++b)
; #pragma unroll
;       for (int m = 0; m < 4; ++m)
; #pragma unroll
;         for (int n = 0; n < 2; ++n) acc[a][b][m][n] = (f32x4){0.f, 0.f, 0.f, 0.f};
;   bf16x8 At[4][2], B0[2][2], B1[2][2];
;   D_STAGE_B(G_SB(0, 0), 0, 0); D_STAGE_A(G_SA(0, 0), 0, 0); D_STAGE_B(G_SB(0, 1), 1, 0); D_STAGE_A(G_SA(0, 1), 1, 0);
;   if (wr == 1) G_BAR();
;   G_WAIT_V(4); G_BAR();
;   D_STAGE_B(G_SB(1, 0), 0, 1); D_STAGE_A(G_SA(1, 0), 0, 1); D_STAGE_B(G_SB(1, 1), 1, 1);
;   G_WAIT_V(6); G_BAR();
.LBB0_276:
	v_lshlrev_b32_e32 v10, 6, v10
	v_lshlrev_b32_e32 v5, 6, v5
	v_sub_u32_e32 v9, v9, v10
	v_sub_u32_e32 v3, v3, v5
	s_lshl_b32 s4, s13, 8
	v_lshlrev_b32_e32 v8, 5, v8
	v_ashrrev_i16_sdwa v9, v148, sext(v9) dst_sel:DWORD dst_unused:UNUSED_PAD src0_sel:DWORD src1_sel:BYTE_0
	v_lshlrev_b32_e32 v2, 5, v2
	v_ashrrev_i16_sdwa v3, v148, sext(v3) dst_sel:DWORD dst_unused:UNUSED_PAD src0_sel:DWORD src1_sel:BYTE_0
	v_and_b32_e32 v8, 32, v8
	v_bfe_i32 v9, v9, 0, 16
	v_and_b32_e32 v2, 32, v2
	v_bfe_i32 v3, v3, 0, 16
	s_or_b32 s29, s4, 0x80
	v_add_lshl_u32 v8, v8, v9, 1
	v_add_lshl_u32 v2, v2, v3, 1
	s_ashr_i32 s0, s17, 4
	v_add_u32_e32 v3, s29, v6
	s_lshl_b32 s1, s0, 20
	v_lshl_add_u32 v130, v3, 12, v2
	v_lshl_add_u32 v3, v7, 12, v8
	s_ashr_i32 s25, s24, 6
	v_lshl_add_u32 v1, v1, 12, v2
	s_or_b32 s28, s1, 0x80000
	v_add_u32_e32 v131, s1, v3
	v_add_u32_e32 v134, s1, v1
	s_lshl_b32 s1, s25, 10
	v_add_u32_e32 v132, s28, v3
	v_add_u32_e32 v3, s4, v4
	v_add_u32_e32 v135, s28, v1
	s_add_i32 s28, s1, 0
	v_add_u32_e32 v9, s4, v11
	v_lshl_add_u32 v133, v3, 12, v2
	s_add_i32 s33, s28, 0x10010
	s_mov_b32 m0, s33
	s_nop 0
	buffer_load_dwordx4 v133, s[8:11], s5 offen lds
	v_lshl_add_u32 v128, v9, 12, v8
	s_add_i32 s39, s28, 0x12010
	s_mov_b32 m0, s39
	s_nop 0
	buffer_load_dwordx4 v128, s[8:11], s5 offen lds
	s_add_i32 s1, s28, 16
	s_mov_b32 m0, s1
	s_nop 0
	buffer_load_dwordx4 v134, s[20:23], s5 offen lds
	s_add_i32 s42, s28, 0x2010
	s_mov_b32 m0, s42
	s_nop 0
	buffer_load_dwordx4 v131, s[20:23], s5 offen lds
	v_add_u32_e32 v1, s29, v12
	s_add_i32 s43, s28, 0x14010
	s_mov_b32 m0, s43
	s_nop 0
	buffer_load_dwordx4 v130, s[8:11], s5 offen lds
	v_lshl_add_u32 v136, v1, 12, v8
	s_add_i32 s54, s28, 0x16010
	s_mov_b32 m0, s54
	s_nop 0
	buffer_load_dwordx4 v136, s[8:11], s5 offen lds
	s_add_i32 s60, s28, 0x4010
	s_mov_b32 m0, s60
	s_nop 0
	buffer_load_dwordx4 v135, s[20:23], s5 offen lds
	s_add_i32 s61, s28, 0x6010
	s_mov_b32 m0, s61
	s_nop 0
	buffer_load_dwordx4 v132, s[20:23], s5 offen lds
	s_ashr_i32 s29, s24, 8
	s_cmp_lg_u32 s29, 1
	s_cbranch_scc1 .LBB0_278
	s_barrier
.LBB0_278:
	s_waitcnt vmcnt(4)
	s_barrier
	s_add_i32 s62, s28, 0x18010
	s_mov_b32 m0, s62
	s_nop 4
	buffer_load_dwordx4 v133, s[8:11], s68 offen lds
	s_add_i32 s63, s28, 0x1a010
	s_mov_b32 m0, s63
	s_nop 4
	buffer_load_dwordx4 v128, s[8:11], s68 offen lds
	s_add_i32 s64, s28, 0x8010
	s_mov_b32 m0, s64
	s_nop 0
	buffer_load_dwordx4 v134, s[20:23], s68 offen lds
	v_and_b32_e32 v1, 48, v0
	v_lshlrev_b32_e32 v2, 6, v0
	s_movk_i32 s30, 0x3c0
	v_lshlrev_b32_e32 v0, 2, v0
	s_add_i32 s65, s28, 0xa010
	s_mov_b32 m0, s65
	s_nop 0
	buffer_load_dwordx4 v131, s[20:23], s68 offen lds
	s_and_b32 s25, s25, 3
	s_lshl_b32 s55, s29, 6
	s_lshl_b32 s29, s29, 13
	v_and_or_b32 v1, v2, s30, v1
	v_and_b32_e32 v0, 32, v0
	s_add_i32 s66, s28, 0x1c010
	s_mov_b32 m0, s66
	s_nop 0
	buffer_load_dwordx4 v130, s[8:11], s68 offen lds
	v_bitop3_b32 v2, v1, s29, v0 bitop3:0xde
	s_lshl_b32 s29, s25, 12
	s_add_i32 s67, s28, 0x1e010
	s_mov_b32 m0, s67
	s_nop 0
	buffer_load_dwordx4 v136, s[8:11], s68 offen lds
	v_bitop3_b32 v1, v1, s29, v0 bitop3:0xde
	s_waitcnt vmcnt(6)
	v_mov_b32_e32 v0, 0
	v_add_u32_e32 v137, 0, v1
	s_add_i32 vcc_lo, s28, 0xc010
	s_add_i32 vcc_hi, s28, 0xe010
	s_mov_b32 s29, 0
	s_movk_i32 s28, 0x180
	v_add_u32_e32 v138, 0, v2
	v_mov_b32_e32 v1, v0
	v_mov_b32_e32 v2, v0
	v_mov_b32_e32 v3, v0
	v_mov_b32_e32 v4, v0
	v_mov_b32_e32 v5, v0
	v_mov_b32_e32 v6, v0
	v_mov_b32_e32 v7, v0
	v_mov_b32_e32 v16, v0
	v_mov_b32_e32 v17, v0
	v_mov_b32_e32 v18, v0
	v_mov_b32_e32 v19, v0
	v_mov_b32_e32 v20, v0
	v_mov_b32_e32 v21, v0
	v_mov_b32_e32 v22, v0
	v_mov_b32_e32 v23, v0
	v_mov_b32_e32 v32, v0
	v_mov_b32_e32 v33, v0
	v_mov_b32_e32 v34, v0
	v_mov_b32_e32 v35, v0
	v_mov_b32_e32 v36, v0
	v_mov_b32_e32 v37, v0
	v_mov_b32_e32 v38, v0
	v_mov_b32_e32 v39, v0
	v_mov_b32_e32 v48, v0
	v_mov_b32_e32 v49, v0
	v_mov_b32_e32 v50, v0
	v_mov_b32_e32 v51, v0
	v_mov_b32_e32 v52, v0
	v_mov_b32_e32 v53, v0
	v_mov_b32_e32 v54, v0
	v_mov_b32_e32 v55, v0
	v_mov_b32_e32 v8, v0
	v_mov_b32_e32 v9, v0
	v_mov_b32_e32 v10, v0
	v_mov_b32_e32 v11, v0
	v_mov_b32_e32 v12, v0
	v_mov_b32_e32 v13, v0
	v_mov_b32_e32 v14, v0
	v_mov_b32_e32 v15, v0
	v_mov_b32_e32 v24, v0
	v_mov_b32_e32 v25, v0
	v_mov_b32_e32 v26, v0
	v_mov_b32_e32 v27, v0
	v_mov_b32_e32 v28, v0
	v_mov_b32_e32 v29, v0
	v_mov_b32_e32 v30, v0
	v_mov_b32_e32 v31, v0
	v_mov_b32_e32 v40, v0
	v_mov_b32_e32 v41, v0
	v_mov_b32_e32 v42, v0
	v_mov_b32_e32 v43, v0
	v_mov_b32_e32 v44, v0
	v_mov_b32_e32 v45, v0
	v_mov_b32_e32 v46, v0
	v_mov_b32_e32 v47, v0
	v_mov_b32_e32 v56, v0
	v_mov_b32_e32 v57, v0
	v_mov_b32_e32 v58, v0
	v_mov_b32_e32 v59, v0
	v_mov_b32_e32 v60, v0
	v_mov_b32_e32 v61, v0
	v_mov_b32_e32 v62, v0
	v_mov_b32_e32 v63, v0
	v_mov_b32_e32 v64, v0
	v_mov_b32_e32 v65, v0
	v_mov_b32_e32 v66, v0
	v_mov_b32_e32 v67, v0
	v_mov_b32_e32 v68, v0
	v_mov_b32_e32 v69, v0
	v_mov_b32_e32 v70, v0
	v_mov_b32_e32 v71, v0
	v_mov_b32_e32 v80, v0
	v_mov_b32_e32 v81, v0
	v_mov_b32_e32 v82, v0
	v_mov_b32_e32 v83, v0
	v_mov_b32_e32 v84, v0
	v_mov_b32_e32 v85, v0
	v_mov_b32_e32 v86, v0
	v_mov_b32_e32 v87, v0
	v_mov_b32_e32 v96, v0
	v_mov_b32_e32 v97, v0
	v_mov_b32_e32 v98, v0
	v_mov_b32_e32 v99, v0
	v_mov_b32_e32 v100, v0
	v_mov_b32_e32 v101, v0
	v_mov_b32_e32 v102, v0
	v_mov_b32_e32 v103, v0
	v_mov_b32_e32 v112, v0
	v_mov_b32_e32 v113, v0
	v_mov_b32_e32 v114, v0
	v_mov_b32_e32 v115, v0
	v_mov_b32_e32 v116, v0
	v_mov_b32_e32 v117, v0
	v_mov_b32_e32 v118, v0
	v_mov_b32_e32 v119, v0
	v_mov_b32_e32 v72, v0
	v_mov_b32_e32 v73, v0
	v_mov_b32_e32 v74, v0
	v_mov_b32_e32 v75, v0
	v_mov_b32_e32 v76, v0
	v_mov_b32_e32 v77, v0
	v_mov_b32_e32 v78, v0
	v_mov_b32_e32 v79, v0
	v_mov_b32_e32 v88, v0
	v_mov_b32_e32 v89, v0
	v_mov_b32_e32 v90, v0
	v_mov_b32_e32 v91, v0
	v_mov_b32_e32 v92, v0
	v_mov_b32_e32 v93, v0
	v_mov_b32_e32 v94, v0
	v_mov_b32_e32 v95, v0
	v_mov_b32_e32 v104, v0
	v_mov_b32_e32 v105, v0
	v_mov_b32_e32 v106, v0
	v_mov_b32_e32 v107, v0
	v_mov_b32_e32 v108, v0
	v_mov_b32_e32 v109, v0
	v_mov_b32_e32 v110, v0
	v_mov_b32_e32 v111, v0
	v_mov_b32_e32 v120, v0
	v_mov_b32_e32 v121, v0
	v_mov_b32_e32 v122, v0
	v_mov_b32_e32 v123, v0
	v_mov_b32_e32 v124, v0
	v_mov_b32_e32 v125, v0
	v_mov_b32_e32 v126, v0
	v_mov_b32_e32 v127, v0
	v_add_u32_e32 v139, 0x10010, v137
	v_add_u32_e32 v140, 0x14010, v137
	s_barrier
; #define G_BAR() __builtin_amdgcn_s_barrier()
; #define G_SCHED() __builtin_amdgcn_sched_barrier(0)
; #define D_STAGE_A(slot, half, kt) D_STAGE(rsA, voffA, slot, half, kt)
; #define D_STAGE_B(slot, half, kt) D_STAGE(rsB, voffB, slot, half, kt)
; #define D_LDA(dst, slot) do { _Pragma("unroll") for (int m = 0; m < 4; ++m) _Pragma("unroll") for (int k = 0; k < 2; ++k) \
;     dst[m][k] = *(const LDS_AS bf16x8*)(lds + (slot) + aoff + m * 2048 + k * 1024); } while (0)
; #define D_LDB(dst, slot) do { _Pragma("unroll") for (int n = 0; n < 2; ++n) _Pragma("unroll") for (int k = 0; k < 2; ++k) \
;     dst[n][k] = *(const LDS_AS bf16x8*)(lds + (slot) + boff + n * 2048 + k * 1024); } while (0)
; #define D_MMA(ai, bj, At, Bf) do { __builtin_amdgcn_s_setprio(1); _Pragma("unroll") for (int m = 0; m < 4; ++m) _Pragma("unroll") for (int n = 0; n < 2; ++n) _Pragma("unroll") for (int k = 0; k < 2; ++k) \
;     acc[ai][bj][m][n] = __builtin_amdgcn_mfma_f32_16x16x32_bf16(Bf[n][k], At[m][k], acc[ai][bj][m][n], 0, 0, 0); __builtin_amdgcn_s_setprio(0); } while (0)
; #define D_WAIT_L(n) asm volatile("s_waitcnt lgkmcnt(" #n ")" ::: "memory")
; #define D_STAGE_A(slot, half, kt) D_STAGE(rsA, voffA, slot, half, kt)
; #define D_STAGE_B(slot, half, kt) do { _Pragma("unroll") for (int _i = 0; _i < 2; ++_i) { const unsigned _m0 = ldsw + (unsigned)((slot) + _i * 8192); const unsigned _so = (unsigned)(kt) * 128u + (half) * bt_half + _i * bt_piece; \
;     asm volatile("s_mov_b32 m0, %0\n\ts_nop 4\n\tbuffer_load_dwordx4 %1, %2, %3 offen lds" :: "s"(_m0), "v"(voffB0), "s"(rsB), "s"(_so) : "m0", "memory"); } } while (0)
; template <class Cfg>
; DI void gemm256dma_unit(LDS_AS unsigned char* lds, const Cfg& cfg) {
;     ...
;   for (int t = 0; t < nt; t += 2) {
;     const int t1 = t + 1;
;     const int t2 = (t + 2 < nt) ? t + 2 : 0;
;     const int t3 = (t + 2 < nt) ? t + 3 : 1;
;     D_LDB(B0, G_SB(0, 0)); G_SCHED(); D_LDA(At, G_SA(0, 0)); D_STAGE_A(G_SA(1, 1), 1, t1);
;     D_WAIT_L(8); G_BAR(); D_WAIT_L(0); G_SCHED(); D_MMA(0, 0, At, B0); G_BAR(); G_SCHED();
;     D_LDB(B1, G_SB(0, 1)); D_STAGE_B(G_SB(0, 0), 0, t2);
;     G_BAR(); D_WAIT_L(0); G_SCHED(); D_MMA(0, 1, At, B1); G_BAR(); G_SCHED();
;     D_LDA(At, G_SA(0, 1)); D_STAGE_A(G_SA(0, 0), 0, t2);
;     G_BAR(); D_WAIT_L(0); G_SCHED(); D_MMA(1, 0, At, B0); G_BAR(); G_SCHED();
.LBB0_279:
	ds_read_b128 v[142:145], v139
	ds_read_b128 v[150:153], v139 offset:1024
	ds_read_b128 v[154:157], v139 offset:2048
	ds_read_b128 v[158:161], v139 offset:3072
	s_add_i32 s30, s29, 2
	s_add_i32 s38, s28, 0xffffff00
	s_add_i32 s31, s28, 0xffffff80
	s_cmp_lt_u32 s29, 30
	s_cselect_b32 s96, s31, 0
	s_cselect_b32 s31, s28, 0x80
	s_addk_i32 s28, 0x100
	s_cmp_gt_u32 s29, 29
	ds_read_b128 v[162:165], v138 offset:16
	ds_read_b128 v[166:169], v138 offset:1040
	ds_read_b128 v[170:173], v138 offset:2064
	ds_read_b128 v[174:177], v138 offset:3088
	ds_read_b128 v[178:181], v138 offset:4112
	ds_read_b128 v[182:185], v138 offset:5136
	ds_read_b128 v[186:189], v138 offset:6160
	ds_read_b128 v[192:195], v138 offset:7184
	s_mov_b32 m0, vcc_lo
	s_nop 0
	buffer_load_dwordx4 v135, s[20:23], s38 offen lds
	s_nop 0
	s_mov_b32 m0, vcc_hi
	s_nop 0
	buffer_load_dwordx4 v132, s[20:23], s38 offen lds
	s_waitcnt lgkmcnt(8)
	s_barrier
	s_waitcnt lgkmcnt(0)
	s_setprio 1
	s_waitcnt lgkmcnt(7)
	v_mfma_f32_16x16x32_bf16 v[124:127], v[142:145], v[162:165], v[124:127]
	v_mfma_f32_16x16x32_bf16 v[120:123], v[154:157], v[162:165], v[120:123]
	s_waitcnt lgkmcnt(5)
	v_mfma_f32_16x16x32_bf16 v[108:111], v[142:145], v[170:173], v[108:111]
	v_mfma_f32_16x16x32_bf16 v[104:107], v[154:157], v[170:173], v[104:107]
	s_waitcnt lgkmcnt(3)
	v_mfma_f32_16x16x32_bf16 v[92:95], v[142:145], v[178:181], v[92:95]
	v_mfma_f32_16x16x32_bf16 v[88:91], v[154:157], v[178:181], v[88:91]
	s_waitcnt lgkmcnt(1)
	v_mfma_f32_16x16x32_bf16 v[76:79], v[142:145], v[186:189], v[76:79]
	v_mfma_f32_16x16x32_bf16 v[72:75], v[154:157], v[186:189], v[72:75]
	v_mfma_f32_16x16x32_bf16 v[124:127], v[150:153], v[166:169], v[124:127]
	v_mfma_f32_16x16x32_bf16 v[120:123], v[158:161], v[166:169], v[120:123]
	v_mfma_f32_16x16x32_bf16 v[108:111], v[150:153], v[174:177], v[108:111]
	v_mfma_f32_16x16x32_bf16 v[104:107], v[158:161], v[174:177], v[104:107]
	v_mfma_f32_16x16x32_bf16 v[92:95], v[150:153], v[182:185], v[92:95]
	v_mfma_f32_16x16x32_bf16 v[88:91], v[158:161], v[182:185], v[88:91]
	s_waitcnt lgkmcnt(0)
	v_mfma_f32_16x16x32_bf16 v[76:79], v[150:153], v[192:195], v[76:79]
	v_mfma_f32_16x16x32_bf16 v[72:75], v[158:161], v[192:195], v[72:75]
	s_setprio 0
	s_barrier
	ds_read_b128 v[196:199], v140
	ds_read_b128 v[200:203], v140 offset:1024
	ds_read_b128 v[204:207], v140 offset:2048
	ds_read_b128 v[208:211], v140 offset:3072
	s_mov_b32 m0, s33
	s_nop 0
	buffer_load_dwordx4 v133, s[8:11], s96 offen lds
	s_nop 0
	s_mov_b32 m0, s39
	s_nop 0
	buffer_load_dwordx4 v128, s[8:11], s96 offen lds
	s_barrier
	s_waitcnt lgkmcnt(0)
	s_setprio 1
	s_waitcnt lgkmcnt(3)
	v_mfma_f32_16x16x32_bf16 v[116:119], v[196:199], v[162:165], v[116:119]
	s_waitcnt lgkmcnt(1)
	v_mfma_f32_16x16x32_bf16 v[112:115], v[204:207], v[162:165], v[112:115]
	v_mfma_f32_16x16x32_bf16 v[100:103], v[196:199], v[170:173], v[100:103]
	v_mfma_f32_16x16x32_bf16 v[96:99], v[204:207], v[170:173], v[96:99]
	v_mfma_f32_16x16x32_bf16 v[84:87], v[196:199], v[178:181], v[84:87]
	v_mfma_f32_16x16x32_bf16 v[80:83], v[204:207], v[178:181], v[80:83]
	v_mfma_f32_16x16x32_bf16 v[68:71], v[196:199], v[186:189], v[68:71]
	v_mfma_f32_16x16x32_bf16 v[64:67], v[204:207], v[186:189], v[64:67]
	v_mfma_f32_16x16x32_bf16 v[116:119], v[200:203], v[166:169], v[116:119]
	s_waitcnt lgkmcnt(0)
	v_mfma_f32_16x16x32_bf16 v[112:115], v[208:211], v[166:169], v[112:115]
	v_mfma_f32_16x16x32_bf16 v[100:103], v[200:203], v[174:177], v[100:103]
	v_mfma_f32_16x16x32_bf16 v[96:99], v[208:211], v[174:177], v[96:99]
	v_mfma_f32_16x16x32_bf16 v[84:87], v[200:203], v[182:185], v[84:87]
	v_mfma_f32_16x16x32_bf16 v[80:83], v[208:211], v[182:185], v[80:83]
	v_mfma_f32_16x16x32_bf16 v[68:71], v[200:203], v[192:195], v[68:71]
	v_mfma_f32_16x16x32_bf16 v[64:67], v[208:211], v[192:195], v[64:67]
	s_setprio 0
	s_barrier
	ds_read_b128 v[162:165], v138 offset:16400
	ds_read_b128 v[166:169], v138 offset:17424
	ds_read_b128 v[170:173], v138 offset:18448
	ds_read_b128 v[174:177], v138 offset:19472
	ds_read_b128 v[178:181], v138 offset:20496
	ds_read_b128 v[182:185], v138 offset:21520
	ds_read_b128 v[186:189], v138 offset:22544
	ds_read_b128 v[192:195], v138 offset:23568
	s_mov_b32 m0, s1
	s_nop 0
	buffer_load_dwordx4 v134, s[20:23], s96 offen lds
	s_nop 0
	s_mov_b32 m0, s42
	s_nop 0
	buffer_load_dwordx4 v131, s[20:23], s96 offen lds
	s_barrier
	s_waitcnt lgkmcnt(0)
	s_setprio 1
	s_waitcnt lgkmcnt(7)
	v_mfma_f32_16x16x32_bf16 v[60:63], v[142:145], v[162:165], v[60:63]
	v_mfma_f32_16x16x32_bf16 v[56:59], v[154:157], v[162:165], v[56:59]
	s_waitcnt lgkmcnt(5)
	v_mfma_f32_16x16x32_bf16 v[44:47], v[142:145], v[170:173], v[44:47]
	v_mfma_f32_16x16x32_bf16 v[40:43], v[154:157], v[170:173], v[40:43]
	s_waitcnt lgkmcnt(3)
	v_mfma_f32_16x16x32_bf16 v[28:31], v[142:145], v[178:181], v[28:31]
	v_mfma_f32_16x16x32_bf16 v[24:27], v[154:157], v[178:181], v[24:27]
	s_waitcnt lgkmcnt(1)
	v_mfma_f32_16x16x32_bf16 v[12:15], v[142:145], v[186:189], v[12:15]
	v_mfma_f32_16x16x32_bf16 v[8:11], v[154:157], v[186:189], v[8:11]
	v_mfma_f32_16x16x32_bf16 v[60:63], v[150:153], v[166:169], v[60:63]
	v_mfma_f32_16x16x32_bf16 v[56:59], v[158:161], v[166:169], v[56:59]
	v_mfma_f32_16x16x32_bf16 v[44:47], v[150:153], v[174:177], v[44:47]
	v_mfma_f32_16x16x32_bf16 v[40:43], v[158:161], v[174:177], v[40:43]
	v_mfma_f32_16x16x32_bf16 v[28:31], v[150:153], v[182:185], v[28:31]
	v_mfma_f32_16x16x32_bf16 v[24:27], v[158:161], v[182:185], v[24:27]
	s_waitcnt lgkmcnt(0)
	v_mfma_f32_16x16x32_bf16 v[12:15], v[150:153], v[192:195], v[12:15]
	v_mfma_f32_16x16x32_bf16 v[8:11], v[158:161], v[192:195], v[8:11]
	s_setprio 0
	s_barrier
; #define G_WAIT_V(n) asm volatile("s_waitcnt vmcnt(" #n ")" ::: "memory")
; #define G_BAR() __builtin_amdgcn_s_barrier()
; #define G_SCHED() __builtin_amdgcn_sched_barrier(0)
; #define D_STAGE_A(slot, half, kt) D_STAGE(rsA, voffA, slot, half, kt)
; #define D_STAGE_B(slot, half, kt) D_STAGE(rsB, voffB, slot, half, kt)
; #define D_LDA(dst, slot) do { _Pragma("unroll") for (int m = 0; m < 4; ++m) _Pragma("unroll") for (int k = 0; k < 2; ++k) \
;     dst[m][k] = *(const LDS_AS bf16x8*)(lds + (slot) + aoff + m * 2048 + k * 1024); } while (0)
; #define D_LDB(dst, slot) do { _Pragma("unroll") for (int n = 0; n < 2; ++n) _Pragma("unroll") for (int k = 0; k < 2; ++k) \
;     dst[n][k] = *(const LDS_AS bf16x8*)(lds + (slot) + boff + n * 2048 + k * 1024); } while (0)
; #define D_MMA(ai, bj, At, Bf) do { __builtin_amdgcn_s_setprio(1); _Pragma("unroll") for (int m = 0; m < 4; ++m) _Pragma("unroll") for (int n = 0; n < 2; ++n) _Pragma("unroll") for (int k = 0; k < 2; ++k) \
;     acc[ai][bj][m][n] = __builtin_amdgcn_mfma_f32_16x16x32_bf16(Bf[n][k], At[m][k], acc[ai][bj][m][n], 0, 0, 0); __builtin_amdgcn_s_setprio(0); } while (0)
; #define D_WAIT_L(n) asm volatile("s_waitcnt lgkmcnt(" #n ")" ::: "memory")
; #define D_STAGE_A(slot, half, kt) D_STAGE(rsA, voffA, slot, half, kt)
; #define D_STAGE_B(slot, half, kt) do { _Pragma("unroll") for (int _i = 0; _i < 2; ++_i) { const unsigned _m0 = ldsw + (unsigned)((slot) + _i * 8192); const unsigned _so = (unsigned)(kt) * 128u + (half) * bt_half + _i * bt_piece; \
;     asm volatile("s_mov_b32 m0, %0\n\ts_nop 4\n\tbuffer_load_dwordx4 %1, %2, %3 offen lds" :: "s"(_m0), "v"(voffB0), "s"(rsB), "s"(_so) : "m0", "memory"); } } while (0)
; #define D_WAIT_L(n) asm volatile("s_waitcnt lgkmcnt(" #n ")" ::: "memory")
; template <class Cfg>
; DI void gemm256dma_unit(LDS_AS unsigned char* lds, const Cfg& cfg) {
;     ...
;     D_STAGE_B(G_SB(0, 1), 1, t2);
;     G_WAIT_V(6); G_BAR(); G_SCHED(); D_MMA(1, 1, At, B1); G_BAR(); G_SCHED();
;     D_LDB(B0, G_SB(1, 0)); G_SCHED(); D_LDA(At, G_SA(1, 0)); D_STAGE_A(G_SA(0, 1), 1, t2);
;     D_WAIT_L(8); G_BAR(); D_WAIT_L(0); G_SCHED(); D_MMA(0, 0, At, B0); G_BAR(); G_SCHED();
;     D_LDB(B1, G_SB(1, 1)); D_STAGE_B(G_SB(1, 0), 0, t3);
;     G_BAR(); D_WAIT_L(0); G_SCHED(); D_MMA(0, 1, At, B1); G_BAR(); G_SCHED();
	s_mov_b32 m0, s43
	s_nop 0
	buffer_load_dwordx4 v130, s[8:11], s96 offen lds
	s_nop 0
	s_mov_b32 m0, s54
	s_nop 0
	buffer_load_dwordx4 v136, s[8:11], s96 offen lds
	s_waitcnt vmcnt(6)
	s_barrier
	s_setprio 1
	v_mfma_f32_16x16x32_bf16 v[52:55], v[196:199], v[162:165], v[52:55]
	v_mfma_f32_16x16x32_bf16 v[48:51], v[204:207], v[162:165], v[48:51]
	v_mfma_f32_16x16x32_bf16 v[36:39], v[196:199], v[170:173], v[36:39]
	v_mfma_f32_16x16x32_bf16 v[32:35], v[204:207], v[170:173], v[32:35]
	v_mfma_f32_16x16x32_bf16 v[20:23], v[196:199], v[178:181], v[20:23]
	v_mfma_f32_16x16x32_bf16 v[16:19], v[204:207], v[178:181], v[16:19]
	v_mfma_f32_16x16x32_bf16 v[4:7], v[196:199], v[186:189], v[4:7]
	v_mfma_f32_16x16x32_bf16 v[0:3], v[204:207], v[186:189], v[0:3]
	v_mfma_f32_16x16x32_bf16 v[52:55], v[200:203], v[166:169], v[52:55]
	v_mfma_f32_16x16x32_bf16 v[48:51], v[208:211], v[166:169], v[48:51]
	v_mfma_f32_16x16x32_bf16 v[36:39], v[200:203], v[174:177], v[36:39]
	v_mfma_f32_16x16x32_bf16 v[32:35], v[208:211], v[174:177], v[32:35]
	v_mfma_f32_16x16x32_bf16 v[20:23], v[200:203], v[182:185], v[20:23]
	v_mfma_f32_16x16x32_bf16 v[16:19], v[208:211], v[182:185], v[16:19]
	v_mfma_f32_16x16x32_bf16 v[4:7], v[200:203], v[192:195], v[4:7]
	v_mfma_f32_16x16x32_bf16 v[0:3], v[208:211], v[192:195], v[0:3]
	s_setprio 0
	s_barrier
	v_add_u32_e32 v141, 0x18010, v137
	ds_read_b128 v[142:145], v141
	ds_read_b128 v[150:153], v141 offset:1024
	ds_read_b128 v[154:157], v141 offset:2048
	ds_read_b128 v[158:161], v141 offset:3072
	ds_read_b128 v[162:165], v138 offset:32784
	ds_read_b128 v[166:169], v138 offset:33808
	ds_read_b128 v[170:173], v138 offset:34832
	ds_read_b128 v[174:177], v138 offset:35856
	ds_read_b128 v[178:181], v138 offset:36880
	ds_read_b128 v[182:185], v138 offset:37904
	ds_read_b128 v[186:189], v138 offset:38928
	ds_read_b128 v[192:195], v138 offset:39952
	s_mov_b32 m0, s60
	s_nop 0
	buffer_load_dwordx4 v135, s[20:23], s96 offen lds
	s_nop 0
	s_mov_b32 m0, s61
	s_nop 0
	buffer_load_dwordx4 v132, s[20:23], s96 offen lds
	s_waitcnt lgkmcnt(8)
	s_barrier
	s_waitcnt lgkmcnt(0)
	s_setprio 1
	s_waitcnt lgkmcnt(7)
	v_mfma_f32_16x16x32_bf16 v[124:127], v[142:145], v[162:165], v[124:127]
	v_mfma_f32_16x16x32_bf16 v[120:123], v[154:157], v[162:165], v[120:123]
	s_waitcnt lgkmcnt(5)
	v_mfma_f32_16x16x32_bf16 v[108:111], v[142:145], v[170:173], v[108:111]
	v_mfma_f32_16x16x32_bf16 v[104:107], v[154:157], v[170:173], v[104:107]
	s_waitcnt lgkmcnt(3)
	v_mfma_f32_16x16x32_bf16 v[92:95], v[142:145], v[178:181], v[92:95]
	v_mfma_f32_16x16x32_bf16 v[88:91], v[154:157], v[178:181], v[88:91]
	s_waitcnt lgkmcnt(1)
	v_mfma_f32_16x16x32_bf16 v[76:79], v[142:145], v[186:189], v[76:79]
	v_mfma_f32_16x16x32_bf16 v[72:75], v[154:157], v[186:189], v[72:75]
	v_mfma_f32_16x16x32_bf16 v[124:127], v[150:153], v[166:169], v[124:127]
	v_mfma_f32_16x16x32_bf16 v[120:123], v[158:161], v[166:169], v[120:123]
	v_mfma_f32_16x16x32_bf16 v[108:111], v[150:153], v[174:177], v[108:111]
	v_mfma_f32_16x16x32_bf16 v[104:107], v[158:161], v[174:177], v[104:107]
	v_mfma_f32_16x16x32_bf16 v[92:95], v[150:153], v[182:185], v[92:95]
	v_mfma_f32_16x16x32_bf16 v[88:91], v[158:161], v[182:185], v[88:91]
	s_waitcnt lgkmcnt(0)
	v_mfma_f32_16x16x32_bf16 v[76:79], v[150:153], v[192:195], v[76:79]
	v_mfma_f32_16x16x32_bf16 v[72:75], v[158:161], v[192:195], v[72:75]
	s_setprio 0
	s_barrier
	v_add_u32_e32 v141, 0x1c010, v137
	ds_read_b128 v[196:199], v141
	ds_read_b128 v[200:203], v141 offset:1024
	ds_read_b128 v[204:207], v141 offset:2048
	ds_read_b128 v[208:211], v141 offset:3072
	s_mov_b32 m0, s62
	s_nop 0
	buffer_load_dwordx4 v133, s[8:11], s31 offen lds
	s_nop 0
	s_mov_b32 m0, s63
	s_nop 0
	buffer_load_dwordx4 v128, s[8:11], s31 offen lds
	s_barrier
; #define G_WAIT_V(n) asm volatile("s_waitcnt vmcnt(" #n ")" ::: "memory")
; #define G_BAR() __builtin_amdgcn_s_barrier()
; #define G_SCHED() __builtin_amdgcn_sched_barrier(0)
; #define D_STAGE_A(slot, half, kt) D_STAGE(rsA, voffA, slot, half, kt)
; #define D_STAGE_B(slot, half, kt) D_STAGE(rsB, voffB, slot, half, kt)
; #define D_LDA(dst, slot) do { _Pragma("unroll") for (int m = 0; m < 4; ++m) _Pragma("unroll") for (int k = 0; k < 2; ++k) \
;     dst[m][k] = *(const LDS_AS bf16x8*)(lds + (slot) + aoff + m * 2048 + k * 1024); } while (0)
; #define D_MMA(ai, bj, At, Bf) do { __builtin_amdgcn_s_setprio(1); _Pragma("unroll") for (int m = 0; m < 4; ++m) _Pragma("unroll") for (int n = 0; n < 2; ++n) _Pragma("unroll") for (int k = 0; k < 2; ++k) \
;     acc[ai][bj][m][n] = __builtin_amdgcn_mfma_f32_16x16x32_bf16(Bf[n][k], At[m][k], acc[ai][bj][m][n], 0, 0, 0); __builtin_amdgcn_s_setprio(0); } while (0)
; #define D_WAIT_L(n) asm volatile("s_waitcnt lgkmcnt(" #n ")" ::: "memory")
; #define D_STAGE_A(slot, half, kt) D_STAGE(rsA, voffA, slot, half, kt)
; #define D_STAGE_B(slot, half, kt) do { _Pragma("unroll") for (int _i = 0; _i < 2; ++_i) { const unsigned _m0 = ldsw + (unsigned)((slot) + _i * 8192); const unsigned _so = (unsigned)(kt) * 128u + (half) * bt_half + _i * bt_piece; \
;     asm volatile("s_mov_b32 m0, %0\n\ts_nop 4\n\tbuffer_load_dwordx4 %1, %2, %3 offen lds" :: "s"(_m0), "v"(voffB0), "s"(rsB), "s"(_so) : "m0", "memory"); } } while (0)
; #define D_LDA(dst, slot) do { _Pragma("unroll") for (int m = 0; m < 4; ++m) { \
;     const i32x4 _lo = *(const LDS_AS i32x4*)(lds + (slot) + aoff[0] + m * 2048); const i32x4 _hi = *(const LDS_AS i32x4*)(lds + (slot) + aoff[1] + m * 2048); \
;     dst[m] = __builtin_shufflevector(_lo, _hi, 0, 1, 2, 3, 4, 5, 6, 7); } } while (0)
; #define D_WAIT_L(n) asm volatile("s_waitcnt lgkmcnt(" #n ")" ::: "memory")
; template <class Cfg>
; DI void gemm256dma_unit(LDS_AS unsigned char* lds, const Cfg& cfg) {
;     ...
;     G_BAR(); D_WAIT_L(0); G_SCHED(); D_MMA(0, 1, At, B1); G_BAR(); G_SCHED();
;     D_LDA(At, G_SA(1, 1)); D_STAGE_A(G_SA(1, 0), 0, t3);
;     G_BAR(); D_WAIT_L(0); G_SCHED(); D_MMA(1, 0, At, B0); G_BAR(); G_SCHED();
;     D_STAGE_B(G_SB(1, 1), 1, t3);
;     G_WAIT_V(6); G_BAR(); G_SCHED(); D_MMA(1, 1, At, B1); G_BAR(); G_SCHED();
;   }
;   G_WAIT_V(0);
;   if (wr == 0) G_BAR();
	s_waitcnt lgkmcnt(0)
	s_setprio 1
	s_waitcnt lgkmcnt(3)
	v_mfma_f32_16x16x32_bf16 v[116:119], v[196:199], v[162:165], v[116:119]
	s_waitcnt lgkmcnt(1)
	v_mfma_f32_16x16x32_bf16 v[112:115], v[204:207], v[162:165], v[112:115]
	v_mfma_f32_16x16x32_bf16 v[100:103], v[196:199], v[170:173], v[100:103]
	v_mfma_f32_16x16x32_bf16 v[96:99], v[204:207], v[170:173], v[96:99]
	v_mfma_f32_16x16x32_bf16 v[84:87], v[196:199], v[178:181], v[84:87]
	v_mfma_f32_16x16x32_bf16 v[80:83], v[204:207], v[178:181], v[80:83]
	v_mfma_f32_16x16x32_bf16 v[68:71], v[196:199], v[186:189], v[68:71]
	v_mfma_f32_16x16x32_bf16 v[64:67], v[204:207], v[186:189], v[64:67]
	v_mfma_f32_16x16x32_bf16 v[116:119], v[200:203], v[166:169], v[116:119]
	s_waitcnt lgkmcnt(0)
	v_mfma_f32_16x16x32_bf16 v[112:115], v[208:211], v[166:169], v[112:115]
	v_mfma_f32_16x16x32_bf16 v[100:103], v[200:203], v[174:177], v[100:103]
	v_mfma_f32_16x16x32_bf16 v[96:99], v[208:211], v[174:177], v[96:99]
	v_mfma_f32_16x16x32_bf16 v[84:87], v[200:203], v[182:185], v[84:87]
	v_mfma_f32_16x16x32_bf16 v[80:83], v[208:211], v[182:185], v[80:83]
	v_mfma_f32_16x16x32_bf16 v[68:71], v[200:203], v[192:195], v[68:71]
	v_mfma_f32_16x16x32_bf16 v[64:67], v[208:211], v[192:195], v[64:67]
	s_setprio 0
	s_barrier
	ds_read_b128 v[162:165], v138 offset:49168
	ds_read_b128 v[166:169], v138 offset:50192
	ds_read_b128 v[170:173], v138 offset:51216
	ds_read_b128 v[174:177], v138 offset:52240
	ds_read_b128 v[178:181], v138 offset:53264
	ds_read_b128 v[182:185], v138 offset:54288
	ds_read_b128 v[186:189], v138 offset:55312
	ds_read_b128 v[192:195], v138 offset:56336
	s_mov_b32 m0, s64
	s_nop 0
	buffer_load_dwordx4 v134, s[20:23], s31 offen lds
	s_nop 0
	s_mov_b32 m0, s65
	s_nop 0
	buffer_load_dwordx4 v131, s[20:23], s31 offen lds
	s_barrier
	s_waitcnt lgkmcnt(0)
	s_setprio 1
	s_waitcnt lgkmcnt(7)
	v_mfma_f32_16x16x32_bf16 v[60:63], v[142:145], v[162:165], v[60:63]
	v_mfma_f32_16x16x32_bf16 v[56:59], v[154:157], v[162:165], v[56:59]
	s_waitcnt lgkmcnt(5)
	v_mfma_f32_16x16x32_bf16 v[44:47], v[142:145], v[170:173], v[44:47]
	v_mfma_f32_16x16x32_bf16 v[40:43], v[154:157], v[170:173], v[40:43]
	s_waitcnt lgkmcnt(3)
	v_mfma_f32_16x16x32_bf16 v[28:31], v[142:145], v[178:181], v[28:31]
	v_mfma_f32_16x16x32_bf16 v[24:27], v[154:157], v[178:181], v[24:27]
	s_waitcnt lgkmcnt(1)
	v_mfma_f32_16x16x32_bf16 v[12:15], v[142:145], v[186:189], v[12:15]
	v_mfma_f32_16x16x32_bf16 v[8:11], v[154:157], v[186:189], v[8:11]
	v_mfma_f32_16x16x32_bf16 v[60:63], v[150:153], v[166:169], v[60:63]
	v_mfma_f32_16x16x32_bf16 v[56:59], v[158:161], v[166:169], v[56:59]
	v_mfma_f32_16x16x32_bf16 v[44:47], v[150:153], v[174:177], v[44:47]
	v_mfma_f32_16x16x32_bf16 v[40:43], v[158:161], v[174:177], v[40:43]
	v_mfma_f32_16x16x32_bf16 v[28:31], v[150:153], v[182:185], v[28:31]
	v_mfma_f32_16x16x32_bf16 v[24:27], v[158:161], v[182:185], v[24:27]
	s_waitcnt lgkmcnt(0)
	v_mfma_f32_16x16x32_bf16 v[12:15], v[150:153], v[192:195], v[12:15]
	v_mfma_f32_16x16x32_bf16 v[8:11], v[158:161], v[192:195], v[8:11]
	s_setprio 0
	s_barrier
	s_mov_b32 m0, s66
	s_nop 0
	buffer_load_dwordx4 v130, s[8:11], s31 offen lds
	s_nop 0
	s_mov_b32 m0, s67
	s_nop 0
	buffer_load_dwordx4 v136, s[8:11], s31 offen lds
	s_waitcnt vmcnt(6)
	s_barrier
	s_setprio 1
	v_mfma_f32_16x16x32_bf16 v[52:55], v[196:199], v[162:165], v[52:55]
	v_mfma_f32_16x16x32_bf16 v[48:51], v[204:207], v[162:165], v[48:51]
	v_mfma_f32_16x16x32_bf16 v[36:39], v[196:199], v[170:173], v[36:39]
	v_mfma_f32_16x16x32_bf16 v[32:35], v[204:207], v[170:173], v[32:35]
	v_mfma_f32_16x16x32_bf16 v[20:23], v[196:199], v[178:181], v[20:23]
	v_mfma_f32_16x16x32_bf16 v[16:19], v[204:207], v[178:181], v[16:19]
	v_mfma_f32_16x16x32_bf16 v[4:7], v[196:199], v[186:189], v[4:7]
	v_mfma_f32_16x16x32_bf16 v[0:3], v[204:207], v[186:189], v[0:3]
	v_mfma_f32_16x16x32_bf16 v[52:55], v[200:203], v[166:169], v[52:55]
	v_mfma_f32_16x16x32_bf16 v[48:51], v[208:211], v[166:169], v[48:51]
	v_mfma_f32_16x16x32_bf16 v[36:39], v[200:203], v[174:177], v[36:39]
	v_mfma_f32_16x16x32_bf16 v[32:35], v[208:211], v[174:177], v[32:35]
	v_mfma_f32_16x16x32_bf16 v[20:23], v[200:203], v[182:185], v[20:23]
	v_mfma_f32_16x16x32_bf16 v[16:19], v[208:211], v[182:185], v[16:19]
	v_mfma_f32_16x16x32_bf16 v[4:7], v[200:203], v[192:195], v[4:7]
	v_mfma_f32_16x16x32_bf16 v[0:3], v[208:211], v[192:195], v[0:3]
	s_setprio 0
	s_barrier
	s_mov_b32 s29, s30
	s_cbranch_scc0 .LBB0_279
	s_waitcnt vmcnt(0)
	s_cmpk_lt_u32 s24, 0x100
	s_cbranch_scc0 .LBB0_282
	s_barrier

; #define OPAQUE_TID(P) (((P).wid0 << 6) | lane_id_now())
; DI int tcol_p64(int lc) { return (lc & ~0x30) | ((lc & 0x10) << 1) | ((lc & 0x20) >> 1); }
; DI int tcol_adj(int R) { return (R & 3) | (((R >> 4) & 1) << 2) | (((R >> 2) & 3) << 3) | (R & 0x60); }
; #define D_STAGE_A(slot, half, kt) D_STAGE(rsA, voffA, slot, half, kt)
; #define D_STAGE_B(slot, half, kt) D_STAGE(rsB, voffB, slot, half, kt)
; #define D_STAGE_A(slot, half, kt) D_STAGE(rsA, voffA, slot, half, kt)
;   DI unsigned a_bytes() const { return (unsigned)NTOK * 4096u; }
; template <class Cfg>
; DI void gemm256dma_unit(LDS_AS unsigned char* lds, const Cfg& cfg) {
;   const int tid = OPAQUE_TID(cfg.p), wid = __builtin_amdgcn_readfirstlane(tid >> 6), lane = tid & 63, wr = wid >> 2, wc = wid & 3, fr = lane & 15, fq = lane >> 4;
;   const int nt = cfg.nkt();
;   unsigned voffA[2][2], voffB[2][2];
; #pragma unroll
;   for (int i = 0; i < 2; ++i) {
;     int R, C; stage_rc(tid * 16 + i * 8192, R, C);
;     voffA[0][i] = cfg.a_rowoff(R) + (unsigned)C * 2u;
;     voffA[1][i] = cfg.a_rowoff(128 + R) + (unsigned)C * 2u;
;     voffB[0][i] = cfg.bt_rowoff(0, R) + (unsigned)C * 2u;
;     voffB[1][i] = cfg.bt_rowoff(1, R) + (unsigned)C * 2u;
;   }
;   const __amdgpu_buffer_rsrc_t rsA = __builtin_amdgcn_make_buffer_rsrc((void*)cfg.a_base(), 0, cfg.a_bytes(), 0x00020000);
;   const __amdgpu_buffer_rsrc_t rsB = __builtin_amdgcn_make_buffer_rsrc((void*)cfg.bt_base(), 0, cfg.bt_bytes(), 0x00020000);
;   const unsigned ldsw = (unsigned)__builtin_amdgcn_readfirstlane((int)(unsigned)(size_t)lds) + (unsigned)wid * 1024u;
;     ...
;   const int aoff = lds_byte(wr * 64 + fr, fq * 8), boff = lds_byte(wc * 32 + fr, fq * 8);
;     ...
;   f32x4 acc[2][2][4][2];
; #pragma unroll
;   for (int a = 0; a < 2; ++a)
; #pragma unroll
;     for (int b = 0; b < 2; ++b)
; #pragma unroll
;       for (int m = 0; m < 4; ++m)
; #pragma unroll
;         for (int n = 0; n < 2; ++n) acc[a][b][m][n] = (f32x4){0.f, 0.f, 0.f, 0.f};
;   bf16x8 At[4][2], B0[2][2], B1[2][2];
;   D_STAGE_B(G_SB(0, 0), 0, 0); D_STAGE_A(G_SA(0, 0), 0, 0); D_STAGE_B(G_SB(0, 1), 1, 0); D_STAGE_A(G_SA(0, 1), 1, 0);
;   DI unsigned bt_rowoff(int h, int R) const {
;     const bool rope = ((pn * 4 + 2 * h + ((R >> 6) & 1)) % 3) == 2;
;     return (unsigned)(pn * 256 + 128 * h + (rope ? tcol_p64(R) : tcol_adj(R))) * 1024u;
;   }
.LBB0_811:
	s_mul_hi_i32 s4, s24, 0x2aaaaaab
	s_lshr_b32 s2, s4, 31
	s_add_i32 s4, s4, s2
	s_mul_i32 s2, s4, 6
	s_sub_i32 s17, s24, s2
	v_readlane_b32 s2, v255, 12
	v_mbcnt_lo_u32_b32 v0, -1, 0
	v_mbcnt_hi_u32_b32 v0, -1, v0
	s_lshl_b32 s5, s17, 2
	s_nop 0
	v_or_b32_e32 v1, s2, v0
	v_ashrrev_i32_e32 v2, 31, v1
	v_lshrrev_b32_e32 v2, 26, v2
	v_readfirstlane_b32 s16, v1
	v_lshlrev_b32_e32 v7, 4, v1
	v_add_u32_e32 v2, v1, v2
	v_bfe_i32 v1, v1, 27, 1
	v_lshrrev_b32_e32 v1, 22, v1
	v_add_u32_e32 v1, v7, v1
	v_and_b32_e32 v1, 0xfffffc00, v1
	v_sub_u32_e32 v1, v7, v1
	v_lshrrev_b32_e32 v3, 4, v1
	v_bitop3_b32 v3, v3, v1, 32 bitop3:0x6c
	v_ashrrev_i32_e32 v4, 31, v3
	v_ashrrev_i32_e32 v2, 6, v2
	v_lshrrev_b32_e32 v4, 26, v4
	v_lshlrev_b32_e32 v1, 3, v2
	v_add_u32_e32 v4, v3, v4
	v_and_b32_e32 v1, -16, v1
	v_ashrrev_i32_e32 v4, 6, v4
	v_add_u32_e32 v1, v4, v1
	v_bfe_u32 v6, v1, 6, 1
	v_or_b32_e32 v5, s5, v6
	v_mul_hi_i32 v8, v5, s20
	v_lshrrev_b32_e32 v9, 31, v8
	v_add_u32_e32 v8, v8, v9
	v_lshl_add_u32 v8, v8, 1, v8
	v_sub_u32_e32 v5, v5, v8
	v_cmp_ne_u32_e32 vcc, 2, v5
	v_lshrrev_b32_e32 v5, 2, v1
	v_lshlrev_b32_e32 v12, 1, v1
	v_and_b32_e32 v8, 0x63, v1
	v_and_b32_e32 v9, 4, v5
	v_and_b32_e32 v10, 24, v12
	s_and_saveexec_b64 s[2:3], vcc
	s_xor_b64 s[2:3], exec, s[2:3]
	v_or3_b32 v5, v9, v8, v10
	s_or_saveexec_b64 s[2:3], s[2:3]
	v_lshrrev_b32_e32 v13, 1, v1
	v_and_b32_e32 v11, 0xffffffcf, v1
	v_and_b32_e32 v12, 32, v12
	v_and_b32_e32 v13, 16, v13
	s_xor_b64 exec, exec, s[2:3]
	v_or3_b32 v5, v12, v11, v13
	s_or_b64 exec, exec, s[2:3]
	s_or_b32 s18, s5, 2
	v_or_b32_e32 v6, s18, v6
	v_mul_hi_i32 v14, v6, s20
	v_lshrrev_b32_e32 v15, 31, v14
	v_add_u32_e32 v14, v14, v15
	v_lshl_add_u32 v14, v14, 1, v14
	v_sub_u32_e32 v6, v6, v14
	v_cmp_ne_u32_e32 vcc, 2, v6
	s_and_saveexec_b64 s[2:3], vcc
	s_xor_b64 s[2:3], exec, s[2:3]
	v_or3_b32 v6, v9, v8, v10
	s_andn2_saveexec_b64 s[2:3], s[2:3]
	v_or3_b32 v6, v12, v11, v13
	s_or_b64 exec, exec, s[2:3]
	v_add_u32_e32 v7, 0x2000, v7
	v_ashrrev_i32_e32 v8, 31, v7
	v_lshrrev_b32_e32 v8, 22, v8
	v_add_u32_e32 v8, v7, v8
	v_ashrrev_i32_e32 v8, 10, v8
	v_mul_i32_i24_e32 v9, 0x400, v8
	v_sub_u32_e32 v7, v7, v9
	v_lshrrev_b32_e32 v9, 4, v7
	v_bitop3_b32 v9, v9, v7, 32 bitop3:0x6c
	v_ashrrev_i32_e32 v10, 31, v9
	v_lshrrev_b32_e32 v10, 26, v10
	v_lshlrev_b32_e32 v7, 3, v8
	v_add_u32_e32 v10, v9, v10
	v_and_b32_e32 v7, -16, v7
	v_ashrrev_i32_e32 v10, 6, v10
	v_add_u32_e32 v7, v10, v7
	v_bfe_u32 v12, v7, 6, 1
	v_or_b32_e32 v11, s5, v12
	v_mul_hi_i32 v13, v11, s20
	v_lshrrev_b32_e32 v14, 31, v13
	v_add_u32_e32 v13, v13, v14
	v_lshl_add_u32 v13, v13, 1, v13
	v_sub_u32_e32 v11, v11, v13
	v_cmp_ne_u32_e32 vcc, 2, v11
	v_lshrrev_b32_e32 v11, 2, v7
	v_lshlrev_b32_e32 v17, 1, v7
	v_and_b32_e32 v13, 0x63, v7
	v_and_b32_e32 v14, 4, v11
	v_and_b32_e32 v15, 24, v17
	s_and_saveexec_b64 s[2:3], vcc
	s_xor_b64 s[2:3], exec, s[2:3]
	v_or3_b32 v11, v14, v13, v15
	s_or_saveexec_b64 s[2:3], s[2:3]
	v_lshrrev_b32_e32 v18, 1, v7
	v_and_b32_e32 v16, 0xffffffcf, v7
	v_and_b32_e32 v17, 32, v17
	v_and_b32_e32 v18, 16, v18
	s_xor_b64 exec, exec, s[2:3]
	v_or3_b32 v11, v17, v16, v18
	s_or_b64 exec, exec, s[2:3]
	v_or_b32_e32 v12, s18, v12
	v_mul_hi_i32 v19, v12, s20
	v_lshrrev_b32_e32 v20, 31, v19
	v_add_u32_e32 v19, v19, v20
	v_lshl_add_u32 v19, v19, 1, v19
	v_sub_u32_e32 v12, v12, v19
	v_cmp_ne_u32_e32 vcc, 2, v12
	s_and_saveexec_b64 s[2:3], vcc
	s_xor_b64 s[2:3], exec, s[2:3]
	v_or3_b32 v12, v14, v13, v15
	s_andn2_saveexec_b64 s[2:3], s[2:3]
	v_or3_b32 v12, v17, v16, v18
	s_or_b64 exec, exec, s[2:3]
	v_lshlrev_b32_e32 v10, 6, v10
	v_lshlrev_b32_e32 v4, 6, v4
	v_sub_u32_e32 v9, v9, v10
	v_sub_u32_e32 v3, v3, v4
	s_lshl_b32 s25, s17, 8
	v_lshlrev_b32_e32 v8, 5, v8
	v_ashrrev_i16_sdwa v9, v138, sext(v9) dst_sel:DWORD dst_unused:UNUSED_PAD src0_sel:DWORD src1_sel:BYTE_0
	v_lshlrev_b32_e32 v2, 5, v2
	v_ashrrev_i16_sdwa v3, v138, sext(v3) dst_sel:DWORD dst_unused:UNUSED_PAD src0_sel:DWORD src1_sel:BYTE_0
	v_and_b32_e32 v8, 32, v8
	v_bfe_i32 v9, v9, 0, 16
	v_and_b32_e32 v2, 32, v2
	v_bfe_i32 v3, v3, 0, 16
	s_or_b32 s17, s25, 0x80
	v_add_lshl_u32 v8, v8, v9, 1
	v_add_lshl_u32 v2, v2, v3, 1
	v_add_u32_e32 v3, s17, v6
	s_lshl_b32 s2, s4, 18
	v_lshl_add_u32 v129, v3, 10, v2
	v_lshl_add_u32 v3, v7, 10, v8
	s_ashr_i32 s18, s16, 6
	v_lshl_add_u32 v1, v1, 10, v2
	s_or_b32 s3, s2, 0x20000
	v_add_u32_e32 v130, s2, v3
	v_add_u32_e32 v133, s2, v1
	s_lshl_b32 s2, s18, 10
	v_add_u32_e32 v131, s3, v3
	v_add_u32_e32 v3, s25, v5
	s_add_i32 s43, s2, 0
	v_add_u32_e32 v9, s25, v11
	v_lshl_add_u32 v132, v3, 10, v2
	v_add_u32_e32 v134, s3, v1
	s_add_i32 s3, s43, 0x10010
	s_mov_b32 m0, s3
	s_nop 0
	buffer_load_dwordx4 v132, s[8:11], s22 offen lds
	v_lshl_add_u32 v128, v9, 10, v8
	s_add_i32 s19, s43, 0x12010
	s_mov_b32 m0, s19
	s_nop 0
	buffer_load_dwordx4 v128, s[8:11], s22 offen lds
	s_add_i32 s2, s43, 16
	s_mov_b32 m0, s2
	s_nop 0
	buffer_load_dwordx4 v133, s[12:15], s22 offen lds
	s_add_i32 s26, s43, 0x2010
	s_mov_b32 m0, s26
	s_nop 0
	buffer_load_dwordx4 v130, s[12:15], s22 offen lds
	v_add_u32_e32 v1, s17, v12
	s_add_i32 s27, s43, 0x14010
	s_mov_b32 m0, s27
	s_nop 0
	buffer_load_dwordx4 v129, s[8:11], s22 offen lds
	v_lshl_add_u32 v135, v1, 10, v8
	s_add_i32 s28, s43, 0x16010
	s_mov_b32 m0, s28
	s_nop 0
	buffer_load_dwordx4 v135, s[8:11], s22 offen lds
	s_add_i32 s30, s43, 0x4010
	s_mov_b32 m0, s30
	s_nop 0
	buffer_load_dwordx4 v134, s[12:15], s22 offen lds
	s_add_i32 s31, s43, 0x6010
	s_mov_b32 m0, s31
	s_nop 0
	buffer_load_dwordx4 v131, s[12:15], s22 offen lds
	s_ashr_i32 s33, s16, 8
	s_cmp_lg_u32 s33, 1
	s_cbranch_scc1 .LBB0_829
	s_barrier
; #define G_WAIT_V(n) asm volatile("s_waitcnt vmcnt(" #n ")" ::: "memory")
; #define G_BAR() __builtin_amdgcn_s_barrier()
; #define G_SCHED() __builtin_amdgcn_sched_barrier(0)
; #define D_STAGE_A(slot, half, kt) D_STAGE(rsA, voffA, slot, half, kt)
; #define D_STAGE_B(slot, half, kt) D_STAGE(rsB, voffB, slot, half, kt)
; #define D_LDA(dst, slot) do { _Pragma("unroll") for (int m = 0; m < 4; ++m) _Pragma("unroll") for (int k = 0; k < 2; ++k) \
;     dst[m][k] = *(const LDS_AS bf16x8*)(lds + (slot) + aoff + m * 2048 + k * 1024); } while (0)
; #define D_LDB(dst, slot) do { _Pragma("unroll") for (int n = 0; n < 2; ++n) _Pragma("unroll") for (int k = 0; k < 2; ++k) \
;     dst[n][k] = *(const LDS_AS bf16x8*)(lds + (slot) + boff + n * 2048 + k * 1024); } while (0)
; #define D_MMA(ai, bj, At, Bf) do { __builtin_amdgcn_s_setprio(1); _Pragma("unroll") for (int m = 0; m < 4; ++m) _Pragma("unroll") for (int n = 0; n < 2; ++n) _Pragma("unroll") for (int k = 0; k < 2; ++k) \
;     acc[ai][bj][m][n] = __builtin_amdgcn_mfma_f32_16x16x32_bf16(Bf[n][k], At[m][k], acc[ai][bj][m][n], 0, 0, 0); __builtin_amdgcn_s_setprio(0); } while (0)
; template <class Cfg>
; DI void gemm256dma_unit(LDS_AS unsigned char* lds, const Cfg& cfg) {
;     ...
;   f32x4 acc[2][2][4][2];
; #pragma unroll
;   for (int a = 0; a < 2; ++a)
; #pragma unroll
;     for (int b = 0; b < 2; ++b)
; #pragma unroll
;       for (int m = 0; m < 4; ++m)
; #pragma unroll
;         for (int n = 0; n < 2; ++n) acc[a][b][m][n] = (f32x4){0.f, 0.f, 0.f, 0.f};
;   bf16x8 At[4][2], B0[2][2], B1[2][2];
;   D_STAGE_B(G_SB(0, 0), 0, 0); D_STAGE_A(G_SA(0, 0), 0, 0); D_STAGE_B(G_SB(0, 1), 1, 0); D_STAGE_A(G_SA(0, 1), 1, 0);
;   if (wr == 1) G_BAR();
;   G_WAIT_V(4); G_BAR();
;   D_STAGE_B(G_SB(1, 0), 0, 1); D_STAGE_A(G_SA(1, 0), 0, 1); D_STAGE_B(G_SB(1, 1), 1, 1);
;   G_WAIT_V(6); G_BAR();
; #pragma clang loop unroll(disable)
;   for (int t = 0; t < nt; t += 2) {
;     const int t1 = t + 1;
;     const int t2 = (t + 2 < nt) ? t + 2 : 0;
;     const int t3 = (t + 2 < nt) ? t + 3 : 1;
;     D_LDB(B0, G_SB(0, 0)); G_SCHED(); D_LDA(At, G_SA(0, 0)); D_STAGE_A(G_SA(1, 1), 1, t1);
;     D_WAIT_L(8); G_BAR(); D_WAIT_L(0); G_SCHED(); D_MMA(0, 0, At, B0); G_BAR(); G_SCHED();
;     D_LDB(B1, G_SB(0, 1)); D_STAGE_B(G_SB(0, 0), 0, t2);
;     G_BAR(); D_WAIT_L(0); G_SCHED(); D_MMA(0, 1, At, B1); G_BAR(); G_SCHED();
.LBB0_829:
	v_and_b32_e32 v1, 48, v0
	v_lshlrev_b32_e32 v2, 6, v0
	s_movk_i32 s34, 0x3c0
	v_lshlrev_b32_e32 v0, 2, v0
	s_and_b32 s18, s18, 3
	s_lshl_b32 s29, s33, 6
	s_lshl_b32 s33, s33, 13
	v_and_or_b32 v1, v2, s34, v1
	v_and_b32_e32 v0, 32, v0
	v_bitop3_b32 v2, v1, s33, v0 bitop3:0xde
	s_lshl_b32 s33, s18, 12
	v_bitop3_b32 v1, v1, s33, v0 bitop3:0xde
	s_waitcnt vmcnt(4)
	s_barrier
	s_add_i32 s33, s43, 0x18010
	s_mov_b32 m0, s33
	s_nop 0
	buffer_load_dwordx4 v132, s[8:11], s21 offen lds
	s_add_i32 s34, s43, 0x1a010
	s_mov_b32 m0, s34
	s_nop 0
	buffer_load_dwordx4 v128, s[8:11], s21 offen lds
	s_add_i32 s35, s43, 0x8010
	s_mov_b32 m0, s35
	s_nop 0
	buffer_load_dwordx4 v133, s[12:15], s21 offen lds
	s_add_i32 s36, s43, 0xa010
	s_mov_b32 m0, s36
	s_nop 0
	buffer_load_dwordx4 v130, s[12:15], s21 offen lds
	s_add_i32 s37, s43, 0x1c010
	s_mov_b32 m0, s37
	s_nop 0
	buffer_load_dwordx4 v129, s[8:11], s21 offen lds
	s_add_i32 s39, s43, 0x1e010
	s_mov_b32 m0, s39
	s_nop 0
	buffer_load_dwordx4 v135, s[8:11], s21 offen lds
	s_waitcnt vmcnt(6)
	v_mov_b32_e32 v0, 0
	s_add_i32 s42, s43, 0xc010
	s_add_i32 s43, s43, 0xe010
	s_mov_b32 s47, 0
	s_movk_i32 s46, 0x180
	v_add_u32_e32 v136, 0, v1
	v_add_u32_e32 v137, 0, v2
	v_mov_b32_e32 v1, v0
	v_mov_b32_e32 v2, v0
	v_mov_b32_e32 v3, v0
	v_mov_b32_e32 v4, v0
	v_mov_b32_e32 v5, v0
	v_mov_b32_e32 v6, v0
	v_mov_b32_e32 v7, v0
	v_mov_b32_e32 v16, v0
	v_mov_b32_e32 v17, v0
	v_mov_b32_e32 v18, v0
	v_mov_b32_e32 v19, v0
	v_mov_b32_e32 v20, v0
	v_mov_b32_e32 v21, v0
	v_mov_b32_e32 v22, v0
	v_mov_b32_e32 v23, v0
	v_mov_b32_e32 v32, v0
	v_mov_b32_e32 v33, v0
	v_mov_b32_e32 v34, v0
	v_mov_b32_e32 v35, v0
	v_mov_b32_e32 v36, v0
	v_mov_b32_e32 v37, v0
	v_mov_b32_e32 v38, v0
	v_mov_b32_e32 v39, v0
	v_mov_b32_e32 v48, v0
	v_mov_b32_e32 v49, v0
	v_mov_b32_e32 v50, v0
	v_mov_b32_e32 v51, v0
	v_mov_b32_e32 v52, v0
	v_mov_b32_e32 v53, v0
	v_mov_b32_e32 v54, v0
	v_mov_b32_e32 v55, v0
	v_mov_b32_e32 v8, v0
	v_mov_b32_e32 v9, v0
	v_mov_b32_e32 v10, v0
	v_mov_b32_e32 v11, v0
	v_mov_b32_e32 v12, v0
	v_mov_b32_e32 v13, v0
	v_mov_b32_e32 v14, v0
	v_mov_b32_e32 v15, v0
	v_mov_b32_e32 v24, v0
	v_mov_b32_e32 v25, v0
	v_mov_b32_e32 v26, v0
	v_mov_b32_e32 v27, v0
	v_mov_b32_e32 v28, v0
	v_mov_b32_e32 v29, v0
	v_mov_b32_e32 v30, v0
	v_mov_b32_e32 v31, v0
	v_mov_b32_e32 v40, v0
	v_mov_b32_e32 v41, v0
	v_mov_b32_e32 v42, v0
	v_mov_b32_e32 v43, v0
	v_mov_b32_e32 v44, v0
	v_mov_b32_e32 v45, v0
	v_mov_b32_e32 v46, v0
	v_mov_b32_e32 v47, v0
	v_mov_b32_e32 v56, v0
	v_mov_b32_e32 v57, v0
	v_mov_b32_e32 v58, v0
	v_mov_b32_e32 v59, v0
	v_mov_b32_e32 v60, v0
	v_mov_b32_e32 v61, v0
	v_mov_b32_e32 v62, v0
	v_mov_b32_e32 v63, v0
	v_mov_b32_e32 v64, v0
	v_mov_b32_e32 v65, v0
	v_mov_b32_e32 v66, v0
	v_mov_b32_e32 v67, v0
	v_mov_b32_e32 v68, v0
	v_mov_b32_e32 v69, v0
	v_mov_b32_e32 v70, v0
	v_mov_b32_e32 v71, v0
	v_mov_b32_e32 v80, v0
	v_mov_b32_e32 v81, v0
	v_mov_b32_e32 v82, v0
	v_mov_b32_e32 v83, v0
	v_mov_b32_e32 v84, v0
	v_mov_b32_e32 v85, v0
	v_mov_b32_e32 v86, v0
	v_mov_b32_e32 v87, v0
	v_mov_b32_e32 v96, v0
	v_mov_b32_e32 v97, v0
	v_mov_b32_e32 v98, v0
	v_mov_b32_e32 v99, v0
	v_mov_b32_e32 v100, v0
	v_mov_b32_e32 v101, v0
	v_mov_b32_e32 v102, v0
	v_mov_b32_e32 v103, v0
	v_mov_b32_e32 v112, v0
	v_mov_b32_e32 v113, v0
	v_mov_b32_e32 v114, v0
	v_mov_b32_e32 v115, v0
	v_mov_b32_e32 v116, v0
	v_mov_b32_e32 v117, v0
	v_mov_b32_e32 v118, v0
	v_mov_b32_e32 v119, v0
	v_mov_b32_e32 v72, v0
	v_mov_b32_e32 v73, v0
	v_mov_b32_e32 v74, v0
	v_mov_b32_e32 v75, v0
	v_mov_b32_e32 v76, v0
	v_mov_b32_e32 v77, v0
	v_mov_b32_e32 v78, v0
	v_mov_b32_e32 v79, v0
	v_mov_b32_e32 v88, v0
	v_mov_b32_e32 v89, v0
	v_mov_b32_e32 v90, v0
	v_mov_b32_e32 v91, v0
	v_mov_b32_e32 v92, v0
	v_mov_b32_e32 v93, v0
	v_mov_b32_e32 v94, v0
	v_mov_b32_e32 v95, v0
	v_mov_b32_e32 v104, v0
	v_mov_b32_e32 v105, v0
	v_mov_b32_e32 v106, v0
	v_mov_b32_e32 v107, v0
	v_mov_b32_e32 v108, v0
	v_mov_b32_e32 v109, v0
	v_mov_b32_e32 v110, v0
	v_mov_b32_e32 v111, v0
	v_mov_b32_e32 v120, v0
	v_mov_b32_e32 v121, v0
	v_mov_b32_e32 v122, v0
	v_mov_b32_e32 v123, v0
	v_mov_b32_e32 v124, v0
	v_mov_b32_e32 v125, v0
	v_mov_b32_e32 v126, v0
	v_mov_b32_e32 v127, v0
	s_barrier
.LBB0_830:
	v_add_u32_e32 v139, 0x10010, v136
	ds_read_b128 v[140:143], v139
	ds_read_b128 v[144:147], v139 offset:1024
	ds_read_b128 v[148:151], v139 offset:2048
	ds_read_b128 v[152:155], v139 offset:3072
	s_add_i32 s54, s47, 2
	s_add_i32 s38, s46, 0xffffff00
	s_add_i32 s55, s46, 0xffffff80
	s_cmp_lt_u32 s47, 6
	s_cselect_b32 s60, s55, 0
	s_cselect_b32 s55, s46, 0x80
	s_addk_i32 s46, 0x100
	s_cmp_gt_u32 s47, 5
	ds_read_b128 v[156:159], v137 offset:16
	ds_read_b128 v[160:163], v137 offset:1040
	ds_read_b128 v[164:167], v137 offset:2064
	ds_read_b128 v[168:171], v137 offset:3088
	ds_read_b128 v[172:175], v137 offset:4112
	ds_read_b128 v[176:179], v137 offset:5136
	ds_read_b128 v[180:183], v137 offset:6160
	ds_read_b128 v[184:187], v137 offset:7184
	s_mov_b32 m0, s42
	s_nop 0
	buffer_load_dwordx4 v134, s[12:15], s38 offen lds
	s_nop 0
	s_mov_b32 m0, s43
	s_nop 0
	buffer_load_dwordx4 v131, s[12:15], s38 offen lds
	s_waitcnt lgkmcnt(8)
	s_barrier
; #define G_WAIT_V(n) asm volatile("s_waitcnt vmcnt(" #n ")" ::: "memory")
; #define G_BAR() __builtin_amdgcn_s_barrier()
; #define G_SCHED() __builtin_amdgcn_sched_barrier(0)
; #define D_STAGE_A(slot, half, kt) D_STAGE(rsA, voffA, slot, half, kt)
; #define D_STAGE_B(slot, half, kt) D_STAGE(rsB, voffB, slot, half, kt)
; #define D_LDA(dst, slot) do { _Pragma("unroll") for (int m = 0; m < 4; ++m) _Pragma("unroll") for (int k = 0; k < 2; ++k) \
;     dst[m][k] = *(const LDS_AS bf16x8*)(lds + (slot) + aoff + m * 2048 + k * 1024); } while (0)
; #define D_LDB(dst, slot) do { _Pragma("unroll") for (int n = 0; n < 2; ++n) _Pragma("unroll") for (int k = 0; k < 2; ++k) \
;     dst[n][k] = *(const LDS_AS bf16x8*)(lds + (slot) + boff + n * 2048 + k * 1024); } while (0)
; #define D_MMA(ai, bj, At, Bf) do { __builtin_amdgcn_s_setprio(1); _Pragma("unroll") for (int m = 0; m < 4; ++m) _Pragma("unroll") for (int n = 0; n < 2; ++n) _Pragma("unroll") for (int k = 0; k < 2; ++k) \
;     acc[ai][bj][m][n] = __builtin_amdgcn_mfma_f32_16x16x32_bf16(Bf[n][k], At[m][k], acc[ai][bj][m][n], 0, 0, 0); __builtin_amdgcn_s_setprio(0); } while (0)
; #define D_WAIT_L(n) asm volatile("s_waitcnt lgkmcnt(" #n ")" ::: "memory")
; #define D_STAGE_A(slot, half, kt) D_STAGE(rsA, voffA, slot, half, kt)
; #define D_WAIT_L(n) asm volatile("s_waitcnt lgkmcnt(" #n ")" ::: "memory")
; template <class Cfg>
; DI void gemm256dma_unit(LDS_AS unsigned char* lds, const Cfg& cfg) {
;     ...
;     D_WAIT_L(8); G_BAR(); D_WAIT_L(0); G_SCHED(); D_MMA(0, 0, At, B0); G_BAR(); G_SCHED();
;     D_LDB(B1, G_SB(0, 1)); D_STAGE_B(G_SB(0, 0), 0, t2);
;     G_BAR(); D_WAIT_L(0); G_SCHED(); D_MMA(0, 1, At, B1); G_BAR(); G_SCHED();
;     D_LDA(At, G_SA(0, 1)); D_STAGE_A(G_SA(0, 0), 0, t2);
;     G_BAR(); D_WAIT_L(0); G_SCHED(); D_MMA(1, 0, At, B0); G_BAR(); G_SCHED();
;     D_STAGE_B(G_SB(0, 1), 1, t2);
;     G_WAIT_V(6); G_BAR(); G_SCHED(); D_MMA(1, 1, At, B1); G_BAR(); G_SCHED();
;     D_LDB(B0, G_SB(1, 0)); G_SCHED(); D_LDA(At, G_SA(1, 0)); D_STAGE_A(G_SA(0, 1), 1, t2);
;     D_WAIT_L(8); G_BAR(); D_WAIT_L(0); G_SCHED(); D_MMA(0, 0, At, B0); G_BAR(); G_SCHED();
;     D_LDB(B1, G_SB(1, 1)); D_STAGE_B(G_SB(1, 0), 0, t3);
;     G_BAR(); D_WAIT_L(0); G_SCHED(); D_MMA(0, 1, At, B1); G_BAR(); G_SCHED();
	s_waitcnt lgkmcnt(0)
	s_setprio 1
	s_waitcnt lgkmcnt(7)
	v_mfma_f32_16x16x32_bf16 v[124:127], v[140:143], v[156:159], v[124:127]
	v_mfma_f32_16x16x32_bf16 v[120:123], v[148:151], v[156:159], v[120:123]
	s_waitcnt lgkmcnt(5)
	v_mfma_f32_16x16x32_bf16 v[108:111], v[140:143], v[164:167], v[108:111]
	v_mfma_f32_16x16x32_bf16 v[104:107], v[148:151], v[164:167], v[104:107]
	s_waitcnt lgkmcnt(3)
	v_mfma_f32_16x16x32_bf16 v[92:95], v[140:143], v[172:175], v[92:95]
	v_mfma_f32_16x16x32_bf16 v[88:91], v[148:151], v[172:175], v[88:91]
	s_waitcnt lgkmcnt(1)
	v_mfma_f32_16x16x32_bf16 v[76:79], v[140:143], v[180:183], v[76:79]
	v_mfma_f32_16x16x32_bf16 v[72:75], v[148:151], v[180:183], v[72:75]
	v_mfma_f32_16x16x32_bf16 v[124:127], v[144:147], v[160:163], v[124:127]
	v_mfma_f32_16x16x32_bf16 v[120:123], v[152:155], v[160:163], v[120:123]
	v_mfma_f32_16x16x32_bf16 v[108:111], v[144:147], v[168:171], v[108:111]
	v_mfma_f32_16x16x32_bf16 v[104:107], v[152:155], v[168:171], v[104:107]
	v_mfma_f32_16x16x32_bf16 v[92:95], v[144:147], v[176:179], v[92:95]
	v_mfma_f32_16x16x32_bf16 v[88:91], v[152:155], v[176:179], v[88:91]
	s_waitcnt lgkmcnt(0)
	v_mfma_f32_16x16x32_bf16 v[76:79], v[144:147], v[184:187], v[76:79]
	v_mfma_f32_16x16x32_bf16 v[72:75], v[152:155], v[184:187], v[72:75]
	s_setprio 0
	s_barrier
	v_add_u32_e32 v139, 0x14010, v136
	ds_read_b128 v[192:195], v139
	ds_read_b128 v[196:199], v139 offset:1024
	ds_read_b128 v[200:203], v139 offset:2048
	ds_read_b128 v[204:207], v139 offset:3072
	s_mov_b32 m0, s3
	s_nop 0
	buffer_load_dwordx4 v132, s[8:11], s60 offen lds
	s_nop 0
	s_mov_b32 m0, s19
	s_nop 0
	buffer_load_dwordx4 v128, s[8:11], s60 offen lds
	s_barrier
	s_waitcnt lgkmcnt(0)
	s_setprio 1
	s_waitcnt lgkmcnt(3)
	v_mfma_f32_16x16x32_bf16 v[116:119], v[192:195], v[156:159], v[116:119]
	s_waitcnt lgkmcnt(1)
	v_mfma_f32_16x16x32_bf16 v[112:115], v[200:203], v[156:159], v[112:115]
	v_mfma_f32_16x16x32_bf16 v[100:103], v[192:195], v[164:167], v[100:103]
	v_mfma_f32_16x16x32_bf16 v[96:99], v[200:203], v[164:167], v[96:99]
	v_mfma_f32_16x16x32_bf16 v[84:87], v[192:195], v[172:175], v[84:87]
	v_mfma_f32_16x16x32_bf16 v[80:83], v[200:203], v[172:175], v[80:83]
	v_mfma_f32_16x16x32_bf16 v[68:71], v[192:195], v[180:183], v[68:71]
	v_mfma_f32_16x16x32_bf16 v[64:67], v[200:203], v[180:183], v[64:67]
	v_mfma_f32_16x16x32_bf16 v[116:119], v[196:199], v[160:163], v[116:119]
	s_waitcnt lgkmcnt(0)
	v_mfma_f32_16x16x32_bf16 v[112:115], v[204:207], v[160:163], v[112:115]
	v_mfma_f32_16x16x32_bf16 v[100:103], v[196:199], v[168:171], v[100:103]
	v_mfma_f32_16x16x32_bf16 v[96:99], v[204:207], v[168:171], v[96:99]
	v_mfma_f32_16x16x32_bf16 v[84:87], v[196:199], v[176:179], v[84:87]
	v_mfma_f32_16x16x32_bf16 v[80:83], v[204:207], v[176:179], v[80:83]
	v_mfma_f32_16x16x32_bf16 v[68:71], v[196:199], v[184:187], v[68:71]
	v_mfma_f32_16x16x32_bf16 v[64:67], v[204:207], v[184:187], v[64:67]
	s_setprio 0
	s_barrier
	ds_read_b128 v[156:159], v137 offset:16400
	ds_read_b128 v[160:163], v137 offset:17424
	ds_read_b128 v[164:167], v137 offset:18448
	ds_read_b128 v[168:171], v137 offset:19472
	ds_read_b128 v[172:175], v137 offset:20496
	ds_read_b128 v[176:179], v137 offset:21520
	ds_read_b128 v[180:183], v137 offset:22544
	ds_read_b128 v[184:187], v137 offset:23568
	s_mov_b32 m0, s2
	s_nop 0
	buffer_load_dwordx4 v133, s[12:15], s60 offen lds
	s_nop 0
	s_mov_b32 m0, s26
	s_nop 0
	buffer_load_dwordx4 v130, s[12:15], s60 offen lds
	s_barrier
	s_waitcnt lgkmcnt(0)
	s_setprio 1
	s_waitcnt lgkmcnt(7)
	v_mfma_f32_16x16x32_bf16 v[60:63], v[140:143], v[156:159], v[60:63]
	v_mfma_f32_16x16x32_bf16 v[56:59], v[148:151], v[156:159], v[56:59]
	s_waitcnt lgkmcnt(5)
	v_mfma_f32_16x16x32_bf16 v[44:47], v[140:143], v[164:167], v[44:47]
	v_mfma_f32_16x16x32_bf16 v[40:43], v[148:151], v[164:167], v[40:43]
	s_waitcnt lgkmcnt(3)
	v_mfma_f32_16x16x32_bf16 v[28:31], v[140:143], v[172:175], v[28:31]
	v_mfma_f32_16x16x32_bf16 v[24:27], v[148:151], v[172:175], v[24:27]
	s_waitcnt lgkmcnt(1)
	v_mfma_f32_16x16x32_bf16 v[12:15], v[140:143], v[180:183], v[12:15]
	v_mfma_f32_16x16x32_bf16 v[8:11], v[148:151], v[180:183], v[8:11]
	v_mfma_f32_16x16x32_bf16 v[60:63], v[144:147], v[160:163], v[60:63]
	v_mfma_f32_16x16x32_bf16 v[56:59], v[152:155], v[160:163], v[56:59]
	v_mfma_f32_16x16x32_bf16 v[44:47], v[144:147], v[168:171], v[44:47]
	v_mfma_f32_16x16x32_bf16 v[40:43], v[152:155], v[168:171], v[40:43]
	v_mfma_f32_16x16x32_bf16 v[28:31], v[144:147], v[176:179], v[28:31]
	v_mfma_f32_16x16x32_bf16 v[24:27], v[152:155], v[176:179], v[24:27]
	s_waitcnt lgkmcnt(0)
	v_mfma_f32_16x16x32_bf16 v[12:15], v[144:147], v[184:187], v[12:15]
	v_mfma_f32_16x16x32_bf16 v[8:11], v[152:155], v[184:187], v[8:11]
	s_setprio 0
	s_barrier
	s_mov_b32 m0, s27
	s_nop 0
	buffer_load_dwordx4 v129, s[8:11], s60 offen lds
	s_nop 0
	s_mov_b32 m0, s28
	s_nop 0
	buffer_load_dwordx4 v135, s[8:11], s60 offen lds
	s_waitcnt vmcnt(6)
	s_barrier
	s_setprio 1
	v_mfma_f32_16x16x32_bf16 v[52:55], v[192:195], v[156:159], v[52:55]
	v_mfma_f32_16x16x32_bf16 v[48:51], v[200:203], v[156:159], v[48:51]
	v_mfma_f32_16x16x32_bf16 v[36:39], v[192:195], v[164:167], v[36:39]
	v_mfma_f32_16x16x32_bf16 v[32:35], v[200:203], v[164:167], v[32:35]
	v_mfma_f32_16x16x32_bf16 v[20:23], v[192:195], v[172:175], v[20:23]
	v_mfma_f32_16x16x32_bf16 v[16:19], v[200:203], v[172:175], v[16:19]
	v_mfma_f32_16x16x32_bf16 v[4:7], v[192:195], v[180:183], v[4:7]
	v_mfma_f32_16x16x32_bf16 v[0:3], v[200:203], v[180:183], v[0:3]
	v_mfma_f32_16x16x32_bf16 v[52:55], v[196:199], v[160:163], v[52:55]
	v_mfma_f32_16x16x32_bf16 v[48:51], v[204:207], v[160:163], v[48:51]
	v_mfma_f32_16x16x32_bf16 v[36:39], v[196:199], v[168:171], v[36:39]
	v_mfma_f32_16x16x32_bf16 v[32:35], v[204:207], v[168:171], v[32:35]
	v_mfma_f32_16x16x32_bf16 v[20:23], v[196:199], v[176:179], v[20:23]
	v_mfma_f32_16x16x32_bf16 v[16:19], v[204:207], v[176:179], v[16:19]
	v_mfma_f32_16x16x32_bf16 v[4:7], v[196:199], v[184:187], v[4:7]
	v_mfma_f32_16x16x32_bf16 v[0:3], v[204:207], v[184:187], v[0:3]
	s_setprio 0
	s_barrier
; #define G_WAIT_V(n) asm volatile("s_waitcnt vmcnt(" #n ")" ::: "memory")
; #define G_BAR() __builtin_amdgcn_s_barrier()
; #define G_SCHED() __builtin_amdgcn_sched_barrier(0)
; #define D_STAGE_A(slot, half, kt) D_STAGE(rsA, voffA, slot, half, kt)
; #define D_STAGE_B(slot, half, kt) D_STAGE(rsB, voffB, slot, half, kt)
; #define D_LDA(dst, slot) do { _Pragma("unroll") for (int m = 0; m < 4; ++m) _Pragma("unroll") for (int k = 0; k < 2; ++k) \
;     dst[m][k] = *(const LDS_AS bf16x8*)(lds + (slot) + aoff + m * 2048 + k * 1024); } while (0)
; #define D_LDB(dst, slot) do { _Pragma("unroll") for (int n = 0; n < 2; ++n) _Pragma("unroll") for (int k = 0; k < 2; ++k) \
;     dst[n][k] = *(const LDS_AS bf16x8*)(lds + (slot) + boff + n * 2048 + k * 1024); } while (0)
; #define D_MMA(ai, bj, At, Bf) do { __builtin_amdgcn_s_setprio(1); _Pragma("unroll") for (int m = 0; m < 4; ++m) _Pragma("unroll") for (int n = 0; n < 2; ++n) _Pragma("unroll") for (int k = 0; k < 2; ++k) \
;     acc[ai][bj][m][n] = __builtin_amdgcn_mfma_f32_16x16x32_bf16(Bf[n][k], At[m][k], acc[ai][bj][m][n], 0, 0, 0); __builtin_amdgcn_s_setprio(0); } while (0)
; #define D_WAIT_L(n) asm volatile("s_waitcnt lgkmcnt(" #n ")" ::: "memory")
; #define D_STAGE_A(slot, half, kt) D_STAGE(rsA, voffA, slot, half, kt)
; #define D_LDA(dst, slot) do { _Pragma("unroll") for (int m = 0; m < 4; ++m) { \
;     const i32x4 _lo = *(const LDS_AS i32x4*)(lds + (slot) + aoff[0] + m * 2048); const i32x4 _hi = *(const LDS_AS i32x4*)(lds + (slot) + aoff[1] + m * 2048); \
;     dst[m] = __builtin_shufflevector(_lo, _hi, 0, 1, 2, 3, 4, 5, 6, 7); } } while (0)
; template <class Cfg>
; DI void gemm256dma_unit(LDS_AS unsigned char* lds, const Cfg& cfg) {
;     ...
;     D_LDB(B0, G_SB(1, 0)); G_SCHED(); D_LDA(At, G_SA(1, 0)); D_STAGE_A(G_SA(0, 1), 1, t2);
;     D_WAIT_L(8); G_BAR(); D_WAIT_L(0); G_SCHED(); D_MMA(0, 0, At, B0); G_BAR(); G_SCHED();
;     D_LDB(B1, G_SB(1, 1)); D_STAGE_B(G_SB(1, 0), 0, t3);
;     G_BAR(); D_WAIT_L(0); G_SCHED(); D_MMA(0, 1, At, B1); G_BAR(); G_SCHED();
;     D_LDA(At, G_SA(1, 1)); D_STAGE_A(G_SA(1, 0), 0, t3);
;     G_BAR(); D_WAIT_L(0); G_SCHED(); D_MMA(1, 0, At, B0); G_BAR(); G_SCHED();
;     D_STAGE_B(G_SB(1, 1), 1, t3);
;     G_WAIT_V(6); G_BAR(); G_SCHED(); D_MMA(1, 1, At, B1); G_BAR(); G_SCHED();
;   }
;   G_WAIT_V(0);
;   if (wr == 0) G_BAR();
	v_add_u32_e32 v139, 0x18010, v136
	ds_read_b128 v[140:143], v139
	ds_read_b128 v[144:147], v139 offset:1024
	ds_read_b128 v[148:151], v139 offset:2048
	ds_read_b128 v[152:155], v139 offset:3072
	ds_read_b128 v[156:159], v137 offset:32784
	ds_read_b128 v[160:163], v137 offset:33808
	ds_read_b128 v[164:167], v137 offset:34832
	ds_read_b128 v[168:171], v137 offset:35856
	ds_read_b128 v[172:175], v137 offset:36880
	ds_read_b128 v[176:179], v137 offset:37904
	ds_read_b128 v[180:183], v137 offset:38928
	ds_read_b128 v[184:187], v137 offset:39952
	s_mov_b32 m0, s30
	s_nop 0
	buffer_load_dwordx4 v134, s[12:15], s60 offen lds
	s_nop 0
	s_mov_b32 m0, s31
	s_nop 0
	buffer_load_dwordx4 v131, s[12:15], s60 offen lds
	s_waitcnt lgkmcnt(8)
	s_barrier
	s_waitcnt lgkmcnt(0)
	s_setprio 1
	s_waitcnt lgkmcnt(7)
	v_mfma_f32_16x16x32_bf16 v[124:127], v[140:143], v[156:159], v[124:127]
	v_mfma_f32_16x16x32_bf16 v[120:123], v[148:151], v[156:159], v[120:123]
	s_waitcnt lgkmcnt(5)
	v_mfma_f32_16x16x32_bf16 v[108:111], v[140:143], v[164:167], v[108:111]
	v_mfma_f32_16x16x32_bf16 v[104:107], v[148:151], v[164:167], v[104:107]
	s_waitcnt lgkmcnt(3)
	v_mfma_f32_16x16x32_bf16 v[92:95], v[140:143], v[172:175], v[92:95]
	v_mfma_f32_16x16x32_bf16 v[88:91], v[148:151], v[172:175], v[88:91]
	s_waitcnt lgkmcnt(1)
	v_mfma_f32_16x16x32_bf16 v[76:79], v[140:143], v[180:183], v[76:79]
	v_mfma_f32_16x16x32_bf16 v[72:75], v[148:151], v[180:183], v[72:75]
	v_mfma_f32_16x16x32_bf16 v[124:127], v[144:147], v[160:163], v[124:127]
	v_mfma_f32_16x16x32_bf16 v[120:123], v[152:155], v[160:163], v[120:123]
	v_mfma_f32_16x16x32_bf16 v[108:111], v[144:147], v[168:171], v[108:111]
	v_mfma_f32_16x16x32_bf16 v[104:107], v[152:155], v[168:171], v[104:107]
	v_mfma_f32_16x16x32_bf16 v[92:95], v[144:147], v[176:179], v[92:95]
	v_mfma_f32_16x16x32_bf16 v[88:91], v[152:155], v[176:179], v[88:91]
	s_waitcnt lgkmcnt(0)
	v_mfma_f32_16x16x32_bf16 v[76:79], v[144:147], v[184:187], v[76:79]
	v_mfma_f32_16x16x32_bf16 v[72:75], v[152:155], v[184:187], v[72:75]
	s_setprio 0
	s_barrier
	v_add_u32_e32 v139, 0x1c010, v136
	ds_read_b128 v[192:195], v139
	ds_read_b128 v[196:199], v139 offset:1024
	ds_read_b128 v[200:203], v139 offset:2048
	ds_read_b128 v[204:207], v139 offset:3072
	s_mov_b32 m0, s33
	s_nop 0
	buffer_load_dwordx4 v132, s[8:11], s55 offen lds
	s_nop 0
	s_mov_b32 m0, s34
	s_nop 0
	buffer_load_dwordx4 v128, s[8:11], s55 offen lds
	s_barrier
	s_waitcnt lgkmcnt(0)
	s_setprio 1
	s_waitcnt lgkmcnt(3)
	v_mfma_f32_16x16x32_bf16 v[116:119], v[192:195], v[156:159], v[116:119]
	s_waitcnt lgkmcnt(1)
	v_mfma_f32_16x16x32_bf16 v[112:115], v[200:203], v[156:159], v[112:115]
	v_mfma_f32_16x16x32_bf16 v[100:103], v[192:195], v[164:167], v[100:103]
	v_mfma_f32_16x16x32_bf16 v[96:99], v[200:203], v[164:167], v[96:99]
	v_mfma_f32_16x16x32_bf16 v[84:87], v[192:195], v[172:175], v[84:87]
	v_mfma_f32_16x16x32_bf16 v[80:83], v[200:203], v[172:175], v[80:83]
	v_mfma_f32_16x16x32_bf16 v[68:71], v[192:195], v[180:183], v[68:71]
	v_mfma_f32_16x16x32_bf16 v[64:67], v[200:203], v[180:183], v[64:67]
	v_mfma_f32_16x16x32_bf16 v[116:119], v[196:199], v[160:163], v[116:119]
	s_waitcnt lgkmcnt(0)
	v_mfma_f32_16x16x32_bf16 v[112:115], v[204:207], v[160:163], v[112:115]
	v_mfma_f32_16x16x32_bf16 v[100:103], v[196:199], v[168:171], v[100:103]
	v_mfma_f32_16x16x32_bf16 v[96:99], v[204:207], v[168:171], v[96:99]
	v_mfma_f32_16x16x32_bf16 v[84:87], v[196:199], v[176:179], v[84:87]
	v_mfma_f32_16x16x32_bf16 v[80:83], v[204:207], v[176:179], v[80:83]
	v_mfma_f32_16x16x32_bf16 v[68:71], v[196:199], v[184:187], v[68:71]
	v_mfma_f32_16x16x32_bf16 v[64:67], v[204:207], v[184:187], v[64:67]
	s_setprio 0
	s_barrier
	ds_read_b128 v[156:159], v137 offset:49168
	ds_read_b128 v[160:163], v137 offset:50192
	ds_read_b128 v[164:167], v137 offset:51216
	ds_read_b128 v[168:171], v137 offset:52240
	ds_read_b128 v[172:175], v137 offset:53264
	ds_read_b128 v[176:179], v137 offset:54288
	ds_read_b128 v[180:183], v137 offset:55312
	ds_read_b128 v[184:187], v137 offset:56336
	s_mov_b32 m0, s35
	s_nop 0
	buffer_load_dwordx4 v133, s[12:15], s55 offen lds
	s_nop 0
	s_mov_b32 m0, s36
	s_nop 0
	buffer_load_dwordx4 v130, s[12:15], s55 offen lds
	s_barrier
	s_waitcnt lgkmcnt(0)
	s_setprio 1
	s_waitcnt lgkmcnt(7)
	v_mfma_f32_16x16x32_bf16 v[60:63], v[140:143], v[156:159], v[60:63]
	v_mfma_f32_16x16x32_bf16 v[56:59], v[148:151], v[156:159], v[56:59]
	s_waitcnt lgkmcnt(5)
	v_mfma_f32_16x16x32_bf16 v[44:47], v[140:143], v[164:167], v[44:47]
	v_mfma_f32_16x16x32_bf16 v[40:43], v[148:151], v[164:167], v[40:43]
	s_waitcnt lgkmcnt(3)
	v_mfma_f32_16x16x32_bf16 v[28:31], v[140:143], v[172:175], v[28:31]
	v_mfma_f32_16x16x32_bf16 v[24:27], v[148:151], v[172:175], v[24:27]
	s_waitcnt lgkmcnt(1)
	v_mfma_f32_16x16x32_bf16 v[12:15], v[140:143], v[180:183], v[12:15]
	v_mfma_f32_16x16x32_bf16 v[8:11], v[148:151], v[180:183], v[8:11]
	v_mfma_f32_16x16x32_bf16 v[60:63], v[144:147], v[160:163], v[60:63]
	v_mfma_f32_16x16x32_bf16 v[56:59], v[152:155], v[160:163], v[56:59]
	v_mfma_f32_16x16x32_bf16 v[44:47], v[144:147], v[168:171], v[44:47]
	v_mfma_f32_16x16x32_bf16 v[40:43], v[152:155], v[168:171], v[40:43]
	v_mfma_f32_16x16x32_bf16 v[28:31], v[144:147], v[176:179], v[28:31]
	v_mfma_f32_16x16x32_bf16 v[24:27], v[152:155], v[176:179], v[24:27]
	s_waitcnt lgkmcnt(0)
	v_mfma_f32_16x16x32_bf16 v[12:15], v[144:147], v[184:187], v[12:15]
	v_mfma_f32_16x16x32_bf16 v[8:11], v[152:155], v[184:187], v[8:11]
	s_setprio 0
	s_barrier
	s_mov_b32 m0, s37
	s_nop 0
	buffer_load_dwordx4 v129, s[8:11], s55 offen lds
	s_nop 0
	s_mov_b32 m0, s39
	s_nop 0
	buffer_load_dwordx4 v135, s[8:11], s55 offen lds
	s_waitcnt vmcnt(6)
	s_barrier
	s_setprio 1
	v_mfma_f32_16x16x32_bf16 v[52:55], v[192:195], v[156:159], v[52:55]
	v_mfma_f32_16x16x32_bf16 v[48:51], v[200:203], v[156:159], v[48:51]
	v_mfma_f32_16x16x32_bf16 v[36:39], v[192:195], v[164:167], v[36:39]
	v_mfma_f32_16x16x32_bf16 v[32:35], v[200:203], v[164:167], v[32:35]
	v_mfma_f32_16x16x32_bf16 v[20:23], v[192:195], v[172:175], v[20:23]
	v_mfma_f32_16x16x32_bf16 v[16:19], v[200:203], v[172:175], v[16:19]
	v_mfma_f32_16x16x32_bf16 v[4:7], v[192:195], v[180:183], v[4:7]
	v_mfma_f32_16x16x32_bf16 v[0:3], v[200:203], v[180:183], v[0:3]
	v_mfma_f32_16x16x32_bf16 v[52:55], v[196:199], v[160:163], v[52:55]
	v_mfma_f32_16x16x32_bf16 v[48:51], v[204:207], v[160:163], v[48:51]
	v_mfma_f32_16x16x32_bf16 v[36:39], v[196:199], v[168:171], v[36:39]
	v_mfma_f32_16x16x32_bf16 v[32:35], v[204:207], v[168:171], v[32:35]
	v_mfma_f32_16x16x32_bf16 v[20:23], v[196:199], v[176:179], v[20:23]
	v_mfma_f32_16x16x32_bf16 v[16:19], v[204:207], v[176:179], v[16:19]
	v_mfma_f32_16x16x32_bf16 v[4:7], v[196:199], v[184:187], v[4:7]
	v_mfma_f32_16x16x32_bf16 v[0:3], v[204:207], v[184:187], v[0:3]
	s_setprio 0
	s_barrier
	s_mov_b32 s47, s54
	s_cbranch_scc0 .LBB0_830
	s_waitcnt vmcnt(0)
	s_cmpk_lt_u32 s16, 0x100
	s_cbranch_scc0 .LBB0_833
	s_barrier

; #define OPAQUE_TID(P) (((P).wid0 << 6) | lane_id_now())
; #define G_WAIT_V(n) asm volatile("s_waitcnt vmcnt(" #n ")" ::: "memory")
; #define G_BAR() __builtin_amdgcn_s_barrier()
; #define D_STAGE_A(slot, half, kt) D_STAGE(rsA, voffA, slot, half, kt)
; #define D_STAGE_B(slot, half, kt) D_STAGE(rsB, voffB, slot, half, kt)
; #define D_STAGE_A(slot, half, kt) D_STAGE(rsA, voffA, slot, half, kt)
;   DI unsigned bt_rowoff(int h, int R) const { return (unsigned)(pn * 256 + 128 * h + (pn < 15 ? tcol_adj(R) : tcol_p64(R))) * 4096u; }
;   DI unsigned a_bytes() const { return (unsigned)NTOK * 4096u; }
; template <class Cfg>
; DI void gemm256dma_unit(LDS_AS unsigned char* lds, const Cfg& cfg) {
;   const int tid = OPAQUE_TID(cfg.p), wid = __builtin_amdgcn_readfirstlane(tid >> 6), lane = tid & 63, wr = wid >> 2, wc = wid & 3, fr = lane & 15, fq = lane >> 4;
;   const int nt = cfg.nkt();
;   unsigned voffA[2][2], voffB[2][2];
; #pragma unroll
;   for (int i = 0; i < 2; ++i) {
;     int R, C; stage_rc(tid * 16 + i * 8192, R, C);
;     voffA[0][i] = cfg.a_rowoff(R) + (unsigned)C * 2u;
;     voffA[1][i] = cfg.a_rowoff(128 + R) + (unsigned)C * 2u;
;     voffB[0][i] = cfg.bt_rowoff(0, R) + (unsigned)C * 2u;
;     voffB[1][i] = cfg.bt_rowoff(1, R) + (unsigned)C * 2u;
;   }
;   const __amdgpu_buffer_rsrc_t rsA = __builtin_amdgcn_make_buffer_rsrc((void*)cfg.a_base(), 0, cfg.a_bytes(), 0x00020000);
;   const __amdgpu_buffer_rsrc_t rsB = __builtin_amdgcn_make_buffer_rsrc((void*)cfg.bt_base(), 0, cfg.bt_bytes(), 0x00020000);
;   const unsigned ldsw = (unsigned)__builtin_amdgcn_readfirstlane((int)(unsigned)(size_t)lds) + (unsigned)wid * 1024u;
;     ...
;   const int aoff = lds_byte(wr * 64 + fr, fq * 8), boff = lds_byte(wc * 32 + fr, fq * 8);
;     ...
;   f32x4 acc[2][2][4][2];
; #pragma unroll
;   for (int a = 0; a < 2; ++a)
; #pragma unroll
;     for (int b = 0; b < 2; ++b)
; #pragma unroll
;       for (int m = 0; m < 4; ++m)
; #pragma unroll
;         for (int n = 0; n < 2; ++n) acc[a][b][m][n] = (f32x4){0.f, 0.f, 0.f, 0.f};
;   bf16x8 At[4][2], B0[2][2], B1[2][2];
;   D_STAGE_B(G_SB(0, 0), 0, 0); D_STAGE_A(G_SA(0, 0), 0, 0); D_STAGE_B(G_SB(0, 1), 1, 0); D_STAGE_A(G_SA(0, 1), 1, 0);
;   if (wr == 1) G_BAR();
;   G_WAIT_V(4); G_BAR();
;   D_STAGE_B(G_SB(1, 0), 0, 1); D_STAGE_A(G_SA(1, 0), 0, 1); D_STAGE_B(G_SB(1, 1), 1, 1);
;   G_WAIT_V(6); G_BAR();
.LBB0_953:
	v_readlane_b32 s8, v255, 12
	v_mbcnt_lo_u32_b32 v0, -1, 0
	v_mbcnt_hi_u32_b32 v0, -1, v0
	s_ashr_i32 s14, s10, 3
	s_lshl_b32 s9, s14, 17
	v_or_b32_e32 v1, s8, v0
	v_ashrrev_i32_e32 v3, 31, v1
	v_lshrrev_b32_e32 v3, 26, v3
	v_readfirstlane_b32 s16, v1
	v_lshlrev_b32_e32 v2, 4, v1
	v_add_u32_e32 v3, v1, v3
	v_bfe_i32 v1, v1, 27, 1
	v_lshrrev_b32_e32 v1, 22, v1
	v_add_u32_e32 v1, v2, v1
	v_and_b32_e32 v1, 0xfffffc00, v1
	v_sub_u32_e32 v1, v2, v1
	v_lshrrev_b32_e32 v4, 4, v1
	v_bitop3_b32 v1, v4, v1, 32 bitop3:0x6c
	v_ashrrev_i32_e32 v5, 31, v1
	v_lshrrev_b32_e32 v5, 26, v5
	v_add_u32_e32 v5, v1, v5
	v_ashrrev_i32_e32 v6, 6, v5
	v_and_b32_e32 v5, 0xc0, v5
	v_ashrrev_i32_e32 v3, 6, v3
	v_sub_u32_e32 v1, v1, v5
	v_lshlrev_b32_e32 v4, 3, v3
	v_lshlrev_b32_e32 v3, 5, v3
	v_ashrrev_i16_sdwa v1, v128, sext(v1) dst_sel:DWORD dst_unused:UNUSED_PAD src0_sel:DWORD src1_sel:BYTE_0
	v_and_b32_e32 v4, -16, v4
	v_and_b32_e32 v3, 32, v3
	v_bfe_i32 v1, v1, 0, 16
	v_add_u32_e32 v4, v6, v4
	v_add_lshl_u32 v1, v3, v1, 1
	s_or_b32 s17, s9, 0x10000
	v_lshl_add_u32 v3, v4, 9, v1
	v_lshlrev_b32_e32 v5, 1, v4
	s_lshl_b32 s15, s10, 8
	v_add_u32_e32 v129, s9, v3
	v_add_u32_e32 v130, s17, v3
	v_lshrrev_b32_e32 v3, 2, v4
	v_and_b32_e32 v5, 24, v5
	s_and_b32 s15, s15, 0x700
	v_and_b32_e32 v3, 4, v3
	v_and_or_b32 v4, v4, s11, v5
	v_or3_b32 v3, v4, v3, s15
	v_lshl_add_u32 v131, v3, 9, v1
	v_add_u32_e32 v1, 0x2000, v2
	v_ashrrev_i32_e32 v2, 31, v1
	v_lshrrev_b32_e32 v2, 22, v2
	v_add_u32_e32 v2, v1, v2
	v_ashrrev_i32_e32 v2, 10, v2
	v_mul_i32_i24_e32 v3, 0x400, v2
	v_sub_u32_e32 v1, v1, v3
	v_lshrrev_b32_e32 v3, 4, v1
	v_bitop3_b32 v1, v3, v1, 32 bitop3:0x6c
	v_ashrrev_i32_e32 v4, 31, v1
	v_lshrrev_b32_e32 v4, 26, v4
	v_add_u32_e32 v4, v1, v4
	v_ashrrev_i32_e32 v5, 6, v4
	v_and_b32_e32 v4, 0xc0, v4
	v_sub_u32_e32 v1, v1, v4
	v_lshlrev_b32_e32 v3, 3, v2
	v_lshlrev_b32_e32 v2, 5, v2
	v_ashrrev_i16_sdwa v1, v128, sext(v1) dst_sel:DWORD dst_unused:UNUSED_PAD src0_sel:DWORD src1_sel:BYTE_0
	v_and_b32_e32 v3, -16, v3
	v_and_b32_e32 v2, 32, v2
	v_bfe_i32 v1, v1, 0, 16
	v_add_u32_e32 v3, v5, v3
	v_add_lshl_u32 v1, v2, v1, 1
	v_lshl_add_u32 v2, v3, 9, v1
	v_lshlrev_b32_e32 v4, 1, v3
	s_ashr_i32 s26, s16, 6
	v_add_u32_e32 v133, s9, v2
	v_add_u32_e32 v134, s17, v2
	v_lshrrev_b32_e32 v2, 2, v3
	v_and_b32_e32 v4, 24, v4
	s_lshl_b32 s9, s26, 10
	v_and_b32_e32 v2, 4, v2
	v_and_or_b32 v3, v3, s11, v4
	s_add_i32 s9, s9, 0
	v_or3_b32 v2, v3, v2, s15
	s_add_i32 s17, s9, 0x10010
	s_mov_b32 m0, s17
	s_nop 0
	buffer_load_dwordx4 v131, s[0:3], s12 offen lds
	v_lshl_add_u32 v135, v2, 9, v1
	s_add_i32 s18, s9, 0x12010
	s_mov_b32 m0, s18
	s_nop 0
	buffer_load_dwordx4 v135, s[0:3], s12 offen lds
	s_add_i32 s19, s9, 16
	s_mov_b32 m0, s19
	s_nop 0
	buffer_load_dwordx4 v129, s[4:7], s12 offen lds
	s_add_i32 s20, s9, 0x2010
	s_mov_b32 m0, s20
	s_nop 0
	buffer_load_dwordx4 v133, s[4:7], s12 offen lds
	v_add_u32_e32 v132, 0x10000, v131
	s_add_i32 s21, s9, 0x14010
	s_mov_b32 m0, s21
	s_nop 0
	buffer_load_dwordx4 v132, s[0:3], s12 offen lds
	v_add_u32_e32 v136, 0x10000, v135
	s_add_i32 s22, s9, 0x16010
	s_mov_b32 m0, s22
	s_nop 0
	buffer_load_dwordx4 v136, s[0:3], s12 offen lds
	s_add_i32 s23, s9, 0x4010
	s_mov_b32 m0, s23
	s_nop 0
	buffer_load_dwordx4 v130, s[4:7], s12 offen lds
	s_add_i32 s25, s9, 0x6010
	s_mov_b32 m0, s25
	s_nop 0
	buffer_load_dwordx4 v134, s[4:7], s12 offen lds
	s_ashr_i32 s8, s16, 8
	s_cmp_lg_u32 s8, 1
	s_cbranch_scc1 .LBB0_955
	s_barrier
.LBB0_955:
	s_lshl_b32 s26, s26, 5
	v_and_b32_e32 v1, 48, v0
	v_lshlrev_b32_e32 v2, 6, v0
	s_movk_i32 s27, 0x3c0
	v_lshlrev_b32_e32 v0, 2, v0
	s_and_b32 s26, s26, 0x60
	s_lshl_b32 s24, s8, 6
	v_and_or_b32 v1, v2, s27, v1
	v_and_b32_e32 v0, 32, v0
	s_lshl_b32 s8, s8, 13
	s_lshl_b32 s27, s26, 7
	v_bitop3_b32 v2, v1, s8, v0 bitop3:0xde
	v_bitop3_b32 v1, s27, v1, v0 bitop3:0xf6
	s_waitcnt vmcnt(4)
	s_barrier
	s_add_i32 s27, s9, 0x18010
	s_mov_b32 m0, s27
	s_nop 0
	buffer_load_dwordx4 v131, s[0:3], s13 offen lds
	s_add_i32 s28, s9, 0x1a010
	s_mov_b32 m0, s28
	s_nop 0
	buffer_load_dwordx4 v135, s[0:3], s13 offen lds
	s_add_i32 s29, s9, 0x8010
	s_mov_b32 m0, s29
	s_nop 0
	buffer_load_dwordx4 v129, s[4:7], s13 offen lds
	s_add_i32 s30, s9, 0xa010
	s_mov_b32 m0, s30
	s_nop 0
	buffer_load_dwordx4 v133, s[4:7], s13 offen lds
	s_add_i32 s31, s9, 0x1c010
	s_mov_b32 m0, s31
	s_nop 0
	buffer_load_dwordx4 v132, s[0:3], s13 offen lds
	s_add_i32 s34, s9, 0x1e010
	s_mov_b32 m0, s34
	s_nop 0
	buffer_load_dwordx4 v136, s[0:3], s13 offen lds
	s_waitcnt vmcnt(6)
; #define G_WAIT_V(n) asm volatile("s_waitcnt vmcnt(" #n ")" ::: "memory")
; #define G_BAR() __builtin_amdgcn_s_barrier()
; #define G_SCHED() __builtin_amdgcn_sched_barrier(0)
; #define D_STAGE_A(slot, half, kt) D_STAGE(rsA, voffA, slot, half, kt)
; #define D_STAGE_B(slot, half, kt) D_STAGE(rsB, voffB, slot, half, kt)
; #define D_LDA(dst, slot) do { _Pragma("unroll") for (int m = 0; m < 4; ++m) _Pragma("unroll") for (int k = 0; k < 2; ++k) \
;     dst[m][k] = *(const LDS_AS bf16x8*)(lds + (slot) + aoff + m * 2048 + k * 1024); } while (0)
; #define D_LDB(dst, slot) do { _Pragma("unroll") for (int n = 0; n < 2; ++n) _Pragma("unroll") for (int k = 0; k < 2; ++k) \
;     dst[n][k] = *(const LDS_AS bf16x8*)(lds + (slot) + boff + n * 2048 + k * 1024); } while (0)
; #define D_WAIT_L(n) asm volatile("s_waitcnt lgkmcnt(" #n ")" ::: "memory")
; #define D_STAGE_A(slot, half, kt) D_STAGE(rsA, voffA, slot, half, kt)
; #define D_WAIT_L(n) asm volatile("s_waitcnt lgkmcnt(" #n ")" ::: "memory")
; template <class Cfg>
; DI void gemm256dma_unit(LDS_AS unsigned char* lds, const Cfg& cfg) {
;     ...
;   f32x4 acc[2][2][4][2];
; #pragma unroll
;   for (int a = 0; a < 2; ++a)
; #pragma unroll
;     for (int b = 0; b < 2; ++b)
; #pragma unroll
;       for (int m = 0; m < 4; ++m)
; #pragma unroll
;         for (int n = 0; n < 2; ++n) acc[a][b][m][n] = (f32x4){0.f, 0.f, 0.f, 0.f};
;   bf16x8 At[4][2], B0[2][2], B1[2][2];
;   D_STAGE_B(G_SB(0, 0), 0, 0); D_STAGE_A(G_SA(0, 0), 0, 0); D_STAGE_B(G_SB(0, 1), 1, 0); D_STAGE_A(G_SA(0, 1), 1, 0);
;   if (wr == 1) G_BAR();
;   G_WAIT_V(4); G_BAR();
;   D_STAGE_B(G_SB(1, 0), 0, 1); D_STAGE_A(G_SA(1, 0), 0, 1); D_STAGE_B(G_SB(1, 1), 1, 1);
;   G_WAIT_V(6); G_BAR();
; #pragma clang loop unroll(disable)
;   for (int t = 0; t < nt; t += 2) {
;     const int t1 = t + 1;
;     const int t2 = (t + 2 < nt) ? t + 2 : 0;
;     const int t3 = (t + 2 < nt) ? t + 3 : 1;
;     D_LDB(B0, G_SB(0, 0)); G_SCHED(); D_LDA(At, G_SA(0, 0)); D_STAGE_A(G_SA(1, 1), 1, t1);
;     D_WAIT_L(8); G_BAR(); D_WAIT_L(0); G_SCHED(); D_MMA(0, 0, At, B0); G_BAR(); G_SCHED();
;     D_LDB(B1, G_SB(0, 1)); D_STAGE_B(G_SB(0, 0), 0, t2);
;     G_BAR(); D_WAIT_L(0); G_SCHED(); D_MMA(0, 1, At, B1); G_BAR(); G_SCHED();
;     D_LDA(At, G_SA(0, 1)); D_STAGE_A(G_SA(0, 0), 0, t2);
;     G_BAR(); D_WAIT_L(0); G_SCHED(); D_MMA(1, 0, At, B0); G_BAR(); G_SCHED();
	v_mov_b32_e32 v0, 0
	v_add_u32_e32 v1, 0, v1
	s_movk_i32 s37, 0x80
	s_add_i32 s35, s9, 0xc010
	s_add_i32 s36, s9, 0xe010
	s_mov_b64 s[8:9], -1
	v_add_u32_e32 v137, 0x10010, v1
	v_add_u32_e32 v138, 0, v2
	v_add_u32_e32 v139, 0x14010, v1
	v_add_u32_e32 v140, 0x18010, v1
	v_add_u32_e32 v141, 0x1c010, v1
	v_mov_b32_e32 v1, v0
	v_mov_b32_e32 v2, v0
	v_mov_b32_e32 v3, v0
	v_mov_b32_e32 v4, v0
	v_mov_b32_e32 v5, v0
	v_mov_b32_e32 v6, v0
	v_mov_b32_e32 v7, v0
	v_mov_b32_e32 v8, v0
	v_mov_b32_e32 v9, v0
	v_mov_b32_e32 v10, v0
	v_mov_b32_e32 v11, v0
	v_mov_b32_e32 v12, v0
	v_mov_b32_e32 v13, v0
	v_mov_b32_e32 v14, v0
	v_mov_b32_e32 v15, v0
	v_mov_b32_e32 v24, v0
	v_mov_b32_e32 v25, v0
	v_mov_b32_e32 v26, v0
	v_mov_b32_e32 v27, v0
	v_mov_b32_e32 v28, v0
	v_mov_b32_e32 v29, v0
	v_mov_b32_e32 v30, v0
	v_mov_b32_e32 v31, v0
	v_mov_b32_e32 v40, v0
	v_mov_b32_e32 v41, v0
	v_mov_b32_e32 v42, v0
	v_mov_b32_e32 v43, v0
	v_mov_b32_e32 v44, v0
	v_mov_b32_e32 v45, v0
	v_mov_b32_e32 v46, v0
	v_mov_b32_e32 v47, v0
	v_mov_b32_e32 v16, v0
	v_mov_b32_e32 v17, v0
	v_mov_b32_e32 v18, v0
	v_mov_b32_e32 v19, v0
	v_mov_b32_e32 v20, v0
	v_mov_b32_e32 v21, v0
	v_mov_b32_e32 v22, v0
	v_mov_b32_e32 v23, v0
	v_mov_b32_e32 v32, v0
	v_mov_b32_e32 v33, v0
	v_mov_b32_e32 v34, v0
	v_mov_b32_e32 v35, v0
	v_mov_b32_e32 v36, v0
	v_mov_b32_e32 v37, v0
	v_mov_b32_e32 v38, v0
	v_mov_b32_e32 v39, v0
	v_mov_b32_e32 v48, v0
	v_mov_b32_e32 v49, v0
	v_mov_b32_e32 v50, v0
	v_mov_b32_e32 v51, v0
	v_mov_b32_e32 v52, v0
	v_mov_b32_e32 v53, v0
	v_mov_b32_e32 v54, v0
	v_mov_b32_e32 v55, v0
	v_mov_b32_e32 v56, v0
	v_mov_b32_e32 v57, v0
	v_mov_b32_e32 v58, v0
	v_mov_b32_e32 v59, v0
	v_mov_b32_e32 v60, v0
	v_mov_b32_e32 v61, v0
	v_mov_b32_e32 v62, v0
	v_mov_b32_e32 v63, v0
	v_mov_b32_e32 v64, v0
	v_mov_b32_e32 v65, v0
	v_mov_b32_e32 v66, v0
	v_mov_b32_e32 v67, v0
	v_mov_b32_e32 v68, v0
	v_mov_b32_e32 v69, v0
	v_mov_b32_e32 v70, v0
	v_mov_b32_e32 v71, v0
	v_mov_b32_e32 v72, v0
	v_mov_b32_e32 v73, v0
	v_mov_b32_e32 v74, v0
	v_mov_b32_e32 v75, v0
	v_mov_b32_e32 v76, v0
	v_mov_b32_e32 v77, v0
	v_mov_b32_e32 v78, v0
	v_mov_b32_e32 v79, v0
	v_mov_b32_e32 v88, v0
	v_mov_b32_e32 v89, v0
	v_mov_b32_e32 v90, v0
	v_mov_b32_e32 v91, v0
	v_mov_b32_e32 v92, v0
	v_mov_b32_e32 v93, v0
	v_mov_b32_e32 v94, v0
	v_mov_b32_e32 v95, v0
	v_mov_b32_e32 v104, v0
	v_mov_b32_e32 v105, v0
	v_mov_b32_e32 v106, v0
	v_mov_b32_e32 v107, v0
	v_mov_b32_e32 v108, v0
	v_mov_b32_e32 v109, v0
	v_mov_b32_e32 v110, v0
	v_mov_b32_e32 v111, v0
	v_mov_b32_e32 v80, v0
	v_mov_b32_e32 v81, v0
	v_mov_b32_e32 v82, v0
	v_mov_b32_e32 v83, v0
	v_mov_b32_e32 v84, v0
	v_mov_b32_e32 v85, v0
	v_mov_b32_e32 v86, v0
	v_mov_b32_e32 v87, v0
	v_mov_b32_e32 v96, v0
	v_mov_b32_e32 v97, v0
	v_mov_b32_e32 v98, v0
	v_mov_b32_e32 v99, v0
	v_mov_b32_e32 v100, v0
	v_mov_b32_e32 v101, v0
	v_mov_b32_e32 v102, v0
	v_mov_b32_e32 v103, v0
	v_mov_b32_e32 v112, v0
	v_mov_b32_e32 v113, v0
	v_mov_b32_e32 v114, v0
	v_mov_b32_e32 v115, v0
	v_mov_b32_e32 v116, v0
	v_mov_b32_e32 v117, v0
	v_mov_b32_e32 v118, v0
	v_mov_b32_e32 v119, v0
	v_mov_b32_e32 v120, v0
	v_mov_b32_e32 v121, v0
	v_mov_b32_e32 v122, v0
	v_mov_b32_e32 v123, v0
	v_mov_b32_e32 v124, v0
	v_mov_b32_e32 v125, v0
	v_mov_b32_e32 v126, v0
	v_mov_b32_e32 v127, v0
	s_barrier
.LBB0_956:
	v_cndmask_b32_e64 v142, 0, 1, s[8:9]
	v_cmp_ne_u32_e32 vcc, 1, v142
	ds_read_b128 v[142:145], v137
	ds_read_b128 v[146:149], v137 offset:1024
	ds_read_b128 v[150:153], v137 offset:2048
	ds_read_b128 v[154:157], v137 offset:3072
	s_and_b64 s[8:9], s[8:9], exec
	s_movk_i32 s8, 0x180
	s_cselect_b32 s9, 0x100, 0
	s_cselect_b32 s8, s8, 0x80
	ds_read_b128 v[158:161], v138 offset:16
	ds_read_b128 v[162:165], v138 offset:1040
	ds_read_b128 v[166:169], v138 offset:2064
	ds_read_b128 v[170:173], v138 offset:3088
	ds_read_b128 v[174:177], v138 offset:4112
	ds_read_b128 v[178:181], v138 offset:5136
	ds_read_b128 v[182:185], v138 offset:6160
	ds_read_b128 v[186:189], v138 offset:7184
	s_mov_b32 m0, s35
	s_nop 0
	buffer_load_dwordx4 v130, s[4:7], s37 offen lds
	s_nop 0
	s_mov_b32 m0, s36
	s_nop 0
	buffer_load_dwordx4 v134, s[4:7], s37 offen lds
	s_waitcnt lgkmcnt(8)
	s_barrier
	s_waitcnt lgkmcnt(0)
	s_setprio 1
	s_waitcnt lgkmcnt(7)
	v_mfma_f32_16x16x32_bf16 v[124:127], v[142:145], v[158:161], v[124:127]
	v_mfma_f32_16x16x32_bf16 v[120:123], v[150:153], v[158:161], v[120:123]
	s_waitcnt lgkmcnt(5)
	v_mfma_f32_16x16x32_bf16 v[116:119], v[142:145], v[166:169], v[116:119]
	v_mfma_f32_16x16x32_bf16 v[112:115], v[150:153], v[166:169], v[112:115]
	s_waitcnt lgkmcnt(3)
	v_mfma_f32_16x16x32_bf16 v[100:103], v[142:145], v[174:177], v[100:103]
	v_mfma_f32_16x16x32_bf16 v[96:99], v[150:153], v[174:177], v[96:99]
	s_waitcnt lgkmcnt(1)
	v_mfma_f32_16x16x32_bf16 v[84:87], v[142:145], v[182:185], v[84:87]
	v_mfma_f32_16x16x32_bf16 v[80:83], v[150:153], v[182:185], v[80:83]
	v_mfma_f32_16x16x32_bf16 v[124:127], v[146:149], v[162:165], v[124:127]
	v_mfma_f32_16x16x32_bf16 v[120:123], v[154:157], v[162:165], v[120:123]
	v_mfma_f32_16x16x32_bf16 v[116:119], v[146:149], v[170:173], v[116:119]
	v_mfma_f32_16x16x32_bf16 v[112:115], v[154:157], v[170:173], v[112:115]
	v_mfma_f32_16x16x32_bf16 v[100:103], v[146:149], v[178:181], v[100:103]
	v_mfma_f32_16x16x32_bf16 v[96:99], v[154:157], v[178:181], v[96:99]
	s_waitcnt lgkmcnt(0)
	v_mfma_f32_16x16x32_bf16 v[84:87], v[146:149], v[186:189], v[84:87]
	v_mfma_f32_16x16x32_bf16 v[80:83], v[154:157], v[186:189], v[80:83]
	s_setprio 0
	s_barrier
	ds_read_b128 v[192:195], v139
	ds_read_b128 v[196:199], v139 offset:1024
	ds_read_b128 v[200:203], v139 offset:2048
	ds_read_b128 v[204:207], v139 offset:3072
	s_mov_b32 m0, s17
	s_nop 0
	buffer_load_dwordx4 v131, s[0:3], s9 offen lds
	s_nop 0
	s_mov_b32 m0, s18
	s_nop 0
	buffer_load_dwordx4 v135, s[0:3], s9 offen lds
	s_barrier
; #define G_WAIT_V(n) asm volatile("s_waitcnt vmcnt(" #n ")" ::: "memory")
; #define G_BAR() __builtin_amdgcn_s_barrier()
; #define G_SCHED() __builtin_amdgcn_sched_barrier(0)
; #define D_STAGE_A(slot, half, kt) D_STAGE(rsA, voffA, slot, half, kt)
; #define D_STAGE_B(slot, half, kt) D_STAGE(rsB, voffB, slot, half, kt)
; #define D_LDA(dst, slot) do { _Pragma("unroll") for (int m = 0; m < 4; ++m) _Pragma("unroll") for (int k = 0; k < 2; ++k) \
;     dst[m][k] = *(const LDS_AS bf16x8*)(lds + (slot) + aoff + m * 2048 + k * 1024); } while (0)
; #define D_LDB(dst, slot) do { _Pragma("unroll") for (int n = 0; n < 2; ++n) _Pragma("unroll") for (int k = 0; k < 2; ++k) \
;     dst[n][k] = *(const LDS_AS bf16x8*)(lds + (slot) + boff + n * 2048 + k * 1024); } while (0)
; #define D_MMA(ai, bj, At, Bf) do { __builtin_amdgcn_s_setprio(1); _Pragma("unroll") for (int m = 0; m < 4; ++m) _Pragma("unroll") for (int n = 0; n < 2; ++n) _Pragma("unroll") for (int k = 0; k < 2; ++k) \
;     acc[ai][bj][m][n] = __builtin_amdgcn_mfma_f32_16x16x32_bf16(Bf[n][k], At[m][k], acc[ai][bj][m][n], 0, 0, 0); __builtin_amdgcn_s_setprio(0); } while (0)
; #define D_WAIT_L(n) asm volatile("s_waitcnt lgkmcnt(" #n ")" ::: "memory")
; #define D_STAGE_A(slot, half, kt) D_STAGE(rsA, voffA, slot, half, kt)
; #define D_WAIT_L(n) asm volatile("s_waitcnt lgkmcnt(" #n ")" ::: "memory")
; template <class Cfg>
; DI void gemm256dma_unit(LDS_AS unsigned char* lds, const Cfg& cfg) {
;     ...
;     G_BAR(); D_WAIT_L(0); G_SCHED(); D_MMA(0, 1, At, B1); G_BAR(); G_SCHED();
;     D_LDA(At, G_SA(0, 1)); D_STAGE_A(G_SA(0, 0), 0, t2);
;     G_BAR(); D_WAIT_L(0); G_SCHED(); D_MMA(1, 0, At, B0); G_BAR(); G_SCHED();
;     D_STAGE_B(G_SB(0, 1), 1, t2);
;     G_WAIT_V(6); G_BAR(); G_SCHED(); D_MMA(1, 1, At, B1); G_BAR(); G_SCHED();
;     D_LDB(B0, G_SB(1, 0)); G_SCHED(); D_LDA(At, G_SA(1, 0)); D_STAGE_A(G_SA(0, 1), 1, t2);
;     D_WAIT_L(8); G_BAR(); D_WAIT_L(0); G_SCHED(); D_MMA(0, 0, At, B0); G_BAR(); G_SCHED();
;     D_LDB(B1, G_SB(1, 1)); D_STAGE_B(G_SB(1, 0), 0, t3);
;     G_BAR(); D_WAIT_L(0); G_SCHED(); D_MMA(0, 1, At, B1); G_BAR(); G_SCHED();
;     D_LDA(At, G_SA(1, 1)); D_STAGE_A(G_SA(1, 0), 0, t3);
	s_waitcnt lgkmcnt(0)
	s_setprio 1
	s_waitcnt lgkmcnt(3)
	v_mfma_f32_16x16x32_bf16 v[108:111], v[192:195], v[158:161], v[108:111]
	s_waitcnt lgkmcnt(1)
	v_mfma_f32_16x16x32_bf16 v[104:107], v[200:203], v[158:161], v[104:107]
	v_mfma_f32_16x16x32_bf16 v[92:95], v[192:195], v[166:169], v[92:95]
	v_mfma_f32_16x16x32_bf16 v[88:91], v[200:203], v[166:169], v[88:91]
	v_mfma_f32_16x16x32_bf16 v[76:79], v[192:195], v[174:177], v[76:79]
	v_mfma_f32_16x16x32_bf16 v[72:75], v[200:203], v[174:177], v[72:75]
	v_mfma_f32_16x16x32_bf16 v[68:71], v[192:195], v[182:185], v[68:71]
	v_mfma_f32_16x16x32_bf16 v[64:67], v[200:203], v[182:185], v[64:67]
	v_mfma_f32_16x16x32_bf16 v[108:111], v[196:199], v[162:165], v[108:111]
	s_waitcnt lgkmcnt(0)
	v_mfma_f32_16x16x32_bf16 v[104:107], v[204:207], v[162:165], v[104:107]
	v_mfma_f32_16x16x32_bf16 v[92:95], v[196:199], v[170:173], v[92:95]
	v_mfma_f32_16x16x32_bf16 v[88:91], v[204:207], v[170:173], v[88:91]
	v_mfma_f32_16x16x32_bf16 v[76:79], v[196:199], v[178:181], v[76:79]
	v_mfma_f32_16x16x32_bf16 v[72:75], v[204:207], v[178:181], v[72:75]
	v_mfma_f32_16x16x32_bf16 v[68:71], v[196:199], v[186:189], v[68:71]
	v_mfma_f32_16x16x32_bf16 v[64:67], v[204:207], v[186:189], v[64:67]
	s_setprio 0
	s_barrier
	ds_read_b128 v[158:161], v138 offset:16400
	ds_read_b128 v[162:165], v138 offset:17424
	ds_read_b128 v[166:169], v138 offset:18448
	ds_read_b128 v[170:173], v138 offset:19472
	ds_read_b128 v[174:177], v138 offset:20496
	ds_read_b128 v[178:181], v138 offset:21520
	ds_read_b128 v[182:185], v138 offset:22544
	ds_read_b128 v[186:189], v138 offset:23568
	s_mov_b32 m0, s19
	s_nop 0
	buffer_load_dwordx4 v129, s[4:7], s9 offen lds
	s_nop 0
	s_mov_b32 m0, s20
	s_nop 0
	buffer_load_dwordx4 v133, s[4:7], s9 offen lds
	s_barrier
	s_waitcnt lgkmcnt(0)
	s_setprio 1
	s_waitcnt lgkmcnt(7)
	v_mfma_f32_16x16x32_bf16 v[60:63], v[142:145], v[158:161], v[60:63]
	v_mfma_f32_16x16x32_bf16 v[56:59], v[150:153], v[158:161], v[56:59]
	s_waitcnt lgkmcnt(5)
	v_mfma_f32_16x16x32_bf16 v[52:55], v[142:145], v[166:169], v[52:55]
	v_mfma_f32_16x16x32_bf16 v[48:51], v[150:153], v[166:169], v[48:51]
	s_waitcnt lgkmcnt(3)
	v_mfma_f32_16x16x32_bf16 v[36:39], v[142:145], v[174:177], v[36:39]
	v_mfma_f32_16x16x32_bf16 v[32:35], v[150:153], v[174:177], v[32:35]
	s_waitcnt lgkmcnt(1)
	v_mfma_f32_16x16x32_bf16 v[20:23], v[142:145], v[182:185], v[20:23]
	v_mfma_f32_16x16x32_bf16 v[16:19], v[150:153], v[182:185], v[16:19]
	v_mfma_f32_16x16x32_bf16 v[60:63], v[146:149], v[162:165], v[60:63]
	v_mfma_f32_16x16x32_bf16 v[56:59], v[154:157], v[162:165], v[56:59]
	v_mfma_f32_16x16x32_bf16 v[52:55], v[146:149], v[170:173], v[52:55]
	v_mfma_f32_16x16x32_bf16 v[48:51], v[154:157], v[170:173], v[48:51]
	v_mfma_f32_16x16x32_bf16 v[36:39], v[146:149], v[178:181], v[36:39]
	v_mfma_f32_16x16x32_bf16 v[32:35], v[154:157], v[178:181], v[32:35]
	s_waitcnt lgkmcnt(0)
	v_mfma_f32_16x16x32_bf16 v[20:23], v[146:149], v[186:189], v[20:23]
	v_mfma_f32_16x16x32_bf16 v[16:19], v[154:157], v[186:189], v[16:19]
	s_setprio 0
	s_barrier
	s_mov_b32 m0, s21
	s_nop 0
	buffer_load_dwordx4 v132, s[0:3], s9 offen lds
	s_nop 0
	s_mov_b32 m0, s22
	s_nop 0
	buffer_load_dwordx4 v136, s[0:3], s9 offen lds
	s_waitcnt vmcnt(6)
	s_barrier
	s_setprio 1
	v_mfma_f32_16x16x32_bf16 v[44:47], v[192:195], v[158:161], v[44:47]
	v_mfma_f32_16x16x32_bf16 v[40:43], v[200:203], v[158:161], v[40:43]
	v_mfma_f32_16x16x32_bf16 v[28:31], v[192:195], v[166:169], v[28:31]
	v_mfma_f32_16x16x32_bf16 v[24:27], v[200:203], v[166:169], v[24:27]
	v_mfma_f32_16x16x32_bf16 v[12:15], v[192:195], v[174:177], v[12:15]
	v_mfma_f32_16x16x32_bf16 v[8:11], v[200:203], v[174:177], v[8:11]
	v_mfma_f32_16x16x32_bf16 v[4:7], v[192:195], v[182:185], v[4:7]
	v_mfma_f32_16x16x32_bf16 v[0:3], v[200:203], v[182:185], v[0:3]
	v_mfma_f32_16x16x32_bf16 v[44:47], v[196:199], v[162:165], v[44:47]
	v_mfma_f32_16x16x32_bf16 v[40:43], v[204:207], v[162:165], v[40:43]
	v_mfma_f32_16x16x32_bf16 v[28:31], v[196:199], v[170:173], v[28:31]
	v_mfma_f32_16x16x32_bf16 v[24:27], v[204:207], v[170:173], v[24:27]
	v_mfma_f32_16x16x32_bf16 v[12:15], v[196:199], v[178:181], v[12:15]
	v_mfma_f32_16x16x32_bf16 v[8:11], v[204:207], v[178:181], v[8:11]
	v_mfma_f32_16x16x32_bf16 v[4:7], v[196:199], v[186:189], v[4:7]
	v_mfma_f32_16x16x32_bf16 v[0:3], v[204:207], v[186:189], v[0:3]
	s_setprio 0
	s_barrier
	ds_read_b128 v[142:145], v140
	ds_read_b128 v[146:149], v140 offset:1024
	ds_read_b128 v[150:153], v140 offset:2048
	ds_read_b128 v[154:157], v140 offset:3072
	ds_read_b128 v[158:161], v138 offset:32784
	ds_read_b128 v[162:165], v138 offset:33808
	ds_read_b128 v[166:169], v138 offset:34832
	ds_read_b128 v[170:173], v138 offset:35856
	ds_read_b128 v[174:177], v138 offset:36880
	ds_read_b128 v[178:181], v138 offset:37904
	ds_read_b128 v[182:185], v138 offset:38928
	ds_read_b128 v[186:189], v138 offset:39952
	s_mov_b32 m0, s23
	s_nop 0
	buffer_load_dwordx4 v130, s[4:7], s9 offen lds
	s_nop 0
	s_mov_b32 m0, s25
	s_nop 0
	buffer_load_dwordx4 v134, s[4:7], s9 offen lds
	s_waitcnt lgkmcnt(8)
	s_barrier
; #define G_WAIT_V(n) asm volatile("s_waitcnt vmcnt(" #n ")" ::: "memory")
; #define G_BAR() __builtin_amdgcn_s_barrier()
; #define G_SCHED() __builtin_amdgcn_sched_barrier(0)
; #define D_STAGE_A(slot, half, kt) D_STAGE(rsA, voffA, slot, half, kt)
; #define D_STAGE_B(slot, half, kt) D_STAGE(rsB, voffB, slot, half, kt)
; #define D_LDA(dst, slot) do { _Pragma("unroll") for (int m = 0; m < 4; ++m) _Pragma("unroll") for (int k = 0; k < 2; ++k) \
;     dst[m][k] = *(const LDS_AS bf16x8*)(lds + (slot) + aoff + m * 2048 + k * 1024); } while (0)
; #define D_MMA(ai, bj, At, Bf) do { __builtin_amdgcn_s_setprio(1); _Pragma("unroll") for (int m = 0; m < 4; ++m) _Pragma("unroll") for (int n = 0; n < 2; ++n) _Pragma("unroll") for (int k = 0; k < 2; ++k) \
;     acc[ai][bj][m][n] = __builtin_amdgcn_mfma_f32_16x16x32_bf16(Bf[n][k], At[m][k], acc[ai][bj][m][n], 0, 0, 0); __builtin_amdgcn_s_setprio(0); } while (0)
; #define D_WAIT_L(n) asm volatile("s_waitcnt lgkmcnt(" #n ")" ::: "memory")
; #define D_STAGE_A(slot, half, kt) D_STAGE(rsA, voffA, slot, half, kt)
; #define D_STAGE_B(slot, half, kt) do { _Pragma("unroll") for (int _i = 0; _i < 2; ++_i) { const unsigned _m0 = ldsw + (unsigned)((slot) + _i * 8192); const unsigned _so = (unsigned)(kt) * 128u + (half) * bt_half + _i * bt_piece; \
;     asm volatile("s_mov_b32 m0, %0\n\ts_nop 4\n\tbuffer_load_dwordx4 %1, %2, %3 offen lds" :: "s"(_m0), "v"(voffB0), "s"(rsB), "s"(_so) : "m0", "memory"); } } while (0)
; #define D_LDA(dst, slot) do { _Pragma("unroll") for (int m = 0; m < 4; ++m) { \
;     const i32x4 _lo = *(const LDS_AS i32x4*)(lds + (slot) + aoff[0] + m * 2048); const i32x4 _hi = *(const LDS_AS i32x4*)(lds + (slot) + aoff[1] + m * 2048); \
;     dst[m] = __builtin_shufflevector(_lo, _hi, 0, 1, 2, 3, 4, 5, 6, 7); } } while (0)
; #define D_WAIT_L(n) asm volatile("s_waitcnt lgkmcnt(" #n ")" ::: "memory")
; template <class Cfg>
; DI void gemm256dma_unit(LDS_AS unsigned char* lds, const Cfg& cfg) {
;     ...
;     D_LDA(At, G_SA(1, 1)); D_STAGE_A(G_SA(1, 0), 0, t3);
;     G_BAR(); D_WAIT_L(0); G_SCHED(); D_MMA(1, 0, At, B0); G_BAR(); G_SCHED();
;     D_STAGE_B(G_SB(1, 1), 1, t3);
;     G_WAIT_V(6); G_BAR(); G_SCHED(); D_MMA(1, 1, At, B1); G_BAR(); G_SCHED();
;   }
;   G_WAIT_V(0);
;   if (wr == 0) G_BAR();
	s_waitcnt lgkmcnt(0)
	s_setprio 1
	s_waitcnt lgkmcnt(7)
	v_mfma_f32_16x16x32_bf16 v[124:127], v[142:145], v[158:161], v[124:127]
	v_mfma_f32_16x16x32_bf16 v[120:123], v[150:153], v[158:161], v[120:123]
	s_waitcnt lgkmcnt(5)
	v_mfma_f32_16x16x32_bf16 v[116:119], v[142:145], v[166:169], v[116:119]
	v_mfma_f32_16x16x32_bf16 v[112:115], v[150:153], v[166:169], v[112:115]
	s_waitcnt lgkmcnt(3)
	v_mfma_f32_16x16x32_bf16 v[100:103], v[142:145], v[174:177], v[100:103]
	v_mfma_f32_16x16x32_bf16 v[96:99], v[150:153], v[174:177], v[96:99]
	s_waitcnt lgkmcnt(1)
	v_mfma_f32_16x16x32_bf16 v[84:87], v[142:145], v[182:185], v[84:87]
	v_mfma_f32_16x16x32_bf16 v[80:83], v[150:153], v[182:185], v[80:83]
	v_mfma_f32_16x16x32_bf16 v[124:127], v[146:149], v[162:165], v[124:127]
	v_mfma_f32_16x16x32_bf16 v[120:123], v[154:157], v[162:165], v[120:123]
	v_mfma_f32_16x16x32_bf16 v[116:119], v[146:149], v[170:173], v[116:119]
	v_mfma_f32_16x16x32_bf16 v[112:115], v[154:157], v[170:173], v[112:115]
	v_mfma_f32_16x16x32_bf16 v[100:103], v[146:149], v[178:181], v[100:103]
	v_mfma_f32_16x16x32_bf16 v[96:99], v[154:157], v[178:181], v[96:99]
	s_waitcnt lgkmcnt(0)
	v_mfma_f32_16x16x32_bf16 v[84:87], v[146:149], v[186:189], v[84:87]
	v_mfma_f32_16x16x32_bf16 v[80:83], v[154:157], v[186:189], v[80:83]
	s_setprio 0
	s_barrier
	ds_read_b128 v[192:195], v141
	ds_read_b128 v[196:199], v141 offset:1024
	ds_read_b128 v[200:203], v141 offset:2048
	ds_read_b128 v[204:207], v141 offset:3072
	s_mov_b32 m0, s27
	s_nop 0
	buffer_load_dwordx4 v131, s[0:3], s8 offen lds
	s_nop 0
	s_mov_b32 m0, s28
	s_nop 0
	buffer_load_dwordx4 v135, s[0:3], s8 offen lds
	s_barrier
	s_waitcnt lgkmcnt(0)
	s_setprio 1
	s_waitcnt lgkmcnt(3)
	v_mfma_f32_16x16x32_bf16 v[108:111], v[192:195], v[158:161], v[108:111]
	s_waitcnt lgkmcnt(1)
	v_mfma_f32_16x16x32_bf16 v[104:107], v[200:203], v[158:161], v[104:107]
	v_mfma_f32_16x16x32_bf16 v[92:95], v[192:195], v[166:169], v[92:95]
	v_mfma_f32_16x16x32_bf16 v[88:91], v[200:203], v[166:169], v[88:91]
	v_mfma_f32_16x16x32_bf16 v[76:79], v[192:195], v[174:177], v[76:79]
	v_mfma_f32_16x16x32_bf16 v[72:75], v[200:203], v[174:177], v[72:75]
	v_mfma_f32_16x16x32_bf16 v[68:71], v[192:195], v[182:185], v[68:71]
	v_mfma_f32_16x16x32_bf16 v[64:67], v[200:203], v[182:185], v[64:67]
	v_mfma_f32_16x16x32_bf16 v[108:111], v[196:199], v[162:165], v[108:111]
	s_waitcnt lgkmcnt(0)
	v_mfma_f32_16x16x32_bf16 v[104:107], v[204:207], v[162:165], v[104:107]
	v_mfma_f32_16x16x32_bf16 v[92:95], v[196:199], v[170:173], v[92:95]
	v_mfma_f32_16x16x32_bf16 v[88:91], v[204:207], v[170:173], v[88:91]
	v_mfma_f32_16x16x32_bf16 v[76:79], v[196:199], v[178:181], v[76:79]
	v_mfma_f32_16x16x32_bf16 v[72:75], v[204:207], v[178:181], v[72:75]
	v_mfma_f32_16x16x32_bf16 v[68:71], v[196:199], v[186:189], v[68:71]
	v_mfma_f32_16x16x32_bf16 v[64:67], v[204:207], v[186:189], v[64:67]
	s_setprio 0
	s_barrier
	ds_read_b128 v[158:161], v138 offset:49168
	ds_read_b128 v[162:165], v138 offset:50192
	ds_read_b128 v[166:169], v138 offset:51216
	ds_read_b128 v[170:173], v138 offset:52240
	ds_read_b128 v[174:177], v138 offset:53264
	ds_read_b128 v[178:181], v138 offset:54288
	ds_read_b128 v[182:185], v138 offset:55312
	ds_read_b128 v[186:189], v138 offset:56336
	s_mov_b32 m0, s29
	s_nop 0
	buffer_load_dwordx4 v129, s[4:7], s8 offen lds
	s_nop 0
	s_mov_b32 m0, s30
	s_nop 0
	buffer_load_dwordx4 v133, s[4:7], s8 offen lds
	s_barrier
	s_waitcnt lgkmcnt(0)
	s_setprio 1
	s_waitcnt lgkmcnt(7)
	v_mfma_f32_16x16x32_bf16 v[60:63], v[142:145], v[158:161], v[60:63]
	v_mfma_f32_16x16x32_bf16 v[56:59], v[150:153], v[158:161], v[56:59]
	s_waitcnt lgkmcnt(5)
	v_mfma_f32_16x16x32_bf16 v[52:55], v[142:145], v[166:169], v[52:55]
	v_mfma_f32_16x16x32_bf16 v[48:51], v[150:153], v[166:169], v[48:51]
	s_waitcnt lgkmcnt(3)
	v_mfma_f32_16x16x32_bf16 v[36:39], v[142:145], v[174:177], v[36:39]
	v_mfma_f32_16x16x32_bf16 v[32:35], v[150:153], v[174:177], v[32:35]
	s_waitcnt lgkmcnt(1)
	v_mfma_f32_16x16x32_bf16 v[20:23], v[142:145], v[182:185], v[20:23]
	v_mfma_f32_16x16x32_bf16 v[16:19], v[150:153], v[182:185], v[16:19]
	v_mfma_f32_16x16x32_bf16 v[60:63], v[146:149], v[162:165], v[60:63]
	v_mfma_f32_16x16x32_bf16 v[56:59], v[154:157], v[162:165], v[56:59]
	v_mfma_f32_16x16x32_bf16 v[52:55], v[146:149], v[170:173], v[52:55]
	v_mfma_f32_16x16x32_bf16 v[48:51], v[154:157], v[170:173], v[48:51]
	v_mfma_f32_16x16x32_bf16 v[36:39], v[146:149], v[178:181], v[36:39]
	v_mfma_f32_16x16x32_bf16 v[32:35], v[154:157], v[178:181], v[32:35]
	s_waitcnt lgkmcnt(0)
	v_mfma_f32_16x16x32_bf16 v[20:23], v[146:149], v[186:189], v[20:23]
	v_mfma_f32_16x16x32_bf16 v[16:19], v[154:157], v[186:189], v[16:19]
	s_setprio 0
	s_barrier
	s_mov_b32 m0, s31
	s_nop 0
	buffer_load_dwordx4 v132, s[0:3], s8 offen lds
	s_nop 0
	s_mov_b32 m0, s34
	s_nop 0
	buffer_load_dwordx4 v136, s[0:3], s8 offen lds
	s_waitcnt vmcnt(6)
	s_barrier
	s_setprio 1
	v_mfma_f32_16x16x32_bf16 v[44:47], v[192:195], v[158:161], v[44:47]
	v_mfma_f32_16x16x32_bf16 v[40:43], v[200:203], v[158:161], v[40:43]
	v_mfma_f32_16x16x32_bf16 v[28:31], v[192:195], v[166:169], v[28:31]
	v_mfma_f32_16x16x32_bf16 v[24:27], v[200:203], v[166:169], v[24:27]
	v_mfma_f32_16x16x32_bf16 v[12:15], v[192:195], v[174:177], v[12:15]
	v_mfma_f32_16x16x32_bf16 v[8:11], v[200:203], v[174:177], v[8:11]
	v_mfma_f32_16x16x32_bf16 v[4:7], v[192:195], v[182:185], v[4:7]
	v_mfma_f32_16x16x32_bf16 v[0:3], v[200:203], v[182:185], v[0:3]
	v_mfma_f32_16x16x32_bf16 v[44:47], v[196:199], v[162:165], v[44:47]
	v_mfma_f32_16x16x32_bf16 v[40:43], v[204:207], v[162:165], v[40:43]
	v_mfma_f32_16x16x32_bf16 v[28:31], v[196:199], v[170:173], v[28:31]
	v_mfma_f32_16x16x32_bf16 v[24:27], v[204:207], v[170:173], v[24:27]
	v_mfma_f32_16x16x32_bf16 v[12:15], v[196:199], v[178:181], v[12:15]
	v_mfma_f32_16x16x32_bf16 v[8:11], v[204:207], v[178:181], v[8:11]
	v_mfma_f32_16x16x32_bf16 v[4:7], v[196:199], v[186:189], v[4:7]
	v_mfma_f32_16x16x32_bf16 v[0:3], v[204:207], v[186:189], v[0:3]
	s_setprio 0
	s_barrier
	s_mov_b64 s[8:9], 0
	s_movk_i32 s37, 0x180
	s_cbranch_vccz .LBB0_956
	s_waitcnt vmcnt(0)
	s_cmpk_lt_u32 s16, 0x100
	s_cbranch_scc0 .LBB0_952
	s_barrier
	s_branch .LBB0_952

; #define LDS_AS __attribute__((address_space(3)))
; DI void attn_step_end_ml() { asm volatile("s_waitcnt vmcnt(4)" ::: "memory"); __builtin_amdgcn_s_barrier(); }
; DI void attn_mla_item(const Params& p, LDS_AS unsigned char* lds, const AttnCtx& c, int qb, int nsteps) {
;   const int lane = c.lane, l31 = lane & 31, hh = lane >> 5;
;   const size_t tokbase = (size_t)c.b * SEQ;
;   bf16x8 qf[12];
;   {
;     const bf16_t* qp = p.mq + (tokbase + qb * 32 + l31) * 1536 + c.hd * 192 + 8 * hh;
; #pragma unroll
;     for (int s = 0; s < 12; ++s) qf[s] = *(const bf16x8*)(qp + 16 * s);
;   }
;   f32x16 o[4];
; #pragma unroll
;   for (int d = 0; d < 4; ++d)
; #pragma unroll
;     for (int i = 0; i < 16; ++i) o[d][i] = 0.f;
;   float mrun = -1e30f, lrun = 0.f;
;   attn_issue(c, nsteps - 1, 0);
;   attn_issue(c, nsteps - 2, 1);
;   attn_step_end_ml();
; DI void phase_attn(const Params& p, LDS_AS unsigned char* lds, char* smem, int bid, int nb) {
;     ...
; #pragma unroll 1
;   for (int rnd = 0; rnd * nb < 512; ++rnd) {
;     const int s = __builtin_amdgcn_readfirstlane(rnd * nb + ((rnd & 1) ? nb - 1 - bid : bid));
;     if (s >= 512) break;
;     const int q8 = ((rnd & 1) && (nb & 7) == 0) ? 7 - (s & 7) : (s & 7);
;     const int bh = q8 * 4 + ((s >> 3) & 3), ch = 15 - (s >> 5);
;     c.b = bh >> 3; c.hd = bh & 7;
;     c.voff_sbk = drow * 6144u + (unsigned)(1024 + c.hd * 128) * 2u + dch * 16u;
;     c.voff_sbv = drow * 6144u + (unsigned)(2048 + c.hd * 128) * 2u + dch * 16u;
;     c.voff_mlk = drow * 4096u + (unsigned)(c.hd * 256) * 2u + dch * 16u;
;     c.voff_mlv = drow * 4096u + (unsigned)(c.hd * 256 + 128) * 2u + dch * 16u;
;     c.voff_r = rrow * 128u + rch * 16u;
;     if (c.wv < 4) attn_sb_item(p, lds, c, 4 * ch + w4, 4 * ch + 4);
;     else attn_mla_item(p, lds, c, 4 * ch + w4, 4 * ch + 4);
.LBB0_1016:
	s_bitcmp1_b32 s49, 0
	s_cselect_b64 s[84:85], -1, 0
	s_and_b64 s[38:39], s[84:85], exec
	v_readlane_b32 s4, v255, 17
	v_readlane_b32 s5, v255, 21
	s_cselect_b32 s33, s5, s4
	s_add_i32 s33, s33, s0
	s_cmpk_gt_i32 s33, 0x1ff
	s_mov_b64 s[78:79], -1
	s_cbranch_scc1 .LBB0_1015
	v_readlane_b32 s4, v255, 23
	v_readlane_b32 s5, v255, 24
	s_and_b32 s0, s33, 7
	s_and_b64 s[38:39], s[4:5], s[84:85]
	s_xor_b32 s42, s0, 7
	s_and_b64 s[38:39], s[38:39], exec
	s_cselect_b32 s38, s42, s0
	s_ashr_i32 s42, s33, 3
	s_lshl_b32 s0, s38, 2
	s_bfe_u32 s39, s33, 0x20003
	s_and_b32 s33, s42, -4
	s_and_b32 s0, s0, 4
	s_sub_i32 s43, 60, s33
	v_readlane_b32 s4, v255, 30
	s_or_b32 s76, s0, s39
	s_or_b32 s39, s43, s4
	s_lshl_b32 s38, s38, 10
	s_and_b32 s55, s38, 0x1800
	s_lshl_b32 s38, s39, 5
	v_readlane_b32 s4, v255, 25
	s_lshl_b32 s0, s76, 8
	v_lshl_add_u32 v168, s76, 9, v165
	s_add_i32 s38, s55, s38
	v_readlane_b32 s5, v255, 26
	v_add_u32_e32 v166, s0, v136
	v_add_u32_e32 v167, s0, v137
	v_or_b32_e32 v169, 0x100, v168
	s_sub_i32 s33, 64, s33
	v_or_b32_e32 v132, s38, v139
	v_mov_b32_e32 v133, v0
	s_and_b64 vcc, exec, s[4:5]
	s_cbranch_vccz .LBB0_1039
	v_readlane_b32 s4, v254, 56
	v_readlane_b32 s18, v255, 6
	v_readlane_b32 s19, v255, 7
	s_movk_i32 s38, 0xc00
	v_mov_b32_e32 v131, v0
	v_mov_b64_e32 v[2:3], s[18:19]
	v_mad_u64_u32 v[2:3], s[62:63], v132, s38, v[2:3]
	s_mul_i32 s62, s76, 0x180
	s_mov_b32 s63, s1
	v_lshl_add_u64 v[2:3], v[2:3], 0, s[62:63]
	v_lshl_add_u64 v[2:3], v[2:3], 0, v[130:131]
	global_load_dwordx4 v[82:85], v[2:3], off
	global_load_dwordx4 v[86:89], v[2:3], off offset:32
	global_load_dwordx4 v[90:93], v[2:3], off offset:64
	global_load_dwordx4 v[94:97], v[2:3], off offset:96
	global_load_dwordx4 v[98:101], v[2:3], off offset:128
	global_load_dwordx4 v[102:105], v[2:3], off offset:160
	global_load_dwordx4 v[106:109], v[2:3], off offset:192
	global_load_dwordx4 v[110:113], v[2:3], off offset:224
	global_load_dwordx4 v[114:117], v[2:3], off offset:256
	global_load_dwordx4 v[118:121], v[2:3], off offset:288
	global_load_dwordx4 v[122:125], v[2:3], off offset:320
	global_load_dwordx4 v[126:129], v[2:3], off offset:352
	s_lshl_b32 s38, s43, 5
	s_add_i32 s38, s55, s38
	s_addk_i32 s38, 0x60
	s_mul_i32 s46, s38, 0x1800
	s_mov_b32 m0, s77
	s_nop 0
	buffer_load_dwordx4 v166, s[64:67], s46 offen lds
	s_lshl_b32 s38, s38, 12
	s_mov_b32 m0, s72
	s_nop 0
	buffer_load_dwordx4 v167, s[64:67], s46 offen lds
	v_readlane_b32 s4, v255, 27
	s_mov_b32 m0, s73
	s_nop 0
	buffer_load_dwordx4 v168, s[68:71], s38 offen lds
	s_mov_b32 s61, 0
	s_mov_b32 m0, s74
	s_nop 0
	buffer_load_dwordx4 v169, s[68:71], s38 offen lds
	s_lshl_b32 s38, s33, 5
	s_add_i32 s38, s55, s38
	s_sub_i32 s38, s38, 64
	s_mul_i32 s46, s38, 0x1800
	s_mov_b32 m0, s75
	s_nop 0
	buffer_load_dwordx4 v166, s[64:67], s46 offen lds
	s_lshl_b32 s38, s38, 12
	s_mov_b32 m0, s86
	s_nop 0
	buffer_load_dwordx4 v167, s[64:67], s46 offen lds
	s_mov_b32 s46, 0
	s_mov_b32 m0, s87
	s_nop 0
	buffer_load_dwordx4 v168, s[68:71], s38 offen lds
	v_readlane_b32 s5, v254, 57
	s_mov_b32 m0, s4
	s_nop 0
	buffer_load_dwordx4 v169, s[68:71], s38 offen lds
	s_waitcnt vmcnt(4)
	s_and_b32 s38, s39, 0x1ffffffe
	s_sub_i32 s62, s33, s38
	s_or_b32 s39, s43, 2
	s_cmp_lt_i32 s62, 3
	v_readlane_b32 s6, v254, 58
	v_readlane_b32 s7, v254, 59
	v_readlane_b32 s8, v254, 60
	v_readlane_b32 s9, v254, 61
	v_readlane_b32 s10, v254, 62
	v_readlane_b32 s11, v254, 63
	v_readlane_b32 s12, v255, 0
	v_readlane_b32 s13, v255, 1
	v_readlane_b32 s14, v255, 2
	v_readlane_b32 s15, v255, 3
	v_readlane_b32 s16, v255, 4
	v_readlane_b32 s17, v255, 5
	s_barrier
	s_cbranch_scc1 .LBB0_1025
	s_lshl_b32 s38, s42, 5
	s_and_b32 s38, s38, 0xffffff80
	s_sub_i32 s38, s55, s38
	s_addk_i32 s38, 0x7a0
	s_add_i32 s62, s62, -2
	s_mul_i32 s63, s38, 0x1800
	s_lshl_b32 s84, s38, 12
	s_branch .LBB0_1021

; #define AT_DMA(rs, voff, soff, m0v) asm volatile("s_mov_b32 m0, %0\n\ts_nop 4\n\tbuffer_load_dwordx4 %1, %2, %3 offen lds" :: "s"(m0v), "v"(voff), "s"(rs), "s"(soff) : "m0", "memory")
; DI void attn_issue(const AttnCtx& c, int kb, int bufsel) {
;   const unsigned tok = (unsigned)(c.b * SEQ + kb * 32);
;   const unsigned bb = c.ldsb + (unsigned)bufsel * AT_BUF + (unsigned)c.wv * 1024u;
;   AT_DMA(c.rsQKV, c.voff_sbk, tok * 6144u, bb + AT_SBK); AT_DMA(c.rsQKV, c.voff_sbv, tok * 6144u, bb + AT_SBV);
;   AT_DMA(c.rsMKV, c.voff_mlk, tok * 4096u, bb + AT_MLK); AT_DMA(c.rsMKV, c.voff_mlv, tok * 4096u, bb + AT_MLV);
;   if (c.wv < 4) AT_DMA(c.rsKR, c.voff_r, tok * 128u, bb + AT_MLR);
; }
; DI void attn_step_end() { asm volatile("s_waitcnt vmcnt(0)" ::: "memory"); __builtin_amdgcn_s_barrier(); }
; DI void attn_step_end_sb() { asm volatile("s_waitcnt vmcnt(5)" ::: "memory"); __builtin_amdgcn_s_barrier(); }
; DI void attn_step_end_ml() { asm volatile("s_waitcnt vmcnt(4)" ::: "memory"); __builtin_amdgcn_s_barrier(); }
; DI void attn_mla_item(const Params& p, LDS_AS unsigned char* lds, const AttnCtx& c, int qb, int nsteps) {
;     ...
; #pragma unroll 1
;   for (; s < nskip; ++s) { if (s + 2 < nsteps) { attn_issue(c, nsteps - 3 - s, rb == 0 ? 2 : rb - 1); attn_step_end_ml(); } else attn_step_end(); rb = rb == 2 ? 0 : rb + 1; }
.LBB0_1023:
	s_andn2_b64 vcc, exec, s[78:79]
	s_cbranch_vccnz .LBB0_1020
	s_mul_i32 s38, s61, 0x9000
	s_add_i32 s38, s38, 0xffff7000
	s_cmp_lg_u32 s61, 0
	s_cselect_b32 s38, s38, 0x12000
	s_add_i32 s38, s38, s77
	s_mov_b32 m0, s38
	s_nop 4
	buffer_load_dwordx4 v166, s[64:67], s63 offen lds
	s_add_i32 s78, s38, 0x2000
	s_mov_b32 m0, s78
	s_nop 0
	buffer_load_dwordx4 v167, s[64:67], s63 offen lds
	s_add_i32 s78, s38, 0x4000
	s_mov_b32 m0, s78
	s_nop 0
	buffer_load_dwordx4 v168, s[68:71], s84 offen lds
	s_addk_i32 s38, 0x7000
	s_mov_b32 m0, s38
	s_nop 0
	buffer_load_dwordx4 v169, s[68:71], s84 offen lds
	s_waitcnt vmcnt(4)
	s_barrier
	s_branch .LBB0_1020

; #define AT_DMA(rs, voff, soff, m0v) asm volatile("s_mov_b32 m0, %0\n\ts_nop 4\n\tbuffer_load_dwordx4 %1, %2, %3 offen lds" :: "s"(m0v), "v"(voff), "s"(rs), "s"(soff) : "m0", "memory")
; DI void attn_issue(const AttnCtx& c, int kb, int bufsel) {
;   const unsigned tok = (unsigned)(c.b * SEQ + kb * 32);
;   const unsigned bb = c.ldsb + (unsigned)bufsel * AT_BUF + (unsigned)c.wv * 1024u;
;   AT_DMA(c.rsQKV, c.voff_sbk, tok * 6144u, bb + AT_SBK); AT_DMA(c.rsQKV, c.voff_sbv, tok * 6144u, bb + AT_SBV);
;   AT_DMA(c.rsMKV, c.voff_mlk, tok * 4096u, bb + AT_MLK); AT_DMA(c.rsMKV, c.voff_mlv, tok * 4096u, bb + AT_MLV);
;   if (c.wv < 4) AT_DMA(c.rsKR, c.voff_r, tok * 128u, bb + AT_MLR);
; }
; DI void attn_mla_item(const Params& p, LDS_AS unsigned char* lds, const AttnCtx& c, int qb, int nsteps) {
;     ...
;   for (; s < nsteps; ++s) {
;     const int kb = nsteps - 1 - s;
;     if (s + 2 < nsteps) { attn_issue(c, kb - 2, rb == 0 ? 2 : rb - 1); }
.LBB0_1030:
	s_andn2_b64 vcc, exec, s[84:85]
	s_cbranch_vccnz .LBB0_1032
	s_add_i32 s38, s96, 0xffff7000
	s_cmp_lg_u32 s61, 0
	s_cselect_b32 s38, s38, 0x12000
	s_add_i32 s38, s38, s77
	s_mov_b32 m0, s38
	s_nop 4
	buffer_load_dwordx4 v166, s[64:67], s63 offen lds
	s_add_i32 s84, s38, 0x2000
	s_mov_b32 m0, s84
	s_nop 0
	buffer_load_dwordx4 v167, s[64:67], s63 offen lds
	s_add_i32 s84, s38, 0x4000
	s_mov_b32 m0, s84
	s_nop 0
	buffer_load_dwordx4 v168, s[68:71], s62 offen lds
	s_addk_i32 s38, 0x7000
	s_mov_b32 m0, s38
	s_nop 0
	buffer_load_dwordx4 v169, s[68:71], s62 offen lds
	s_mov_b32 s38, s96

; #define LDS_AS __attribute__((address_space(3)))
; #define AT_DMA(rs, voff, soff, m0v) asm volatile("s_mov_b32 m0, %0\n\ts_nop 4\n\tbuffer_load_dwordx4 %1, %2, %3 offen lds" :: "s"(m0v), "v"(voff), "s"(rs), "s"(soff) : "m0", "memory")
; DI void attn_step_end_sb() { asm volatile("s_waitcnt vmcnt(5)" ::: "memory"); __builtin_amdgcn_s_barrier(); }
; DI void attn_issue(const AttnCtx& c, int kb, int bufsel) {
;   const unsigned tok = (unsigned)(c.b * SEQ + kb * 32);
;   const unsigned bb = c.ldsb + (unsigned)bufsel * AT_BUF + (unsigned)c.wv * 1024u;
;   AT_DMA(c.rsQKV, c.voff_sbk, tok * 6144u, bb + AT_SBK); AT_DMA(c.rsQKV, c.voff_sbv, tok * 6144u, bb + AT_SBV);
;   AT_DMA(c.rsMKV, c.voff_mlk, tok * 4096u, bb + AT_MLK); AT_DMA(c.rsMKV, c.voff_mlv, tok * 4096u, bb + AT_MLV);
;   if (c.wv < 4) AT_DMA(c.rsKR, c.voff_r, tok * 128u, bb + AT_MLR);
; }
; DI void attn_sb_item(const Params& p, LDS_AS unsigned char* lds, const AttnCtx& c, int qb, int nsteps) {
;   const int lane = c.lane, l31 = lane & 31, hh = lane >> 5;
;   const size_t tokbase = (size_t)c.b * SEQ;
;   bf16x8 qf[8];
;   {
;     const bf16_t* qp = p.qkv + (tokbase + qb * 32 + l31) * 3072 + c.hd * 128 + 8 * hh;
; #pragma unroll
;     for (int s = 0; s < 8; ++s) qf[s] = *(const bf16x8*)(qp + 16 * s);
;   }
;   f32x16 o[4];
; #pragma unroll
;   for (int d = 0; d < 4; ++d)
; #pragma unroll
;     for (int i = 0; i < 16; ++i) o[d][i] = 0.f;
;   float csum = 0.f;
;   attn_issue(c, nsteps - 1, 0);
;   attn_issue(c, nsteps - 2, 1);
;   attn_step_end_sb();
.LBB0_1039:
	s_and_b64 vcc, exec, s[78:79]
	s_cbranch_vccz .LBB0_1014
	v_readlane_b32 s4, v254, 56
	v_readlane_b32 s6, v254, 58
	v_readlane_b32 s7, v254, 59
	v_readlane_b32 s8, v254, 60
	v_readlane_b32 s9, v254, 61
	v_readlane_b32 s10, v254, 62
	v_readlane_b32 s11, v254, 63
	v_readlane_b32 s5, v254, 57
	s_mov_b32 s8, s72
	s_mov_b32 s9, s73
	s_mov_b32 s10, s74
	s_mov_b32 s11, s75
	s_mov_b64 s[74:75], s[6:7]
	s_mov_b64 s[72:73], s[4:5]
	v_mov_b64_e32 v[2:3], s[74:75]
	s_movk_i32 s4, 0x1800
	v_mad_u64_u32 v[2:3], s[38:39], v132, s4, v[2:3]
	v_lshl_add_u64 v[2:3], v[2:3], 0, s[0:1]
	v_mov_b32_e32 v131, v0
	v_lshl_add_u64 v[2:3], v[2:3], 0, v[130:131]
	global_load_dwordx4 v[98:101], v[2:3], off
	global_load_dwordx4 v[102:105], v[2:3], off offset:32
	global_load_dwordx4 v[106:109], v[2:3], off offset:64
	global_load_dwordx4 v[110:113], v[2:3], off offset:96
	global_load_dwordx4 v[114:117], v[2:3], off offset:128
	global_load_dwordx4 v[118:121], v[2:3], off offset:160
	global_load_dwordx4 v[122:125], v[2:3], off offset:192
	global_load_dwordx4 v[126:129], v[2:3], off offset:224
	s_lshl_b32 s0, s43, 5
	s_add_i32 s0, s55, s0
	s_addk_i32 s0, 0x60
	s_mul_i32 s38, s0, 0x1800
	s_mov_b32 m0, s77
	s_nop 0
	buffer_load_dwordx4 v166, s[64:67], s38 offen lds
	s_mov_b32 s72, s8
	s_mov_b32 m0, s72
	s_nop 0
	buffer_load_dwordx4 v167, s[64:67], s38 offen lds
	s_mov_b32 s73, s9
	s_lshl_b32 s38, s0, 12
	s_mov_b32 m0, s73
	s_nop 0
	buffer_load_dwordx4 v168, s[68:71], s38 offen lds
	s_lshl_b32 s0, s0, 7
	s_mov_b32 m0, s10
	s_nop 0
	buffer_load_dwordx4 v169, s[68:71], s38 offen lds
	v_readlane_b32 s12, v255, 0
	v_readlane_b32 s13, v255, 1
	v_readlane_b32 s14, v255, 2
	v_readlane_b32 s15, v255, 3
	v_readlane_b32 s4, v255, 28
	s_mov_b32 m0, s4
	s_nop 4
	buffer_load_dwordx4 v138, s[12:15], s0 offen lds
	s_lshl_b32 s0, s33, 5
	s_add_i32 s0, s55, s0
	s_sub_i32 s0, s0, 64
	v_readlane_b32 s16, v255, 4
	s_mov_b32 s75, s11
	s_mul_i32 s38, s0, 0x1800
	s_mov_b32 m0, s75
	s_nop 0
	buffer_load_dwordx4 v166, s[64:67], s38 offen lds
	s_mov_b32 s16, s86
	s_mov_b32 m0, s16
	s_nop 4
	buffer_load_dwordx4 v167, s[64:67], s38 offen lds
	s_lshl_b32 s38, s0, 12
	s_mov_b32 m0, s87
	s_nop 0
	buffer_load_dwordx4 v168, s[68:71], s38 offen lds
	v_readlane_b32 s4, v255, 27
	s_mov_b32 m0, s4
	s_nop 4
	buffer_load_dwordx4 v169, s[68:71], s38 offen lds
	s_lshl_b32 s0, s0, 7
	v_readlane_b32 s4, v255, 29
	s_mov_b32 m0, s4
	s_nop 4
	buffer_load_dwordx4 v138, s[12:15], s0 offen lds
	s_waitcnt vmcnt(5)
	v_readlane_b32 s4, v255, 31
	v_readlane_b32 s5, v255, 32
	s_mov_b32 s74, s10
	s_or_b32 s43, s43, 2
	s_mov_b32 s46, 0
	s_andn2_b64 vcc, exec, s[4:5]
	s_mov_b32 s39, 0
	v_readlane_b32 s17, v255, 5
	v_readlane_b32 s18, v255, 6
	v_readlane_b32 s19, v255, 7
	s_barrier
	s_cbranch_vccnz .LBB0_1048
	s_lshl_b32 s0, s42, 5
	s_and_b32 s0, s0, 0xffffff80
	s_sub_i32 s0, s55, s0
	s_add_i32 s38, s0, 0x7a0
	s_mul_i32 s0, s38, 0x1800
	s_lshl_b32 s46, s38, 12
	s_lshl_b32 s61, s38, 7
	s_mov_b32 s62, 0
	s_branch .LBB0_1043

; #define AT_DMA(rs, voff, soff, m0v) asm volatile("s_mov_b32 m0, %0\n\ts_nop 4\n\tbuffer_load_dwordx4 %1, %2, %3 offen lds" :: "s"(m0v), "v"(voff), "s"(rs), "s"(soff) : "m0", "memory")
; DI void attn_issue(const AttnCtx& c, int kb, int bufsel) {
;   const unsigned tok = (unsigned)(c.b * SEQ + kb * 32);
;   const unsigned bb = c.ldsb + (unsigned)bufsel * AT_BUF + (unsigned)c.wv * 1024u;
;   AT_DMA(c.rsQKV, c.voff_sbk, tok * 6144u, bb + AT_SBK); AT_DMA(c.rsQKV, c.voff_sbv, tok * 6144u, bb + AT_SBV);
;   AT_DMA(c.rsMKV, c.voff_mlk, tok * 4096u, bb + AT_MLK); AT_DMA(c.rsMKV, c.voff_mlv, tok * 4096u, bb + AT_MLV);
;   if (c.wv < 4) AT_DMA(c.rsKR, c.voff_r, tok * 128u, bb + AT_MLR);
; }
; DI void attn_step_end() { asm volatile("s_waitcnt vmcnt(0)" ::: "memory"); __builtin_amdgcn_s_barrier(); }
; DI void attn_step_end_sb() { asm volatile("s_waitcnt vmcnt(5)" ::: "memory"); __builtin_amdgcn_s_barrier(); }
; DI void attn_sb_item(const Params& p, LDS_AS unsigned char* lds, const AttnCtx& c, int qb, int nsteps) {
;     ...
; #pragma unroll 1
;   for (; s < nskip; ++s) { if (s + 2 < nsteps) { attn_issue(c, nsteps - 3 - s, rb == 0 ? 2 : rb - 1); attn_step_end_sb(); } else attn_step_end(); rb = rb == 2 ? 0 : rb + 1; }
.LBB0_1045:
	s_andn2_b64 vcc, exec, s[78:79]
	s_cbranch_vccnz .LBB0_1042
	s_mul_i32 s38, s39, 0x9000
	s_add_i32 s38, s38, 0xffff7000
	s_cmp_lg_u32 s39, 0
	s_cselect_b32 s38, s38, 0x12000
	s_add_i32 s38, s38, s77
	s_mov_b32 m0, s38
	s_nop 4
	buffer_load_dwordx4 v166, s[64:67], s0 offen lds
	s_add_i32 s63, s38, 0x2000
	s_mov_b32 m0, s63
	s_nop 0
	buffer_load_dwordx4 v167, s[64:67], s0 offen lds
	s_add_i32 s63, s38, 0x4000
	s_mov_b32 m0, s63
	s_nop 0
	buffer_load_dwordx4 v168, s[68:71], s46 offen lds
	s_add_i32 s63, s38, 0x7000
	s_mov_b32 m0, s63
	s_nop 0
	buffer_load_dwordx4 v169, s[68:71], s46 offen lds
	v_readlane_b32 s4, v254, 56
	s_addk_i32 s38, 0x6000
	v_readlane_b32 s12, v255, 0
	v_readlane_b32 s13, v255, 1
	v_readlane_b32 s14, v255, 2
	v_readlane_b32 s15, v255, 3
	s_mov_b32 m0, s38
	s_nop 4
	buffer_load_dwordx4 v138, s[12:15], s61 offen lds
	s_waitcnt vmcnt(5)
	v_readlane_b32 s5, v254, 57
	v_readlane_b32 s6, v254, 58
	v_readlane_b32 s7, v254, 59
	v_readlane_b32 s8, v254, 60
	v_readlane_b32 s9, v254, 61
	v_readlane_b32 s10, v254, 62
	v_readlane_b32 s11, v254, 63
	v_readlane_b32 s16, v255, 4
	v_readlane_b32 s17, v255, 5
	v_readlane_b32 s18, v255, 6
	v_readlane_b32 s19, v255, 7
	s_barrier
	s_branch .LBB0_1042

; #define AT_DMA(rs, voff, soff, m0v) asm volatile("s_mov_b32 m0, %0\n\ts_nop 4\n\tbuffer_load_dwordx4 %1, %2, %3 offen lds" :: "s"(m0v), "v"(voff), "s"(rs), "s"(soff) : "m0", "memory")
; DI void attn_issue(const AttnCtx& c, int kb, int bufsel) {
;   const unsigned tok = (unsigned)(c.b * SEQ + kb * 32);
;   const unsigned bb = c.ldsb + (unsigned)bufsel * AT_BUF + (unsigned)c.wv * 1024u;
;   AT_DMA(c.rsQKV, c.voff_sbk, tok * 6144u, bb + AT_SBK); AT_DMA(c.rsQKV, c.voff_sbv, tok * 6144u, bb + AT_SBV);
;   AT_DMA(c.rsMKV, c.voff_mlk, tok * 4096u, bb + AT_MLK); AT_DMA(c.rsMKV, c.voff_mlv, tok * 4096u, bb + AT_MLV);
;   if (c.wv < 4) AT_DMA(c.rsKR, c.voff_r, tok * 128u, bb + AT_MLR);
; }
; DI void attn_sb_item(const Params& p, LDS_AS unsigned char* lds, const AttnCtx& c, int qb, int nsteps) {
;     ...
;   for (; s < nsteps; ++s) {
;     const int kb = nsteps - 1 - s;
;     if (s + 2 < nsteps) { attn_issue(c, kb - 2, rb == 0 ? 2 : rb - 1); }
.LBB0_1053:
	s_andn2_b64 vcc, exec, s[84:85]
	s_cbranch_vccnz .LBB0_1055
	s_add_i32 s38, s62, 0xffff7000
	s_cmp_lg_u32 s39, 0
	s_cselect_b32 s38, s38, 0x12000
	s_add_i32 s38, s38, s77
	s_mov_b32 m0, s38
	s_nop 4
	buffer_load_dwordx4 v166, s[64:67], s61 offen lds
	s_add_i32 s63, s38, 0x2000
	s_mov_b32 m0, s63
	s_nop 0
	buffer_load_dwordx4 v167, s[64:67], s61 offen lds
	s_add_i32 s63, s38, 0x4000
	s_mov_b32 m0, s63
	s_nop 0
	buffer_load_dwordx4 v168, s[68:71], s55 offen lds
	s_add_i32 s63, s38, 0x7000
	s_mov_b32 m0, s63
	s_nop 0
	buffer_load_dwordx4 v169, s[68:71], s55 offen lds
	v_readlane_b32 s4, v254, 56
	s_addk_i32 s38, 0x6000
	v_readlane_b32 s12, v255, 0
	v_readlane_b32 s13, v255, 1
	v_readlane_b32 s14, v255, 2
	v_readlane_b32 s15, v255, 3
	s_mov_b32 m0, s38
	s_nop 4
	buffer_load_dwordx4 v138, s[12:15], s42 offen lds
	s_mov_b32 s38, s62
	v_readlane_b32 s5, v254, 57
	v_readlane_b32 s6, v254, 58
	v_readlane_b32 s7, v254, 59
	v_readlane_b32 s8, v254, 60
	v_readlane_b32 s9, v254, 61
	v_readlane_b32 s10, v254, 62
	v_readlane_b32 s11, v254, 63
	v_readlane_b32 s16, v255, 4
	v_readlane_b32 s17, v255, 5
	v_readlane_b32 s18, v255, 6
	v_readlane_b32 s19, v255, 7

; #define OPAQUE_TID(P) (((P).wid0 << 6) | lane_id_now())
; template <int NS, bool STREAM_ONLY = false>
; DI void convert_experts_dma(const Params& p, LDS_AS unsigned char* lds, int bid, int nb) {
;   const int tid = OPAQUE_TID(p), wid = __builtin_amdgcn_readfirstlane(tid >> 6), lane = tid & 63;
;   constexpr int NT = 32 * 1536;
;   const int nvalid = bid < NT / CVG ? CVG * ((NT / CVG - bid + nb - 1) / nb) : 0;
;     ...
;   const __amdgpu_buffer_rsrc_t rs1 = __builtin_amdgcn_make_buffer_rsrc((void*)p.w_gate_up, 0, 0x40000000u, 0x00020000);
;   const __amdgpu_buffer_rsrc_t rs2 = __builtin_amdgcn_make_buffer_rsrc((void*)p.w_down, 0, 0x20000000u, 0x00020000);
;   const __amdgpu_buffer_rsrc_t rs0 = __builtin_amdgcn_make_buffer_rsrc((void*)p.w_down, 0, 0u, 0x00020000);
;   const unsigned vo1 = ((unsigned)lane >> 4) * 16384u + ((((unsigned)lane & 15u) ^ (unsigned)wid) << 4);
;   const unsigned vo2 = ((unsigned)lane >> 4) * 8192u + ((((unsigned)lane & 15u) ^ (unsigned)wid) << 4);
;   const unsigned ldsw = (unsigned)__builtin_amdgcn_readfirstlane((int)(unsigned)(size_t)lds) + (unsigned)wid * 4096u;
;   const int n = 8 * wid + (lane >> 3), kc = lane & 7;
;   const unsigned roff = (unsigned)kc * 4096u + ((((unsigned)n >> 2) ^ (unsigned)kc) << 4) + (((unsigned)n & 3u) << 2);
;     ...
;   CVD_ISSUE(0, 0); CVD_ISSUE(1, 1); CVD_ISSUE(2, 2);
;   if (NS == 5) CVD_ISSUE(3, 3);
.LBB0_1123:
	s_ashr_i32 s21, s0, 6
	v_readlane_b32 s24, v254, 6
	v_readlane_b32 s25, v254, 7
	v_readlane_b32 s29, v254, 11
	s_lshl_b32 s0, s21, 12
	s_and_b32 s9, s25, 0xffff
	s_and_b32 s5, s29, 0xffff
	s_add_i32 s19, s0, 0
	s_lshl_b32 s22, s54, 2
	v_bfe_u32 v1, v0, 4, 2
	s_cmp_gt_i32 s18, 0
	v_lshlrev_b32_e32 v4, 14, v1
	v_bitop3_b32 v5, s21, v0, 15 bitop3:0x78
	s_cselect_b64 s[12:13], -1, 0
	s_cmpk_gt_i32 s22, 0x3fff
	v_readlane_b32 s28, v254, 10
	v_lshl_add_u32 v4, v5, 4, v4
	v_lshlrev_b32_e32 v1, 13, v1
	s_cselect_b64 s[0:1], -1, 0
	s_cmpk_lt_i32 s22, 0x4000
	s_mov_b32 s7, 0x20000
	s_mov_b32 s10, 2.0
	s_brev_b32 s2, 4
	s_mov_b32 s4, s28
	v_sub_u32_e32 v5, v4, v1
	s_cselect_b64 s[14:15], -1, 0
	s_mov_b64 s[16:17], -1
	s_and_b64 vcc, exec, s[12:13]
	v_readlane_b32 s26, v254, 8
	v_readlane_b32 s27, v254, 9
	v_readlane_b32 s30, v254, 12
	v_readlane_b32 s31, v254, 13
	s_cbranch_vccnz .LBB0_1125
	v_cndmask_b32_e64 v1, v5, v4, s[0:1]
	s_mov_b32 s3, 0
	s_mov_b32 m0, s19
	s_nop 0
	buffer_load_dwordx4 v1, s[4:7], s3 offen lds
	s_add_i32 s8, s19, 0x400
	s_mov_b32 m0, s8
	s_nop 0
	buffer_load_dwordx4 v1, s[4:7], s3 offen lds
	s_add_i32 s8, s19, 0x800
	s_mov_b32 m0, s8
	s_nop 0
	buffer_load_dwordx4 v1, s[4:7], s3 offen lds
	s_add_i32 s8, s19, 0xc00
	s_mov_b32 m0, s8
	s_nop 0
	buffer_load_dwordx4 v1, s[4:7], s3 offen lds
	s_mov_b64 s[16:17], 0
.LBB0_1125:
	s_andn2_b64 vcc, exec, s[16:17]
	s_lshl_b32 s20, s21, 4
	s_cbranch_vccnz .LBB0_1130
	s_add_i32 s8, s22, 0xffffc000
	s_lshr_b32 s3, s22, 9
	s_lshr_b32 s8, s8, 10
	s_and_b64 s[16:17], s[0:1], exec
	s_cselect_b32 s3, s8, s3
	s_and_b32 s8, s22, 0x1ff
	s_bitset1_b32 s8, 10
	s_and_b32 s11, s22, 0x3ff
	s_and_b64 s[16:17], s[0:1], exec
	s_cselect_b32 s8, s11, s8
	s_add_i32 s16, s8, 0xfffffc00
	s_bfe_u32 s11, s22, 0x40006
	s_lshr_b32 s23, s16, 5
	s_and_b64 s[16:17], s[0:1], exec
	s_cselect_b32 s11, s11, s23
	s_cselect_b32 s16, 63, 31
	s_lshl_b32 s3, s3, 11
	s_lshl_b32 s11, s11, 7
	s_add_i32 s3, s3, s20
	s_and_b32 s8, s8, s16
	s_add_i32 s3, s3, s11
	s_and_b64 s[0:1], s[0:1], exec
	s_cselect_b32 s0, 14, 13
	s_lshl_b32 s0, s3, s0
	s_lshl_b32 s1, s8, 8
	s_or_b32 s16, s0, s1
	s_add_i32 s24, s19, 0x400
	s_add_i32 s23, s19, 0x800
	s_add_i32 s17, s19, 0xc00
	s_andn2_b64 vcc, exec, s[14:15]
	s_mov_b64 s[0:1], -1
	s_cbranch_vccnz .LBB0_1128
	s_mov_b32 s0, s4
	s_mov_b32 s1, s5
	s_mov_b32 s3, s7
	s_mov_b32 m0, s19
	s_nop 0
	buffer_load_dwordx4 v5, s[0:3], s16 offen lds
	s_or_b32 s8, s16, 0x8000
	s_mov_b32 m0, s24
	s_nop 0
	buffer_load_dwordx4 v5, s[0:3], s8 offen lds
	s_add_i32 s8, s16, 0x10000
	s_mov_b32 m0, s23
	s_nop 0
	buffer_load_dwordx4 v5, s[0:3], s8 offen lds
	s_add_i32 s8, s16, 0x18000
	s_mov_b32 m0, s17
	s_nop 0
	buffer_load_dwordx4 v5, s[0:3], s8 offen lds
	s_mov_b64 s[0:1], 0
.LBB0_1128:
	s_andn2_b64 vcc, exec, s[0:1]
	s_cbranch_vccnz .LBB0_1130
	v_readlane_b32 s60, v254, 6
	s_mov_b32 s8, s60
	s_mov_b32 s11, s7
	s_mov_b32 m0, s19
	s_nop 4
	buffer_load_dwordx4 v4, s[8:11], s16 offen lds
	s_add_i32 s0, s16, 0x10000
	s_mov_b32 m0, s24
	s_nop 0
	buffer_load_dwordx4 v4, s[8:11], s0 offen lds
	s_add_i32 s0, s16, 0x20000
	s_mov_b32 m0, s23
	s_nop 0
	buffer_load_dwordx4 v4, s[8:11], s0 offen lds
	s_add_i32 s0, s16, 0x30000
	s_mov_b32 m0, s17
	s_nop 0
	buffer_load_dwordx4 v4, s[8:11], s0 offen lds
	v_readlane_b32 s61, v254, 7
	v_readlane_b32 s62, v254, 8
	v_readlane_b32 s63, v254, 9
	v_readlane_b32 s64, v254, 10
	v_readlane_b32 s65, v254, 11
	v_readlane_b32 s66, v254, 12
	v_readlane_b32 s67, v254, 13
.LBB0_1130:
	s_cmpk_gt_i32 s22, 0x3ffe
	s_cselect_b64 s[0:1], -1, 0
	s_cmpk_lt_i32 s22, 0x3fff
	s_cselect_b64 s[14:15], -1, 0
	s_add_i32 s23, s19, 0x8000
	s_mov_b32 s3, 0
	s_cmp_gt_i32 s18, 1
	s_mov_b64 s[16:17], -1
	s_cbranch_scc1 .LBB0_1132
	v_cndmask_b32_e64 v1, v5, v4, s[0:1]
	s_mov_b32 m0, s23
	s_nop 0
	buffer_load_dwordx4 v1, s[4:7], s3 offen lds
	s_add_i32 s8, s19, 0x8400
	s_mov_b32 m0, s8
	s_nop 0
	buffer_load_dwordx4 v1, s[4:7], s3 offen lds
	s_add_i32 s8, s19, 0x8800
	s_mov_b32 m0, s8
	s_nop 0
	buffer_load_dwordx4 v1, s[4:7], s3 offen lds
	s_add_i32 s8, s19, 0x8c00
	s_mov_b32 m0, s8
	s_nop 0
	buffer_load_dwordx4 v1, s[4:7], s3 offen lds
	s_mov_b64 s[16:17], 0
; template <int NS, bool STREAM_ONLY = false>
; DI void convert_experts_dma(const Params& p, LDS_AS unsigned char* lds, int bid, int nb) {
;     ...
;   CVD_ISSUE(0, 0); CVD_ISSUE(1, 1); CVD_ISSUE(2, 2);
;   if (NS == 5) CVD_ISSUE(3, 3);
.LBB0_1132:
	s_andn2_b64 vcc, exec, s[16:17]
	s_cbranch_vccnz .LBB0_1137
	s_add_i32 s8, s22, 0xffffc001
	s_lshr_b32 s3, s22, 9
	s_lshr_b32 s8, s8, 10
	s_and_b64 s[16:17], s[0:1], exec
	s_cselect_b32 s3, s8, s3
	s_and_b32 s8, s22, 0x1fe
	s_add_i32 s11, s22, 1
	s_or_b32 s8, s8, 0x401
	s_and_b32 s24, s11, 0x3ff
	s_and_b64 s[16:17], s[0:1], exec
	s_cselect_b32 s8, s24, s8
	s_add_i32 s16, s8, 0xfffffc00
	s_bfe_u32 s11, s11, 0x40006
	s_lshr_b32 s24, s16, 5
	s_and_b64 s[16:17], s[0:1], exec
	s_cselect_b32 s11, s11, s24
	s_cselect_b32 s16, 63, 31
	s_lshl_b32 s3, s3, 11
	s_lshl_b32 s11, s11, 7
	s_add_i32 s3, s3, s20
	s_and_b32 s8, s8, s16
	s_add_i32 s3, s3, s11
	s_and_b64 s[0:1], s[0:1], exec
	s_cselect_b32 s0, 14, 13
	s_lshl_b32 s0, s3, s0
	s_lshl_b32 s1, s8, 8
	s_or_b32 s16, s0, s1
	s_add_i32 s25, s19, 0x8400
	s_add_i32 s24, s19, 0x8800
	s_add_i32 s17, s19, 0x8c00
	s_andn2_b64 vcc, exec, s[14:15]
	s_mov_b64 s[0:1], -1
	s_cbranch_vccnz .LBB0_1135
	s_mov_b32 s0, s4
	s_mov_b32 s1, s5
	s_mov_b32 s3, s7
	s_mov_b32 m0, s23
	s_nop 0
	buffer_load_dwordx4 v5, s[0:3], s16 offen lds
	s_or_b32 s8, s16, 0x8000
	s_mov_b32 m0, s25
	s_nop 0
	buffer_load_dwordx4 v5, s[0:3], s8 offen lds
	s_add_i32 s8, s16, 0x10000
	s_mov_b32 m0, s24
	s_nop 0
	buffer_load_dwordx4 v5, s[0:3], s8 offen lds
	s_add_i32 s8, s16, 0x18000
	s_mov_b32 m0, s17
	s_nop 0
	buffer_load_dwordx4 v5, s[0:3], s8 offen lds
	s_mov_b64 s[0:1], 0
.LBB0_1135:
	s_andn2_b64 vcc, exec, s[0:1]
	s_cbranch_vccnz .LBB0_1137
	v_readlane_b32 s60, v254, 6
	s_mov_b32 s8, s60
	s_mov_b32 s11, s7
	s_mov_b32 m0, s23
	s_nop 4
	buffer_load_dwordx4 v4, s[8:11], s16 offen lds
	s_add_i32 s0, s16, 0x10000
	s_mov_b32 m0, s25
	s_nop 0
	buffer_load_dwordx4 v4, s[8:11], s0 offen lds
	s_add_i32 s0, s16, 0x20000
	s_mov_b32 m0, s24
	s_nop 0
	buffer_load_dwordx4 v4, s[8:11], s0 offen lds
	s_add_i32 s0, s16, 0x30000
	s_mov_b32 m0, s17
	s_nop 0
	buffer_load_dwordx4 v4, s[8:11], s0 offen lds
	v_readlane_b32 s61, v254, 7
	v_readlane_b32 s62, v254, 8
	v_readlane_b32 s63, v254, 9
	v_readlane_b32 s64, v254, 10
	v_readlane_b32 s65, v254, 11
	v_readlane_b32 s66, v254, 12
	v_readlane_b32 s67, v254, 13
.LBB0_1137:
	s_or_b32 s3, s22, 2
	s_cmpk_gt_i32 s3, 0x3fff
	s_cselect_b64 s[0:1], -1, 0
	s_cmpk_lt_i32 s3, 0x4000
	s_cselect_b64 s[14:15], -1, 0
	s_add_i32 s23, s19, 0x10000
	s_mov_b32 s8, 0
	s_cmp_gt_i32 s18, 2
	s_mov_b64 s[16:17], -1
	s_cbranch_scc1 .LBB0_1139
	v_cndmask_b32_e64 v1, v5, v4, s[0:1]
	s_mov_b32 m0, s23
	s_nop 0
	buffer_load_dwordx4 v1, s[4:7], s8 offen lds
	s_add_i32 s11, s19, 0x10400
	s_mov_b32 m0, s11
	s_nop 0
	buffer_load_dwordx4 v1, s[4:7], s8 offen lds
	s_add_i32 s11, s19, 0x10800
	s_mov_b32 m0, s11
	s_nop 0
	buffer_load_dwordx4 v1, s[4:7], s8 offen lds
	s_add_i32 s11, s19, 0x10c00
	s_mov_b32 m0, s11
	s_nop 0
	buffer_load_dwordx4 v1, s[4:7], s8 offen lds
	s_mov_b64 s[16:17], 0
.LBB0_1139:
	s_andn2_b64 vcc, exec, s[16:17]
	s_cbranch_vccnz .LBB0_1144
	s_add_i32 s11, s22, 0xffffc002
	s_lshr_b32 s8, s22, 9
	s_lshr_b32 s11, s11, 10
	s_and_b64 s[16:17], s[0:1], exec
	s_cselect_b32 s8, s11, s8
	s_and_b32 s3, s3, 0x1ff
	s_add_i32 s11, s22, 2
	s_bitset1_b32 s3, 10
	s_and_b32 s24, s11, 0x3ff
	s_and_b64 s[16:17], s[0:1], exec
	s_cselect_b32 s3, s24, s3
	s_add_i32 s16, s3, 0xfffffc00
	s_bfe_u32 s11, s11, 0x40006
	s_lshr_b32 s24, s16, 5
	s_and_b64 s[16:17], s[0:1], exec
	s_cselect_b32 s11, s11, s24
	s_cselect_b32 s16, 63, 31
	s_lshl_b32 s8, s8, 11
	s_lshl_b32 s11, s11, 7
	s_add_i32 s8, s8, s20
	s_and_b32 s3, s3, s16
	s_add_i32 s8, s8, s11
	s_and_b64 s[0:1], s[0:1], exec
	s_cselect_b32 s0, 14, 13
	s_lshl_b32 s0, s8, s0
	s_lshl_b32 s1, s3, 8
	s_or_b32 s16, s0, s1
	s_add_i32 s25, s19, 0x10400
	s_add_i32 s24, s19, 0x10800
	s_add_i32 s17, s19, 0x10c00
	s_andn2_b64 vcc, exec, s[14:15]
	s_mov_b64 s[0:1], -1
	s_cbranch_vccnz .LBB0_1142
	s_mov_b32 s0, s4
	s_mov_b32 s1, s5
	s_mov_b32 s3, s7
	s_mov_b32 m0, s23
	s_nop 0
	buffer_load_dwordx4 v5, s[0:3], s16 offen lds
	s_or_b32 s8, s16, 0x8000
	s_mov_b32 m0, s25
	s_nop 0
	buffer_load_dwordx4 v5, s[0:3], s8 offen lds
	s_add_i32 s8, s16, 0x10000
	s_mov_b32 m0, s24
	s_nop 0
	buffer_load_dwordx4 v5, s[0:3], s8 offen lds
	s_add_i32 s8, s16, 0x18000
	s_mov_b32 m0, s17
	s_nop 0
	buffer_load_dwordx4 v5, s[0:3], s8 offen lds
	s_mov_b64 s[0:1], 0

; template <int NS, bool STREAM_ONLY = false>
; DI void convert_experts_dma(const Params& p, LDS_AS unsigned char* lds, int bid, int nb) {
;     ...
;   CVD_ISSUE(0, 0); CVD_ISSUE(1, 1); CVD_ISSUE(2, 2);
;   if (NS == 5) CVD_ISSUE(3, 3);
.LBB0_1144:
	s_or_b32 s3, s22, 3
	s_cmpk_gt_i32 s3, 0x3fff
	s_cselect_b64 s[0:1], -1, 0
	s_cmpk_lt_i32 s3, 0x4000
	s_cselect_b64 s[14:15], -1, 0
	s_add_i32 s23, s19, 0x18000
	s_mov_b32 s8, 0
	s_cmp_gt_i32 s18, 3
	s_mov_b64 s[16:17], -1
	s_cbranch_scc1 .LBB0_1146
	v_cndmask_b32_e64 v1, v5, v4, s[0:1]
	s_mov_b32 m0, s23
	s_nop 0
	buffer_load_dwordx4 v1, s[4:7], s8 offen lds
	s_add_i32 s11, s19, 0x18400
	s_mov_b32 m0, s11
	s_nop 0
	buffer_load_dwordx4 v1, s[4:7], s8 offen lds
	s_add_i32 s11, s19, 0x18800
	s_mov_b32 m0, s11
	s_nop 0
	buffer_load_dwordx4 v1, s[4:7], s8 offen lds
	s_add_i32 s11, s19, 0x18c00
	s_mov_b32 m0, s11
	s_nop 0
	buffer_load_dwordx4 v1, s[4:7], s8 offen lds
	s_mov_b64 s[16:17], 0
.LBB0_1146:
	s_andn2_b64 vcc, exec, s[16:17]
	s_cbranch_vccnz .LBB0_1151
	s_add_i32 s11, s22, 0xffffc003
	s_lshr_b32 s8, s22, 9
	s_lshr_b32 s11, s11, 10
	s_and_b64 s[16:17], s[0:1], exec
	s_cselect_b32 s8, s11, s8
	s_and_b32 s3, s3, 0x1ff
	s_add_i32 s22, s22, 3
	s_bitset1_b32 s3, 10
	s_and_b32 s11, s22, 0x3ff
	s_and_b64 s[16:17], s[0:1], exec
	s_cselect_b32 s3, s11, s3
	s_add_i32 s16, s3, 0xfffffc00
	s_bfe_u32 s11, s22, 0x40006
	s_lshr_b32 s22, s16, 5
	s_and_b64 s[16:17], s[0:1], exec
	s_cselect_b32 s11, s11, s22
	s_cselect_b32 s16, 63, 31
	s_lshl_b32 s8, s8, 11
	s_lshl_b32 s11, s11, 7
	s_add_i32 s8, s8, s20
	s_and_b32 s3, s3, s16
	s_add_i32 s8, s8, s11
	s_and_b64 s[0:1], s[0:1], exec
	s_cselect_b32 s0, 14, 13
	s_lshl_b32 s0, s8, s0
	s_lshl_b32 s1, s3, 8
	s_or_b32 s16, s0, s1
	s_add_i32 s24, s19, 0x18400
	s_add_i32 s22, s19, 0x18800
	s_add_i32 s17, s19, 0x18c00
	s_andn2_b64 vcc, exec, s[14:15]
	s_mov_b64 s[0:1], -1
	s_cbranch_vccnz .LBB0_1149
	s_mov_b32 s0, s4
	s_mov_b32 s1, s5
	s_mov_b32 s3, s7
	s_mov_b32 m0, s23
	s_nop 0
	buffer_load_dwordx4 v5, s[0:3], s16 offen lds
	s_or_b32 s8, s16, 0x8000
	s_mov_b32 m0, s24
	s_nop 0
	buffer_load_dwordx4 v5, s[0:3], s8 offen lds
	s_add_i32 s8, s16, 0x10000
	s_mov_b32 m0, s22
	s_nop 0
	buffer_load_dwordx4 v5, s[0:3], s8 offen lds
	s_add_i32 s8, s16, 0x18000
	s_mov_b32 m0, s17
	s_nop 0
	buffer_load_dwordx4 v5, s[0:3], s8 offen lds
	s_mov_b64 s[0:1], 0
.LBB0_1149:
	s_andn2_b64 vcc, exec, s[0:1]
	s_cbranch_vccnz .LBB0_1151
	v_readlane_b32 s60, v254, 6
	s_mov_b32 s8, s60
	s_mov_b32 s11, s7
	s_mov_b32 m0, s23
	s_nop 4
	buffer_load_dwordx4 v4, s[8:11], s16 offen lds
	s_add_i32 s0, s16, 0x10000
	s_mov_b32 m0, s24
	s_nop 0
	buffer_load_dwordx4 v4, s[8:11], s0 offen lds
	s_add_i32 s0, s16, 0x20000
	s_mov_b32 m0, s22
	s_nop 0
	buffer_load_dwordx4 v4, s[8:11], s0 offen lds
	s_add_i32 s0, s16, 0x30000
	s_mov_b32 m0, s17
	s_nop 0
	buffer_load_dwordx4 v4, s[8:11], s0 offen lds
	v_readlane_b32 s61, v254, 7
	v_readlane_b32 s62, v254, 8
	v_readlane_b32 s63, v254, 9
	v_readlane_b32 s64, v254, 10
	v_readlane_b32 s65, v254, 11
	v_readlane_b32 s66, v254, 12
	v_readlane_b32 s67, v254, 13

; template <int NS, bool STREAM_ONLY = false>
; DI void convert_experts_dma(const Params& p, LDS_AS unsigned char* lds, int bid, int nb) {
;     ...
;   for (int i = 0; i < nvalid; ++i) {
;     if (NS == 4) asm volatile("s_waitcnt vmcnt(8)" ::: "memory");
;     else asm volatile("s_waitcnt vmcnt(12)" ::: "memory");
;     __builtin_amdgcn_s_barrier();
;     __builtin_amdgcn_sched_barrier(0);
;     const int sp = si == 0 ? NS - 1 : si - 1;
;     CVD_ISSUE(i + NS - 1, sp);
.LBB0_1154:
	s_waitcnt vmcnt(12)
	s_barrier
	s_add_i32 s8, s22, 4
	s_lshr_b32 s0, s8, 2
	s_mul_i32 s0, s0, s55
	s_add_i32 s0, s0, s54
	s_lshl_b32 s0, s0, 2
	s_and_b32 s12, s22, 3
	s_or_b32 s3, s0, s12
	s_cmpk_gt_i32 s3, 0x3fff
	s_cselect_b64 s[0:1], -1, 0
	s_cmpk_lt_i32 s3, 0x4000
	s_cselect_b64 s[14:15], -1, 0
	s_lshl_b32 s23, s21, 15
	s_add_i32 s11, s23, 0xffff8000
	s_cmp_lg_u32 s21, 0
	s_cselect_b32 s11, s11, 0x20000
	s_add_i32 s24, s11, s19
	s_cmp_lt_i32 s8, s18
	s_mov_b64 s[16:17], -1
	s_cbranch_scc1 .LBB0_1156
	v_cndmask_b32_e64 v8, v5, v4, s[0:1]
	s_mov_b32 m0, s24
	s_nop 0
	buffer_load_dwordx4 v8, s[4:7], s13 offen lds
	s_add_i32 s8, s24, 0x400
	s_mov_b32 m0, s8
	s_nop 0
	buffer_load_dwordx4 v8, s[4:7], s13 offen lds
	s_add_i32 s8, s24, 0x800
	s_mov_b32 m0, s8
	s_nop 0
	buffer_load_dwordx4 v8, s[4:7], s13 offen lds
	s_add_i32 s8, s24, 0xc00
	s_mov_b32 m0, s8
	s_nop 0
	buffer_load_dwordx4 v8, s[4:7], s13 offen lds
	s_mov_b64 s[16:17], 0
.LBB0_1156:
	s_andn2_b64 vcc, exec, s[16:17]
	s_cbranch_vccnz .LBB0_1161
	s_add_i32 s11, s3, 0xffffc000
	s_lshr_b32 s8, s3, 9
	s_lshr_b32 s11, s11, 10
	s_and_b64 s[16:17], s[0:1], exec
	s_cselect_b32 s8, s11, s8
	s_and_b32 s11, s3, 0x1ff
	s_bitset1_b32 s11, 10
	s_and_b32 s25, s3, 0x3ff
	s_and_b64 s[16:17], s[0:1], exec
	s_cselect_b32 s11, s25, s11
	s_add_i32 s16, s11, 0xfffffc00
	s_bfe_u32 s3, s3, 0x40006
	s_lshr_b32 s25, s16, 5
	s_and_b64 s[16:17], s[0:1], exec
	s_cselect_b32 s3, s3, s25
	s_cselect_b32 s16, 63, 31
	s_lshl_b32 s8, s8, 11
	s_lshl_b32 s3, s3, 7
	s_add_i32 s8, s8, s20
	s_and_b32 s11, s11, s16
	s_add_i32 s8, s8, s3
	s_and_b64 s[0:1], s[0:1], exec
	s_cselect_b32 s0, 14, 13
	s_lshl_b32 s0, s8, s0
	s_lshl_b32 s1, s11, 8
	s_or_b32 s16, s0, s1
	s_add_i32 s26, s24, 0x400
	s_add_i32 s25, s24, 0x800
	s_add_i32 s17, s24, 0xc00
	s_andn2_b64 vcc, exec, s[14:15]
	s_mov_b64 s[0:1], -1
	s_cbranch_vccnz .LBB0_1159
	s_mov_b32 s0, s4
	s_mov_b32 s1, s5
	s_mov_b32 s3, s7
	s_mov_b32 m0, s24
	s_nop 0
	buffer_load_dwordx4 v5, s[0:3], s16 offen lds
	s_or_b32 s8, s16, 0x8000
	s_mov_b32 m0, s26
	s_nop 0
	buffer_load_dwordx4 v5, s[0:3], s8 offen lds
	s_add_i32 s8, s16, 0x10000
	s_mov_b32 m0, s25
	s_nop 0
	buffer_load_dwordx4 v5, s[0:3], s8 offen lds
	s_add_i32 s8, s16, 0x18000
	s_mov_b32 m0, s17
	s_nop 0
	buffer_load_dwordx4 v5, s[0:3], s8 offen lds
	s_mov_b64 s[0:1], 0
.LBB0_1159:
	s_andn2_b64 vcc, exec, s[0:1]
	s_cbranch_vccnz .LBB0_1161
	v_readlane_b32 s60, v254, 6
	s_mov_b32 s8, s60
	s_mov_b32 s11, s7
	s_mov_b32 m0, s24
	s_nop 4
	buffer_load_dwordx4 v4, s[8:11], s16 offen lds
	s_add_i32 s0, s16, 0x10000
	s_mov_b32 m0, s26
	s_nop 0
	buffer_load_dwordx4 v4, s[8:11], s0 offen lds
	s_add_i32 s0, s16, 0x20000
	s_mov_b32 m0, s25
	s_nop 0
	buffer_load_dwordx4 v4, s[8:11], s0 offen lds
	s_add_i32 s0, s16, 0x30000
	s_mov_b32 m0, s17
	s_nop 0
	buffer_load_dwordx4 v4, s[8:11], s0 offen lds
	v_readlane_b32 s61, v254, 7
	v_readlane_b32 s62, v254, 8
	v_readlane_b32 s63, v254, 9
	v_readlane_b32 s64, v254, 10
	v_readlane_b32 s65, v254, 11
	v_readlane_b32 s66, v254, 12
	v_readlane_b32 s67, v254, 13

; #define OPAQUE_TID(P) (((P).wid0 << 6) | lane_id_now())
; template <int NS, bool STREAM_ONLY = false>
; DI void convert_experts_dma(const Params& p, LDS_AS unsigned char* lds, int bid, int nb) {
;   const int tid = OPAQUE_TID(p), wid = __builtin_amdgcn_readfirstlane(tid >> 6), lane = tid & 63;
;   constexpr int NT = 32 * 1536;
;   const int nvalid = bid < NT / CVG ? CVG * ((NT / CVG - bid + nb - 1) / nb) : 0;
;     ...
;   const __amdgpu_buffer_rsrc_t rs1 = __builtin_amdgcn_make_buffer_rsrc((void*)p.w_gate_up, 0, 0x40000000u, 0x00020000);
;   const __amdgpu_buffer_rsrc_t rs2 = __builtin_amdgcn_make_buffer_rsrc((void*)p.w_down, 0, 0x20000000u, 0x00020000);
;   const __amdgpu_buffer_rsrc_t rs0 = __builtin_amdgcn_make_buffer_rsrc((void*)p.w_down, 0, 0u, 0x00020000);
;   const unsigned vo1 = ((unsigned)lane >> 4) * 16384u + ((((unsigned)lane & 15u) ^ (unsigned)wid) << 4);
;   const unsigned vo2 = ((unsigned)lane >> 4) * 8192u + ((((unsigned)lane & 15u) ^ (unsigned)wid) << 4);
;   const unsigned ldsw = (unsigned)__builtin_amdgcn_readfirstlane((int)(unsigned)(size_t)lds) + (unsigned)wid * 4096u;
;   const int n = 8 * wid + (lane >> 3), kc = lane & 7;
;   const unsigned roff = (unsigned)kc * 4096u + ((((unsigned)n >> 2) ^ (unsigned)kc) << 4) + (((unsigned)n & 3u) << 2);
;     ...
;   CVD_ISSUE(0, 0); CVD_ISSUE(1, 1); CVD_ISSUE(2, 2);
.LBB0_1183:
	s_ashr_i32 s23, s0, 6
	v_readlane_b32 s24, v254, 6
	s_lshl_b32 s0, s23, 12
	v_readlane_b32 s25, v254, 7
	v_readlane_b32 s29, v254, 11
	s_add_i32 s24, s0, 0
	s_and_b32 s9, s25, 0xffff
	s_and_b32 s5, s29, 0xffff
	s_add_i32 s21, s24, 16
	s_lshl_b32 s25, s97, 2
	v_bfe_u32 v1, v0, 4, 2
	s_cmp_gt_i32 s20, 0
	v_lshlrev_b32_e32 v2, 14, v1
	v_bitop3_b32 v3, s23, v0, 15 bitop3:0x78
	s_cselect_b64 s[14:15], -1, 0
	s_cmpk_gt_i32 s25, 0x3fff
	v_readlane_b32 s28, v254, 10
	v_lshl_add_u32 v2, v3, 4, v2
	v_lshlrev_b32_e32 v1, 13, v1
	s_cselect_b64 s[0:1], -1, 0
	s_cmpk_lt_i32 s25, 0x4000
	s_mov_b32 s7, 0x20000
	s_mov_b32 s10, 2.0
	s_brev_b32 s2, 4
	s_mov_b32 s4, s28
	s_mov_b32 s6, 0
	v_sub_u32_e32 v3, v2, v1
	s_cselect_b64 s[16:17], -1, 0
	s_mov_b64 s[18:19], -1
	s_and_b64 vcc, exec, s[14:15]
	v_readlane_b32 s26, v254, 8
	v_readlane_b32 s27, v254, 9
	v_readlane_b32 s30, v254, 12
	v_readlane_b32 s31, v254, 13
	s_cbranch_vccnz .LBB0_1185
	v_cndmask_b32_e64 v1, v3, v2, s[0:1]
	s_mov_b32 m0, s21
	s_nop 0
	buffer_load_dwordx4 v1, s[4:7], s6 offen lds
	s_add_i32 s3, s24, 0x410
	s_mov_b32 m0, s3
	s_nop 0
	buffer_load_dwordx4 v1, s[4:7], s6 offen lds
	s_add_i32 s3, s24, 0x810
	s_mov_b32 m0, s3
	s_nop 0
	buffer_load_dwordx4 v1, s[4:7], s6 offen lds
	s_add_i32 s3, s24, 0xc10
	s_mov_b32 m0, s3
	s_nop 0
	buffer_load_dwordx4 v1, s[4:7], s6 offen lds
	s_mov_b64 s[18:19], 0
.LBB0_1185:
	s_andn2_b64 vcc, exec, s[18:19]
	s_lshl_b32 s22, s23, 4
	s_cbranch_vccnz .LBB0_1190
	s_add_i32 s8, s25, 0xffffc000
	s_lshr_b32 s3, s25, 9
	s_lshr_b32 s8, s8, 10
	s_and_b64 s[18:19], s[0:1], exec
	s_cselect_b32 s3, s8, s3
	s_and_b32 s8, s25, 0x1ff
	s_bitset1_b32 s8, 10
	s_and_b32 s11, s25, 0x3ff
	s_and_b64 s[18:19], s[0:1], exec
	s_cselect_b32 s8, s11, s8
	s_add_i32 s18, s8, 0xfffffc00
	s_bfe_u32 s11, s25, 0x40006
	s_lshr_b32 s26, s18, 5
	s_and_b64 s[18:19], s[0:1], exec
	s_cselect_b32 s11, s11, s26
	s_cselect_b32 s18, 63, 31
	s_lshl_b32 s3, s3, 11
	s_lshl_b32 s11, s11, 7
	s_add_i32 s3, s3, s22
	s_and_b32 s8, s8, s18
	s_add_i32 s3, s3, s11
	s_and_b64 s[0:1], s[0:1], exec
	s_cselect_b32 s0, 14, 13
	s_lshl_b32 s0, s3, s0
	s_lshl_b32 s1, s8, 8
	s_or_b32 s18, s0, s1
	s_add_i32 s27, s24, 0x410
	s_add_i32 s26, s24, 0x810
	s_add_i32 s19, s24, 0xc10
	s_andn2_b64 vcc, exec, s[16:17]
	s_mov_b64 s[0:1], -1
	s_cbranch_vccnz .LBB0_1188
	s_mov_b32 s0, s4
	s_mov_b32 s1, s5
	s_mov_b32 s3, s7
	s_mov_b32 m0, s21
	s_nop 0
	buffer_load_dwordx4 v3, s[0:3], s18 offen lds
	s_or_b32 s8, s18, 0x8000
	s_mov_b32 m0, s27
	s_nop 0
	buffer_load_dwordx4 v3, s[0:3], s8 offen lds
	s_add_i32 s8, s18, 0x10000
	s_mov_b32 m0, s26
	s_nop 0
	buffer_load_dwordx4 v3, s[0:3], s8 offen lds
	s_add_i32 s8, s18, 0x18000
	s_mov_b32 m0, s19
	s_nop 0
	buffer_load_dwordx4 v3, s[0:3], s8 offen lds
	s_mov_b64 s[0:1], 0
.LBB0_1188:
	s_andn2_b64 vcc, exec, s[0:1]
	s_cbranch_vccnz .LBB0_1190
	v_readlane_b32 s60, v254, 6
	s_mov_b32 s8, s60
	s_mov_b32 s11, s7
	s_mov_b32 m0, s21
	s_nop 4
	buffer_load_dwordx4 v2, s[8:11], s18 offen lds
	s_add_i32 s0, s18, 0x10000
	s_mov_b32 m0, s27
	s_nop 0
	buffer_load_dwordx4 v2, s[8:11], s0 offen lds
	s_add_i32 s0, s18, 0x20000
	s_mov_b32 m0, s26
	s_nop 0
	buffer_load_dwordx4 v2, s[8:11], s0 offen lds
	s_add_i32 s0, s18, 0x30000
	s_mov_b32 m0, s19
	s_nop 0
	buffer_load_dwordx4 v2, s[8:11], s0 offen lds
	v_readlane_b32 s61, v254, 7
	v_readlane_b32 s62, v254, 8
	v_readlane_b32 s63, v254, 9
	v_readlane_b32 s64, v254, 10
	v_readlane_b32 s65, v254, 11
	v_readlane_b32 s66, v254, 12
	v_readlane_b32 s67, v254, 13
.LBB0_1190:
	s_cmpk_gt_i32 s25, 0x3ffe
	s_cselect_b64 s[0:1], -1, 0
	s_cmpk_lt_i32 s25, 0x3fff
	s_cselect_b64 s[16:17], -1, 0
	s_add_i32 s26, s24, 0x8010
	s_mov_b32 s3, 0
	s_cmp_gt_i32 s20, 1
	s_mov_b64 s[18:19], -1
	s_cbranch_scc1 .LBB0_1192
	v_cndmask_b32_e64 v1, v3, v2, s[0:1]
	s_mov_b32 m0, s26
	s_nop 0
	buffer_load_dwordx4 v1, s[4:7], s3 offen lds
	s_add_i32 s8, s24, 0x8410
	s_mov_b32 m0, s8
	s_nop 0
	buffer_load_dwordx4 v1, s[4:7], s3 offen lds
	s_add_i32 s8, s24, 0x8810
	s_mov_b32 m0, s8
	s_nop 0
	buffer_load_dwordx4 v1, s[4:7], s3 offen lds
	s_add_i32 s8, s24, 0x8c10
	s_mov_b32 m0, s8
	s_nop 0
	buffer_load_dwordx4 v1, s[4:7], s3 offen lds
	s_mov_b64 s[18:19], 0
; template <int NS, bool STREAM_ONLY = false>
; DI void convert_experts_dma(const Params& p, LDS_AS unsigned char* lds, int bid, int nb) {
;     ...
;   CVD_ISSUE(0, 0); CVD_ISSUE(1, 1); CVD_ISSUE(2, 2);
.LBB0_1192:
	s_andn2_b64 vcc, exec, s[18:19]
	s_cbranch_vccnz .LBB0_1197
	s_add_i32 s8, s25, 0xffffc001
	s_lshr_b32 s3, s25, 9
	s_lshr_b32 s8, s8, 10
	s_and_b64 s[18:19], s[0:1], exec
	s_cselect_b32 s3, s8, s3
	s_and_b32 s8, s25, 0x1fe
	s_add_i32 s11, s25, 1
	s_or_b32 s8, s8, 0x401
	s_and_b32 s27, s11, 0x3ff
	s_and_b64 s[18:19], s[0:1], exec
	s_cselect_b32 s8, s27, s8
	s_add_i32 s18, s8, 0xfffffc00
	s_bfe_u32 s11, s11, 0x40006
	s_lshr_b32 s27, s18, 5
	s_and_b64 s[18:19], s[0:1], exec
	s_cselect_b32 s11, s11, s27
	s_cselect_b32 s18, 63, 31
	s_lshl_b32 s3, s3, 11
	s_lshl_b32 s11, s11, 7
	s_add_i32 s3, s3, s22
	s_and_b32 s8, s8, s18
	s_add_i32 s3, s3, s11
	s_and_b64 s[0:1], s[0:1], exec
	s_cselect_b32 s0, 14, 13
	s_lshl_b32 s0, s3, s0
	s_lshl_b32 s1, s8, 8
	s_or_b32 s18, s0, s1
	s_add_i32 s28, s24, 0x8410
	s_add_i32 s27, s24, 0x8810
	s_add_i32 s19, s24, 0x8c10
	s_andn2_b64 vcc, exec, s[16:17]
	s_mov_b64 s[0:1], -1
	s_cbranch_vccnz .LBB0_1195
	s_mov_b32 s0, s4
	s_mov_b32 s1, s5
	s_mov_b32 s3, s7
	s_mov_b32 m0, s26
	s_nop 0
	buffer_load_dwordx4 v3, s[0:3], s18 offen lds
	s_or_b32 s8, s18, 0x8000
	s_mov_b32 m0, s28
	s_nop 0
	buffer_load_dwordx4 v3, s[0:3], s8 offen lds
	s_add_i32 s8, s18, 0x10000
	s_mov_b32 m0, s27
	s_nop 0
	buffer_load_dwordx4 v3, s[0:3], s8 offen lds
	s_add_i32 s8, s18, 0x18000
	s_mov_b32 m0, s19
	s_nop 0
	buffer_load_dwordx4 v3, s[0:3], s8 offen lds
	s_mov_b64 s[0:1], 0
.LBB0_1195:
	s_andn2_b64 vcc, exec, s[0:1]
	s_cbranch_vccnz .LBB0_1197
	v_readlane_b32 s60, v254, 6
	s_mov_b32 s8, s60
	s_mov_b32 s11, s7
	s_mov_b32 m0, s26
	s_nop 4
	buffer_load_dwordx4 v2, s[8:11], s18 offen lds
	s_add_i32 s0, s18, 0x10000
	s_mov_b32 m0, s28
	s_nop 0
	buffer_load_dwordx4 v2, s[8:11], s0 offen lds
	s_add_i32 s0, s18, 0x20000
	s_mov_b32 m0, s27
	s_nop 0
	buffer_load_dwordx4 v2, s[8:11], s0 offen lds
	s_add_i32 s0, s18, 0x30000
	s_mov_b32 m0, s19
	s_nop 0
	buffer_load_dwordx4 v2, s[8:11], s0 offen lds
	v_readlane_b32 s61, v254, 7
	v_readlane_b32 s62, v254, 8
	v_readlane_b32 s63, v254, 9
	v_readlane_b32 s64, v254, 10
	v_readlane_b32 s65, v254, 11
	v_readlane_b32 s66, v254, 12
	v_readlane_b32 s67, v254, 13
.LBB0_1197:
	s_or_b32 s3, s25, 2
	s_cmpk_gt_i32 s3, 0x3fff
	s_cselect_b64 s[0:1], -1, 0
	s_cmpk_lt_i32 s3, 0x4000
	s_cselect_b64 s[16:17], -1, 0
	s_add_i32 s26, s24, 0x10010
	s_mov_b32 s8, 0
	s_cmp_gt_i32 s20, 2
	s_mov_b64 s[18:19], -1
	s_cbranch_scc1 .LBB0_1199
	v_cndmask_b32_e64 v1, v3, v2, s[0:1]
	s_mov_b32 m0, s26
	s_nop 0
	buffer_load_dwordx4 v1, s[4:7], s8 offen lds
	s_add_i32 s11, s24, 0x10410
	s_mov_b32 m0, s11
	s_nop 0
	buffer_load_dwordx4 v1, s[4:7], s8 offen lds
	s_add_i32 s11, s24, 0x10810
	s_mov_b32 m0, s11
	s_nop 0
	buffer_load_dwordx4 v1, s[4:7], s8 offen lds
	s_add_i32 s11, s24, 0x10c10
	s_mov_b32 m0, s11
	s_nop 0
	buffer_load_dwordx4 v1, s[4:7], s8 offen lds
	s_mov_b64 s[18:19], 0
.LBB0_1199:
	s_andn2_b64 vcc, exec, s[18:19]
	s_cbranch_vccnz .LBB0_1204
	s_add_i32 s11, s25, 0xffffc002
	s_lshr_b32 s8, s25, 9
	s_lshr_b32 s11, s11, 10
	s_and_b64 s[18:19], s[0:1], exec
	s_cselect_b32 s8, s11, s8
	s_and_b32 s3, s3, 0x1ff
	s_add_i32 s25, s25, 2
	s_bitset1_b32 s3, 10
	s_and_b32 s11, s25, 0x3ff
	s_and_b64 s[18:19], s[0:1], exec
	s_cselect_b32 s3, s11, s3
	s_add_i32 s18, s3, 0xfffffc00
	s_bfe_u32 s11, s25, 0x40006
	s_lshr_b32 s25, s18, 5
	s_and_b64 s[18:19], s[0:1], exec
	s_cselect_b32 s11, s11, s25
	s_cselect_b32 s18, 63, 31
	s_lshl_b32 s8, s8, 11
	s_lshl_b32 s11, s11, 7
	s_add_i32 s8, s8, s22
	s_and_b32 s3, s3, s18
	s_add_i32 s8, s8, s11
	s_and_b64 s[0:1], s[0:1], exec
	s_cselect_b32 s0, 14, 13
	s_lshl_b32 s0, s8, s0
	s_lshl_b32 s1, s3, 8
	s_or_b32 s18, s0, s1
	s_add_i32 s27, s24, 0x10410
	s_add_i32 s25, s24, 0x10810
	s_add_i32 s19, s24, 0x10c10
	s_andn2_b64 vcc, exec, s[16:17]
	s_mov_b64 s[0:1], -1
	s_cbranch_vccnz .LBB0_1202
	s_mov_b32 s0, s4
	s_mov_b32 s1, s5
	s_mov_b32 s3, s7
	s_mov_b32 m0, s26
	s_nop 0
	buffer_load_dwordx4 v3, s[0:3], s18 offen lds
	s_or_b32 s8, s18, 0x8000
	s_mov_b32 m0, s27
	s_nop 0
	buffer_load_dwordx4 v3, s[0:3], s8 offen lds
	s_add_i32 s8, s18, 0x10000
	s_mov_b32 m0, s25
	s_nop 0
	buffer_load_dwordx4 v3, s[0:3], s8 offen lds
	s_add_i32 s8, s18, 0x18000
	s_mov_b32 m0, s19
	s_nop 0
	buffer_load_dwordx4 v3, s[0:3], s8 offen lds
	s_mov_b64 s[0:1], 0
.LBB0_1202:
	s_andn2_b64 vcc, exec, s[0:1]
	s_cbranch_vccnz .LBB0_1204
	v_readlane_b32 s60, v254, 6
	s_mov_b32 s8, s60
	s_mov_b32 s11, s7
	s_mov_b32 m0, s26
	s_nop 4
	buffer_load_dwordx4 v2, s[8:11], s18 offen lds
	s_add_i32 s0, s18, 0x10000
	s_mov_b32 m0, s27
	s_nop 0
	buffer_load_dwordx4 v2, s[8:11], s0 offen lds
	s_add_i32 s0, s18, 0x20000
	s_mov_b32 m0, s25
	s_nop 0
	buffer_load_dwordx4 v2, s[8:11], s0 offen lds
	s_add_i32 s0, s18, 0x30000
	s_mov_b32 m0, s19
	s_nop 0
	buffer_load_dwordx4 v2, s[8:11], s0 offen lds
	v_readlane_b32 s61, v254, 7
	v_readlane_b32 s62, v254, 8
	v_readlane_b32 s63, v254, 9
	v_readlane_b32 s64, v254, 10
	v_readlane_b32 s65, v254, 11
	v_readlane_b32 s66, v254, 12
	v_readlane_b32 s67, v254, 13

; template <int NS, bool STREAM_ONLY = false>
; DI void convert_experts_dma(const Params& p, LDS_AS unsigned char* lds, int bid, int nb) {
;     ...
;   for (int i = 0; i < nvalid; ++i) {
;     if (NS == 4) asm volatile("s_waitcnt vmcnt(8)" ::: "memory");
;     else asm volatile("s_waitcnt vmcnt(12)" ::: "memory");
;     __builtin_amdgcn_s_barrier();
;     __builtin_amdgcn_sched_barrier(0);
;     const int sp = si == 0 ? NS - 1 : si - 1;
;     CVD_ISSUE(i + NS - 1, sp);
.LBB0_1207:
	s_waitcnt vmcnt(8)
	s_barrier
	s_add_i32 s8, s24, 3
	s_lshr_b32 s0, s8, 2
	s_mul_i32 s0, s0, s96
	s_add_i32 s0, s0, s97
	s_lshl_b32 s0, s0, 2
	s_and_b32 s1, s8, 3
	s_or_b32 s3, s0, s1
	s_cmpk_gt_i32 s3, 0x3fff
	s_cselect_b64 s[0:1], -1, 0
	s_cmpk_lt_i32 s3, 0x4000
	s_cselect_b64 s[16:17], -1, 0
	s_lshl_b32 s25, s23, 15
	s_add_i32 s11, s25, 0xffff8000
	s_cmp_lg_u32 s23, 0
	s_cselect_b32 s11, s11, 0x18000
	s_add_i32 s14, s11, s21
	s_cmp_lt_i32 s8, s20
	s_mov_b64 s[18:19], -1
	s_cbranch_scc1 .LBB0_1209
	v_cndmask_b32_e64 v6, v3, v2, s[0:1]
	s_mov_b32 m0, s14
	s_nop 0
	buffer_load_dwordx4 v6, s[4:7], s15 offen lds
	s_add_i32 s8, s14, 0x400
	s_mov_b32 m0, s8
	s_nop 0
	buffer_load_dwordx4 v6, s[4:7], s15 offen lds
	s_add_i32 s8, s14, 0x800
	s_mov_b32 m0, s8
	s_nop 0
	buffer_load_dwordx4 v6, s[4:7], s15 offen lds
	s_add_i32 s8, s14, 0xc00
	s_mov_b32 m0, s8
	s_nop 0
	buffer_load_dwordx4 v6, s[4:7], s15 offen lds
	s_mov_b64 s[18:19], 0
.LBB0_1209:
	s_andn2_b64 vcc, exec, s[18:19]
	s_cbranch_vccnz .LBB0_1214
	s_add_i32 s11, s3, 0xffffc000
	s_lshr_b32 s8, s3, 9
	s_lshr_b32 s11, s11, 10
	s_and_b64 s[18:19], s[0:1], exec
	s_cselect_b32 s8, s11, s8
	s_and_b32 s11, s3, 0x1ff
	s_bitset1_b32 s11, 10
	s_and_b32 s26, s3, 0x3ff
	s_and_b64 s[18:19], s[0:1], exec
	s_cselect_b32 s11, s26, s11
	s_add_i32 s18, s11, 0xfffffc00
	s_bfe_u32 s3, s3, 0x40006
	s_lshr_b32 s26, s18, 5
	s_and_b64 s[18:19], s[0:1], exec
	s_cselect_b32 s3, s3, s26
	s_cselect_b32 s18, 63, 31
	s_lshl_b32 s8, s8, 11
	s_lshl_b32 s3, s3, 7
	s_add_i32 s8, s8, s22
	s_and_b32 s11, s11, s18
	s_add_i32 s8, s8, s3
	s_and_b64 s[0:1], s[0:1], exec
	s_cselect_b32 s0, 14, 13
	s_lshl_b32 s0, s8, s0
	s_lshl_b32 s1, s11, 8
	s_or_b32 s18, s0, s1
	s_add_i32 s27, s14, 0x400
	s_add_i32 s26, s14, 0x800
	s_add_i32 s19, s14, 0xc00
	s_andn2_b64 vcc, exec, s[16:17]
	s_mov_b64 s[0:1], -1
	s_cbranch_vccnz .LBB0_1212
	s_mov_b32 s0, s4
	s_mov_b32 s1, s5
	s_mov_b32 s3, s7
	s_mov_b32 m0, s14
	s_nop 0
	buffer_load_dwordx4 v3, s[0:3], s18 offen lds
	s_or_b32 s8, s18, 0x8000
	s_mov_b32 m0, s27
	s_nop 0
	buffer_load_dwordx4 v3, s[0:3], s8 offen lds
	s_add_i32 s8, s18, 0x10000
	s_mov_b32 m0, s26
	s_nop 0
	buffer_load_dwordx4 v3, s[0:3], s8 offen lds
	s_add_i32 s8, s18, 0x18000
	s_mov_b32 m0, s19
	s_nop 0
	buffer_load_dwordx4 v3, s[0:3], s8 offen lds
	s_mov_b64 s[0:1], 0
.LBB0_1212:
	s_andn2_b64 vcc, exec, s[0:1]
	s_cbranch_vccnz .LBB0_1214
	v_readlane_b32 s60, v254, 6
	s_mov_b32 s8, s60
	s_mov_b32 s11, s7
	s_mov_b32 m0, s14
	s_nop 4
	buffer_load_dwordx4 v2, s[8:11], s18 offen lds
	s_add_i32 s0, s18, 0x10000
	s_mov_b32 m0, s27
	s_nop 0
	buffer_load_dwordx4 v2, s[8:11], s0 offen lds
	s_add_i32 s0, s18, 0x20000
	s_mov_b32 m0, s26
	s_nop 0
	buffer_load_dwordx4 v2, s[8:11], s0 offen lds
	s_add_i32 s0, s18, 0x30000
	s_mov_b32 m0, s19
	s_nop 0
	buffer_load_dwordx4 v2, s[8:11], s0 offen lds
	v_readlane_b32 s61, v254, 7
	v_readlane_b32 s62, v254, 8
	v_readlane_b32 s63, v254, 9
	v_readlane_b32 s64, v254, 10
	v_readlane_b32 s65, v254, 11
	v_readlane_b32 s66, v254, 12
	v_readlane_b32 s67, v254, 13

; #define OPAQUE_TID(P) (((P).wid0 << 6) | lane_id_now())
; #define G_WAIT_V(n) asm volatile("s_waitcnt vmcnt(" #n ")" ::: "memory")
; #define G_BAR() __builtin_amdgcn_s_barrier()
; #define D_STAGE_A(slot, half, kt) D_STAGE(rsA, voffA, slot, half, kt)
; #define D_STAGE_B(slot, half, kt) D_STAGE(rsB, voffB, slot, half, kt)
; #define D_STAGE_A(slot, half, kt) D_STAGE(rsA, voffA, slot, half, kt)
;   DI unsigned bt_rowoff(int h, int R) const { return (unsigned)(pn * 256 + 128 * h + (pn < 15 ? tcol_adj(R) : tcol_p64(R))) * 4096u; }
;   DI unsigned a_bytes() const { return (unsigned)NTOK * 4096u; }
; template <class Cfg>
; DI void gemm256dma_unit(LDS_AS unsigned char* lds, const Cfg& cfg) {
;   const int tid = OPAQUE_TID(cfg.p), wid = __builtin_amdgcn_readfirstlane(tid >> 6), lane = tid & 63, wr = wid >> 2, wc = wid & 3, fr = lane & 15, fq = lane >> 4;
;   const int nt = cfg.nkt();
;   unsigned voffA[2][2], voffB[2][2];
; #pragma unroll
;   for (int i = 0; i < 2; ++i) {
;     int R, C; stage_rc(tid * 16 + i * 8192, R, C);
;     voffA[0][i] = cfg.a_rowoff(R) + (unsigned)C * 2u;
;     voffA[1][i] = cfg.a_rowoff(128 + R) + (unsigned)C * 2u;
;     voffB[0][i] = cfg.bt_rowoff(0, R) + (unsigned)C * 2u;
;     voffB[1][i] = cfg.bt_rowoff(1, R) + (unsigned)C * 2u;
;   }
;   const __amdgpu_buffer_rsrc_t rsA = __builtin_amdgcn_make_buffer_rsrc((void*)cfg.a_base(), 0, cfg.a_bytes(), 0x00020000);
;   const __amdgpu_buffer_rsrc_t rsB = __builtin_amdgcn_make_buffer_rsrc((void*)cfg.bt_base(), 0, cfg.bt_bytes(), 0x00020000);
;   const unsigned ldsw = (unsigned)__builtin_amdgcn_readfirstlane((int)(unsigned)(size_t)lds) + (unsigned)wid * 1024u;
;     ...
;   const int aoff = lds_byte(wr * 64 + fr, fq * 8), boff = lds_byte(wc * 32 + fr, fq * 8);
;     ...
;   f32x4 acc[2][2][4][2];
; #pragma unroll
;   for (int a = 0; a < 2; ++a)
; #pragma unroll
;     for (int b = 0; b < 2; ++b)
; #pragma unroll
;       for (int m = 0; m < 4; ++m)
; #pragma unroll
;         for (int n = 0; n < 2; ++n) acc[a][b][m][n] = (f32x4){0.f, 0.f, 0.f, 0.f};
;   bf16x8 At[4][2], B0[2][2], B1[2][2];
;   D_STAGE_B(G_SB(0, 0), 0, 0); D_STAGE_A(G_SA(0, 0), 0, 0); D_STAGE_B(G_SB(0, 1), 1, 0); D_STAGE_A(G_SA(0, 1), 1, 0);
;   if (wr == 1) G_BAR();
;   G_WAIT_V(4); G_BAR();
;   D_STAGE_B(G_SB(1, 0), 0, 1); D_STAGE_A(G_SA(1, 0), 0, 1); D_STAGE_B(G_SB(1, 1), 1, 1);
;   G_WAIT_V(6); G_BAR();
.LBB0_1263:
	v_mbcnt_lo_u32_b32 v0, -1, 0
	v_mbcnt_hi_u32_b32 v0, -1, v0
	s_ashr_i32 s10, s9, 3
	v_or_b32_e32 v1, s87, v0
	v_ashrrev_i32_e32 v3, 31, v1
	v_lshrrev_b32_e32 v3, 26, v3
	v_readfirstlane_b32 s12, v1
	v_lshlrev_b32_e32 v2, 4, v1
	v_add_u32_e32 v3, v1, v3
	v_bfe_i32 v1, v1, 27, 1
	v_lshrrev_b32_e32 v1, 22, v1
	v_add_u32_e32 v1, v2, v1
	v_and_b32_e32 v1, 0xfffffc00, v1
	v_sub_u32_e32 v1, v2, v1
	v_lshrrev_b32_e32 v4, 4, v1
	v_bitop3_b32 v1, v4, v1, 32 bitop3:0x6c
	v_ashrrev_i32_e32 v5, 31, v1
	v_lshrrev_b32_e32 v5, 26, v5
	v_add_u32_e32 v5, v1, v5
	v_ashrrev_i32_e32 v6, 6, v5
	v_and_b32_e32 v5, 0xc0, v5
	v_ashrrev_i32_e32 v3, 6, v3
	v_sub_u32_e32 v1, v1, v5
	v_lshlrev_b32_e32 v4, 3, v3
	v_lshlrev_b32_e32 v3, 5, v3
	v_ashrrev_i16_sdwa v1, v132, sext(v1) dst_sel:DWORD dst_unused:UNUSED_PAD src0_sel:DWORD src1_sel:BYTE_0
	v_and_b32_e32 v4, -16, v4
	v_and_b32_e32 v3, 32, v3
	v_bfe_i32 v1, v1, 0, 16
	s_lshl_b32 s13, s10, 20
	v_add_u32_e32 v4, v6, v4
	v_add_lshl_u32 v1, v3, v1, 1
	s_or_b32 s14, s13, 0x80000
	v_lshl_add_u32 v3, v4, 12, v1
	v_lshlrev_b32_e32 v5, 1, v4
	s_lshl_b32 s11, s9, 8
	s_waitcnt vmcnt(8)
	v_add_u32_e32 v128, s13, v3
	v_add_u32_e32 v129, s14, v3
	v_lshrrev_b32_e32 v3, 2, v4
	v_and_b32_e32 v5, 24, v5
	s_and_b32 s11, s11, 0x700
	v_and_b32_e32 v3, 4, v3
	v_and_or_b32 v4, v4, s5, v5
	v_or3_b32 v3, v4, v3, s11
	v_lshl_add_u32 v130, v3, 12, v1
	v_add_u32_e32 v1, 0x2000, v2
	v_ashrrev_i32_e32 v2, 31, v1
	v_lshrrev_b32_e32 v2, 22, v2
	v_add_u32_e32 v2, v1, v2
	v_ashrrev_i32_e32 v2, 10, v2
	v_mul_i32_i24_e32 v3, 0x400, v2
	v_sub_u32_e32 v1, v1, v3
	v_lshrrev_b32_e32 v3, 4, v1
	v_bitop3_b32 v1, v3, v1, 32 bitop3:0x6c
	v_ashrrev_i32_e32 v4, 31, v1
	v_lshrrev_b32_e32 v4, 26, v4
	v_add_u32_e32 v4, v1, v4
	v_ashrrev_i32_e32 v5, 6, v4
	v_and_b32_e32 v4, 0xc0, v4
	v_sub_u32_e32 v1, v1, v4
	v_lshlrev_b32_e32 v3, 3, v2
	v_lshlrev_b32_e32 v2, 5, v2
	v_ashrrev_i16_sdwa v1, v132, sext(v1) dst_sel:DWORD dst_unused:UNUSED_PAD src0_sel:DWORD src1_sel:BYTE_0
	v_and_b32_e32 v3, -16, v3
	v_and_b32_e32 v2, 32, v2
	v_bfe_i32 v1, v1, 0, 16
	v_add_u32_e32 v3, v5, v3
	v_add_lshl_u32 v1, v2, v1, 1
	v_lshl_add_u32 v2, v3, 12, v1
	v_lshlrev_b32_e32 v4, 1, v3
	s_ashr_i32 s23, s12, 6
	v_add_u32_e32 v133, s13, v2
	v_add_u32_e32 v134, s14, v2
	v_lshrrev_b32_e32 v2, 2, v3
	v_and_b32_e32 v4, 24, v4
	s_lshl_b32 s13, s23, 10
	v_and_b32_e32 v2, 4, v2
	v_and_or_b32 v3, v3, s5, v4
	s_add_i32 s30, s13, 0
	v_or3_b32 v2, v3, v2, s11
	s_add_i32 s13, s30, 0x10010
	s_mov_b32 m0, s13
	s_nop 0
	buffer_load_dwordx4 v130, s[44:47], s6 offen lds
	v_lshl_add_u32 v135, v2, 12, v1
	s_add_i32 s14, s30, 0x12010
	s_mov_b32 m0, s14
	s_nop 0
	buffer_load_dwordx4 v135, s[44:47], s6 offen lds
	s_add_i32 s15, s30, 16
	s_mov_b32 m0, s15
	s_nop 0
	buffer_load_dwordx4 v128, s[0:3], s6 offen lds
	s_add_i32 s16, s30, 0x2010
	s_mov_b32 m0, s16
	s_nop 0
	buffer_load_dwordx4 v133, s[0:3], s6 offen lds
	v_add_u32_e32 v131, 0x80000, v130
	s_add_i32 s17, s30, 0x14010
	s_mov_b32 m0, s17
	s_nop 0
	buffer_load_dwordx4 v131, s[44:47], s6 offen lds
	v_add_u32_e32 v136, 0x80000, v135
	s_add_i32 s19, s30, 0x16010
	s_mov_b32 m0, s19
	s_nop 0
	buffer_load_dwordx4 v136, s[44:47], s6 offen lds
	s_add_i32 s20, s30, 0x4010
	s_mov_b32 m0, s20
	s_nop 0
	buffer_load_dwordx4 v129, s[0:3], s6 offen lds
	s_add_i32 s22, s30, 0x6010
	s_mov_b32 m0, s22
	s_nop 0
	buffer_load_dwordx4 v134, s[0:3], s6 offen lds
	s_ashr_i32 s18, s12, 8
	s_cmp_lg_u32 s18, 1
	s_cbranch_scc1 .LBB0_1265
	s_barrier
.LBB0_1265:
	s_lshl_b32 s23, s23, 5
	s_lshl_b32 s21, s18, 6
	v_and_b32_e32 v1, 48, v0
	v_lshlrev_b32_e32 v2, 6, v0
	v_lshlrev_b32_e32 v0, 2, v0
	s_lshl_b32 s24, s18, 13
	s_and_b32 s18, s23, 0x60
	v_and_or_b32 v1, v2, s7, v1
	v_and_b32_e32 v0, 32, v0
	s_lshl_b32 s23, s18, 7
	v_bitop3_b32 v2, v1, s24, v0 bitop3:0xde
	v_bitop3_b32 v1, s23, v1, v0 bitop3:0xf6
	s_waitcnt vmcnt(4)
	s_barrier
	s_add_i32 s23, s30, 0x18010
	s_mov_b32 m0, s23
	s_nop 0
	buffer_load_dwordx4 v130, s[44:47], s8 offen lds
	s_add_i32 s24, s30, 0x1a010
	s_mov_b32 m0, s24
	s_nop 0
	buffer_load_dwordx4 v135, s[44:47], s8 offen lds
	s_add_i32 s25, s30, 0x8010
	s_mov_b32 m0, s25
	s_nop 0
	buffer_load_dwordx4 v128, s[0:3], s8 offen lds
	s_add_i32 s26, s30, 0xa010
	s_mov_b32 m0, s26
	s_nop 0
	buffer_load_dwordx4 v133, s[0:3], s8 offen lds
	s_add_i32 s27, s30, 0x1c010
	s_mov_b32 m0, s27
	s_nop 0
	buffer_load_dwordx4 v131, s[44:47], s8 offen lds
	s_add_i32 s28, s30, 0x1e010
	s_mov_b32 m0, s28
	s_nop 0
	buffer_load_dwordx4 v136, s[44:47], s8 offen lds
	s_waitcnt vmcnt(6)
; #define G_WAIT_V(n) asm volatile("s_waitcnt vmcnt(" #n ")" ::: "memory")
; #define G_BAR() __builtin_amdgcn_s_barrier()
; #define G_SCHED() __builtin_amdgcn_sched_barrier(0)
; #define D_STAGE_A(slot, half, kt) D_STAGE(rsA, voffA, slot, half, kt)
; #define D_STAGE_B(slot, half, kt) D_STAGE(rsB, voffB, slot, half, kt)
; #define D_LDA(dst, slot) do { _Pragma("unroll") for (int m = 0; m < 4; ++m) _Pragma("unroll") for (int k = 0; k < 2; ++k) \
;     dst[m][k] = *(const LDS_AS bf16x8*)(lds + (slot) + aoff + m * 2048 + k * 1024); } while (0)
; #define D_LDB(dst, slot) do { _Pragma("unroll") for (int n = 0; n < 2; ++n) _Pragma("unroll") for (int k = 0; k < 2; ++k) \
;     dst[n][k] = *(const LDS_AS bf16x8*)(lds + (slot) + boff + n * 2048 + k * 1024); } while (0)
; #define D_MMA(ai, bj, At, Bf) do { __builtin_amdgcn_s_setprio(1); _Pragma("unroll") for (int m = 0; m < 4; ++m) _Pragma("unroll") for (int n = 0; n < 2; ++n) _Pragma("unroll") for (int k = 0; k < 2; ++k) \
;     acc[ai][bj][m][n] = __builtin_amdgcn_mfma_f32_16x16x32_bf16(Bf[n][k], At[m][k], acc[ai][bj][m][n], 0, 0, 0); __builtin_amdgcn_s_setprio(0); } while (0)
; #define D_WAIT_L(n) asm volatile("s_waitcnt lgkmcnt(" #n ")" ::: "memory")
; #define D_STAGE_A(slot, half, kt) D_STAGE(rsA, voffA, slot, half, kt)
; template <class Cfg>
; DI void gemm256dma_unit(LDS_AS unsigned char* lds, const Cfg& cfg) {
;     ...
;   f32x4 acc[2][2][4][2];
; #pragma unroll
;   for (int a = 0; a < 2; ++a)
; #pragma unroll
;     for (int b = 0; b < 2; ++b)
; #pragma unroll
;       for (int m = 0; m < 4; ++m)
; #pragma unroll
;         for (int n = 0; n < 2; ++n) acc[a][b][m][n] = (f32x4){0.f, 0.f, 0.f, 0.f};
;   bf16x8 At[4][2], B0[2][2], B1[2][2];
;   D_STAGE_B(G_SB(0, 0), 0, 0); D_STAGE_A(G_SA(0, 0), 0, 0); D_STAGE_B(G_SB(0, 1), 1, 0); D_STAGE_A(G_SA(0, 1), 1, 0);
;   if (wr == 1) G_BAR();
;   G_WAIT_V(4); G_BAR();
;   D_STAGE_B(G_SB(1, 0), 0, 1); D_STAGE_A(G_SA(1, 0), 0, 1); D_STAGE_B(G_SB(1, 1), 1, 1);
;   G_WAIT_V(6); G_BAR();
; #pragma clang loop unroll(disable)
;   for (int t = 0; t < nt; t += 2) {
;     const int t1 = t + 1;
;     const int t2 = (t + 2 < nt) ? t + 2 : 0;
;     const int t3 = (t + 2 < nt) ? t + 3 : 1;
;     D_LDB(B0, G_SB(0, 0)); G_SCHED(); D_LDA(At, G_SA(0, 0)); D_STAGE_A(G_SA(1, 1), 1, t1);
;     D_WAIT_L(8); G_BAR(); D_WAIT_L(0); G_SCHED(); D_MMA(0, 0, At, B0); G_BAR(); G_SCHED();
	v_mov_b32_e32 v0, 0
	v_add_u32_e32 v1, 0, v1
	s_add_i32 s29, s30, 0xc010
	s_add_i32 s30, s30, 0xe010
	s_mov_b32 s33, 0
	s_movk_i32 s31, 0x180
	v_add_u32_e32 v137, 0x10010, v1
	v_add_u32_e32 v138, 0, v2
	v_add_u32_e32 v139, 0x14010, v1
	v_add_u32_e32 v140, 0x18010, v1
	v_add_u32_e32 v141, 0x1c010, v1
	v_mov_b32_e32 v1, v0
	v_mov_b32_e32 v2, v0
	v_mov_b32_e32 v3, v0
	v_mov_b32_e32 v4, v0
	v_mov_b32_e32 v5, v0
	v_mov_b32_e32 v6, v0
	v_mov_b32_e32 v7, v0
	v_mov_b32_e32 v16, v0
	v_mov_b32_e32 v17, v0
	v_mov_b32_e32 v18, v0
	v_mov_b32_e32 v19, v0
	v_mov_b32_e32 v20, v0
	v_mov_b32_e32 v21, v0
	v_mov_b32_e32 v22, v0
	v_mov_b32_e32 v23, v0
	v_mov_b32_e32 v32, v0
	v_mov_b32_e32 v33, v0
	v_mov_b32_e32 v34, v0
	v_mov_b32_e32 v35, v0
	v_mov_b32_e32 v36, v0
	v_mov_b32_e32 v37, v0
	v_mov_b32_e32 v38, v0
	v_mov_b32_e32 v39, v0
	v_mov_b32_e32 v48, v0
	v_mov_b32_e32 v49, v0
	v_mov_b32_e32 v50, v0
	v_mov_b32_e32 v51, v0
	v_mov_b32_e32 v52, v0
	v_mov_b32_e32 v53, v0
	v_mov_b32_e32 v54, v0
	v_mov_b32_e32 v55, v0
	v_mov_b32_e32 v8, v0
	v_mov_b32_e32 v9, v0
	v_mov_b32_e32 v10, v0
	v_mov_b32_e32 v11, v0
	v_mov_b32_e32 v12, v0
	v_mov_b32_e32 v13, v0
	v_mov_b32_e32 v14, v0
	v_mov_b32_e32 v15, v0
	v_mov_b32_e32 v24, v0
	v_mov_b32_e32 v25, v0
	v_mov_b32_e32 v26, v0
	v_mov_b32_e32 v27, v0
	v_mov_b32_e32 v28, v0
	v_mov_b32_e32 v29, v0
	v_mov_b32_e32 v30, v0
	v_mov_b32_e32 v31, v0
	v_mov_b32_e32 v40, v0
	v_mov_b32_e32 v41, v0
	v_mov_b32_e32 v42, v0
	v_mov_b32_e32 v43, v0
	v_mov_b32_e32 v44, v0
	v_mov_b32_e32 v45, v0
	v_mov_b32_e32 v46, v0
	v_mov_b32_e32 v47, v0
	v_mov_b32_e32 v56, v0
	v_mov_b32_e32 v57, v0
	v_mov_b32_e32 v58, v0
	v_mov_b32_e32 v59, v0
	v_mov_b32_e32 v60, v0
	v_mov_b32_e32 v61, v0
	v_mov_b32_e32 v62, v0
	v_mov_b32_e32 v63, v0
	v_mov_b32_e32 v64, v0
	v_mov_b32_e32 v65, v0
	v_mov_b32_e32 v66, v0
	v_mov_b32_e32 v67, v0
	v_mov_b32_e32 v68, v0
	v_mov_b32_e32 v69, v0
	v_mov_b32_e32 v70, v0
	v_mov_b32_e32 v71, v0
	v_mov_b32_e32 v80, v0
	v_mov_b32_e32 v81, v0
	v_mov_b32_e32 v82, v0
	v_mov_b32_e32 v83, v0
	v_mov_b32_e32 v84, v0
	v_mov_b32_e32 v85, v0
	v_mov_b32_e32 v86, v0
	v_mov_b32_e32 v87, v0
	v_mov_b32_e32 v96, v0
	v_mov_b32_e32 v97, v0
	v_mov_b32_e32 v98, v0
	v_mov_b32_e32 v99, v0
	v_mov_b32_e32 v100, v0
	v_mov_b32_e32 v101, v0
	v_mov_b32_e32 v102, v0
	v_mov_b32_e32 v103, v0
	v_mov_b32_e32 v112, v0
	v_mov_b32_e32 v113, v0
	v_mov_b32_e32 v114, v0
	v_mov_b32_e32 v115, v0
	v_mov_b32_e32 v116, v0
	v_mov_b32_e32 v117, v0
	v_mov_b32_e32 v118, v0
	v_mov_b32_e32 v119, v0
	v_mov_b32_e32 v72, v0
	v_mov_b32_e32 v73, v0
	v_mov_b32_e32 v74, v0
	v_mov_b32_e32 v75, v0
	v_mov_b32_e32 v76, v0
	v_mov_b32_e32 v77, v0
	v_mov_b32_e32 v78, v0
	v_mov_b32_e32 v79, v0
	v_mov_b32_e32 v88, v0
	v_mov_b32_e32 v89, v0
	v_mov_b32_e32 v90, v0
	v_mov_b32_e32 v91, v0
	v_mov_b32_e32 v92, v0
	v_mov_b32_e32 v93, v0
	v_mov_b32_e32 v94, v0
	v_mov_b32_e32 v95, v0
	v_mov_b32_e32 v104, v0
	v_mov_b32_e32 v105, v0
	v_mov_b32_e32 v106, v0
	v_mov_b32_e32 v107, v0
	v_mov_b32_e32 v108, v0
	v_mov_b32_e32 v109, v0
	v_mov_b32_e32 v110, v0
	v_mov_b32_e32 v111, v0
	v_mov_b32_e32 v120, v0
	v_mov_b32_e32 v121, v0
	v_mov_b32_e32 v122, v0
	v_mov_b32_e32 v123, v0
	v_mov_b32_e32 v124, v0
	v_mov_b32_e32 v125, v0
	v_mov_b32_e32 v126, v0
	v_mov_b32_e32 v127, v0
	s_barrier
.LBB0_1266:
	ds_read_b128 v[142:145], v137
	ds_read_b128 v[146:149], v137 offset:1024
	ds_read_b128 v[150:153], v137 offset:2048
	ds_read_b128 v[154:157], v137 offset:3072
	s_add_i32 s34, s33, 2
	s_add_i32 s36, s31, 0xffffff00
	s_add_i32 s35, s31, 0xffffff80
	s_cmp_lt_u32 s33, 30
	s_cselect_b32 s37, s35, 0
	s_cselect_b32 s35, s31, 0x80
	s_addk_i32 s31, 0x100
	s_cmp_gt_u32 s33, 29
	ds_read_b128 v[158:161], v138 offset:16
	ds_read_b128 v[162:165], v138 offset:1040
	ds_read_b128 v[166:169], v138 offset:2064
	ds_read_b128 v[170:173], v138 offset:3088
	ds_read_b128 v[174:177], v138 offset:4112
	ds_read_b128 v[178:181], v138 offset:5136
	ds_read_b128 v[182:185], v138 offset:6160
	ds_read_b128 v[186:189], v138 offset:7184
	s_mov_b32 m0, s29
	s_nop 0
	buffer_load_dwordx4 v129, s[0:3], s36 offen lds
	s_nop 0
	s_mov_b32 m0, s30
	s_nop 0
	buffer_load_dwordx4 v134, s[0:3], s36 offen lds
	s_waitcnt lgkmcnt(8)
	s_barrier
	s_waitcnt lgkmcnt(0)
	s_setprio 1
	s_waitcnt lgkmcnt(7)
	v_mfma_f32_16x16x32_bf16 v[124:127], v[142:145], v[158:161], v[124:127]
	v_mfma_f32_16x16x32_bf16 v[120:123], v[150:153], v[158:161], v[120:123]
	s_waitcnt lgkmcnt(5)
	v_mfma_f32_16x16x32_bf16 v[108:111], v[142:145], v[166:169], v[108:111]
	v_mfma_f32_16x16x32_bf16 v[104:107], v[150:153], v[166:169], v[104:107]
	s_waitcnt lgkmcnt(3)
	v_mfma_f32_16x16x32_bf16 v[92:95], v[142:145], v[174:177], v[92:95]
	v_mfma_f32_16x16x32_bf16 v[88:91], v[150:153], v[174:177], v[88:91]
	s_waitcnt lgkmcnt(1)
	v_mfma_f32_16x16x32_bf16 v[76:79], v[142:145], v[182:185], v[76:79]
	v_mfma_f32_16x16x32_bf16 v[72:75], v[150:153], v[182:185], v[72:75]
	v_mfma_f32_16x16x32_bf16 v[124:127], v[146:149], v[162:165], v[124:127]
	v_mfma_f32_16x16x32_bf16 v[120:123], v[154:157], v[162:165], v[120:123]
	v_mfma_f32_16x16x32_bf16 v[108:111], v[146:149], v[170:173], v[108:111]
	v_mfma_f32_16x16x32_bf16 v[104:107], v[154:157], v[170:173], v[104:107]
	v_mfma_f32_16x16x32_bf16 v[92:95], v[146:149], v[178:181], v[92:95]
	v_mfma_f32_16x16x32_bf16 v[88:91], v[154:157], v[178:181], v[88:91]
	s_waitcnt lgkmcnt(0)
	v_mfma_f32_16x16x32_bf16 v[76:79], v[146:149], v[186:189], v[76:79]
	v_mfma_f32_16x16x32_bf16 v[72:75], v[154:157], v[186:189], v[72:75]
	s_setprio 0
	s_barrier
; #define G_WAIT_V(n) asm volatile("s_waitcnt vmcnt(" #n ")" ::: "memory")
; #define G_BAR() __builtin_amdgcn_s_barrier()
; #define G_SCHED() __builtin_amdgcn_sched_barrier(0)
; #define D_STAGE_A(slot, half, kt) D_STAGE(rsA, voffA, slot, half, kt)
; #define D_STAGE_B(slot, half, kt) D_STAGE(rsB, voffB, slot, half, kt)
; #define D_LDA(dst, slot) do { _Pragma("unroll") for (int m = 0; m < 4; ++m) _Pragma("unroll") for (int k = 0; k < 2; ++k) \
;     dst[m][k] = *(const LDS_AS bf16x8*)(lds + (slot) + aoff + m * 2048 + k * 1024); } while (0)
; #define D_LDB(dst, slot) do { _Pragma("unroll") for (int n = 0; n < 2; ++n) _Pragma("unroll") for (int k = 0; k < 2; ++k) \
;     dst[n][k] = *(const LDS_AS bf16x8*)(lds + (slot) + boff + n * 2048 + k * 1024); } while (0)
; #define D_MMA(ai, bj, At, Bf) do { __builtin_amdgcn_s_setprio(1); _Pragma("unroll") for (int m = 0; m < 4; ++m) _Pragma("unroll") for (int n = 0; n < 2; ++n) _Pragma("unroll") for (int k = 0; k < 2; ++k) \
;     acc[ai][bj][m][n] = __builtin_amdgcn_mfma_f32_16x16x32_bf16(Bf[n][k], At[m][k], acc[ai][bj][m][n], 0, 0, 0); __builtin_amdgcn_s_setprio(0); } while (0)
; #define D_WAIT_L(n) asm volatile("s_waitcnt lgkmcnt(" #n ")" ::: "memory")
; #define D_STAGE_A(slot, half, kt) D_STAGE(rsA, voffA, slot, half, kt)
; #define D_STAGE_B(slot, half, kt) do { _Pragma("unroll") for (int _i = 0; _i < 2; ++_i) { const unsigned _m0 = ldsw + (unsigned)((slot) + _i * 8192); const unsigned _so = (unsigned)(kt) * 128u + (half) * bt_half + _i * bt_piece; \
;     asm volatile("s_mov_b32 m0, %0\n\ts_nop 4\n\tbuffer_load_dwordx4 %1, %2, %3 offen lds" :: "s"(_m0), "v"(voffB0), "s"(rsB), "s"(_so) : "m0", "memory"); } } while (0)
; template <class Cfg>
; DI void gemm256dma_unit(LDS_AS unsigned char* lds, const Cfg& cfg) {
;     ...
;     D_LDB(B1, G_SB(0, 1)); D_STAGE_B(G_SB(0, 0), 0, t2);
;     G_BAR(); D_WAIT_L(0); G_SCHED(); D_MMA(0, 1, At, B1); G_BAR(); G_SCHED();
;     D_LDA(At, G_SA(0, 1)); D_STAGE_A(G_SA(0, 0), 0, t2);
;     G_BAR(); D_WAIT_L(0); G_SCHED(); D_MMA(1, 0, At, B0); G_BAR(); G_SCHED();
;     D_STAGE_B(G_SB(0, 1), 1, t2);
;     G_WAIT_V(6); G_BAR(); G_SCHED(); D_MMA(1, 1, At, B1); G_BAR(); G_SCHED();
;     D_LDB(B0, G_SB(1, 0)); G_SCHED(); D_LDA(At, G_SA(1, 0)); D_STAGE_A(G_SA(0, 1), 1, t2);
;     D_WAIT_L(8); G_BAR(); D_WAIT_L(0); G_SCHED(); D_MMA(0, 0, At, B0); G_BAR(); G_SCHED();
	ds_read_b128 v[192:195], v139
	ds_read_b128 v[196:199], v139 offset:1024
	ds_read_b128 v[200:203], v139 offset:2048
	ds_read_b128 v[204:207], v139 offset:3072
	s_mov_b32 m0, s13
	s_nop 0
	buffer_load_dwordx4 v130, s[44:47], s37 offen lds
	s_nop 0
	s_mov_b32 m0, s14
	s_nop 0
	buffer_load_dwordx4 v135, s[44:47], s37 offen lds
	s_barrier
	s_waitcnt lgkmcnt(0)
	s_setprio 1
	s_waitcnt lgkmcnt(3)
	v_mfma_f32_16x16x32_bf16 v[116:119], v[192:195], v[158:161], v[116:119]
	s_waitcnt lgkmcnt(1)
	v_mfma_f32_16x16x32_bf16 v[112:115], v[200:203], v[158:161], v[112:115]
	v_mfma_f32_16x16x32_bf16 v[100:103], v[192:195], v[166:169], v[100:103]
	v_mfma_f32_16x16x32_bf16 v[96:99], v[200:203], v[166:169], v[96:99]
	v_mfma_f32_16x16x32_bf16 v[84:87], v[192:195], v[174:177], v[84:87]
	v_mfma_f32_16x16x32_bf16 v[80:83], v[200:203], v[174:177], v[80:83]
	v_mfma_f32_16x16x32_bf16 v[68:71], v[192:195], v[182:185], v[68:71]
	v_mfma_f32_16x16x32_bf16 v[64:67], v[200:203], v[182:185], v[64:67]
	v_mfma_f32_16x16x32_bf16 v[116:119], v[196:199], v[162:165], v[116:119]
	s_waitcnt lgkmcnt(0)
	v_mfma_f32_16x16x32_bf16 v[112:115], v[204:207], v[162:165], v[112:115]
	v_mfma_f32_16x16x32_bf16 v[100:103], v[196:199], v[170:173], v[100:103]
	v_mfma_f32_16x16x32_bf16 v[96:99], v[204:207], v[170:173], v[96:99]
	v_mfma_f32_16x16x32_bf16 v[84:87], v[196:199], v[178:181], v[84:87]
	v_mfma_f32_16x16x32_bf16 v[80:83], v[204:207], v[178:181], v[80:83]
	v_mfma_f32_16x16x32_bf16 v[68:71], v[196:199], v[186:189], v[68:71]
	v_mfma_f32_16x16x32_bf16 v[64:67], v[204:207], v[186:189], v[64:67]
	s_setprio 0
	s_barrier
	ds_read_b128 v[158:161], v138 offset:16400
	ds_read_b128 v[162:165], v138 offset:17424
	ds_read_b128 v[166:169], v138 offset:18448
	ds_read_b128 v[170:173], v138 offset:19472
	ds_read_b128 v[174:177], v138 offset:20496
	ds_read_b128 v[178:181], v138 offset:21520
	ds_read_b128 v[182:185], v138 offset:22544
	ds_read_b128 v[186:189], v138 offset:23568
	s_mov_b32 m0, s15
	s_nop 0
	buffer_load_dwordx4 v128, s[0:3], s37 offen lds
	s_nop 0
	s_mov_b32 m0, s16
	s_nop 0
	buffer_load_dwordx4 v133, s[0:3], s37 offen lds
	s_barrier
	s_waitcnt lgkmcnt(0)
	s_setprio 1
	s_waitcnt lgkmcnt(7)
	v_mfma_f32_16x16x32_bf16 v[60:63], v[142:145], v[158:161], v[60:63]
	v_mfma_f32_16x16x32_bf16 v[56:59], v[150:153], v[158:161], v[56:59]
	s_waitcnt lgkmcnt(5)
	v_mfma_f32_16x16x32_bf16 v[44:47], v[142:145], v[166:169], v[44:47]
	v_mfma_f32_16x16x32_bf16 v[40:43], v[150:153], v[166:169], v[40:43]
	s_waitcnt lgkmcnt(3)
	v_mfma_f32_16x16x32_bf16 v[28:31], v[142:145], v[174:177], v[28:31]
	v_mfma_f32_16x16x32_bf16 v[24:27], v[150:153], v[174:177], v[24:27]
	s_waitcnt lgkmcnt(1)
	v_mfma_f32_16x16x32_bf16 v[12:15], v[142:145], v[182:185], v[12:15]
	v_mfma_f32_16x16x32_bf16 v[8:11], v[150:153], v[182:185], v[8:11]
	v_mfma_f32_16x16x32_bf16 v[60:63], v[146:149], v[162:165], v[60:63]
	v_mfma_f32_16x16x32_bf16 v[56:59], v[154:157], v[162:165], v[56:59]
	v_mfma_f32_16x16x32_bf16 v[44:47], v[146:149], v[170:173], v[44:47]
	v_mfma_f32_16x16x32_bf16 v[40:43], v[154:157], v[170:173], v[40:43]
	v_mfma_f32_16x16x32_bf16 v[28:31], v[146:149], v[178:181], v[28:31]
	v_mfma_f32_16x16x32_bf16 v[24:27], v[154:157], v[178:181], v[24:27]
	s_waitcnt lgkmcnt(0)
	v_mfma_f32_16x16x32_bf16 v[12:15], v[146:149], v[186:189], v[12:15]
	v_mfma_f32_16x16x32_bf16 v[8:11], v[154:157], v[186:189], v[8:11]
	s_setprio 0
	s_barrier
	s_mov_b32 m0, s17
	s_nop 0
	buffer_load_dwordx4 v131, s[44:47], s37 offen lds
	s_nop 0
	s_mov_b32 m0, s19
	s_nop 0
	buffer_load_dwordx4 v136, s[44:47], s37 offen lds
	s_waitcnt vmcnt(6)
	s_barrier
	s_setprio 1
	v_mfma_f32_16x16x32_bf16 v[52:55], v[192:195], v[158:161], v[52:55]
	v_mfma_f32_16x16x32_bf16 v[48:51], v[200:203], v[158:161], v[48:51]
	v_mfma_f32_16x16x32_bf16 v[36:39], v[192:195], v[166:169], v[36:39]
	v_mfma_f32_16x16x32_bf16 v[32:35], v[200:203], v[166:169], v[32:35]
	v_mfma_f32_16x16x32_bf16 v[20:23], v[192:195], v[174:177], v[20:23]
	v_mfma_f32_16x16x32_bf16 v[16:19], v[200:203], v[174:177], v[16:19]
	v_mfma_f32_16x16x32_bf16 v[4:7], v[192:195], v[182:185], v[4:7]
	v_mfma_f32_16x16x32_bf16 v[0:3], v[200:203], v[182:185], v[0:3]
	v_mfma_f32_16x16x32_bf16 v[52:55], v[196:199], v[162:165], v[52:55]
	v_mfma_f32_16x16x32_bf16 v[48:51], v[204:207], v[162:165], v[48:51]
	v_mfma_f32_16x16x32_bf16 v[36:39], v[196:199], v[170:173], v[36:39]
	v_mfma_f32_16x16x32_bf16 v[32:35], v[204:207], v[170:173], v[32:35]
	v_mfma_f32_16x16x32_bf16 v[20:23], v[196:199], v[178:181], v[20:23]
	v_mfma_f32_16x16x32_bf16 v[16:19], v[204:207], v[178:181], v[16:19]
	v_mfma_f32_16x16x32_bf16 v[4:7], v[196:199], v[186:189], v[4:7]
	v_mfma_f32_16x16x32_bf16 v[0:3], v[204:207], v[186:189], v[0:3]
	s_setprio 0
	s_barrier
	ds_read_b128 v[142:145], v140
	ds_read_b128 v[146:149], v140 offset:1024
	ds_read_b128 v[150:153], v140 offset:2048
	ds_read_b128 v[154:157], v140 offset:3072
	ds_read_b128 v[158:161], v138 offset:32784
	ds_read_b128 v[162:165], v138 offset:33808
	ds_read_b128 v[166:169], v138 offset:34832
	ds_read_b128 v[170:173], v138 offset:35856
	ds_read_b128 v[174:177], v138 offset:36880
	ds_read_b128 v[178:181], v138 offset:37904
	ds_read_b128 v[182:185], v138 offset:38928
	ds_read_b128 v[186:189], v138 offset:39952
	s_mov_b32 m0, s20
	s_nop 0
	buffer_load_dwordx4 v129, s[0:3], s37 offen lds
	s_nop 0
	s_mov_b32 m0, s22
	s_nop 0
	buffer_load_dwordx4 v134, s[0:3], s37 offen lds
	s_waitcnt lgkmcnt(8)
	s_barrier
; #define G_WAIT_V(n) asm volatile("s_waitcnt vmcnt(" #n ")" ::: "memory")
; #define G_BAR() __builtin_amdgcn_s_barrier()
; #define G_SCHED() __builtin_amdgcn_sched_barrier(0)
; #define D_STAGE_A(slot, half, kt) D_STAGE(rsA, voffA, slot, half, kt)
; #define D_STAGE_B(slot, half, kt) D_STAGE(rsB, voffB, slot, half, kt)
; #define D_LDA(dst, slot) do { _Pragma("unroll") for (int m = 0; m < 4; ++m) _Pragma("unroll") for (int k = 0; k < 2; ++k) \
;     dst[m][k] = *(const LDS_AS bf16x8*)(lds + (slot) + aoff + m * 2048 + k * 1024); } while (0)
; #define D_LDB(dst, slot) do { _Pragma("unroll") for (int n = 0; n < 2; ++n) _Pragma("unroll") for (int k = 0; k < 2; ++k) \
;     dst[n][k] = *(const LDS_AS bf16x8*)(lds + (slot) + boff + n * 2048 + k * 1024); } while (0)
; #define D_MMA(ai, bj, At, Bf) do { __builtin_amdgcn_s_setprio(1); _Pragma("unroll") for (int m = 0; m < 4; ++m) _Pragma("unroll") for (int n = 0; n < 2; ++n) _Pragma("unroll") for (int k = 0; k < 2; ++k) \
;     acc[ai][bj][m][n] = __builtin_amdgcn_mfma_f32_16x16x32_bf16(Bf[n][k], At[m][k], acc[ai][bj][m][n], 0, 0, 0); __builtin_amdgcn_s_setprio(0); } while (0)
; #define D_WAIT_L(n) asm volatile("s_waitcnt lgkmcnt(" #n ")" ::: "memory")
; #define D_STAGE_A(slot, half, kt) D_STAGE(rsA, voffA, slot, half, kt)
; #define D_STAGE_B(slot, half, kt) do { _Pragma("unroll") for (int _i = 0; _i < 2; ++_i) { const unsigned _m0 = ldsw + (unsigned)((slot) + _i * 8192); const unsigned _so = (unsigned)(kt) * 128u + (half) * bt_half + _i * bt_piece; \
;     asm volatile("s_mov_b32 m0, %0\n\ts_nop 4\n\tbuffer_load_dwordx4 %1, %2, %3 offen lds" :: "s"(_m0), "v"(voffB0), "s"(rsB), "s"(_so) : "m0", "memory"); } } while (0)
; #define D_WAIT_L(n) asm volatile("s_waitcnt lgkmcnt(" #n ")" ::: "memory")
; template <class Cfg>
; DI void gemm256dma_unit(LDS_AS unsigned char* lds, const Cfg& cfg) {
;     ...
;     D_WAIT_L(8); G_BAR(); D_WAIT_L(0); G_SCHED(); D_MMA(0, 0, At, B0); G_BAR(); G_SCHED();
;     D_LDB(B1, G_SB(1, 1)); D_STAGE_B(G_SB(1, 0), 0, t3);
;     G_BAR(); D_WAIT_L(0); G_SCHED(); D_MMA(0, 1, At, B1); G_BAR(); G_SCHED();
;     D_LDA(At, G_SA(1, 1)); D_STAGE_A(G_SA(1, 0), 0, t3);
;     G_BAR(); D_WAIT_L(0); G_SCHED(); D_MMA(1, 0, At, B0); G_BAR(); G_SCHED();
;     D_STAGE_B(G_SB(1, 1), 1, t3);
;     G_WAIT_V(6); G_BAR(); G_SCHED(); D_MMA(1, 1, At, B1); G_BAR(); G_SCHED();
;   }
;   G_WAIT_V(0);
;   if (wr == 0) G_BAR();
	s_waitcnt lgkmcnt(0)
	s_setprio 1
	s_waitcnt lgkmcnt(7)
	v_mfma_f32_16x16x32_bf16 v[124:127], v[142:145], v[158:161], v[124:127]
	v_mfma_f32_16x16x32_bf16 v[120:123], v[150:153], v[158:161], v[120:123]
	s_waitcnt lgkmcnt(5)
	v_mfma_f32_16x16x32_bf16 v[108:111], v[142:145], v[166:169], v[108:111]
	v_mfma_f32_16x16x32_bf16 v[104:107], v[150:153], v[166:169], v[104:107]
	s_waitcnt lgkmcnt(3)
	v_mfma_f32_16x16x32_bf16 v[92:95], v[142:145], v[174:177], v[92:95]
	v_mfma_f32_16x16x32_bf16 v[88:91], v[150:153], v[174:177], v[88:91]
	s_waitcnt lgkmcnt(1)
	v_mfma_f32_16x16x32_bf16 v[76:79], v[142:145], v[182:185], v[76:79]
	v_mfma_f32_16x16x32_bf16 v[72:75], v[150:153], v[182:185], v[72:75]
	v_mfma_f32_16x16x32_bf16 v[124:127], v[146:149], v[162:165], v[124:127]
	v_mfma_f32_16x16x32_bf16 v[120:123], v[154:157], v[162:165], v[120:123]
	v_mfma_f32_16x16x32_bf16 v[108:111], v[146:149], v[170:173], v[108:111]
	v_mfma_f32_16x16x32_bf16 v[104:107], v[154:157], v[170:173], v[104:107]
	v_mfma_f32_16x16x32_bf16 v[92:95], v[146:149], v[178:181], v[92:95]
	v_mfma_f32_16x16x32_bf16 v[88:91], v[154:157], v[178:181], v[88:91]
	s_waitcnt lgkmcnt(0)
	v_mfma_f32_16x16x32_bf16 v[76:79], v[146:149], v[186:189], v[76:79]
	v_mfma_f32_16x16x32_bf16 v[72:75], v[154:157], v[186:189], v[72:75]
	s_setprio 0
	s_barrier
	ds_read_b128 v[192:195], v141
	ds_read_b128 v[196:199], v141 offset:1024
	ds_read_b128 v[200:203], v141 offset:2048
	ds_read_b128 v[204:207], v141 offset:3072
	s_mov_b32 m0, s23
	s_nop 0
	buffer_load_dwordx4 v130, s[44:47], s35 offen lds
	s_nop 0
	s_mov_b32 m0, s24
	s_nop 0
	buffer_load_dwordx4 v135, s[44:47], s35 offen lds
	s_barrier
	s_waitcnt lgkmcnt(0)
	s_setprio 1
	s_waitcnt lgkmcnt(3)
	v_mfma_f32_16x16x32_bf16 v[116:119], v[192:195], v[158:161], v[116:119]
	s_waitcnt lgkmcnt(1)
	v_mfma_f32_16x16x32_bf16 v[112:115], v[200:203], v[158:161], v[112:115]
	v_mfma_f32_16x16x32_bf16 v[100:103], v[192:195], v[166:169], v[100:103]
	v_mfma_f32_16x16x32_bf16 v[96:99], v[200:203], v[166:169], v[96:99]
	v_mfma_f32_16x16x32_bf16 v[84:87], v[192:195], v[174:177], v[84:87]
	v_mfma_f32_16x16x32_bf16 v[80:83], v[200:203], v[174:177], v[80:83]
	v_mfma_f32_16x16x32_bf16 v[68:71], v[192:195], v[182:185], v[68:71]
	v_mfma_f32_16x16x32_bf16 v[64:67], v[200:203], v[182:185], v[64:67]
	v_mfma_f32_16x16x32_bf16 v[116:119], v[196:199], v[162:165], v[116:119]
	s_waitcnt lgkmcnt(0)
	v_mfma_f32_16x16x32_bf16 v[112:115], v[204:207], v[162:165], v[112:115]
	v_mfma_f32_16x16x32_bf16 v[100:103], v[196:199], v[170:173], v[100:103]
	v_mfma_f32_16x16x32_bf16 v[96:99], v[204:207], v[170:173], v[96:99]
	v_mfma_f32_16x16x32_bf16 v[84:87], v[196:199], v[178:181], v[84:87]
	v_mfma_f32_16x16x32_bf16 v[80:83], v[204:207], v[178:181], v[80:83]
	v_mfma_f32_16x16x32_bf16 v[68:71], v[196:199], v[186:189], v[68:71]
	v_mfma_f32_16x16x32_bf16 v[64:67], v[204:207], v[186:189], v[64:67]
	s_setprio 0
	s_barrier
	ds_read_b128 v[158:161], v138 offset:49168
	ds_read_b128 v[162:165], v138 offset:50192
	ds_read_b128 v[166:169], v138 offset:51216
	ds_read_b128 v[170:173], v138 offset:52240
	ds_read_b128 v[174:177], v138 offset:53264
	ds_read_b128 v[178:181], v138 offset:54288
	ds_read_b128 v[182:185], v138 offset:55312
	ds_read_b128 v[186:189], v138 offset:56336
	s_mov_b32 m0, s25
	s_nop 0
	buffer_load_dwordx4 v128, s[0:3], s35 offen lds
	s_nop 0
	s_mov_b32 m0, s26
	s_nop 0
	buffer_load_dwordx4 v133, s[0:3], s35 offen lds
	s_barrier
	s_waitcnt lgkmcnt(0)
	s_setprio 1
	s_waitcnt lgkmcnt(7)
	v_mfma_f32_16x16x32_bf16 v[60:63], v[142:145], v[158:161], v[60:63]
	v_mfma_f32_16x16x32_bf16 v[56:59], v[150:153], v[158:161], v[56:59]
	s_waitcnt lgkmcnt(5)
	v_mfma_f32_16x16x32_bf16 v[44:47], v[142:145], v[166:169], v[44:47]
	v_mfma_f32_16x16x32_bf16 v[40:43], v[150:153], v[166:169], v[40:43]
	s_waitcnt lgkmcnt(3)
	v_mfma_f32_16x16x32_bf16 v[28:31], v[142:145], v[174:177], v[28:31]
	v_mfma_f32_16x16x32_bf16 v[24:27], v[150:153], v[174:177], v[24:27]
	s_waitcnt lgkmcnt(1)
	v_mfma_f32_16x16x32_bf16 v[12:15], v[142:145], v[182:185], v[12:15]
	v_mfma_f32_16x16x32_bf16 v[8:11], v[150:153], v[182:185], v[8:11]
	v_mfma_f32_16x16x32_bf16 v[60:63], v[146:149], v[162:165], v[60:63]
	v_mfma_f32_16x16x32_bf16 v[56:59], v[154:157], v[162:165], v[56:59]
	v_mfma_f32_16x16x32_bf16 v[44:47], v[146:149], v[170:173], v[44:47]
	v_mfma_f32_16x16x32_bf16 v[40:43], v[154:157], v[170:173], v[40:43]
	v_mfma_f32_16x16x32_bf16 v[28:31], v[146:149], v[178:181], v[28:31]
	v_mfma_f32_16x16x32_bf16 v[24:27], v[154:157], v[178:181], v[24:27]
	s_waitcnt lgkmcnt(0)
	v_mfma_f32_16x16x32_bf16 v[12:15], v[146:149], v[186:189], v[12:15]
	v_mfma_f32_16x16x32_bf16 v[8:11], v[154:157], v[186:189], v[8:11]
	s_setprio 0
	s_barrier
	s_mov_b32 m0, s27
	s_nop 0
	buffer_load_dwordx4 v131, s[44:47], s35 offen lds
	s_nop 0
	s_mov_b32 m0, s28
	s_nop 0
	buffer_load_dwordx4 v136, s[44:47], s35 offen lds
	s_waitcnt vmcnt(6)
	s_barrier
	s_setprio 1
	v_mfma_f32_16x16x32_bf16 v[52:55], v[192:195], v[158:161], v[52:55]
	v_mfma_f32_16x16x32_bf16 v[48:51], v[200:203], v[158:161], v[48:51]
	v_mfma_f32_16x16x32_bf16 v[36:39], v[192:195], v[166:169], v[36:39]
	v_mfma_f32_16x16x32_bf16 v[32:35], v[200:203], v[166:169], v[32:35]
	v_mfma_f32_16x16x32_bf16 v[20:23], v[192:195], v[174:177], v[20:23]
	v_mfma_f32_16x16x32_bf16 v[16:19], v[200:203], v[174:177], v[16:19]
	v_mfma_f32_16x16x32_bf16 v[4:7], v[192:195], v[182:185], v[4:7]
	v_mfma_f32_16x16x32_bf16 v[0:3], v[200:203], v[182:185], v[0:3]
	v_mfma_f32_16x16x32_bf16 v[52:55], v[196:199], v[162:165], v[52:55]
	v_mfma_f32_16x16x32_bf16 v[48:51], v[204:207], v[162:165], v[48:51]
	v_mfma_f32_16x16x32_bf16 v[36:39], v[196:199], v[170:173], v[36:39]
	v_mfma_f32_16x16x32_bf16 v[32:35], v[204:207], v[170:173], v[32:35]
	v_mfma_f32_16x16x32_bf16 v[20:23], v[196:199], v[178:181], v[20:23]
	v_mfma_f32_16x16x32_bf16 v[16:19], v[204:207], v[178:181], v[16:19]
	v_mfma_f32_16x16x32_bf16 v[4:7], v[196:199], v[186:189], v[4:7]
	v_mfma_f32_16x16x32_bf16 v[0:3], v[204:207], v[186:189], v[0:3]
	s_setprio 0
	s_barrier
	s_mov_b32 s33, s34
	s_cbranch_scc0 .LBB0_1266
	s_waitcnt vmcnt(0)
	s_cmpk_lt_u32 s12, 0x100
	s_cbranch_scc0 .LBB0_1262
	s_barrier
	s_branch .LBB0_1262

; #define G_WAIT_V(n) asm volatile("s_waitcnt vmcnt(" #n ")" ::: "memory")
; #define G_BAR() __builtin_amdgcn_s_barrier()
; #define D_STAGE_A(slot, half, kt) D_STAGE(rsA, voffA, slot, half, kt)
; #define D_STAGE_B(slot, half, kt) D_STAGE(rsB, voffB, slot, half, kt)
; #define D_STAGE_A(slot, half, kt) D_STAGE(rsA, voffA, slot, half, kt)
; #define D_STAGE_B(slot, half, kt) do { _Pragma("unroll") for (int _i = 0; _i < 2; ++_i) { const unsigned _m0 = ldsw + (unsigned)((slot) + _i * 8192); const unsigned _so = (unsigned)(kt) * 128u + (half) * bt_half + _i * bt_piece; \
;     asm volatile("s_mov_b32 m0, %0\n\ts_nop 4\n\tbuffer_load_dwordx4 %1, %2, %3 offen lds" :: "s"(_m0), "v"(voffB0), "s"(rsB), "s"(_so) : "m0", "memory"); } } while (0)
;   DI unsigned bt_rowoff(int h, int R) const { return (unsigned)(pn * 256 + 128 * h + (pn < 15 ? tcol_adj(R) : tcol_p64(R))) * 4096u; }
;   DI unsigned a_bytes() const { return (unsigned)NTOK * 4096u; }
;     ...
;   const unsigned bt_half = cfg.bt_rowoff(1, 0) - cfg.bt_rowoff(0, 0), bt_piece = cfg.bt_rowoff(0, 64) - cfg.bt_rowoff(0, 0);
;   const __amdgpu_buffer_rsrc_t rsA = __builtin_amdgcn_make_buffer_rsrc((void*)cfg.a_base(), 0, cfg.a_bytes(), 0x00020000);
;   const __amdgpu_buffer_rsrc_t rsB = __builtin_amdgcn_make_buffer_rsrc((void*)cfg.bt_base(), 0, cfg.bt_bytes(), 0x00020000);
;   const unsigned ldsw = (unsigned)__builtin_amdgcn_readfirstlane((int)(unsigned)(size_t)lds) + (unsigned)wid * 1024u;
;     ...
;   unsigned aoff[2], boff[2];
; #pragma unroll
;   for (int j = 0; j < 2; ++j) {
;     aoff[j] = (unsigned)(64 * wr + fr) * 128u + 16u * ((2u * fq + j) ^ ((unsigned)fr & 7u));
;     boff[j] = (unsigned)(32 * wc + fr) * 128u + 16u * ((2u * fq + j) ^ ((unsigned)fr & 7u));
;   }
;     ...
;   const int scw = cfg.scale_w(), scx = cfg.scale_x();
;     ...
;   f32x4 acc[2][2][4][2];
; #pragma unroll
;   for (int a = 0; a < 2; ++a)
; #pragma unroll
;     for (int b = 0; b < 2; ++b)
; #pragma unroll
;       for (int m = 0; m < 4; ++m)
; #pragma unroll
;         for (int n = 0; n < 2; ++n) acc[a][b][m][n] = (f32x4){0.f, 0.f, 0.f, 0.f};
;   i32x8 At[4], B0[2], B1[2];
;   if (!PRE) {
;     D_STAGE_B(G_SB(0, 0), 0, 0); D_STAGE_A(G_SA(0, 0), 0, 0); D_STAGE_B(G_SB(0, 1), 1, 0); D_STAGE_A(G_SA(0, 1), 1, 0);
;     D_STAGE_B(G_SB(1, 0), 0, 1); D_STAGE_A(G_SA(1, 0), 0, 1); D_STAGE_B(G_SB(1, 1), 1, 1);
;   }
;   G_WAIT_V(0); G_BAR();
.LBB0_1412:
	s_and_b32 s5, s4, 16
	s_waitcnt vmcnt(3)
	v_lshlrev_b32_e32 v3, 9, v8
	s_add_i32 s5, s5, s64
	v_and_or_b32 v120, v3, s36, v6
	s_waitcnt vmcnt(2)
	v_lshlrev_b32_e32 v3, 9, v7
	s_lshl_b32 s5, s5, 7
	s_and_b32 s4, s4, 0x1fffe0
	v_lshlrev_b32_e32 v2, 1, v2
	v_and_or_b32 v121, v3, s36, v6
	s_add_i32 s5, s5, s4
	v_and_b32_e32 v3, 3, v1
	v_and_b32_e32 v2, 24, v2
	s_ashr_i32 s17, s16, 31
	s_ashr_i32 s22, s15, 8
	v_or3_b32 v2, s5, v3, v2
	s_lshl_b64 s[4:5], s[16:17], 23
	s_add_u32 s4, s50, s4
	s_addc_u32 s5, s51, s5
	s_lshl_b32 s17, s75, 10
	s_add_i32 s76, s17, 0
	v_lshl_or_b32 v122, v2, 11, v6
	s_and_b32 s5, s5, 0xffff
	s_add_i32 s23, s76, 0x10010
	s_mov_b32 m0, s23
	s_nop 0
	buffer_load_dwordx4 v122, s[4:7], s34 offen lds
	s_add_i32 s39, s76, 0x12010
	s_mov_b32 m0, s39
	s_nop 0
	buffer_load_dwordx4 v122, s[4:7], s7 offen lds
	s_waitcnt vmcnt(1)
	v_lshlrev_b32_e32 v2, 9, v5
	s_add_i32 s61, s76, 16
	s_mov_b32 m0, s61
	s_nop 0
	buffer_load_dwordx4 v120, s[8:11], s34 offen lds
	v_and_or_b32 v123, v2, s36, v6
	s_add_i32 s62, s76, 0x2010
	s_mov_b32 m0, s62
	s_nop 0
	buffer_load_dwordx4 v123, s[8:11], s34 offen lds
	s_add_i32 s63, s76, 0x14010
	s_mov_b32 m0, s63
	s_nop 0
	buffer_load_dwordx4 v122, s[4:7], s37 offen lds
	s_add_i32 s66, s76, 0x16010
	s_mov_b32 m0, s66
	s_nop 0
	buffer_load_dwordx4 v122, s[4:7], s56 offen lds
	s_waitcnt vmcnt(0)
	v_lshlrev_b32_e32 v2, 9, v4
	s_add_i32 s67, s76, 0x4010
	s_mov_b32 m0, s67
	s_nop 0
	buffer_load_dwordx4 v121, s[8:11], s34 offen lds
	v_and_or_b32 v124, v2, s36, v6
	s_add_i32 s68, s76, 0x6010
	s_mov_b32 m0, s68
	s_nop 0
	buffer_load_dwordx4 v124, s[8:11], s34 offen lds
	s_add_i32 s69, s76, 0x18010
	s_mov_b32 m0, s69
	s_nop 0
	buffer_load_dwordx4 v122, s[4:7], s35 offen lds
	s_add_i32 s70, s76, 0x1a010
	s_mov_b32 m0, s70
	s_nop 0
	buffer_load_dwordx4 v122, s[4:7], s43 offen lds
	s_add_i32 s71, s76, 0x8010
	s_mov_b32 m0, s71
	s_nop 0
	buffer_load_dwordx4 v120, s[8:11], s35 offen lds
	s_add_i32 s72, s76, 0xa010
	s_mov_b32 m0, s72
	s_nop 0
	buffer_load_dwordx4 v123, s[8:11], s35 offen lds
	s_add_i32 s73, s76, 0x1c010
	s_mov_b32 m0, s73
	s_nop 0
	buffer_load_dwordx4 v122, s[4:7], s44 offen lds
	s_add_i32 s74, s76, 0x1e010
	s_mov_b32 m0, s74
	s_nop 0
	buffer_load_dwordx4 v122, s[4:7], s45 offen lds
	s_waitcnt vmcnt(0)
	s_mov_b32 s42, s97
	s_cmp_lg_u32 s22, 1
	s_barrier
	s_cbranch_scc1 .LBB0_1414
	s_barrier

; #define G_WAIT_V(n) asm volatile("s_waitcnt vmcnt(" #n ")" ::: "memory")
; #define G_BAR() __builtin_amdgcn_s_barrier()
; #define G_SCHED() __builtin_amdgcn_sched_barrier(0)
; #define D_STAGE_A(slot, half, kt) D_STAGE(rsA, voffA, slot, half, kt)
; #define D_STAGE_B(slot, half, kt) D_STAGE(rsB, voffB, slot, half, kt)
; #define D_LDA(dst, slot) do { _Pragma("unroll") for (int m = 0; m < 4; ++m) _Pragma("unroll") for (int k = 0; k < 2; ++k) \
;     dst[m][k] = *(const LDS_AS bf16x8*)(lds + (slot) + aoff + m * 2048 + k * 1024); } while (0)
; #define D_LDB(dst, slot) do { _Pragma("unroll") for (int n = 0; n < 2; ++n) _Pragma("unroll") for (int k = 0; k < 2; ++k) \
;     dst[n][k] = *(const LDS_AS bf16x8*)(lds + (slot) + boff + n * 2048 + k * 1024); } while (0)
; #define D_MMA(ai, bj, At, Bf) do { __builtin_amdgcn_s_setprio(1); _Pragma("unroll") for (int m = 0; m < 4; ++m) _Pragma("unroll") for (int n = 0; n < 2; ++n) _Pragma("unroll") for (int k = 0; k < 2; ++k) \
;     acc[ai][bj][m][n] = __builtin_amdgcn_mfma_f32_16x16x32_bf16(Bf[n][k], At[m][k], acc[ai][bj][m][n], 0, 0, 0); __builtin_amdgcn_s_setprio(0); } while (0)
; #define D_WAIT_L(n) asm volatile("s_waitcnt lgkmcnt(" #n ")" ::: "memory")
; #define D_STAGE_A(slot, half, kt) D_STAGE(rsA, voffA, slot, half, kt)
; #define D_WAIT_L(n) asm volatile("s_waitcnt lgkmcnt(" #n ")" ::: "memory")
;     ...
;   for (int t = 0; t < (F8_PEEL ? nt - 2 : nt); t += 2) {
;     const int t1 = t + 1;
;     const int t2 = (F8_PEEL || t + 2 < nt) ? t + 2 : t;
;     const int t3 = (F8_PEEL || t + 2 < nt) ? t + 3 : t + 1;
;     D_LDB(B0, G_SB(0, 0)); G_SCHED(); D_LDA(At, G_SA(0, 0)); D_STAGE_A(G_SA(1, 1), 1, t1);
;     D_WAIT_L(8); G_BAR(); D_WAIT_L(0); G_SCHED(); D_MMA(0, 0, At, B0); G_BAR(); G_SCHED();
;     D_LDB(B1, G_SB(0, 1)); D_STAGE_B(G_SB(0, 0), 0, t2);
;     G_BAR(); D_WAIT_L(0); G_SCHED(); D_MMA(0, 1, At, B1); G_BAR(); G_SCHED();
;     D_LDA(At, G_SA(0, 1)); D_STAGE_A(G_SA(0, 0), 0, t2);
;     G_BAR(); D_WAIT_L(0); G_SCHED(); D_MMA(1, 0, At, B0); G_BAR(); G_SCHED();
;     D_STAGE_B(G_SB(0, 1), 1, t2);
;     G_WAIT_V(6); G_BAR(); G_SCHED(); D_MMA(1, 1, At, B1); G_BAR(); G_SCHED();
.LBB0_1415:
	s_add_i32 s82, 0, 0x10010
	v_add_u32_e32 v72, s82, v125
	v_add_u32_e32 v73, s82, v126
	ds_read_b128 v[152:155], v72
	ds_read_b128 v[160:163], v72 offset:2048
	ds_read_b128 v[156:159], v73
	ds_read_b128 v[164:167], v73 offset:2048
	s_add_i32 s38, s79, 1
	s_add_i32 s80, s79, 3
	s_add_i32 s78, s79, 2
	s_add_i32 s96, 0, 0x14010
	s_cmp_lt_u32 s79, 14
	s_cselect_b32 s81, s78, s79
	s_cselect_b32 s38, s80, s38
	s_lshl_b32 s86, s81, 7
	s_lshl_b32 s81, s38, 7
	s_add_i32 s97, s86, 0x20000
	s_add_i32 s91, s86, 0x2000
	s_add_i32 s90, s86, 0x22000
	s_add_i32 s87, 0, 0x18010
	s_add_i32 s85, 0, 0x1c010
	s_add_i32 s84, s81, 0x20000
	s_add_i32 s83, s81, 0x2000
	s_add_i32 s82, s81, 0x22000
	s_add_i32 s80, s77, 0x100
	s_cmp_gt_u32 s79, 13
	ds_read_b128 v[168:171], v127 offset:16
	ds_read_b128 v[176:179], v127 offset:2064
	ds_read_b128 v[172:175], v128 offset:16
	ds_read_b128 v[180:183], v128 offset:2064
	ds_read_b128 v[192:195], v127 offset:4112
	ds_read_b128 v[200:203], v127 offset:6160
	ds_read_b128 v[196:199], v128 offset:4112
	ds_read_b128 v[204:207], v128 offset:6160
	s_mov_b32 m0, s75
	s_nop 0
	buffer_load_dwordx4 v121, s[8:11], s77 offen lds
	s_nop 0
	s_mov_b32 m0, s76
	s_nop 0
	buffer_load_dwordx4 v124, s[8:11], s77 offen lds
	s_waitcnt lgkmcnt(8)
	s_barrier
	s_waitcnt lgkmcnt(0)
	s_setprio 1
	s_waitcnt lgkmcnt(5)
	v_mfma_scale_f32_16x16x128_f8f6f4 v[134:137], v[160:167], v[168:175], v[136:139], v149, v148 op_sel_hi:[0,0,0]
	s_waitcnt lgkmcnt(0)
	v_mfma_scale_f32_16x16x128_f8f6f4 v[212:215], v[152:159], v[200:207], v[212:215], v149, v148 op_sel_hi:[0,0,0]
	v_mfma_scale_f32_16x16x128_f8f6f4 v[216:219], v[160:167], v[200:207], v[216:219], v149, v148 op_sel_hi:[0,0,0]
	v_mfma_scale_f32_16x16x128_f8f6f4 v[130:133], v[152:159], v[168:175], v[140:143], v149, v148 op_sel_hi:[0,0,0]
	v_mfma_scale_f32_16x16x128_f8f6f4 v[144:147], v[152:159], v[176:183], v[108:111], v149, v148 op_sel_hi:[0,0,0]
	v_mfma_scale_f32_16x16x128_f8f6f4 v[184:187], v[160:167], v[176:183], v[104:107], v149, v148 op_sel_hi:[0,0,0]
	v_mfma_scale_f32_16x16x128_f8f6f4 v[188:191], v[152:159], v[192:199], v[92:95], v149, v148 op_sel_hi:[0,0,0]
	v_mfma_scale_f32_16x16x128_f8f6f4 v[208:211], v[160:167], v[192:199], v[88:91], v149, v148 op_sel_hi:[0,0,0]
	s_setprio 0
	s_barrier
	v_add_u32_e32 v76, s96, v125
	v_add_u32_e32 v80, s96, v126
	ds_read_b128 v[72:75], v76
	s_nop 1
	ds_read_b128 v[88:91], v76 offset:2048
	ds_read_b128 v[76:79], v80
	ds_read_b128 v[92:95], v80 offset:2048
	s_mov_b32 m0, s23
	s_nop 0
	buffer_load_dwordx4 v122, s[4:7], s86 offen lds
	s_nop 0
	s_mov_b32 m0, s39
	s_nop 0
	buffer_load_dwordx4 v122, s[4:7], s97 offen lds
	s_barrier
	s_waitcnt lgkmcnt(0)
	s_setprio 1
	s_waitcnt lgkmcnt(1)
	v_mfma_scale_f32_16x16x128_f8f6f4 v[68:71], v[72:79], v[200:207], v[68:71], v149, v148 op_sel_hi:[0,0,0]
	s_waitcnt lgkmcnt(0)
	v_mfma_scale_f32_16x16x128_f8f6f4 v[56:59], v[88:95], v[200:207], v[56:59], v149, v148 op_sel_hi:[0,0,0]
	v_mfma_scale_f32_16x16x128_f8f6f4 v[220:223], v[72:79], v[168:175], v[116:119], v149, v148 op_sel_hi:[0,0,0]
	v_mfma_scale_f32_16x16x128_f8f6f4 v[168:171], v[88:95], v[168:175], v[112:115], v149, v148 op_sel_hi:[0,0,0]
	v_mfma_scale_f32_16x16x128_f8f6f4 v[172:175], v[72:79], v[176:183], v[100:103], v149, v148 op_sel_hi:[0,0,0]
	v_mfma_scale_f32_16x16x128_f8f6f4 v[176:179], v[88:95], v[176:183], v[96:99], v149, v148 op_sel_hi:[0,0,0]
	v_mfma_scale_f32_16x16x128_f8f6f4 v[180:183], v[72:79], v[192:199], v[84:87], v149, v148 op_sel_hi:[0,0,0]
	v_mfma_scale_f32_16x16x128_f8f6f4 v[192:195], v[88:95], v[192:199], v[8:11], v149, v148 op_sel_hi:[0,0,0]
	s_setprio 0
	s_barrier
	ds_read_b128 v[80:83], v127 offset:16400
	s_nop 1
	ds_read_b128 v[96:99], v127 offset:18448
	ds_read_b128 v[84:87], v128 offset:16400
	ds_read_b128 v[100:103], v128 offset:18448
	ds_read_b128 v[104:107], v127 offset:20496
	ds_read_b128 v[112:115], v127 offset:22544
	ds_read_b128 v[108:111], v128 offset:20496
	ds_read_b128 v[116:119], v128 offset:22544
	s_mov_b32 m0, s61
	s_nop 0
	buffer_load_dwordx4 v120, s[8:11], s86 offen lds
	s_nop 0
	s_mov_b32 m0, s62
	s_nop 0
	buffer_load_dwordx4 v123, s[8:11], s86 offen lds
	s_barrier
	s_waitcnt lgkmcnt(0)
	s_setprio 1
	s_waitcnt lgkmcnt(5)
	v_mfma_scale_f32_16x16x128_f8f6f4 v[64:67], v[152:159], v[80:87], v[64:67], v149, v148 op_sel_hi:[0,0,0]
	v_mfma_scale_f32_16x16x128_f8f6f4 v[60:63], v[160:167], v[80:87], v[60:63], v149, v148 op_sel_hi:[0,0,0]
	s_waitcnt lgkmcnt(0)
	v_mfma_scale_f32_16x16x128_f8f6f4 v[236:239], v[160:167], v[112:119], v[236:239], v149, v148 op_sel_hi:[0,0,0]
	v_mfma_scale_f32_16x16x128_f8f6f4 v[200:203], v[152:159], v[96:103], v[44:47], v149, v148 op_sel_hi:[0,0,0]
	v_mfma_scale_f32_16x16x128_f8f6f4 v[204:207], v[160:167], v[96:103], v[40:43], v149, v148 op_sel_hi:[0,0,0]
	v_mfma_scale_f32_16x16x128_f8f6f4 v[224:227], v[152:159], v[104:111], v[28:31], v149, v148 op_sel_hi:[0,0,0]
	v_mfma_scale_f32_16x16x128_f8f6f4 v[228:231], v[160:167], v[104:111], v[24:27], v149, v148 op_sel_hi:[0,0,0]
	v_mfma_scale_f32_16x16x128_f8f6f4 v[232:235], v[152:159], v[112:119], v[12:15], v149, v148 op_sel_hi:[0,0,0]
	s_setprio 0
	s_barrier
	s_mov_b32 m0, s63
	s_nop 0
	buffer_load_dwordx4 v122, s[4:7], s91 offen lds
	s_nop 0
	s_mov_b32 m0, s66
	s_nop 0
	buffer_load_dwordx4 v122, s[4:7], s90 offen lds
	s_waitcnt vmcnt(6)
	s_barrier
; #define G_WAIT_V(n) asm volatile("s_waitcnt vmcnt(" #n ")" ::: "memory")
; #define G_BAR() __builtin_amdgcn_s_barrier()
; #define G_SCHED() __builtin_amdgcn_sched_barrier(0)
; #define D_STAGE_A(slot, half, kt) D_STAGE(rsA, voffA, slot, half, kt)
; #define D_STAGE_B(slot, half, kt) D_STAGE(rsB, voffB, slot, half, kt)
; #define D_LDA(dst, slot) do { _Pragma("unroll") for (int m = 0; m < 4; ++m) _Pragma("unroll") for (int k = 0; k < 2; ++k) \
;     dst[m][k] = *(const LDS_AS bf16x8*)(lds + (slot) + aoff + m * 2048 + k * 1024); } while (0)
; #define D_LDB(dst, slot) do { _Pragma("unroll") for (int n = 0; n < 2; ++n) _Pragma("unroll") for (int k = 0; k < 2; ++k) \
;     dst[n][k] = *(const LDS_AS bf16x8*)(lds + (slot) + boff + n * 2048 + k * 1024); } while (0)
; #define D_MMA(ai, bj, At, Bf) do { __builtin_amdgcn_s_setprio(1); _Pragma("unroll") for (int m = 0; m < 4; ++m) _Pragma("unroll") for (int n = 0; n < 2; ++n) _Pragma("unroll") for (int k = 0; k < 2; ++k) \
;     acc[ai][bj][m][n] = __builtin_amdgcn_mfma_f32_16x16x32_bf16(Bf[n][k], At[m][k], acc[ai][bj][m][n], 0, 0, 0); __builtin_amdgcn_s_setprio(0); } while (0)
; #define D_WAIT_L(n) asm volatile("s_waitcnt lgkmcnt(" #n ")" ::: "memory")
; #define D_STAGE_A(slot, half, kt) D_STAGE(rsA, voffA, slot, half, kt)
; #define D_STAGE_B(slot, half, kt) do { _Pragma("unroll") for (int _i = 0; _i < 2; ++_i) { const unsigned _m0 = ldsw + (unsigned)((slot) + _i * 8192); const unsigned _so = (unsigned)(kt) * 128u + (half) * bt_half + _i * bt_piece; \
;     asm volatile("s_mov_b32 m0, %0\n\ts_nop 4\n\tbuffer_load_dwordx4 %1, %2, %3 offen lds" :: "s"(_m0), "v"(voffB0), "s"(rsB), "s"(_so) : "m0", "memory"); } } while (0)
;     ...
;     G_WAIT_V(6); G_BAR(); G_SCHED(); D_MMA(1, 1, At, B1); G_BAR(); G_SCHED();
;     D_LDB(B0, G_SB(1, 0)); G_SCHED(); D_LDA(At, G_SA(1, 0)); D_STAGE_A(G_SA(0, 1), 1, t2);
;     D_WAIT_L(8); G_BAR(); D_WAIT_L(0); G_SCHED(); D_MMA(0, 0, At, B0); G_BAR(); G_SCHED();
;     D_LDB(B1, G_SB(1, 1)); D_STAGE_B(G_SB(1, 0), 0, t3);
;     G_BAR(); D_WAIT_L(0); G_SCHED(); D_MMA(0, 1, At, B1); G_BAR(); G_SCHED();
;     D_LDA(At, G_SA(1, 1)); D_STAGE_A(G_SA(1, 0), 0, t3);
;     G_BAR(); D_WAIT_L(0); G_SCHED(); D_MMA(1, 0, At, B0); G_BAR(); G_SCHED();
;     D_STAGE_B(G_SB(1, 1), 1, t3);
;     G_WAIT_V(6); G_BAR(); G_SCHED(); D_MMA(1, 1, At, B1); G_BAR(); G_SCHED();
;   }
;   if (!F8_PEEL) G_WAIT_V(0);
	s_setprio 1
	v_mfma_scale_f32_16x16x128_f8f6f4 v[52:55], v[72:79], v[80:87], v[52:55], v149, v148 op_sel_hi:[0,0,0]
	v_mfma_scale_f32_16x16x128_f8f6f4 v[48:51], v[88:95], v[80:87], v[48:51], v149, v148 op_sel_hi:[0,0,0]
	v_mfma_scale_f32_16x16x128_f8f6f4 v[240:243], v[72:79], v[96:103], v[36:39], v149, v148 op_sel_hi:[0,0,0]
	v_mfma_scale_f32_16x16x128_f8f6f4 v[244:247], v[88:95], v[96:103], v[32:35], v149, v148 op_sel_hi:[0,0,0]
	v_mfma_scale_f32_16x16x128_f8f6f4 v[248:251], v[72:79], v[104:111], v[20:23], v149, v148 op_sel_hi:[0,0,0]
	v_mfma_scale_f32_16x16x128_f8f6f4 v[80:83], v[88:95], v[104:111], v[16:19], v149, v148 op_sel_hi:[0,0,0]
	v_mfma_scale_f32_16x16x128_f8f6f4 v[72:75], v[72:79], v[112:119], v[4:7], v149, v148 op_sel_hi:[0,0,0]
	v_mfma_scale_f32_16x16x128_f8f6f4 v[76:79], v[88:95], v[112:119], v[0:3], v149, v148 op_sel_hi:[0,0,0]
	s_setprio 0
	s_barrier
	s_nop 3
	v_add_u32_e32 v4, s87, v125
	v_add_u32_e32 v8, s87, v126
	ds_read_b128 v[0:3], v4
	ds_read_b128 v[16:19], v4 offset:2048
	ds_read_b128 v[4:7], v8
	ds_read_b128 v[20:23], v8 offset:2048
	ds_read_b128 v[8:11], v127 offset:32784
	ds_read_b128 v[24:27], v127 offset:34832
	ds_read_b128 v[12:15], v128 offset:32784
	ds_read_b128 v[28:31], v128 offset:34832
	ds_read_b128 v[32:35], v127 offset:36880
	ds_read_b128 v[40:43], v127 offset:38928
	ds_read_b128 v[36:39], v128 offset:36880
	ds_read_b128 v[44:47], v128 offset:38928
	s_mov_b32 m0, s67
	s_nop 0
	buffer_load_dwordx4 v121, s[8:11], s86 offen lds
	s_nop 0
	s_mov_b32 m0, s68
	s_nop 0
	buffer_load_dwordx4 v124, s[8:11], s86 offen lds
	s_waitcnt lgkmcnt(8)
	s_barrier
	s_waitcnt lgkmcnt(0)
	s_setprio 1
	s_waitcnt lgkmcnt(5)
	v_mfma_scale_f32_16x16x128_f8f6f4 v[140:143], v[0:7], v[8:15], v[130:133], v149, v148 op_sel_hi:[0,0,0]
	v_mfma_scale_f32_16x16x128_f8f6f4 v[136:139], v[16:23], v[8:15], v[134:137], v149, v148 op_sel_hi:[0,0,0]
	s_waitcnt lgkmcnt(4)
	v_mfma_scale_f32_16x16x128_f8f6f4 v[108:111], v[0:7], v[24:31], v[144:147], v149, v148 op_sel_hi:[0,0,0]
	v_mfma_scale_f32_16x16x128_f8f6f4 v[104:107], v[16:23], v[24:31], v[184:187], v149, v148 op_sel_hi:[0,0,0]
	s_waitcnt lgkmcnt(1)
	v_mfma_scale_f32_16x16x128_f8f6f4 v[92:95], v[0:7], v[32:39], v[188:191], v149, v148 op_sel_hi:[0,0,0]
	v_mfma_scale_f32_16x16x128_f8f6f4 v[88:91], v[16:23], v[32:39], v[208:211], v149, v148 op_sel_hi:[0,0,0]
	s_waitcnt lgkmcnt(0)
	v_mfma_scale_f32_16x16x128_f8f6f4 v[212:215], v[0:7], v[40:47], v[212:215], v149, v148 op_sel_hi:[0,0,0]
	v_mfma_scale_f32_16x16x128_f8f6f4 v[216:219], v[16:23], v[40:47], v[216:219], v149, v148 op_sel_hi:[0,0,0]
	s_setprio 0
	s_barrier
	v_add_u32_e32 v84, s85, v125
	v_add_u32_e32 v85, s85, v126
	ds_read_b128 v[152:155], v84
	ds_read_b128 v[160:163], v84 offset:2048
	ds_read_b128 v[156:159], v85
	ds_read_b128 v[164:167], v85 offset:2048
	s_mov_b32 m0, s69
	s_nop 0
	buffer_load_dwordx4 v122, s[4:7], s81 offen lds
	s_nop 0
	s_mov_b32 m0, s70
	s_nop 0
	buffer_load_dwordx4 v122, s[4:7], s84 offen lds
	s_barrier
	s_waitcnt lgkmcnt(0)
	s_setprio 1
	s_waitcnt lgkmcnt(1)
	v_mfma_scale_f32_16x16x128_f8f6f4 v[116:119], v[152:159], v[8:15], v[220:223], v149, v148 op_sel_hi:[0,0,0]
	s_waitcnt lgkmcnt(0)
	v_mfma_scale_f32_16x16x128_f8f6f4 v[112:115], v[160:167], v[8:15], v[168:171], v149, v148 op_sel_hi:[0,0,0]
	v_mfma_scale_f32_16x16x128_f8f6f4 v[100:103], v[152:159], v[24:31], v[172:175], v149, v148 op_sel_hi:[0,0,0]
	v_mfma_scale_f32_16x16x128_f8f6f4 v[96:99], v[160:167], v[24:31], v[176:179], v149, v148 op_sel_hi:[0,0,0]
	v_mfma_scale_f32_16x16x128_f8f6f4 v[84:87], v[152:159], v[32:39], v[180:183], v149, v148 op_sel_hi:[0,0,0]
	v_mfma_scale_f32_16x16x128_f8f6f4 v[8:11], v[160:167], v[32:39], v[192:195], v149, v148 op_sel_hi:[0,0,0]
	v_mfma_scale_f32_16x16x128_f8f6f4 v[68:71], v[152:159], v[40:47], v[68:71], v149, v148 op_sel_hi:[0,0,0]
	v_mfma_scale_f32_16x16x128_f8f6f4 v[56:59], v[160:167], v[40:47], v[56:59], v149, v148 op_sel_hi:[0,0,0]
	s_setprio 0
	s_barrier
	ds_read_b128 v[32:35], v127 offset:49168
	ds_read_b128 v[168:171], v127 offset:51216
	ds_read_b128 v[36:39], v128 offset:49168
	ds_read_b128 v[172:175], v128 offset:51216
	ds_read_b128 v[176:179], v127 offset:53264
	ds_read_b128 v[192:195], v127 offset:55312
	ds_read_b128 v[180:183], v128 offset:53264
	ds_read_b128 v[196:199], v128 offset:55312
	s_mov_b32 m0, s71
	s_nop 0
	buffer_load_dwordx4 v120, s[8:11], s81 offen lds
	s_nop 0
	s_mov_b32 m0, s72
	s_nop 0
	buffer_load_dwordx4 v123, s[8:11], s81 offen lds
	s_barrier
	s_waitcnt lgkmcnt(0)
	s_setprio 1
	s_waitcnt lgkmcnt(5)
	v_mfma_scale_f32_16x16x128_f8f6f4 v[64:67], v[0:7], v[32:39], v[64:67], v149, v148 op_sel_hi:[0,0,0]
	v_mfma_scale_f32_16x16x128_f8f6f4 v[60:63], v[16:23], v[32:39], v[60:63], v149, v148 op_sel_hi:[0,0,0]
	s_waitcnt lgkmcnt(4)
	v_mfma_scale_f32_16x16x128_f8f6f4 v[44:47], v[0:7], v[168:175], v[200:203], v149, v148 op_sel_hi:[0,0,0]
	v_mfma_scale_f32_16x16x128_f8f6f4 v[40:43], v[16:23], v[168:175], v[204:207], v149, v148 op_sel_hi:[0,0,0]
	s_waitcnt lgkmcnt(1)
	v_mfma_scale_f32_16x16x128_f8f6f4 v[28:31], v[0:7], v[176:183], v[224:227], v149, v148 op_sel_hi:[0,0,0]
	v_mfma_scale_f32_16x16x128_f8f6f4 v[24:27], v[16:23], v[176:183], v[228:231], v149, v148 op_sel_hi:[0,0,0]
	s_waitcnt lgkmcnt(0)
	v_mfma_scale_f32_16x16x128_f8f6f4 v[12:15], v[0:7], v[192:199], v[232:235], v149, v148 op_sel_hi:[0,0,0]
	v_mfma_scale_f32_16x16x128_f8f6f4 v[236:239], v[16:23], v[192:199], v[236:239], v149, v148 op_sel_hi:[0,0,0]
	s_setprio 0
	s_barrier
	s_mov_b32 m0, s73
	s_nop 0
	buffer_load_dwordx4 v122, s[4:7], s83 offen lds
	s_nop 0
	s_mov_b32 m0, s74
	s_nop 0
	buffer_load_dwordx4 v122, s[4:7], s82 offen lds
	s_waitcnt vmcnt(6)
	s_barrier
	s_setprio 1
	v_mfma_scale_f32_16x16x128_f8f6f4 v[52:55], v[152:159], v[32:39], v[52:55], v149, v148 op_sel_hi:[0,0,0]
	v_mfma_scale_f32_16x16x128_f8f6f4 v[48:51], v[160:167], v[32:39], v[48:51], v149, v148 op_sel_hi:[0,0,0]
	v_mfma_scale_f32_16x16x128_f8f6f4 v[36:39], v[152:159], v[168:175], v[240:243], v149, v148 op_sel_hi:[0,0,0]
	v_mfma_scale_f32_16x16x128_f8f6f4 v[32:35], v[160:167], v[168:175], v[244:247], v149, v148 op_sel_hi:[0,0,0]
	v_mfma_scale_f32_16x16x128_f8f6f4 v[20:23], v[152:159], v[176:183], v[248:251], v149, v148 op_sel_hi:[0,0,0]
	v_mfma_scale_f32_16x16x128_f8f6f4 v[16:19], v[160:167], v[176:183], v[80:83], v149, v148 op_sel_hi:[0,0,0]
	v_mfma_scale_f32_16x16x128_f8f6f4 v[4:7], v[152:159], v[192:199], v[72:75], v149, v148 op_sel_hi:[0,0,0]
	v_mfma_scale_f32_16x16x128_f8f6f4 v[0:3], v[160:167], v[192:199], v[76:79], v149, v148 op_sel_hi:[0,0,0]
	s_setprio 0
	s_barrier
	s_mov_b32 s77, s80
	s_mov_b32 s79, s78
	s_cbranch_scc0 .LBB0_1415
	s_waitcnt vmcnt(0)
	s_cmpk_lt_u32 s15, 0x100
	s_cbranch_scc0 .LBB0_1418
	s_barrier
; #define LDS_AS __attribute__((address_space(3)))
; #define OPAQUE_TID(P) (((P).wid0 << 6) | lane_id_now())
; #define P_STAGE_A(slot, half, kt) do { _Pragma("unroll") for (int _i = 0; _i < 2; ++_i) { const unsigned _m0 = ldsw + (unsigned)((slot) + _i * 8192); const unsigned _so = (unsigned)(kt) * 128u; \
;     asm volatile("s_mov_b32 m0, %0\n\ts_nop 4\n\tbuffer_load_dwordx4 %1, %2, %3 offen lds" :: "s"(_m0), "v"(voffA[half][_i]), "s"(rsA), "s"(_so) : "m0", "memory"); } } while (0)
; #define P_STAGE_B(slot, half, kt) do { _Pragma("unroll") for (int _i = 0; _i < 2; ++_i) { const unsigned _m0 = ldsw + (unsigned)((slot) + _i * 8192); const unsigned _so = (unsigned)(kt) * 128u + (half) * bt_half + _i * bt_piece; \
;     asm volatile("s_mov_b32 m0, %0\n\ts_nop 4\n\tbuffer_load_dwordx4 %1, %2, %3 offen lds" :: "s"(_m0), "v"(voffB0), "s"(rsB), "s"(_so) : "m0", "memory"); } } while (0)
;   DI unsigned bt_rowoff(int h, int R) const { return (unsigned)(pn * 256 + 128 * h + (pn < 15 ? tcol_adj(R) : tcol_p64(R))) * 4096u; }
; template <class Cfg>
; DI void f8dma_issue_prologue_st(LDS_AS unsigned char* lds, const Cfg& cfg) {
;   const int tid = OPAQUE_TID(cfg.p), wid = __builtin_amdgcn_readfirstlane(tid >> 6), lane = tid & 63;
;   const LDS_AS unsigned* stash = (const LDS_AS unsigned*)(lds + F8_STASH);
;   unsigned voffA[2][2], voffB0;
;   voffA[0][0] = stash[tid]; voffA[0][1] = stash[512 + tid]; voffA[1][0] = stash[1024 + tid]; voffA[1][1] = stash[1536 + tid];
;   {
;     const int r = 8 * wid + (lane >> 3);
;     const unsigned cofs = 16u * (((unsigned)lane & 7u) ^ (((unsigned)lane >> 3) & 7u));
;     voffB0 = cfg.bt_rowoff(0, r) + cofs;
;   }
;   const unsigned bt_half = cfg.bt_rowoff(1, 0) - cfg.bt_rowoff(0, 0), bt_piece = cfg.bt_rowoff(0, 64) - cfg.bt_rowoff(0, 0);
;   const __amdgpu_buffer_rsrc_t rsA = __builtin_amdgcn_make_buffer_rsrc((void*)cfg.a_base(), 0, cfg.a_bytes(), 0x00020000);
;   const __amdgpu_buffer_rsrc_t rsB = __builtin_amdgcn_make_buffer_rsrc((void*)cfg.bt_base(), 0, cfg.bt_bytes(), 0x00020000);
;   const unsigned ldsw = (unsigned)__builtin_amdgcn_readfirstlane((int)(unsigned)(size_t)lds) + (unsigned)wid * 1024u;
;     ...
;   P_STAGE_B(G_SB(0, 0), 0, 0); P_STAGE_A(G_SA(0, 0), 0, 0); P_STAGE_B(G_SB(0, 1), 1, 0); P_STAGE_A(G_SA(0, 1), 1, 0);
;   P_STAGE_B(G_SB(1, 0), 0, 1); P_STAGE_A(G_SA(1, 0), 0, 1); P_STAGE_B(G_SB(1, 1), 1, 1);
.LBB0_1418:
	s_and_b64 vcc, exec, s[2:3]
	v_readlane_b32 s87, v255, 12
	s_cbranch_vccnz .LBB0_1420
	v_mbcnt_lo_u32_b32 v76, -1, 0
	v_mbcnt_hi_u32_b32 v76, -1, v76
	s_ashr_i32 s15, s14, 31
	v_or_b32_e32 v72, s87, v76
	v_lshrrev_b32_e32 v77, 3, v76
	v_readfirstlane_b32 s2, v72
	s_ashr_i32 s23, s2, 6
	s_lshl_b32 s2, s23, 3
	s_and_b32 s3, s2, 16
	v_and_or_b32 v78, v77, 4, s2
	s_add_i32 s3, s3, s48
	s_lshl_b32 s3, s3, 7
	s_and_b32 s2, s2, 0x1fffe0
	v_lshlrev_b32_e32 v78, 1, v78
	v_xor_b32_e32 v77, v77, v76
	s_add_i32 s3, s3, s2
	v_and_b32_e32 v78, 24, v78
	v_bfe_u32 v76, v76, 3, 2
	v_or3_b32 v76, s3, v78, v76
	s_lshl_b64 s[2:3], s[14:15], 23
	v_lshl_add_u32 v72, v72, 2, 0
	s_add_u32 s4, s50, s2
	v_add_u32_e32 v74, 0x22410, v72
	s_addc_u32 s2, s51, s3
	ds_read2st64_b32 v[72:73], v74 offset1:8
	ds_read2st64_b32 v[74:75], v74 offset0:16 offset1:24
	v_lshlrev_b32_e32 v77, 4, v77
	s_and_b32 s5, s2, 0xffff
	s_lshl_b32 s2, s23, 10
	v_and_b32_e32 v77, 0x70, v77
	s_add_i32 s2, s2, 0
	v_lshl_or_b32 v76, v76, 11, v77
	s_add_i32 s3, s2, 0x10010
	s_mov_b32 m0, s3
	s_nop 0
	buffer_load_dwordx4 v76, s[4:7], s34 offen lds
	s_add_i32 s3, s2, 0x12010
	s_mov_b32 m0, s3
	s_nop 0
	buffer_load_dwordx4 v76, s[4:7], s7 offen lds
	s_add_i32 s3, s2, 16
	s_waitcnt lgkmcnt(1)
	s_mov_b32 m0, s3
	s_nop 0
	buffer_load_dwordx4 v72, s[8:11], s34 offen lds
	s_add_i32 s3, s2, 0x2010
	s_mov_b32 m0, s3
	s_nop 0
	buffer_load_dwordx4 v73, s[8:11], s34 offen lds
	s_add_i32 s3, s2, 0x14010
	s_mov_b32 m0, s3
	s_nop 0
	buffer_load_dwordx4 v76, s[4:7], s37 offen lds
	s_add_i32 s3, s2, 0x16010
	s_mov_b32 m0, s3
	s_nop 0
	buffer_load_dwordx4 v76, s[4:7], s56 offen lds
	s_add_i32 s3, s2, 0x4010
	s_waitcnt lgkmcnt(0)
	s_mov_b32 m0, s3
	s_nop 0
	buffer_load_dwordx4 v74, s[8:11], s34 offen lds
	s_add_i32 s3, s2, 0x6010
	s_mov_b32 m0, s3
	s_nop 0
	buffer_load_dwordx4 v75, s[8:11], s34 offen lds
	s_add_i32 s3, s2, 0x18010
	s_mov_b32 m0, s3
	s_nop 0
	buffer_load_dwordx4 v76, s[4:7], s35 offen lds
	s_add_i32 s3, s2, 0x1a010
	s_mov_b32 m0, s3
	s_nop 0
	buffer_load_dwordx4 v76, s[4:7], s43 offen lds
	s_add_i32 s3, s2, 0x8010
	s_mov_b32 m0, s3
	s_nop 0
	buffer_load_dwordx4 v72, s[8:11], s35 offen lds
	s_add_i32 s3, s2, 0xa010
	s_mov_b32 m0, s3
	s_nop 0
	buffer_load_dwordx4 v73, s[8:11], s35 offen lds
	s_add_i32 s3, s2, 0x1c010
	s_mov_b32 m0, s3
	s_nop 0
	buffer_load_dwordx4 v76, s[4:7], s44 offen lds
	s_add_i32 s2, s2, 0x1e010
	s_mov_b32 m0, s2
	s_nop 0
	buffer_load_dwordx4 v76, s[4:7], s45 offen lds

; #define G_WAIT_V(n) asm volatile("s_waitcnt vmcnt(" #n ")" ::: "memory")
; #define G_BAR() __builtin_amdgcn_s_barrier()
; #define D_STAGE_A(slot, half, kt) D_STAGE(rsA, voffA, slot, half, kt)
; #define D_STAGE_B(slot, half, kt) D_STAGE(rsB, voffB, slot, half, kt)
; #define D_STAGE_A(slot, half, kt) D_STAGE(rsA, voffA, slot, half, kt)
; #define D_STAGE_B(slot, half, kt) do { _Pragma("unroll") for (int _i = 0; _i < 2; ++_i) { const unsigned _m0 = ldsw + (unsigned)((slot) + _i * 8192); const unsigned _so = (unsigned)(kt) * 128u + (half) * bt_half + _i * bt_piece; \
;     asm volatile("s_mov_b32 m0, %0\n\ts_nop 4\n\tbuffer_load_dwordx4 %1, %2, %3 offen lds" :: "s"(_m0), "v"(voffB0), "s"(rsB), "s"(_so) : "m0", "memory"); } } while (0)
;   DI unsigned bt_rowoff(int h, int R) const { return (unsigned)(pn * 256 + 128 * h + (pn < 15 ? tcol_adj(R) : tcol_p64(R))) * 4096u; }
;   DI unsigned a_bytes() const { return (unsigned)NTOK * 4096u; }
;     ...
;   const unsigned bt_half = cfg.bt_rowoff(1, 0) - cfg.bt_rowoff(0, 0), bt_piece = cfg.bt_rowoff(0, 64) - cfg.bt_rowoff(0, 0);
;   const __amdgpu_buffer_rsrc_t rsA = __builtin_amdgcn_make_buffer_rsrc((void*)cfg.a_base(), 0, cfg.a_bytes(), 0x00020000);
;   const __amdgpu_buffer_rsrc_t rsB = __builtin_amdgcn_make_buffer_rsrc((void*)cfg.bt_base(), 0, cfg.bt_bytes(), 0x00020000);
;   const unsigned ldsw = (unsigned)__builtin_amdgcn_readfirstlane((int)(unsigned)(size_t)lds) + (unsigned)wid * 1024u;
;     ...
;   unsigned aoff[2], boff[2];
; #pragma unroll
;   for (int j = 0; j < 2; ++j) {
;     aoff[j] = (unsigned)(64 * wr + fr) * 128u + 16u * ((2u * fq + j) ^ ((unsigned)fr & 7u));
;     boff[j] = (unsigned)(32 * wc + fr) * 128u + 16u * ((2u * fq + j) ^ ((unsigned)fr & 7u));
;   }
;     ...
;   const int scw = cfg.scale_w(), scx = cfg.scale_x();
;     ...
;   f32x4 acc[2][2][4][2];
; #pragma unroll
;   for (int a = 0; a < 2; ++a)
; #pragma unroll
;     for (int b = 0; b < 2; ++b)
; #pragma unroll
;       for (int m = 0; m < 4; ++m)
; #pragma unroll
;         for (int n = 0; n < 2; ++n) acc[a][b][m][n] = (f32x4){0.f, 0.f, 0.f, 0.f};
;   i32x8 At[4], B0[2], B1[2];
;   if (!PRE) {
;     D_STAGE_B(G_SB(0, 0), 0, 0); D_STAGE_A(G_SA(0, 0), 0, 0); D_STAGE_B(G_SB(0, 1), 1, 0); D_STAGE_A(G_SA(0, 1), 1, 0);
;     D_STAGE_B(G_SB(1, 0), 0, 1); D_STAGE_A(G_SA(1, 0), 0, 1); D_STAGE_B(G_SB(1, 1), 1, 1);
;   }
;   G_WAIT_V(0); G_BAR();
.LBB0_1440:
	s_and_b32 s5, s4, 16
	s_waitcnt vmcnt(3)
	v_lshlrev_b32_e32 v3, 9, v8
	s_add_i32 s5, s5, s64
	v_and_or_b32 v64, v3, s36, v6
	s_waitcnt vmcnt(2)
	v_lshlrev_b32_e32 v3, 9, v7
	s_lshl_b32 s5, s5, 7
	s_and_b32 s4, s4, 0x1fffe0
	v_lshlrev_b32_e32 v2, 1, v2
	v_and_or_b32 v65, v3, s36, v6
	s_add_i32 s5, s5, s4
	v_and_b32_e32 v3, 3, v1
	v_and_b32_e32 v2, 24, v2
	s_ashr_i32 s17, s16, 31
	s_ashr_i32 s20, s15, 8
	v_or3_b32 v2, s5, v3, v2
	s_lshl_b64 s[4:5], s[16:17], 23
	s_add_u32 s4, s50, s4
	s_addc_u32 s5, s51, s5
	s_lshl_b32 s17, s74, 10
	s_add_i32 s75, s17, 0
	v_lshl_or_b32 v66, v2, 11, v6
	s_and_b32 s5, s5, 0xffff
	s_add_i32 s21, s75, 0x10010
	s_mov_b32 m0, s21
	s_nop 0
	buffer_load_dwordx4 v66, s[4:7], s34 offen lds
	s_add_i32 s39, s75, 0x12010
	s_mov_b32 m0, s39
	s_nop 0
	buffer_load_dwordx4 v66, s[4:7], s7 offen lds
	s_waitcnt vmcnt(1)
	v_lshlrev_b32_e32 v2, 9, v5
	s_add_i32 s60, s75, 16
	s_mov_b32 m0, s60
	s_nop 0
	buffer_load_dwordx4 v64, s[8:11], s34 offen lds
	v_and_or_b32 v67, v2, s36, v6
	s_add_i32 s61, s75, 0x2010
	s_mov_b32 m0, s61
	s_nop 0
	buffer_load_dwordx4 v67, s[8:11], s34 offen lds
	s_add_i32 s62, s75, 0x14010
	s_mov_b32 m0, s62
	s_nop 0
	buffer_load_dwordx4 v66, s[4:7], s37 offen lds
	s_add_i32 s63, s75, 0x16010
	s_mov_b32 m0, s63
	s_nop 0
	buffer_load_dwordx4 v66, s[4:7], s56 offen lds
	s_waitcnt vmcnt(0)
	v_lshlrev_b32_e32 v2, 9, v4
	s_add_i32 s66, s75, 0x4010
	s_mov_b32 m0, s66
	s_nop 0
	buffer_load_dwordx4 v65, s[8:11], s34 offen lds
	v_and_or_b32 v68, v2, s36, v6
	s_add_i32 s67, s75, 0x6010
	s_mov_b32 m0, s67
	s_nop 0
	buffer_load_dwordx4 v68, s[8:11], s34 offen lds
	s_add_i32 s68, s75, 0x18010
	s_mov_b32 m0, s68
	s_nop 0
	buffer_load_dwordx4 v66, s[4:7], s35 offen lds
	s_add_i32 s69, s75, 0x1a010
	s_mov_b32 m0, s69
	s_nop 0
	buffer_load_dwordx4 v66, s[4:7], s43 offen lds
	s_add_i32 s70, s75, 0x8010
	s_mov_b32 m0, s70
	s_nop 0
	buffer_load_dwordx4 v64, s[8:11], s35 offen lds
	s_add_i32 s71, s75, 0xa010
	s_mov_b32 m0, s71
	s_nop 0
	buffer_load_dwordx4 v67, s[8:11], s35 offen lds
	s_add_i32 s72, s75, 0x1c010
	s_mov_b32 m0, s72
	s_nop 0
	buffer_load_dwordx4 v66, s[4:7], s44 offen lds
	s_add_i32 s73, s75, 0x1e010
	s_mov_b32 m0, s73
	s_nop 0
	buffer_load_dwordx4 v66, s[4:7], s45 offen lds
	s_waitcnt vmcnt(0)
	s_cmp_lg_u32 s20, 1
	s_barrier
	s_cbranch_scc1 .LBB0_1442
	s_barrier

; #define G_WAIT_V(n) asm volatile("s_waitcnt vmcnt(" #n ")" ::: "memory")
; #define G_BAR() __builtin_amdgcn_s_barrier()
; #define G_SCHED() __builtin_amdgcn_sched_barrier(0)
; #define D_STAGE_A(slot, half, kt) D_STAGE(rsA, voffA, slot, half, kt)
; #define D_STAGE_B(slot, half, kt) D_STAGE(rsB, voffB, slot, half, kt)
; #define D_LDA(dst, slot) do { _Pragma("unroll") for (int m = 0; m < 4; ++m) _Pragma("unroll") for (int k = 0; k < 2; ++k) \
;     dst[m][k] = *(const LDS_AS bf16x8*)(lds + (slot) + aoff + m * 2048 + k * 1024); } while (0)
; #define D_LDB(dst, slot) do { _Pragma("unroll") for (int n = 0; n < 2; ++n) _Pragma("unroll") for (int k = 0; k < 2; ++k) \
;     dst[n][k] = *(const LDS_AS bf16x8*)(lds + (slot) + boff + n * 2048 + k * 1024); } while (0)
; #define D_MMA(ai, bj, At, Bf) do { __builtin_amdgcn_s_setprio(1); _Pragma("unroll") for (int m = 0; m < 4; ++m) _Pragma("unroll") for (int n = 0; n < 2; ++n) _Pragma("unroll") for (int k = 0; k < 2; ++k) \
;     acc[ai][bj][m][n] = __builtin_amdgcn_mfma_f32_16x16x32_bf16(Bf[n][k], At[m][k], acc[ai][bj][m][n], 0, 0, 0); __builtin_amdgcn_s_setprio(0); } while (0)
; #define D_WAIT_L(n) asm volatile("s_waitcnt lgkmcnt(" #n ")" ::: "memory")
; #define D_STAGE_A(slot, half, kt) D_STAGE(rsA, voffA, slot, half, kt)
;     ...
;   for (int t = 0; t < (F8_PEEL ? nt - 2 : nt); t += 2) {
;     const int t1 = t + 1;
;     const int t2 = (F8_PEEL || t + 2 < nt) ? t + 2 : t;
;     const int t3 = (F8_PEEL || t + 2 < nt) ? t + 3 : t + 1;
;     D_LDB(B0, G_SB(0, 0)); G_SCHED(); D_LDA(At, G_SA(0, 0)); D_STAGE_A(G_SA(1, 1), 1, t1);
;     D_WAIT_L(8); G_BAR(); D_WAIT_L(0); G_SCHED(); D_MMA(0, 0, At, B0); G_BAR(); G_SCHED();
;     D_LDB(B1, G_SB(0, 1)); D_STAGE_B(G_SB(0, 0), 0, t2);
;     G_BAR(); D_WAIT_L(0); G_SCHED(); D_MMA(0, 1, At, B1); G_BAR(); G_SCHED();
;     D_LDA(At, G_SA(0, 1)); D_STAGE_A(G_SA(0, 0), 0, t2);
;     G_BAR(); D_WAIT_L(0); G_SCHED(); D_MMA(1, 0, At, B0); G_BAR(); G_SCHED();
;     D_STAGE_B(G_SB(0, 1), 1, t2);
;     G_WAIT_V(6); G_BAR(); G_SCHED(); D_MMA(1, 1, At, B1); G_BAR(); G_SCHED();
;     D_LDB(B0, G_SB(1, 0)); G_SCHED(); D_LDA(At, G_SA(1, 0)); D_STAGE_A(G_SA(0, 1), 1, t2);
;     D_WAIT_L(8); G_BAR(); D_WAIT_L(0); G_SCHED(); D_MMA(0, 0, At, B0); G_BAR(); G_SCHED();
;     D_LDB(B1, G_SB(1, 1)); D_STAGE_B(G_SB(1, 0), 0, t3);
;     G_BAR(); D_WAIT_L(0); G_SCHED(); D_MMA(0, 1, At, B1); G_BAR(); G_SCHED();
.LBB0_1443:
	s_add_i32 s81, 0, 0x10010
	v_add_u32_e32 v73, s81, v69
	v_add_u32_e32 v86, s81, v70
	ds_read_b128 v[74:77], v73
	ds_read_b128 v[82:85], v73 offset:2048
	ds_read_b128 v[78:81], v86
	ds_read_b128 v[86:89], v86 offset:2048
	s_add_i32 s38, s79, 1
	s_add_i32 s78, s79, 3
	s_add_i32 s76, s79, 2
	s_add_i32 s86, 0, 0x14010
	s_cmp_lt_u32 s79, 14
	s_cselect_b32 s80, s76, s79
	s_cselect_b32 s38, s78, s38
	s_lshl_b32 s85, s80, 7
	s_lshl_b32 s80, s38, 7
	s_add_i32 s87, s85, 0x20000
	s_add_i32 s90, s85, 0x2000
	s_add_i32 s91, s85, 0x22000
	s_add_i32 s96, 0, 0x18010
	s_add_i32 s84, 0, 0x1c010
	s_add_i32 s83, s80, 0x20000
	s_add_i32 s82, s80, 0x2000
	s_add_i32 s81, s80, 0x22000
	s_add_i32 s78, s77, 0x100
	s_cmp_gt_u32 s79, 13
	ds_read_b128 v[90:93], v71 offset:16
	ds_read_b128 v[98:101], v71 offset:2064
	ds_read_b128 v[94:97], v72 offset:16
	ds_read_b128 v[102:105], v72 offset:2064
	ds_read_b128 v[106:109], v71 offset:4112
	ds_read_b128 v[114:117], v71 offset:6160
	ds_read_b128 v[110:113], v72 offset:4112
	ds_read_b128 v[118:121], v72 offset:6160
	s_mov_b32 m0, s74
	s_nop 0
	buffer_load_dwordx4 v65, s[8:11], s77 offen lds
	s_nop 0
	s_mov_b32 m0, s75
	s_nop 0
	buffer_load_dwordx4 v68, s[8:11], s77 offen lds
	s_waitcnt lgkmcnt(8)
	s_barrier
	s_waitcnt lgkmcnt(0)
	s_setprio 1
	s_waitcnt lgkmcnt(5)
	v_mfma_scale_f32_16x16x128_f8f6f4 v[56:59], v[74:81], v[90:97], v[56:59], v149, v148 op_sel_hi:[0,0,0]
	v_mfma_scale_f32_16x16x128_f8f6f4 v[60:63], v[82:89], v[90:97], v[60:63], v149, v148 op_sel_hi:[0,0,0]
	s_waitcnt lgkmcnt(4)
	v_mfma_scale_f32_16x16x128_f8f6f4 v[44:47], v[74:81], v[98:105], v[44:47], v149, v148 op_sel_hi:[0,0,0]
	v_mfma_scale_f32_16x16x128_f8f6f4 v[40:43], v[82:89], v[98:105], v[40:43], v149, v148 op_sel_hi:[0,0,0]
	s_waitcnt lgkmcnt(1)
	v_mfma_scale_f32_16x16x128_f8f6f4 v[122:125], v[74:81], v[106:113], v[28:31], v149, v148 op_sel_hi:[0,0,0]
	v_mfma_scale_f32_16x16x128_f8f6f4 v[126:129], v[82:89], v[106:113], v[24:27], v149, v148 op_sel_hi:[0,0,0]
	s_waitcnt lgkmcnt(0)
	v_mfma_scale_f32_16x16x128_f8f6f4 v[130:133], v[74:81], v[114:121], v[12:15], v149, v148 op_sel_hi:[0,0,0]
	v_mfma_scale_f32_16x16x128_f8f6f4 v[134:137], v[82:89], v[114:121], v[8:11], v149, v148 op_sel_hi:[0,0,0]
	s_setprio 0
	s_barrier
	s_nop 3
	v_add_u32_e32 v12, s86, v69
	v_add_u32_e32 v28, s86, v70
	ds_read_b128 v[8:11], v12
	ds_read_b128 v[24:27], v12 offset:2048
	ds_read_b128 v[12:15], v28
	ds_read_b128 v[28:31], v28 offset:2048
	s_mov_b32 m0, s21
	s_nop 0
	buffer_load_dwordx4 v66, s[4:7], s85 offen lds
	s_nop 0
	s_mov_b32 m0, s39
	s_nop 0
	buffer_load_dwordx4 v66, s[4:7], s87 offen lds
	s_barrier
	s_waitcnt lgkmcnt(0)
	s_setprio 1
	s_waitcnt lgkmcnt(1)
	v_mfma_scale_f32_16x16x128_f8f6f4 v[52:55], v[8:15], v[90:97], v[52:55], v149, v148 op_sel_hi:[0,0,0]
	s_waitcnt lgkmcnt(0)
	v_mfma_scale_f32_16x16x128_f8f6f4 v[48:51], v[24:31], v[90:97], v[48:51], v149, v148 op_sel_hi:[0,0,0]
	v_mfma_scale_f32_16x16x128_f8f6f4 v[138:141], v[8:15], v[98:105], v[36:39], v149, v148 op_sel_hi:[0,0,0]
	v_mfma_scale_f32_16x16x128_f8f6f4 v[142:145], v[24:31], v[98:105], v[32:35], v149, v148 op_sel_hi:[0,0,0]
	v_mfma_scale_f32_16x16x128_f8f6f4 v[152:155], v[8:15], v[106:113], v[20:23], v149, v148 op_sel_hi:[0,0,0]
	v_mfma_scale_f32_16x16x128_f8f6f4 v[106:109], v[24:31], v[106:113], v[16:19], v149, v148 op_sel_hi:[0,0,0]
	v_mfma_scale_f32_16x16x128_f8f6f4 v[110:113], v[8:15], v[114:121], v[4:7], v149, v148 op_sel_hi:[0,0,0]
	v_mfma_scale_f32_16x16x128_f8f6f4 v[114:117], v[24:31], v[114:121], v[0:3], v149, v148 op_sel_hi:[0,0,0]
	s_setprio 0
	s_barrier
	s_mov_b32 m0, s60
	s_nop 0
	buffer_load_dwordx4 v64, s[8:11], s85 offen lds
	s_nop 0
	s_mov_b32 m0, s61
	s_nop 0
	buffer_load_dwordx4 v67, s[8:11], s85 offen lds
	s_barrier
	s_waitcnt lgkmcnt(0)
	s_barrier
	s_mov_b32 m0, s62
	s_nop 0
	buffer_load_dwordx4 v66, s[4:7], s90 offen lds
	s_nop 0
	s_mov_b32 m0, s63
	s_nop 0
	buffer_load_dwordx4 v66, s[4:7], s91 offen lds
	s_waitcnt vmcnt(6)
	s_barrier
	s_barrier
	v_add_u32_e32 v4, s96, v69
	v_add_u32_e32 v8, s96, v70
	ds_read_b128 v[0:3], v4
	ds_read_b128 v[16:19], v4 offset:2048
	ds_read_b128 v[4:7], v8
	ds_read_b128 v[20:23], v8 offset:2048
	ds_read_b128 v[32:35], v71 offset:32784
	ds_read_b128 v[74:77], v71 offset:34832
	ds_read_b128 v[36:39], v72 offset:32784
	ds_read_b128 v[78:81], v72 offset:34832
	ds_read_b128 v[82:85], v71 offset:36880
	ds_read_b128 v[90:93], v71 offset:38928
	ds_read_b128 v[86:89], v72 offset:36880
	ds_read_b128 v[94:97], v72 offset:38928
	s_mov_b32 m0, s66
	s_nop 0
	buffer_load_dwordx4 v65, s[8:11], s85 offen lds
	s_nop 0
	s_mov_b32 m0, s67
	s_nop 0
	buffer_load_dwordx4 v68, s[8:11], s85 offen lds
	s_waitcnt lgkmcnt(8)
	s_barrier
; #define LDS_AS __attribute__((address_space(3)))
; #define OPAQUE_TID(P) (((P).wid0 << 6) | lane_id_now())
; #define G_WAIT_V(n) asm volatile("s_waitcnt vmcnt(" #n ")" ::: "memory")
; #define G_BAR() __builtin_amdgcn_s_barrier()
; #define G_SCHED() __builtin_amdgcn_sched_barrier(0)
; #define D_STAGE_A(slot, half, kt) D_STAGE(rsA, voffA, slot, half, kt)
; #define D_STAGE_B(slot, half, kt) D_STAGE(rsB, voffB, slot, half, kt)
; #define D_LDA(dst, slot) do { _Pragma("unroll") for (int m = 0; m < 4; ++m) _Pragma("unroll") for (int k = 0; k < 2; ++k) \
;     dst[m][k] = *(const LDS_AS bf16x8*)(lds + (slot) + aoff + m * 2048 + k * 1024); } while (0)
; template <class Cfg>
; DI void f8dma_issue_prologue_st(LDS_AS unsigned char* lds, const Cfg& cfg) {
;   const int tid = OPAQUE_TID(cfg.p), wid = __builtin_amdgcn_readfirstlane(tid >> 6), lane = tid & 63;
;   const LDS_AS unsigned* stash = (const LDS_AS unsigned*)(lds + F8_STASH);
;   unsigned voffA[2][2], voffB0;
;   voffA[0][0] = stash[tid]; voffA[0][1] = stash[512 + tid]; voffA[1][0] = stash[1024 + tid]; voffA[1][1] = stash[1536 + tid];
;   {
;     const int r = 8 * wid + (lane >> 3);
;     const unsigned cofs = 16u * (((unsigned)lane & 7u) ^ (((unsigned)lane >> 3) & 7u));
;     voffB0 = cfg.bt_rowoff(0, r) + cofs;
;   }
;   const unsigned bt_half = cfg.bt_rowoff(1, 0) - cfg.bt_rowoff(0, 0), bt_piece = cfg.bt_rowoff(0, 64) - cfg.bt_rowoff(0, 0);
;   const __amdgpu_buffer_rsrc_t rsA = __builtin_amdgcn_make_buffer_rsrc((void*)cfg.a_base(), 0, cfg.a_bytes(), 0x00020000);
;   const __amdgpu_buffer_rsrc_t rsB = __builtin_amdgcn_make_buffer_rsrc((void*)cfg.bt_base(), 0, cfg.bt_bytes(), 0x00020000);
;   const unsigned ldsw = (unsigned)__builtin_amdgcn_readfirstlane((int)(unsigned)(size_t)lds) + (unsigned)wid * 1024u;
;     ...
;   P_STAGE_B(G_SB(0, 0), 0, 0); P_STAGE_A(G_SA(0, 0), 0, 0); P_STAGE_B(G_SB(0, 1), 1, 0); P_STAGE_A(G_SA(0, 1), 1, 0);
;   P_STAGE_B(G_SB(1, 0), 0, 1); P_STAGE_A(G_SA(1, 0), 0, 1); P_STAGE_B(G_SB(1, 1), 1, 1);
;     ...
;     G_BAR(); D_WAIT_L(0); G_SCHED(); D_MMA(0, 1, At, B1); G_BAR(); G_SCHED();
;     D_LDA(At, G_SA(1, 1)); D_STAGE_A(G_SA(1, 0), 0, t3);
;     G_BAR(); D_WAIT_L(0); G_SCHED(); D_MMA(1, 0, At, B0); G_BAR(); G_SCHED();
;     D_STAGE_B(G_SB(1, 1), 1, t3);
;     G_WAIT_V(6); G_BAR(); G_SCHED(); D_MMA(1, 1, At, B1); G_BAR(); G_SCHED();
;   }
;   if (!F8_PEEL) G_WAIT_V(0);
	s_waitcnt lgkmcnt(0)
	s_setprio 1
	s_waitcnt lgkmcnt(5)
	v_mfma_scale_f32_16x16x128_f8f6f4 v[56:59], v[0:7], v[32:39], v[56:59], v149, v148 op_sel_hi:[0,0,0]
	v_mfma_scale_f32_16x16x128_f8f6f4 v[60:63], v[16:23], v[32:39], v[60:63], v149, v148 op_sel_hi:[0,0,0]
	s_waitcnt lgkmcnt(4)
	v_mfma_scale_f32_16x16x128_f8f6f4 v[44:47], v[0:7], v[74:81], v[44:47], v149, v148 op_sel_hi:[0,0,0]
	v_mfma_scale_f32_16x16x128_f8f6f4 v[40:43], v[16:23], v[74:81], v[40:43], v149, v148 op_sel_hi:[0,0,0]
	s_waitcnt lgkmcnt(1)
	v_mfma_scale_f32_16x16x128_f8f6f4 v[28:31], v[0:7], v[82:89], v[122:125], v149, v148 op_sel_hi:[0,0,0]
	v_mfma_scale_f32_16x16x128_f8f6f4 v[24:27], v[16:23], v[82:89], v[126:129], v149, v148 op_sel_hi:[0,0,0]
	s_waitcnt lgkmcnt(0)
	v_mfma_scale_f32_16x16x128_f8f6f4 v[12:15], v[0:7], v[90:97], v[130:133], v149, v148 op_sel_hi:[0,0,0]
	v_mfma_scale_f32_16x16x128_f8f6f4 v[8:11], v[16:23], v[90:97], v[134:137], v149, v148 op_sel_hi:[0,0,0]
	s_setprio 0
	s_barrier
	v_add_u32_e32 v4, s84, v69
	v_add_u32_e32 v16, s84, v70
	ds_read_b128 v[0:3], v4
	ds_read_b128 v[98:101], v4 offset:2048
	ds_read_b128 v[4:7], v16
	ds_read_b128 v[102:105], v16 offset:2048
	s_mov_b32 m0, s68
	s_nop 0
	buffer_load_dwordx4 v66, s[4:7], s80 offen lds
	s_nop 0
	s_mov_b32 m0, s69
	s_nop 0
	buffer_load_dwordx4 v66, s[4:7], s83 offen lds
	s_barrier
	s_waitcnt lgkmcnt(0)
	s_setprio 1
	s_waitcnt lgkmcnt(1)
	v_mfma_scale_f32_16x16x128_f8f6f4 v[52:55], v[0:7], v[32:39], v[52:55], v149, v148 op_sel_hi:[0,0,0]
	s_waitcnt lgkmcnt(0)
	v_mfma_scale_f32_16x16x128_f8f6f4 v[48:51], v[98:105], v[32:39], v[48:51], v149, v148 op_sel_hi:[0,0,0]
	v_mfma_scale_f32_16x16x128_f8f6f4 v[36:39], v[0:7], v[74:81], v[138:141], v149, v148 op_sel_hi:[0,0,0]
	v_mfma_scale_f32_16x16x128_f8f6f4 v[32:35], v[98:105], v[74:81], v[142:145], v149, v148 op_sel_hi:[0,0,0]
	v_mfma_scale_f32_16x16x128_f8f6f4 v[20:23], v[0:7], v[82:89], v[152:155], v149, v148 op_sel_hi:[0,0,0]
	v_mfma_scale_f32_16x16x128_f8f6f4 v[16:19], v[98:105], v[82:89], v[106:109], v149, v148 op_sel_hi:[0,0,0]
	v_mfma_scale_f32_16x16x128_f8f6f4 v[4:7], v[0:7], v[90:97], v[110:113], v149, v148 op_sel_hi:[0,0,0]
	v_mfma_scale_f32_16x16x128_f8f6f4 v[0:3], v[98:105], v[90:97], v[114:117], v149, v148 op_sel_hi:[0,0,0]
	s_setprio 0
	s_barrier
	s_mov_b32 m0, s70
	s_nop 0
	buffer_load_dwordx4 v64, s[8:11], s80 offen lds
	s_nop 0
	s_mov_b32 m0, s71
	s_nop 0
	buffer_load_dwordx4 v67, s[8:11], s80 offen lds
	s_barrier
	s_waitcnt lgkmcnt(0)
	s_barrier
	s_mov_b32 m0, s72
	s_nop 0
	buffer_load_dwordx4 v66, s[4:7], s82 offen lds
	s_nop 0
	s_mov_b32 m0, s73
	s_nop 0
	buffer_load_dwordx4 v66, s[4:7], s81 offen lds
	s_waitcnt vmcnt(6)
	s_barrier
	s_barrier
	s_mov_b32 s77, s78
	s_mov_b32 s79, s76
	s_cbranch_scc0 .LBB0_1443
	s_waitcnt vmcnt(0)
	s_cmpk_lt_u32 s15, 0x100
	s_cbranch_scc0 .LBB0_1446
	s_barrier
.LBB0_1446:
	s_and_b64 vcc, exec, s[2:3]
	v_readlane_b32 s87, v255, 12
	s_cbranch_vccnz .LBB0_1448
	v_mbcnt_lo_u32_b32 v68, -1, 0
	v_mbcnt_hi_u32_b32 v68, -1, v68
	s_ashr_i32 s15, s14, 31
	v_or_b32_e32 v64, s87, v68
	v_lshrrev_b32_e32 v69, 3, v68
	v_readfirstlane_b32 s2, v64
	s_ashr_i32 s21, s2, 6
	s_lshl_b32 s2, s21, 3
	s_and_b32 s3, s2, 16
	v_and_or_b32 v70, v69, 4, s2
	s_add_i32 s3, s3, s48
	s_lshl_b32 s3, s3, 7
	s_and_b32 s2, s2, 0x1fffe0
	v_lshlrev_b32_e32 v70, 1, v70
	v_xor_b32_e32 v69, v69, v68
	s_add_i32 s3, s3, s2
	v_and_b32_e32 v70, 24, v70
	v_bfe_u32 v68, v68, 3, 2
	v_or3_b32 v68, s3, v70, v68
	s_lshl_b64 s[2:3], s[14:15], 23
	v_lshl_add_u32 v64, v64, 2, 0
	s_add_u32 s4, s50, s2
	v_add_u32_e32 v66, 0x22410, v64
	s_addc_u32 s2, s51, s3
	ds_read2st64_b32 v[64:65], v66 offset1:8
	ds_read2st64_b32 v[66:67], v66 offset0:16 offset1:24
	v_lshlrev_b32_e32 v69, 4, v69
	s_and_b32 s5, s2, 0xffff
	s_lshl_b32 s2, s21, 10
	v_and_b32_e32 v69, 0x70, v69
	s_add_i32 s2, s2, 0
	v_lshl_or_b32 v68, v68, 11, v69
	s_add_i32 s3, s2, 0x10010
	s_mov_b32 m0, s3
	s_nop 0
	buffer_load_dwordx4 v68, s[4:7], s34 offen lds
	s_add_i32 s3, s2, 0x12010
	s_mov_b32 m0, s3
	s_nop 0
	buffer_load_dwordx4 v68, s[4:7], s7 offen lds
	s_add_i32 s3, s2, 16
	s_waitcnt lgkmcnt(1)
	s_mov_b32 m0, s3
	s_nop 0
	buffer_load_dwordx4 v64, s[8:11], s34 offen lds
	s_add_i32 s3, s2, 0x2010
	s_mov_b32 m0, s3
	s_nop 0
	buffer_load_dwordx4 v65, s[8:11], s34 offen lds
	s_add_i32 s3, s2, 0x14010
	s_mov_b32 m0, s3
	s_nop 0
	buffer_load_dwordx4 v68, s[4:7], s37 offen lds
	s_add_i32 s3, s2, 0x16010
	s_mov_b32 m0, s3
	s_nop 0
	buffer_load_dwordx4 v68, s[4:7], s56 offen lds
	s_add_i32 s3, s2, 0x4010
	s_waitcnt lgkmcnt(0)
	s_mov_b32 m0, s3
	s_nop 0
	buffer_load_dwordx4 v66, s[8:11], s34 offen lds
	s_add_i32 s3, s2, 0x6010
	s_mov_b32 m0, s3
	s_nop 0
	buffer_load_dwordx4 v67, s[8:11], s34 offen lds
	s_add_i32 s3, s2, 0x18010
	s_mov_b32 m0, s3
	s_nop 0
	buffer_load_dwordx4 v68, s[4:7], s35 offen lds
	s_add_i32 s3, s2, 0x1a010
	s_mov_b32 m0, s3
	s_nop 0
	buffer_load_dwordx4 v68, s[4:7], s43 offen lds
	s_add_i32 s3, s2, 0x8010
	s_mov_b32 m0, s3
	s_nop 0
	buffer_load_dwordx4 v64, s[8:11], s35 offen lds
	s_add_i32 s3, s2, 0xa010
	s_mov_b32 m0, s3
	s_nop 0
	buffer_load_dwordx4 v65, s[8:11], s35 offen lds
	s_add_i32 s3, s2, 0x1c010
	s_mov_b32 m0, s3
	s_nop 0
	buffer_load_dwordx4 v68, s[4:7], s44 offen lds
	s_add_i32 s2, s2, 0x1e010
	s_mov_b32 m0, s2
	s_nop 0
	buffer_load_dwordx4 v68, s[4:7], s45 offen lds

; #define G_WAIT_V(n) asm volatile("s_waitcnt vmcnt(" #n ")" ::: "memory")
; #define G_BAR() __builtin_amdgcn_s_barrier()
; #define G_SCHED() __builtin_amdgcn_sched_barrier(0)
; #define D_STAGE_A(slot, half, kt) D_STAGE(rsA, voffA, slot, half, kt)
; #define D_STAGE_B(slot, half, kt) D_STAGE(rsB, voffB, slot, half, kt)
; #define D_LDA(dst, slot) do { _Pragma("unroll") for (int m = 0; m < 4; ++m) _Pragma("unroll") for (int k = 0; k < 2; ++k) \
;     dst[m][k] = *(const LDS_AS bf16x8*)(lds + (slot) + aoff + m * 2048 + k * 1024); } while (0)
; #define D_LDB(dst, slot) do { _Pragma("unroll") for (int n = 0; n < 2; ++n) _Pragma("unroll") for (int k = 0; k < 2; ++k) \
;     dst[n][k] = *(const LDS_AS bf16x8*)(lds + (slot) + boff + n * 2048 + k * 1024); } while (0)
; #define D_MMA(ai, bj, At, Bf) do { __builtin_amdgcn_s_setprio(1); _Pragma("unroll") for (int m = 0; m < 4; ++m) _Pragma("unroll") for (int n = 0; n < 2; ++n) _Pragma("unroll") for (int k = 0; k < 2; ++k) \
;     acc[ai][bj][m][n] = __builtin_amdgcn_mfma_f32_16x16x32_bf16(Bf[n][k], At[m][k], acc[ai][bj][m][n], 0, 0, 0); __builtin_amdgcn_s_setprio(0); } while (0)
; #define D_WAIT_L(n) asm volatile("s_waitcnt lgkmcnt(" #n ")" ::: "memory")
; #define D_STAGE_A(slot, half, kt) D_STAGE(rsA, voffA, slot, half, kt)
; #define D_WAIT_L(n) asm volatile("s_waitcnt lgkmcnt(" #n ")" ::: "memory")
;     ...
;   for (int t = 0; t < (F8_PEEL ? nt - 2 : nt); t += 2) {
;     const int t1 = t + 1;
;     const int t2 = (F8_PEEL || t + 2 < nt) ? t + 2 : t;
;     const int t3 = (F8_PEEL || t + 2 < nt) ? t + 3 : t + 1;
;     D_LDB(B0, G_SB(0, 0)); G_SCHED(); D_LDA(At, G_SA(0, 0)); D_STAGE_A(G_SA(1, 1), 1, t1);
;     D_WAIT_L(8); G_BAR(); D_WAIT_L(0); G_SCHED(); D_MMA(0, 0, At, B0); G_BAR(); G_SCHED();
;     D_LDB(B1, G_SB(0, 1)); D_STAGE_B(G_SB(0, 0), 0, t2);
;     G_BAR(); D_WAIT_L(0); G_SCHED(); D_MMA(0, 1, At, B1); G_BAR(); G_SCHED();
;     D_LDA(At, G_SA(0, 1)); D_STAGE_A(G_SA(0, 0), 0, t2);
;     G_BAR(); D_WAIT_L(0); G_SCHED(); D_MMA(1, 0, At, B0); G_BAR(); G_SCHED();
;     D_STAGE_B(G_SB(0, 1), 1, t2);
;     G_WAIT_V(6); G_BAR(); G_SCHED(); D_MMA(1, 1, At, B1); G_BAR(); G_SCHED();
.LBB0_1483:
	s_add_i32 s77, 0, 0x10010
	v_add_u32_e32 v72, s77, v124
	v_add_u32_e32 v73, s77, v125
	ds_read_b128 v[152:155], v72
	ds_read_b128 v[160:163], v72 offset:2048
	ds_read_b128 v[156:159], v73
	ds_read_b128 v[164:167], v73 offset:2048
	s_add_i32 s38, s73, 1
	s_add_i32 s75, s73, 3
	s_add_i32 s74, s73, 2
	s_add_i32 s85, 0, 0x14010
	s_cmp_lt_u32 s73, 14
	s_cselect_b32 s76, s74, s73
	s_cselect_b32 s38, s75, s38
	s_lshl_b32 s81, s76, 7
	s_lshl_b32 s76, s38, 7
	s_add_i32 s86, s81, 0x20000
	s_add_i32 s83, s81, 0x2000
	s_add_i32 s84, s81, 0x22000
	s_add_i32 s82, 0, 0x18010
	s_add_i32 s80, 0, 0x1c010
	s_add_i32 s79, s76, 0x20000
	s_add_i32 s77, s76, 0x2000
	s_add_i32 s78, s76, 0x22000
	s_add_i32 s75, s72, 0x100
	s_cmp_gt_u32 s73, 13
	ds_read_b128 v[168:171], v127 offset:16
	ds_read_b128 v[176:179], v127 offset:2064
	ds_read_b128 v[172:175], v128 offset:16
	ds_read_b128 v[180:183], v128 offset:2064
	ds_read_b128 v[192:195], v127 offset:4112
	ds_read_b128 v[200:203], v127 offset:6160
	ds_read_b128 v[196:199], v128 offset:4112
	ds_read_b128 v[204:207], v128 offset:6160
	s_waitcnt lgkmcnt(12)
	s_mov_b32 m0, s26
	s_nop 0
	buffer_load_dwordx4 v122, s[8:11], s72 offen lds
	s_nop 0
	s_mov_b32 m0, s62
	s_nop 0
	buffer_load_dwordx4 v123, s[8:11], s72 offen lds
	s_waitcnt lgkmcnt(8)
	s_barrier
	s_waitcnt lgkmcnt(0)
	s_setprio 1
	s_waitcnt lgkmcnt(5)
	v_mfma_scale_f32_16x16x128_f8f6f4 v[134:137], v[160:167], v[168:175], v[136:139], v149, v148 op_sel_hi:[0,0,0]
	s_waitcnt lgkmcnt(0)
	v_mfma_scale_f32_16x16x128_f8f6f4 v[220:223], v[152:159], v[200:207], v[220:223], v149, v148 op_sel_hi:[0,0,0]
	v_mfma_scale_f32_16x16x128_f8f6f4 v[224:227], v[160:167], v[200:207], v[224:227], v149, v148 op_sel_hi:[0,0,0]
	v_mfma_scale_f32_16x16x128_f8f6f4 v[130:133], v[152:159], v[168:175], v[140:143], v149, v148 op_sel_hi:[0,0,0]
	v_mfma_scale_f32_16x16x128_f8f6f4 v[184:187], v[152:159], v[176:183], v[108:111], v149, v148 op_sel_hi:[0,0,0]
	v_mfma_scale_f32_16x16x128_f8f6f4 v[208:211], v[160:167], v[176:183], v[104:107], v149, v148 op_sel_hi:[0,0,0]
	v_mfma_scale_f32_16x16x128_f8f6f4 v[212:215], v[152:159], v[192:199], v[92:95], v149, v148 op_sel_hi:[0,0,0]
	v_mfma_scale_f32_16x16x128_f8f6f4 v[216:219], v[160:167], v[192:199], v[88:91], v149, v148 op_sel_hi:[0,0,0]
	s_setprio 0
	s_barrier
	v_add_u32_e32 v76, s85, v124
	v_add_u32_e32 v80, s85, v125
	ds_read_b128 v[72:75], v76
	s_nop 1
	ds_read_b128 v[88:91], v76 offset:2048
	ds_read_b128 v[76:79], v80
	ds_read_b128 v[92:95], v80 offset:2048
	s_mov_b32 m0, s27
	s_nop 0
	buffer_load_dwordx4 v126, s[4:7], s81 offen lds
	s_nop 0
	s_mov_b32 m0, s63
	s_nop 0
	buffer_load_dwordx4 v126, s[4:7], s86 offen lds
	s_barrier
	s_waitcnt lgkmcnt(0)
	s_setprio 1
	s_waitcnt lgkmcnt(1)
	v_mfma_scale_f32_16x16x128_f8f6f4 v[68:71], v[72:79], v[200:207], v[68:71], v149, v148 op_sel_hi:[0,0,0]
	s_waitcnt lgkmcnt(0)
	v_mfma_scale_f32_16x16x128_f8f6f4 v[56:59], v[88:95], v[200:207], v[56:59], v149, v148 op_sel_hi:[0,0,0]
	v_mfma_scale_f32_16x16x128_f8f6f4 v[228:231], v[72:79], v[168:175], v[116:119], v149, v148 op_sel_hi:[0,0,0]
	v_mfma_scale_f32_16x16x128_f8f6f4 v[168:171], v[88:95], v[168:175], v[112:115], v149, v148 op_sel_hi:[0,0,0]
	v_mfma_scale_f32_16x16x128_f8f6f4 v[172:175], v[72:79], v[176:183], v[100:103], v149, v148 op_sel_hi:[0,0,0]
	v_mfma_scale_f32_16x16x128_f8f6f4 v[176:179], v[88:95], v[176:183], v[96:99], v149, v148 op_sel_hi:[0,0,0]
	v_mfma_scale_f32_16x16x128_f8f6f4 v[180:183], v[72:79], v[192:199], v[84:87], v149, v148 op_sel_hi:[0,0,0]
	v_mfma_scale_f32_16x16x128_f8f6f4 v[192:195], v[88:95], v[192:199], v[8:11], v149, v148 op_sel_hi:[0,0,0]
	s_setprio 0
	s_barrier
	ds_read_b128 v[80:83], v127 offset:16400
	s_nop 1
	ds_read_b128 v[96:99], v127 offset:18448
	ds_read_b128 v[84:87], v128 offset:16400
	ds_read_b128 v[100:103], v128 offset:18448
	ds_read_b128 v[104:107], v127 offset:20496
	ds_read_b128 v[112:115], v127 offset:22544
	ds_read_b128 v[108:111], v128 offset:20496
	ds_read_b128 v[116:119], v128 offset:22544
	s_mov_b32 m0, s17
	s_nop 0
	buffer_load_dwordx4 v120, s[8:11], s81 offen lds
	s_nop 0
	s_mov_b32 m0, s66
	s_nop 0
	buffer_load_dwordx4 v121, s[8:11], s81 offen lds
	s_barrier
	s_waitcnt lgkmcnt(0)
	s_setprio 1
	s_waitcnt lgkmcnt(5)
	v_mfma_scale_f32_16x16x128_f8f6f4 v[64:67], v[152:159], v[80:87], v[64:67], v149, v148 op_sel_hi:[0,0,0]
	v_mfma_scale_f32_16x16x128_f8f6f4 v[60:63], v[160:167], v[80:87], v[60:63], v149, v148 op_sel_hi:[0,0,0]
	s_waitcnt lgkmcnt(0)
	v_mfma_scale_f32_16x16x128_f8f6f4 v[244:247], v[160:167], v[112:119], v[244:247], v149, v148 op_sel_hi:[0,0,0]
	v_mfma_scale_f32_16x16x128_f8f6f4 v[200:203], v[152:159], v[96:103], v[44:47], v149, v148 op_sel_hi:[0,0,0]
	v_mfma_scale_f32_16x16x128_f8f6f4 v[204:207], v[160:167], v[96:103], v[40:43], v149, v148 op_sel_hi:[0,0,0]
	v_mfma_scale_f32_16x16x128_f8f6f4 v[232:235], v[152:159], v[104:111], v[28:31], v149, v148 op_sel_hi:[0,0,0]
	v_mfma_scale_f32_16x16x128_f8f6f4 v[236:239], v[160:167], v[104:111], v[24:27], v149, v148 op_sel_hi:[0,0,0]
	v_mfma_scale_f32_16x16x128_f8f6f4 v[240:243], v[152:159], v[112:119], v[12:15], v149, v148 op_sel_hi:[0,0,0]
	s_setprio 0
	s_barrier
	s_mov_b32 m0, s28
	s_nop 0
	buffer_load_dwordx4 v126, s[4:7], s83 offen lds
	s_nop 0
	s_mov_b32 m0, s67
	s_nop 0
	buffer_load_dwordx4 v126, s[4:7], s84 offen lds
	s_waitcnt vmcnt(6)
	s_barrier
; #define G_WAIT_V(n) asm volatile("s_waitcnt vmcnt(" #n ")" ::: "memory")
; #define G_BAR() __builtin_amdgcn_s_barrier()
; #define G_SCHED() __builtin_amdgcn_sched_barrier(0)
; #define D_STAGE_A(slot, half, kt) D_STAGE(rsA, voffA, slot, half, kt)
; #define D_STAGE_B(slot, half, kt) D_STAGE(rsB, voffB, slot, half, kt)
; #define D_LDA(dst, slot) do { _Pragma("unroll") for (int m = 0; m < 4; ++m) _Pragma("unroll") for (int k = 0; k < 2; ++k) \
;     dst[m][k] = *(const LDS_AS bf16x8*)(lds + (slot) + aoff + m * 2048 + k * 1024); } while (0)
; #define D_LDB(dst, slot) do { _Pragma("unroll") for (int n = 0; n < 2; ++n) _Pragma("unroll") for (int k = 0; k < 2; ++k) \
;     dst[n][k] = *(const LDS_AS bf16x8*)(lds + (slot) + boff + n * 2048 + k * 1024); } while (0)
; #define D_MMA(ai, bj, At, Bf) do { __builtin_amdgcn_s_setprio(1); _Pragma("unroll") for (int m = 0; m < 4; ++m) _Pragma("unroll") for (int n = 0; n < 2; ++n) _Pragma("unroll") for (int k = 0; k < 2; ++k) \
;     acc[ai][bj][m][n] = __builtin_amdgcn_mfma_f32_16x16x32_bf16(Bf[n][k], At[m][k], acc[ai][bj][m][n], 0, 0, 0); __builtin_amdgcn_s_setprio(0); } while (0)
; #define D_WAIT_L(n) asm volatile("s_waitcnt lgkmcnt(" #n ")" ::: "memory")
; #define D_STAGE_A(slot, half, kt) D_STAGE(rsA, voffA, slot, half, kt)
; #define D_STAGE_B(slot, half, kt) do { _Pragma("unroll") for (int _i = 0; _i < 2; ++_i) { const unsigned _m0 = ldsw + (unsigned)((slot) + _i * 8192); const unsigned _so = (unsigned)(kt) * 128u + (half) * bt_half + _i * bt_piece; \
;     asm volatile("s_mov_b32 m0, %0\n\ts_nop 4\n\tbuffer_load_dwordx4 %1, %2, %3 offen lds" :: "s"(_m0), "v"(voffB0), "s"(rsB), "s"(_so) : "m0", "memory"); } } while (0)
;     ...
;     G_WAIT_V(6); G_BAR(); G_SCHED(); D_MMA(1, 1, At, B1); G_BAR(); G_SCHED();
;     D_LDB(B0, G_SB(1, 0)); G_SCHED(); D_LDA(At, G_SA(1, 0)); D_STAGE_A(G_SA(0, 1), 1, t2);
;     D_WAIT_L(8); G_BAR(); D_WAIT_L(0); G_SCHED(); D_MMA(0, 0, At, B0); G_BAR(); G_SCHED();
;     D_LDB(B1, G_SB(1, 1)); D_STAGE_B(G_SB(1, 0), 0, t3);
;     G_BAR(); D_WAIT_L(0); G_SCHED(); D_MMA(0, 1, At, B1); G_BAR(); G_SCHED();
;     D_LDA(At, G_SA(1, 1)); D_STAGE_A(G_SA(1, 0), 0, t3);
;     G_BAR(); D_WAIT_L(0); G_SCHED(); D_MMA(1, 0, At, B0); G_BAR(); G_SCHED();
;     D_STAGE_B(G_SB(1, 1), 1, t3);
;     G_WAIT_V(6); G_BAR(); G_SCHED(); D_MMA(1, 1, At, B1); G_BAR(); G_SCHED();
;   }
;   if (!F8_PEEL) G_WAIT_V(0);
	s_setprio 1
	v_mfma_scale_f32_16x16x128_f8f6f4 v[52:55], v[72:79], v[80:87], v[52:55], v149, v148 op_sel_hi:[0,0,0]
	v_mfma_scale_f32_16x16x128_f8f6f4 v[48:51], v[88:95], v[80:87], v[48:51], v149, v148 op_sel_hi:[0,0,0]
	v_mfma_scale_f32_16x16x128_f8f6f4 v[248:251], v[72:79], v[96:103], v[36:39], v149, v148 op_sel_hi:[0,0,0]
	v_mfma_scale_f32_16x16x128_f8f6f4 v[188:191], v[88:95], v[96:103], v[32:35], v149, v148 op_sel_hi:[0,0,0]
	v_mfma_scale_f32_16x16x128_f8f6f4 v[144:147], v[72:79], v[104:111], v[20:23], v149, v148 op_sel_hi:[0,0,0]
	v_mfma_scale_f32_16x16x128_f8f6f4 v[80:83], v[88:95], v[104:111], v[16:19], v149, v148 op_sel_hi:[0,0,0]
	v_mfma_scale_f32_16x16x128_f8f6f4 v[72:75], v[72:79], v[112:119], v[4:7], v149, v148 op_sel_hi:[0,0,0]
	v_mfma_scale_f32_16x16x128_f8f6f4 v[76:79], v[88:95], v[112:119], v[0:3], v149, v148 op_sel_hi:[0,0,0]
	s_setprio 0
	s_barrier
	s_nop 3
	v_add_u32_e32 v4, s82, v124
	v_add_u32_e32 v8, s82, v125
	ds_read_b128 v[0:3], v4
	ds_read_b128 v[16:19], v4 offset:2048
	ds_read_b128 v[4:7], v8
	ds_read_b128 v[20:23], v8 offset:2048
	ds_read_b128 v[8:11], v127 offset:32784
	ds_read_b128 v[24:27], v127 offset:34832
	ds_read_b128 v[12:15], v128 offset:32784
	ds_read_b128 v[28:31], v128 offset:34832
	ds_read_b128 v[32:35], v127 offset:36880
	ds_read_b128 v[40:43], v127 offset:38928
	ds_read_b128 v[36:39], v128 offset:36880
	ds_read_b128 v[44:47], v128 offset:38928
	s_mov_b32 m0, s29
	s_nop 0
	buffer_load_dwordx4 v122, s[8:11], s81 offen lds
	s_nop 0
	s_mov_b32 m0, s68
	s_nop 0
	buffer_load_dwordx4 v123, s[8:11], s81 offen lds
	s_waitcnt lgkmcnt(8)
	s_barrier
	s_waitcnt lgkmcnt(0)
	s_setprio 1
	s_waitcnt lgkmcnt(5)
	v_mfma_scale_f32_16x16x128_f8f6f4 v[140:143], v[0:7], v[8:15], v[130:133], v149, v148 op_sel_hi:[0,0,0]
	v_mfma_scale_f32_16x16x128_f8f6f4 v[136:139], v[16:23], v[8:15], v[134:137], v149, v148 op_sel_hi:[0,0,0]
	s_waitcnt lgkmcnt(4)
	v_mfma_scale_f32_16x16x128_f8f6f4 v[108:111], v[0:7], v[24:31], v[184:187], v149, v148 op_sel_hi:[0,0,0]
	v_mfma_scale_f32_16x16x128_f8f6f4 v[104:107], v[16:23], v[24:31], v[208:211], v149, v148 op_sel_hi:[0,0,0]
	s_waitcnt lgkmcnt(1)
	v_mfma_scale_f32_16x16x128_f8f6f4 v[92:95], v[0:7], v[32:39], v[212:215], v149, v148 op_sel_hi:[0,0,0]
	v_mfma_scale_f32_16x16x128_f8f6f4 v[88:91], v[16:23], v[32:39], v[216:219], v149, v148 op_sel_hi:[0,0,0]
	s_waitcnt lgkmcnt(0)
	v_mfma_scale_f32_16x16x128_f8f6f4 v[220:223], v[0:7], v[40:47], v[220:223], v149, v148 op_sel_hi:[0,0,0]
	v_mfma_scale_f32_16x16x128_f8f6f4 v[224:227], v[16:23], v[40:47], v[224:227], v149, v148 op_sel_hi:[0,0,0]
	s_setprio 0
	s_barrier
	v_add_u32_e32 v84, s80, v124
	v_add_u32_e32 v85, s80, v125
	ds_read_b128 v[152:155], v84
	ds_read_b128 v[160:163], v84 offset:2048
	ds_read_b128 v[156:159], v85
	ds_read_b128 v[164:167], v85 offset:2048
	s_mov_b32 m0, s39
	s_nop 0
	buffer_load_dwordx4 v126, s[4:7], s76 offen lds
	s_nop 0
	s_mov_b32 m0, s69
	s_nop 0
	buffer_load_dwordx4 v126, s[4:7], s79 offen lds
	s_barrier
	s_waitcnt lgkmcnt(0)
	s_setprio 1
	s_waitcnt lgkmcnt(1)
	v_mfma_scale_f32_16x16x128_f8f6f4 v[116:119], v[152:159], v[8:15], v[228:231], v149, v148 op_sel_hi:[0,0,0]
	s_waitcnt lgkmcnt(0)
	v_mfma_scale_f32_16x16x128_f8f6f4 v[112:115], v[160:167], v[8:15], v[168:171], v149, v148 op_sel_hi:[0,0,0]
	v_mfma_scale_f32_16x16x128_f8f6f4 v[100:103], v[152:159], v[24:31], v[172:175], v149, v148 op_sel_hi:[0,0,0]
	v_mfma_scale_f32_16x16x128_f8f6f4 v[96:99], v[160:167], v[24:31], v[176:179], v149, v148 op_sel_hi:[0,0,0]
	v_mfma_scale_f32_16x16x128_f8f6f4 v[84:87], v[152:159], v[32:39], v[180:183], v149, v148 op_sel_hi:[0,0,0]
	v_mfma_scale_f32_16x16x128_f8f6f4 v[8:11], v[160:167], v[32:39], v[192:195], v149, v148 op_sel_hi:[0,0,0]
	v_mfma_scale_f32_16x16x128_f8f6f4 v[68:71], v[152:159], v[40:47], v[68:71], v149, v148 op_sel_hi:[0,0,0]
	v_mfma_scale_f32_16x16x128_f8f6f4 v[56:59], v[160:167], v[40:47], v[56:59], v149, v148 op_sel_hi:[0,0,0]
	s_setprio 0
	s_barrier
	ds_read_b128 v[32:35], v127 offset:49168
	ds_read_b128 v[168:171], v127 offset:51216
	ds_read_b128 v[36:39], v128 offset:49168
	ds_read_b128 v[172:175], v128 offset:51216
	ds_read_b128 v[176:179], v127 offset:53264
	ds_read_b128 v[192:195], v127 offset:55312
	ds_read_b128 v[180:183], v128 offset:53264
	ds_read_b128 v[196:199], v128 offset:55312
	s_mov_b32 m0, s60
	s_nop 0
	buffer_load_dwordx4 v120, s[8:11], s76 offen lds
	s_nop 0
	s_mov_b32 m0, s70
	s_nop 0
	buffer_load_dwordx4 v121, s[8:11], s76 offen lds
	s_barrier
	s_waitcnt lgkmcnt(0)
	s_setprio 1
	s_waitcnt lgkmcnt(5)
	v_mfma_scale_f32_16x16x128_f8f6f4 v[64:67], v[0:7], v[32:39], v[64:67], v149, v148 op_sel_hi:[0,0,0]
	v_mfma_scale_f32_16x16x128_f8f6f4 v[60:63], v[16:23], v[32:39], v[60:63], v149, v148 op_sel_hi:[0,0,0]
	s_waitcnt lgkmcnt(4)
	v_mfma_scale_f32_16x16x128_f8f6f4 v[44:47], v[0:7], v[168:175], v[200:203], v149, v148 op_sel_hi:[0,0,0]
	v_mfma_scale_f32_16x16x128_f8f6f4 v[40:43], v[16:23], v[168:175], v[204:207], v149, v148 op_sel_hi:[0,0,0]
	s_waitcnt lgkmcnt(1)
	v_mfma_scale_f32_16x16x128_f8f6f4 v[28:31], v[0:7], v[176:183], v[232:235], v149, v148 op_sel_hi:[0,0,0]
	v_mfma_scale_f32_16x16x128_f8f6f4 v[24:27], v[16:23], v[176:183], v[236:239], v149, v148 op_sel_hi:[0,0,0]
	s_waitcnt lgkmcnt(0)
	v_mfma_scale_f32_16x16x128_f8f6f4 v[12:15], v[0:7], v[192:199], v[240:243], v149, v148 op_sel_hi:[0,0,0]
	v_mfma_scale_f32_16x16x128_f8f6f4 v[244:247], v[16:23], v[192:199], v[244:247], v149, v148 op_sel_hi:[0,0,0]
	s_setprio 0
	s_barrier
	s_mov_b32 m0, s61
	s_nop 0
	buffer_load_dwordx4 v126, s[4:7], s77 offen lds
	s_nop 0
	s_mov_b32 m0, s71
	s_nop 0
	buffer_load_dwordx4 v126, s[4:7], s78 offen lds
	s_waitcnt vmcnt(6)
	s_barrier
	s_setprio 1
	v_mfma_scale_f32_16x16x128_f8f6f4 v[52:55], v[152:159], v[32:39], v[52:55], v149, v148 op_sel_hi:[0,0,0]
	v_mfma_scale_f32_16x16x128_f8f6f4 v[48:51], v[160:167], v[32:39], v[48:51], v149, v148 op_sel_hi:[0,0,0]
	v_mfma_scale_f32_16x16x128_f8f6f4 v[36:39], v[152:159], v[168:175], v[248:251], v149, v148 op_sel_hi:[0,0,0]
	v_mfma_scale_f32_16x16x128_f8f6f4 v[32:35], v[160:167], v[168:175], v[188:191], v149, v148 op_sel_hi:[0,0,0]
	v_mfma_scale_f32_16x16x128_f8f6f4 v[20:23], v[152:159], v[176:183], v[144:147], v149, v148 op_sel_hi:[0,0,0]
	v_mfma_scale_f32_16x16x128_f8f6f4 v[16:19], v[160:167], v[176:183], v[80:83], v149, v148 op_sel_hi:[0,0,0]
	v_mfma_scale_f32_16x16x128_f8f6f4 v[4:7], v[152:159], v[192:199], v[72:75], v149, v148 op_sel_hi:[0,0,0]
	v_mfma_scale_f32_16x16x128_f8f6f4 v[0:3], v[160:167], v[192:199], v[76:79], v149, v148 op_sel_hi:[0,0,0]
	s_setprio 0
	s_barrier
	s_mov_b32 s72, s75
	s_mov_b32 s73, s74
	s_cbranch_scc0 .LBB0_1483
	s_waitcnt vmcnt(0)
	s_cmpk_lt_u32 s15, 0x100
	s_cbranch_scc0 .LBB0_1486
	s_barrier
; #define LDS_AS __attribute__((address_space(3)))
; #define OPAQUE_TID(P) (((P).wid0 << 6) | lane_id_now())
; #define P_STAGE_A(slot, half, kt) do { _Pragma("unroll") for (int _i = 0; _i < 2; ++_i) { const unsigned _m0 = ldsw + (unsigned)((slot) + _i * 8192); const unsigned _so = (unsigned)(kt) * 128u; \
;     asm volatile("s_mov_b32 m0, %0\n\ts_nop 4\n\tbuffer_load_dwordx4 %1, %2, %3 offen lds" :: "s"(_m0), "v"(voffA[half][_i]), "s"(rsA), "s"(_so) : "m0", "memory"); } } while (0)
; #define P_STAGE_B(slot, half, kt) do { _Pragma("unroll") for (int _i = 0; _i < 2; ++_i) { const unsigned _m0 = ldsw + (unsigned)((slot) + _i * 8192); const unsigned _so = (unsigned)(kt) * 128u + (half) * bt_half + _i * bt_piece; \
;     asm volatile("s_mov_b32 m0, %0\n\ts_nop 4\n\tbuffer_load_dwordx4 %1, %2, %3 offen lds" :: "s"(_m0), "v"(voffB0), "s"(rsB), "s"(_so) : "m0", "memory"); } } while (0)
;   DI unsigned bt_rowoff(int h, int R) const { return (unsigned)(pn * 256 + 128 * h + (pn < 15 ? tcol_adj(R) : tcol_p64(R))) * 4096u; }
; template <class Cfg>
; DI void f8dma_issue_prologue_st(LDS_AS unsigned char* lds, const Cfg& cfg) {
;   const int tid = OPAQUE_TID(cfg.p), wid = __builtin_amdgcn_readfirstlane(tid >> 6), lane = tid & 63;
;   const LDS_AS unsigned* stash = (const LDS_AS unsigned*)(lds + F8_STASH);
;   unsigned voffA[2][2], voffB0;
;   voffA[0][0] = stash[tid]; voffA[0][1] = stash[512 + tid]; voffA[1][0] = stash[1024 + tid]; voffA[1][1] = stash[1536 + tid];
;   {
;     const int r = 8 * wid + (lane >> 3);
;     const unsigned cofs = 16u * (((unsigned)lane & 7u) ^ (((unsigned)lane >> 3) & 7u));
;     voffB0 = cfg.bt_rowoff(0, r) + cofs;
;   }
;   const unsigned bt_half = cfg.bt_rowoff(1, 0) - cfg.bt_rowoff(0, 0), bt_piece = cfg.bt_rowoff(0, 64) - cfg.bt_rowoff(0, 0);
;   const __amdgpu_buffer_rsrc_t rsA = __builtin_amdgcn_make_buffer_rsrc((void*)cfg.a_base(), 0, cfg.a_bytes(), 0x00020000);
;   const __amdgpu_buffer_rsrc_t rsB = __builtin_amdgcn_make_buffer_rsrc((void*)cfg.bt_base(), 0, cfg.bt_bytes(), 0x00020000);
;   const unsigned ldsw = (unsigned)__builtin_amdgcn_readfirstlane((int)(unsigned)(size_t)lds) + (unsigned)wid * 1024u;
;     ...
;   P_STAGE_B(G_SB(0, 0), 0, 0); P_STAGE_A(G_SA(0, 0), 0, 0); P_STAGE_B(G_SB(0, 1), 1, 0); P_STAGE_A(G_SA(0, 1), 1, 0);
;   P_STAGE_B(G_SB(1, 0), 0, 1); P_STAGE_A(G_SA(1, 0), 0, 1); P_STAGE_B(G_SB(1, 1), 1, 1);
.LBB0_1486:
	s_and_b64 vcc, exec, s[2:3]
	s_cbranch_vccnz .LBB0_1488
	v_mbcnt_lo_u32_b32 v76, -1, 0
	v_mbcnt_hi_u32_b32 v76, -1, v76
	s_ashr_i32 s15, s14, 31
	v_or_b32_e32 v72, s87, v76
	v_lshrrev_b32_e32 v77, 3, v76
	v_readfirstlane_b32 s4, v72
	s_ashr_i32 s17, s4, 6
	s_lshl_b32 s4, s17, 3
	s_and_b32 s5, s4, 16
	v_and_or_b32 v78, v77, 4, s4
	s_add_i32 s5, s5, s48
	s_lshl_b32 s5, s5, 7
	s_and_b32 s4, s4, 0x1fffe0
	v_lshlrev_b32_e32 v78, 1, v78
	v_xor_b32_e32 v77, v77, v76
	s_add_i32 s5, s5, s4
	v_and_b32_e32 v78, 24, v78
	v_bfe_u32 v76, v76, 3, 2
	v_lshl_add_u32 v72, v72, 2, 0
	v_or3_b32 v76, s5, v78, v76
	s_lshl_b64 s[4:5], s[14:15], 23
	v_add_u32_e32 v74, 0x22410, v72
	s_add_u32 s4, s50, s4
	ds_read2st64_b32 v[72:73], v74 offset1:8
	ds_read2st64_b32 v[74:75], v74 offset0:16 offset1:24
	v_lshlrev_b32_e32 v77, 4, v77
	s_addc_u32 s5, s51, s5
	s_lshl_b32 s15, s17, 10
	v_and_b32_e32 v77, 0x70, v77
	s_add_i32 s15, s15, 0
	v_lshl_or_b32 v76, v76, 11, v77
	s_and_b32 s5, s5, 0xffff
	s_add_i32 s17, s15, 0x10010
	s_mov_b32 m0, s17
	s_nop 0
	buffer_load_dwordx4 v76, s[4:7], s34 offen lds
	s_add_i32 s17, s15, 0x12010
	s_mov_b32 m0, s17
	s_nop 0
	buffer_load_dwordx4 v76, s[4:7], s7 offen lds
	s_add_i32 s17, s15, 16
	s_waitcnt lgkmcnt(1)
	s_mov_b32 m0, s17
	s_nop 0
	buffer_load_dwordx4 v72, s[8:11], s34 offen lds
	s_add_i32 s17, s15, 0x2010
	s_mov_b32 m0, s17
	s_nop 0
	buffer_load_dwordx4 v73, s[8:11], s34 offen lds
	s_add_i32 s17, s15, 0x14010
	s_mov_b32 m0, s17
	s_nop 0
	buffer_load_dwordx4 v76, s[4:7], s37 offen lds
	s_add_i32 s17, s15, 0x16010
	s_mov_b32 m0, s17
	s_nop 0
	buffer_load_dwordx4 v76, s[4:7], s56 offen lds
	s_add_i32 s17, s15, 0x4010
	s_waitcnt lgkmcnt(0)
	s_mov_b32 m0, s17
	s_nop 0
	buffer_load_dwordx4 v74, s[8:11], s34 offen lds
	s_add_i32 s17, s15, 0x6010
	s_mov_b32 m0, s17
	s_nop 0
	buffer_load_dwordx4 v75, s[8:11], s34 offen lds
	s_add_i32 s17, s15, 0x18010
	s_mov_b32 m0, s17
	s_nop 0
	buffer_load_dwordx4 v76, s[4:7], s35 offen lds
	s_add_i32 s17, s15, 0x1a010
	s_mov_b32 m0, s17
	s_nop 0
	buffer_load_dwordx4 v76, s[4:7], s43 offen lds
	s_add_i32 s17, s15, 0x8010
	s_mov_b32 m0, s17
	s_nop 0
	buffer_load_dwordx4 v72, s[8:11], s35 offen lds
	s_add_i32 s17, s15, 0xa010
	s_mov_b32 m0, s17
	s_nop 0
	buffer_load_dwordx4 v73, s[8:11], s35 offen lds
	s_add_i32 s17, s15, 0x1c010
	s_mov_b32 m0, s17
	s_nop 0
	buffer_load_dwordx4 v76, s[4:7], s44 offen lds
	s_add_i32 s15, s15, 0x1e010
	s_mov_b32 m0, s15
	s_nop 0
	buffer_load_dwordx4 v76, s[4:7], s45 offen lds

; #define G_WAIT_V(n) asm volatile("s_waitcnt vmcnt(" #n ")" ::: "memory")
; #define G_BAR() __builtin_amdgcn_s_barrier()
; #define G_SCHED() __builtin_amdgcn_sched_barrier(0)
; #define D_STAGE_A(slot, half, kt) D_STAGE(rsA, voffA, slot, half, kt)
; #define D_STAGE_B(slot, half, kt) D_STAGE(rsB, voffB, slot, half, kt)
; #define D_LDA(dst, slot) do { _Pragma("unroll") for (int m = 0; m < 4; ++m) _Pragma("unroll") for (int k = 0; k < 2; ++k) \
;     dst[m][k] = *(const LDS_AS bf16x8*)(lds + (slot) + aoff + m * 2048 + k * 1024); } while (0)
; #define D_LDB(dst, slot) do { _Pragma("unroll") for (int n = 0; n < 2; ++n) _Pragma("unroll") for (int k = 0; k < 2; ++k) \
;     dst[n][k] = *(const LDS_AS bf16x8*)(lds + (slot) + boff + n * 2048 + k * 1024); } while (0)
; #define D_MMA(ai, bj, At, Bf) do { __builtin_amdgcn_s_setprio(1); _Pragma("unroll") for (int m = 0; m < 4; ++m) _Pragma("unroll") for (int n = 0; n < 2; ++n) _Pragma("unroll") for (int k = 0; k < 2; ++k) \
;     acc[ai][bj][m][n] = __builtin_amdgcn_mfma_f32_16x16x32_bf16(Bf[n][k], At[m][k], acc[ai][bj][m][n], 0, 0, 0); __builtin_amdgcn_s_setprio(0); } while (0)
; #define D_WAIT_L(n) asm volatile("s_waitcnt lgkmcnt(" #n ")" ::: "memory")
; #define D_STAGE_A(slot, half, kt) D_STAGE(rsA, voffA, slot, half, kt)
;     ...
;   for (int t = 0; t < (F8_PEEL ? nt - 2 : nt); t += 2) {
;     const int t1 = t + 1;
;     const int t2 = (F8_PEEL || t + 2 < nt) ? t + 2 : t;
;     const int t3 = (F8_PEEL || t + 2 < nt) ? t + 3 : t + 1;
;     D_LDB(B0, G_SB(0, 0)); G_SCHED(); D_LDA(At, G_SA(0, 0)); D_STAGE_A(G_SA(1, 1), 1, t1);
;     D_WAIT_L(8); G_BAR(); D_WAIT_L(0); G_SCHED(); D_MMA(0, 0, At, B0); G_BAR(); G_SCHED();
;     D_LDB(B1, G_SB(0, 1)); D_STAGE_B(G_SB(0, 0), 0, t2);
;     G_BAR(); D_WAIT_L(0); G_SCHED(); D_MMA(0, 1, At, B1); G_BAR(); G_SCHED();
;     D_LDA(At, G_SA(0, 1)); D_STAGE_A(G_SA(0, 0), 0, t2);
;     G_BAR(); D_WAIT_L(0); G_SCHED(); D_MMA(1, 0, At, B0); G_BAR(); G_SCHED();
;     D_STAGE_B(G_SB(0, 1), 1, t2);
;     G_WAIT_V(6); G_BAR(); G_SCHED(); D_MMA(1, 1, At, B1); G_BAR(); G_SCHED();
;     D_LDB(B0, G_SB(1, 0)); G_SCHED(); D_LDA(At, G_SA(1, 0)); D_STAGE_A(G_SA(0, 1), 1, t2);
;     D_WAIT_L(8); G_BAR(); D_WAIT_L(0); G_SCHED(); D_MMA(0, 0, At, B0); G_BAR(); G_SCHED();
;     D_LDB(B1, G_SB(1, 1)); D_STAGE_B(G_SB(1, 0), 0, t3);
;     G_BAR(); D_WAIT_L(0); G_SCHED(); D_MMA(0, 1, At, B1); G_BAR(); G_SCHED();
.LBB0_1510:
	s_add_i32 s77, 0, 0x10010
	s_waitcnt vmcnt(62)
	v_add_u32_e32 v73, s77, v68
	s_waitcnt vmcnt(49)
	v_add_u32_e32 v86, s77, v69
	ds_read_b128 v[74:77], v73
	ds_read_b128 v[82:85], v73 offset:2048
	ds_read_b128 v[78:81], v86
	s_waitcnt vmcnt(46)
	ds_read_b128 v[86:89], v86 offset:2048
	s_add_i32 s38, s75, 1
	s_add_i32 s74, s75, 3
	s_add_i32 s73, s75, 2
	s_add_i32 s82, 0, 0x14010
	s_cmp_lt_u32 s75, 14
	s_cselect_b32 s76, s73, s75
	s_cselect_b32 s38, s74, s38
	s_lshl_b32 s81, s76, 7
	s_lshl_b32 s76, s38, 7
	s_add_i32 s83, s81, 0x20000
	s_add_i32 s84, s81, 0x2000
	s_add_i32 s85, s81, 0x22000
	s_add_i32 s86, 0, 0x18010
	s_add_i32 s80, 0, 0x1c010
	s_add_i32 s79, s76, 0x20000
	s_add_i32 s77, s76, 0x2000
	s_add_i32 s78, s76, 0x22000
	s_add_i32 s74, s72, 0x100
	s_cmp_gt_u32 s75, 13
	s_waitcnt vmcnt(42)
	ds_read_b128 v[90:93], v71 offset:16
	s_waitcnt vmcnt(34)
	ds_read_b128 v[98:101], v71 offset:2064
	ds_read_b128 v[94:97], v72 offset:16
	s_waitcnt vmcnt(30)
	ds_read_b128 v[102:105], v72 offset:2064
	s_waitcnt vmcnt(26)
	ds_read_b128 v[106:109], v71 offset:4112
	s_waitcnt vmcnt(18)
	ds_read_b128 v[114:117], v71 offset:6160
	ds_read_b128 v[110:113], v72 offset:4112
	s_waitcnt vmcnt(2)
	ds_read_b128 v[118:121], v72 offset:6160
	s_waitcnt lgkmcnt(12)
	s_mov_b32 m0, s26
	s_nop 0
	buffer_load_dwordx4 v66, s[8:11], s72 offen lds
	s_nop 0
	s_mov_b32 m0, s62
	s_nop 0
	buffer_load_dwordx4 v67, s[8:11], s72 offen lds
	s_waitcnt lgkmcnt(8)
	s_barrier
	s_waitcnt lgkmcnt(0)
	s_setprio 1
	s_waitcnt lgkmcnt(5)
	v_mfma_scale_f32_16x16x128_f8f6f4 v[56:59], v[74:81], v[90:97], v[56:59], v149, v148 op_sel_hi:[0,0,0]
	v_mfma_scale_f32_16x16x128_f8f6f4 v[60:63], v[82:89], v[90:97], v[60:63], v149, v148 op_sel_hi:[0,0,0]
	s_waitcnt lgkmcnt(4)
	v_mfma_scale_f32_16x16x128_f8f6f4 v[44:47], v[74:81], v[98:105], v[44:47], v149, v148 op_sel_hi:[0,0,0]
	v_mfma_scale_f32_16x16x128_f8f6f4 v[40:43], v[82:89], v[98:105], v[40:43], v149, v148 op_sel_hi:[0,0,0]
	s_waitcnt vmcnt(0) lgkmcnt(1)
	v_mfma_scale_f32_16x16x128_f8f6f4 v[122:125], v[74:81], v[106:113], v[28:31], v149, v148 op_sel_hi:[0,0,0]
	v_mfma_scale_f32_16x16x128_f8f6f4 v[126:129], v[82:89], v[106:113], v[24:27], v149, v148 op_sel_hi:[0,0,0]
	s_waitcnt lgkmcnt(0)
	v_mfma_scale_f32_16x16x128_f8f6f4 v[130:133], v[74:81], v[114:121], v[12:15], v149, v148 op_sel_hi:[0,0,0]
	v_mfma_scale_f32_16x16x128_f8f6f4 v[134:137], v[82:89], v[114:121], v[8:11], v149, v148 op_sel_hi:[0,0,0]
	s_setprio 0
	s_barrier
	s_nop 3
	v_add_u32_e32 v12, s82, v68
	v_add_u32_e32 v28, s82, v69
	ds_read_b128 v[8:11], v12
	ds_read_b128 v[24:27], v12 offset:2048
	ds_read_b128 v[12:15], v28
	ds_read_b128 v[28:31], v28 offset:2048
	s_mov_b32 m0, s27
	s_nop 0
	buffer_load_dwordx4 v70, s[4:7], s81 offen lds
	s_nop 0
	s_mov_b32 m0, s63
	s_nop 0
	buffer_load_dwordx4 v70, s[4:7], s83 offen lds
	s_barrier
	s_waitcnt lgkmcnt(0)
	s_setprio 1
	s_waitcnt lgkmcnt(1)
	v_mfma_scale_f32_16x16x128_f8f6f4 v[52:55], v[8:15], v[90:97], v[52:55], v149, v148 op_sel_hi:[0,0,0]
	s_waitcnt lgkmcnt(0)
	v_mfma_scale_f32_16x16x128_f8f6f4 v[48:51], v[24:31], v[90:97], v[48:51], v149, v148 op_sel_hi:[0,0,0]
	v_mfma_scale_f32_16x16x128_f8f6f4 v[138:141], v[8:15], v[98:105], v[36:39], v149, v148 op_sel_hi:[0,0,0]
	v_mfma_scale_f32_16x16x128_f8f6f4 v[152:155], v[24:31], v[98:105], v[32:35], v149, v148 op_sel_hi:[0,0,0]
	v_mfma_scale_f32_16x16x128_f8f6f4 v[156:159], v[8:15], v[106:113], v[20:23], v149, v148 op_sel_hi:[0,0,0]
	v_mfma_scale_f32_16x16x128_f8f6f4 v[106:109], v[24:31], v[106:113], v[16:19], v149, v148 op_sel_hi:[0,0,0]
	v_mfma_scale_f32_16x16x128_f8f6f4 v[110:113], v[8:15], v[114:121], v[4:7], v149, v148 op_sel_hi:[0,0,0]
	v_mfma_scale_f32_16x16x128_f8f6f4 v[114:117], v[24:31], v[114:121], v[0:3], v149, v148 op_sel_hi:[0,0,0]
	s_setprio 0
	s_barrier
	s_mov_b32 m0, s17
	s_nop 0
	buffer_load_dwordx4 v64, s[8:11], s81 offen lds
	s_nop 0
	s_mov_b32 m0, s66
	s_nop 0
	buffer_load_dwordx4 v65, s[8:11], s81 offen lds
	s_barrier
	s_waitcnt lgkmcnt(0)
	s_barrier
	s_mov_b32 m0, s28
	s_nop 0
	buffer_load_dwordx4 v70, s[4:7], s84 offen lds
	s_nop 0
	s_mov_b32 m0, s67
	s_nop 0
	buffer_load_dwordx4 v70, s[4:7], s85 offen lds
	s_waitcnt vmcnt(6)
	s_barrier
	s_barrier
	v_add_u32_e32 v4, s86, v68
	v_add_u32_e32 v8, s86, v69
	ds_read_b128 v[0:3], v4
	ds_read_b128 v[16:19], v4 offset:2048
	ds_read_b128 v[4:7], v8
	ds_read_b128 v[20:23], v8 offset:2048
	ds_read_b128 v[32:35], v71 offset:32784
	ds_read_b128 v[74:77], v71 offset:34832
	ds_read_b128 v[36:39], v72 offset:32784
	ds_read_b128 v[78:81], v72 offset:34832
	ds_read_b128 v[82:85], v71 offset:36880
	ds_read_b128 v[90:93], v71 offset:38928
	ds_read_b128 v[86:89], v72 offset:36880
	ds_read_b128 v[94:97], v72 offset:38928
	s_mov_b32 m0, s29
	s_nop 0
	buffer_load_dwordx4 v66, s[8:11], s81 offen lds
	s_nop 0
	s_mov_b32 m0, s68
	s_nop 0
	buffer_load_dwordx4 v67, s[8:11], s81 offen lds
	s_waitcnt lgkmcnt(8)
	s_barrier
; #define LDS_AS __attribute__((address_space(3)))
; #define OPAQUE_TID(P) (((P).wid0 << 6) | lane_id_now())
; #define G_WAIT_V(n) asm volatile("s_waitcnt vmcnt(" #n ")" ::: "memory")
; #define G_BAR() __builtin_amdgcn_s_barrier()
; #define G_SCHED() __builtin_amdgcn_sched_barrier(0)
; #define D_STAGE_A(slot, half, kt) D_STAGE(rsA, voffA, slot, half, kt)
; #define D_STAGE_B(slot, half, kt) D_STAGE(rsB, voffB, slot, half, kt)
; #define D_LDA(dst, slot) do { _Pragma("unroll") for (int m = 0; m < 4; ++m) _Pragma("unroll") for (int k = 0; k < 2; ++k) \
;     dst[m][k] = *(const LDS_AS bf16x8*)(lds + (slot) + aoff + m * 2048 + k * 1024); } while (0)
; template <class Cfg>
; DI void f8dma_issue_prologue_st(LDS_AS unsigned char* lds, const Cfg& cfg) {
;   const int tid = OPAQUE_TID(cfg.p), wid = __builtin_amdgcn_readfirstlane(tid >> 6), lane = tid & 63;
;   const LDS_AS unsigned* stash = (const LDS_AS unsigned*)(lds + F8_STASH);
;   unsigned voffA[2][2], voffB0;
;   voffA[0][0] = stash[tid]; voffA[0][1] = stash[512 + tid]; voffA[1][0] = stash[1024 + tid]; voffA[1][1] = stash[1536 + tid];
;   {
;     const int r = 8 * wid + (lane >> 3);
;     const unsigned cofs = 16u * (((unsigned)lane & 7u) ^ (((unsigned)lane >> 3) & 7u));
;     voffB0 = cfg.bt_rowoff(0, r) + cofs;
;   }
;   const unsigned bt_half = cfg.bt_rowoff(1, 0) - cfg.bt_rowoff(0, 0), bt_piece = cfg.bt_rowoff(0, 64) - cfg.bt_rowoff(0, 0);
;   const __amdgpu_buffer_rsrc_t rsA = __builtin_amdgcn_make_buffer_rsrc((void*)cfg.a_base(), 0, cfg.a_bytes(), 0x00020000);
;   const __amdgpu_buffer_rsrc_t rsB = __builtin_amdgcn_make_buffer_rsrc((void*)cfg.bt_base(), 0, cfg.bt_bytes(), 0x00020000);
;   const unsigned ldsw = (unsigned)__builtin_amdgcn_readfirstlane((int)(unsigned)(size_t)lds) + (unsigned)wid * 1024u;
;     ...
;   P_STAGE_B(G_SB(0, 0), 0, 0); P_STAGE_A(G_SA(0, 0), 0, 0); P_STAGE_B(G_SB(0, 1), 1, 0); P_STAGE_A(G_SA(0, 1), 1, 0);
;   P_STAGE_B(G_SB(1, 0), 0, 1); P_STAGE_A(G_SA(1, 0), 0, 1); P_STAGE_B(G_SB(1, 1), 1, 1);
;     ...
;     G_BAR(); D_WAIT_L(0); G_SCHED(); D_MMA(0, 1, At, B1); G_BAR(); G_SCHED();
;     D_LDA(At, G_SA(1, 1)); D_STAGE_A(G_SA(1, 0), 0, t3);
;     G_BAR(); D_WAIT_L(0); G_SCHED(); D_MMA(1, 0, At, B0); G_BAR(); G_SCHED();
;     D_STAGE_B(G_SB(1, 1), 1, t3);
;     G_WAIT_V(6); G_BAR(); G_SCHED(); D_MMA(1, 1, At, B1); G_BAR(); G_SCHED();
;   }
;   if (!F8_PEEL) G_WAIT_V(0);
	s_waitcnt lgkmcnt(0)
	s_setprio 1
	s_waitcnt lgkmcnt(5)
	v_mfma_scale_f32_16x16x128_f8f6f4 v[56:59], v[0:7], v[32:39], v[56:59], v149, v148 op_sel_hi:[0,0,0]
	v_mfma_scale_f32_16x16x128_f8f6f4 v[60:63], v[16:23], v[32:39], v[60:63], v149, v148 op_sel_hi:[0,0,0]
	s_waitcnt lgkmcnt(4)
	v_mfma_scale_f32_16x16x128_f8f6f4 v[44:47], v[0:7], v[74:81], v[44:47], v149, v148 op_sel_hi:[0,0,0]
	v_mfma_scale_f32_16x16x128_f8f6f4 v[40:43], v[16:23], v[74:81], v[40:43], v149, v148 op_sel_hi:[0,0,0]
	s_waitcnt lgkmcnt(1)
	v_mfma_scale_f32_16x16x128_f8f6f4 v[28:31], v[0:7], v[82:89], v[122:125], v149, v148 op_sel_hi:[0,0,0]
	v_mfma_scale_f32_16x16x128_f8f6f4 v[24:27], v[16:23], v[82:89], v[126:129], v149, v148 op_sel_hi:[0,0,0]
	s_waitcnt lgkmcnt(0)
	v_mfma_scale_f32_16x16x128_f8f6f4 v[12:15], v[0:7], v[90:97], v[130:133], v149, v148 op_sel_hi:[0,0,0]
	v_mfma_scale_f32_16x16x128_f8f6f4 v[8:11], v[16:23], v[90:97], v[134:137], v149, v148 op_sel_hi:[0,0,0]
	s_setprio 0
	s_barrier
	v_add_u32_e32 v4, s80, v68
	v_add_u32_e32 v16, s80, v69
	ds_read_b128 v[0:3], v4
	ds_read_b128 v[98:101], v4 offset:2048
	ds_read_b128 v[4:7], v16
	ds_read_b128 v[102:105], v16 offset:2048
	s_mov_b32 m0, s39
	s_nop 0
	buffer_load_dwordx4 v70, s[4:7], s76 offen lds
	s_nop 0
	s_mov_b32 m0, s69
	s_nop 0
	buffer_load_dwordx4 v70, s[4:7], s79 offen lds
	s_barrier
	s_waitcnt lgkmcnt(0)
	s_setprio 1
	s_waitcnt lgkmcnt(1)
	v_mfma_scale_f32_16x16x128_f8f6f4 v[52:55], v[0:7], v[32:39], v[52:55], v149, v148 op_sel_hi:[0,0,0]
	s_waitcnt lgkmcnt(0)
	v_mfma_scale_f32_16x16x128_f8f6f4 v[48:51], v[98:105], v[32:39], v[48:51], v149, v148 op_sel_hi:[0,0,0]
	v_mfma_scale_f32_16x16x128_f8f6f4 v[36:39], v[0:7], v[74:81], v[138:141], v149, v148 op_sel_hi:[0,0,0]
	v_mfma_scale_f32_16x16x128_f8f6f4 v[32:35], v[98:105], v[74:81], v[152:155], v149, v148 op_sel_hi:[0,0,0]
	v_mfma_scale_f32_16x16x128_f8f6f4 v[20:23], v[0:7], v[82:89], v[156:159], v149, v148 op_sel_hi:[0,0,0]
	v_mfma_scale_f32_16x16x128_f8f6f4 v[16:19], v[98:105], v[82:89], v[106:109], v149, v148 op_sel_hi:[0,0,0]
	v_mfma_scale_f32_16x16x128_f8f6f4 v[4:7], v[0:7], v[90:97], v[110:113], v149, v148 op_sel_hi:[0,0,0]
	v_mfma_scale_f32_16x16x128_f8f6f4 v[0:3], v[98:105], v[90:97], v[114:117], v149, v148 op_sel_hi:[0,0,0]
	s_setprio 0
	s_barrier
	s_mov_b32 m0, s60
	s_nop 0
	buffer_load_dwordx4 v64, s[8:11], s76 offen lds
	s_nop 0
	s_mov_b32 m0, s70
	s_nop 0
	buffer_load_dwordx4 v65, s[8:11], s76 offen lds
	s_barrier
	s_waitcnt lgkmcnt(0)
	s_barrier
	s_mov_b32 m0, s61
	s_nop 0
	buffer_load_dwordx4 v70, s[4:7], s77 offen lds
	s_nop 0
	s_mov_b32 m0, s71
	s_nop 0
	buffer_load_dwordx4 v70, s[4:7], s78 offen lds
	s_waitcnt vmcnt(6)
	s_barrier
	s_barrier
	s_mov_b32 s72, s74
	s_mov_b32 s75, s73
	s_cbranch_scc0 .LBB0_1510
	s_waitcnt vmcnt(0)
	s_cmpk_lt_u32 s15, 0x100
	s_cbranch_scc0 .LBB0_1513
	s_barrier
.LBB0_1513:
	v_readlane_b32 s68, v254, 47
	s_and_b64 vcc, exec, s[2:3]
	v_readlane_b32 s70, v254, 49
	v_readlane_b32 s71, v254, 50
	v_readlane_b32 s69, v254, 48
	s_cbranch_vccnz .LBB0_1515
	v_mbcnt_lo_u32_b32 v68, -1, 0
	v_mbcnt_hi_u32_b32 v68, -1, v68
	s_ashr_i32 s15, s14, 31
	v_or_b32_e32 v64, s87, v68
	v_lshrrev_b32_e32 v69, 3, v68
	v_readfirstlane_b32 s2, v64
	s_ashr_i32 s17, s2, 6
	s_lshl_b32 s2, s17, 3
	s_and_b32 s3, s2, 16
	v_and_or_b32 v70, v69, 4, s2
	s_add_i32 s3, s3, s48
	s_lshl_b32 s3, s3, 7
	s_and_b32 s2, s2, 0x1fffe0
	v_lshlrev_b32_e32 v70, 1, v70
	v_xor_b32_e32 v69, v69, v68
	s_add_i32 s3, s3, s2
	v_and_b32_e32 v70, 24, v70
	v_bfe_u32 v68, v68, 3, 2
	v_or3_b32 v68, s3, v70, v68
	s_lshl_b64 s[2:3], s[14:15], 23
	v_lshl_add_u32 v64, v64, 2, 0
	s_add_u32 s4, s50, s2
	v_add_u32_e32 v66, 0x22410, v64
	s_addc_u32 s2, s51, s3
	ds_read2st64_b32 v[64:65], v66 offset1:8
	ds_read2st64_b32 v[66:67], v66 offset0:16 offset1:24
	v_lshlrev_b32_e32 v69, 4, v69
	s_and_b32 s5, s2, 0xffff
	s_lshl_b32 s2, s17, 10
	v_and_b32_e32 v69, 0x70, v69
	s_add_i32 s2, s2, 0
	v_lshl_or_b32 v68, v68, 11, v69
	s_add_i32 s3, s2, 0x10010
	s_mov_b32 m0, s3
	s_nop 0
	buffer_load_dwordx4 v68, s[4:7], s34 offen lds
	s_add_i32 s3, s2, 0x12010
	s_mov_b32 m0, s3
	s_nop 0
	buffer_load_dwordx4 v68, s[4:7], s7 offen lds
	s_add_i32 s3, s2, 16
	s_waitcnt lgkmcnt(1)
	s_mov_b32 m0, s3
	s_nop 0
	buffer_load_dwordx4 v64, s[8:11], s34 offen lds
	s_add_i32 s3, s2, 0x2010
	s_mov_b32 m0, s3
	s_nop 0
	buffer_load_dwordx4 v65, s[8:11], s34 offen lds
	s_add_i32 s3, s2, 0x14010
	s_mov_b32 m0, s3
	s_nop 0
	buffer_load_dwordx4 v68, s[4:7], s37 offen lds
	s_add_i32 s3, s2, 0x16010
	s_mov_b32 m0, s3
	s_nop 0
	buffer_load_dwordx4 v68, s[4:7], s56 offen lds
	s_add_i32 s3, s2, 0x4010
	s_waitcnt lgkmcnt(0)
	s_mov_b32 m0, s3
	s_nop 0
	buffer_load_dwordx4 v66, s[8:11], s34 offen lds
	s_add_i32 s3, s2, 0x6010
	s_mov_b32 m0, s3
	s_nop 0
	buffer_load_dwordx4 v67, s[8:11], s34 offen lds
	s_add_i32 s3, s2, 0x18010
	s_mov_b32 m0, s3
	s_nop 0
	buffer_load_dwordx4 v68, s[4:7], s35 offen lds
	s_add_i32 s3, s2, 0x1a010
	s_mov_b32 m0, s3
	s_nop 0
	buffer_load_dwordx4 v68, s[4:7], s43 offen lds
	s_add_i32 s3, s2, 0x8010
	s_mov_b32 m0, s3
	s_nop 0
	buffer_load_dwordx4 v64, s[8:11], s35 offen lds
	s_add_i32 s3, s2, 0xa010
	s_mov_b32 m0, s3
	s_nop 0
	buffer_load_dwordx4 v65, s[8:11], s35 offen lds
	s_add_i32 s3, s2, 0x1c010
	s_mov_b32 m0, s3
	s_nop 0
	buffer_load_dwordx4 v68, s[4:7], s44 offen lds
	s_add_i32 s2, s2, 0x1e010
	s_mov_b32 m0, s2
	s_nop 0
	buffer_load_dwordx4 v68, s[4:7], s45 offen lds

; #define G_WAIT_V(n) asm volatile("s_waitcnt vmcnt(" #n ")" ::: "memory")
; #define G_BAR() __builtin_amdgcn_s_barrier()
; #define D_STAGE_A(slot, half, kt) D_STAGE(rsA, voffA, slot, half, kt)
; #define D_STAGE_B(slot, half, kt) D_STAGE(rsB, voffB, slot, half, kt)
; #define D_STAGE_A(slot, half, kt) D_STAGE(rsA, voffA, slot, half, kt)
; #define D_STAGE_B(slot, half, kt) do { _Pragma("unroll") for (int _i = 0; _i < 2; ++_i) { const unsigned _m0 = ldsw + (unsigned)((slot) + _i * 8192); const unsigned _so = (unsigned)(kt) * 128u + (half) * bt_half + _i * bt_piece; \
;     asm volatile("s_mov_b32 m0, %0\n\ts_nop 4\n\tbuffer_load_dwordx4 %1, %2, %3 offen lds" :: "s"(_m0), "v"(voffB0), "s"(rsB), "s"(_so) : "m0", "memory"); } } while (0)
;   DI unsigned bt_rowoff(int h, int R) const { return (unsigned)(pn * 256 + 128 * h + (pn < 15 ? tcol_adj(R) : tcol_p64(R))) * 4096u; }
;   DI unsigned a_bytes() const { return (unsigned)NTOK * 4096u; }
;     ...
;   const unsigned bt_half = cfg.bt_rowoff(1, 0) - cfg.bt_rowoff(0, 0), bt_piece = cfg.bt_rowoff(0, 64) - cfg.bt_rowoff(0, 0);
;   const __amdgpu_buffer_rsrc_t rsA = __builtin_amdgcn_make_buffer_rsrc((void*)cfg.a_base(), 0, cfg.a_bytes(), 0x00020000);
;   const __amdgpu_buffer_rsrc_t rsB = __builtin_amdgcn_make_buffer_rsrc((void*)cfg.bt_base(), 0, cfg.bt_bytes(), 0x00020000);
;   const unsigned ldsw = (unsigned)__builtin_amdgcn_readfirstlane((int)(unsigned)(size_t)lds) + (unsigned)wid * 1024u;
;     ...
;   unsigned aoff[2], boff[2];
; #pragma unroll
;   for (int j = 0; j < 2; ++j) {
;     aoff[j] = (unsigned)(64 * wr + fr) * 128u + 16u * ((2u * fq + j) ^ ((unsigned)fr & 7u));
;     boff[j] = (unsigned)(32 * wc + fr) * 128u + 16u * ((2u * fq + j) ^ ((unsigned)fr & 7u));
;   }
;     ...
;   const int scw = cfg.scale_w(), scx = cfg.scale_x();
;     ...
;   f32x4 acc[2][2][4][2];
; #pragma unroll
;   for (int a = 0; a < 2; ++a)
; #pragma unroll
;     for (int b = 0; b < 2; ++b)
; #pragma unroll
;       for (int m = 0; m < 4; ++m)
; #pragma unroll
;         for (int n = 0; n < 2; ++n) acc[a][b][m][n] = (f32x4){0.f, 0.f, 0.f, 0.f};
;   i32x8 At[4], B0[2], B1[2];
;   if (!PRE) {
;     D_STAGE_B(G_SB(0, 0), 0, 0); D_STAGE_A(G_SA(0, 0), 0, 0); D_STAGE_B(G_SB(0, 1), 1, 0); D_STAGE_A(G_SA(0, 1), 1, 0);
;     D_STAGE_B(G_SB(1, 0), 0, 1); D_STAGE_A(G_SA(1, 0), 0, 1); D_STAGE_B(G_SB(1, 1), 1, 1);
;   }
;   G_WAIT_V(0); G_BAR();
.LBB0_1603:
	s_lshr_b32 s4, s4, 2
	v_lshlrev_b32_e32 v3, 1, v2
	v_and_b32_e32 v2, 0x63, v2
	s_ashr_i32 s15, s14, 31
	s_ashr_i32 s21, s13, 8
	s_lshl_b32 s20, s26, 8
	v_and_or_b32 v2, s4, 4, v2
	s_lshl_b64 s[4:5], s[14:15], 22
	s_add_u32 s4, s52, s4
	v_and_b32_e32 v3, 24, v3
	s_addc_u32 s5, s53, s5
	s_lshl_b32 s15, s67, 10
	v_or3_b32 v2, v2, v3, s20
	s_add_i32 s68, s15, 0
	s_waitcnt vmcnt(5)
	v_lshl_or_b32 v130, v2, 11, v6
	s_and_b32 s5, s5, 0xffff
	s_add_i32 s39, s68, 0x10010
	s_mov_b32 m0, s39
	s_nop 0
	buffer_load_dwordx4 v130, s[4:7], s31 offen lds
	s_add_i32 s50, s68, 0x12010
	s_mov_b32 m0, s50
	s_nop 0
	buffer_load_dwordx4 v130, s[4:7], s7 offen lds
	s_waitcnt vmcnt(3)
	v_lshl_or_b32 v128, v7, 11, v6
	s_add_i32 s51, s68, 16
	s_mov_b32 m0, s51
	s_nop 0
	buffer_load_dwordx4 v128, s[8:11], s31 offen lds
	s_waitcnt vmcnt(1)
	v_lshl_or_b32 v131, v4, 11, v6
	s_add_i32 s54, s68, 0x2010
	s_mov_b32 m0, s54
	s_nop 0
	buffer_load_dwordx4 v131, s[8:11], s31 offen lds
	s_add_i32 s55, s68, 0x14010
	s_mov_b32 m0, s55
	s_nop 0
	buffer_load_dwordx4 v130, s[4:7], s34 offen lds
	s_add_i32 s58, s68, 0x16010
	s_mov_b32 m0, s58
	s_nop 0
	buffer_load_dwordx4 v130, s[4:7], s35 offen lds
	v_lshl_or_b32 v129, v8, 11, v6
	s_add_i32 s59, s68, 0x4010
	s_mov_b32 m0, s59
	s_nop 0
	buffer_load_dwordx4 v129, s[8:11], s31 offen lds
	s_waitcnt vmcnt(0)
	v_lshl_or_b32 v132, v5, 11, v6
	s_add_i32 s60, s68, 0x6010
	s_mov_b32 m0, s60
	s_nop 0
	buffer_load_dwordx4 v132, s[8:11], s31 offen lds
	s_add_i32 s61, s68, 0x18010
	s_mov_b32 m0, s61
	s_nop 0
	buffer_load_dwordx4 v130, s[4:7], s33 offen lds
	s_add_i32 s62, s68, 0x1a010
	s_mov_b32 m0, s62
	s_nop 0
	buffer_load_dwordx4 v130, s[4:7], s36 offen lds
	s_add_i32 s63, s68, 0x8010
	s_mov_b32 m0, s63
	s_nop 0
	buffer_load_dwordx4 v128, s[8:11], s33 offen lds
	s_add_i32 s64, s68, 0xa010
	s_mov_b32 m0, s64
	s_nop 0
	buffer_load_dwordx4 v131, s[8:11], s33 offen lds
	s_add_i32 s65, s68, 0x1c010
	s_mov_b32 m0, s65
	s_nop 0
	buffer_load_dwordx4 v130, s[4:7], s37 offen lds
	s_add_i32 s66, s68, 0x1e010
	s_mov_b32 m0, s66
	s_nop 0
	buffer_load_dwordx4 v130, s[4:7], s42 offen lds
	s_waitcnt vmcnt(0)
	s_cmp_lg_u32 s21, 1
	s_barrier
	s_cbranch_scc1 .LBB0_1605
	s_barrier

; #define G_WAIT_V(n) asm volatile("s_waitcnt vmcnt(" #n ")" ::: "memory")
; #define G_BAR() __builtin_amdgcn_s_barrier()
; #define G_SCHED() __builtin_amdgcn_sched_barrier(0)
; #define D_STAGE_A(slot, half, kt) D_STAGE(rsA, voffA, slot, half, kt)
; #define D_STAGE_B(slot, half, kt) D_STAGE(rsB, voffB, slot, half, kt)
; #define D_LDA(dst, slot) do { _Pragma("unroll") for (int m = 0; m < 4; ++m) _Pragma("unroll") for (int k = 0; k < 2; ++k) \
;     dst[m][k] = *(const LDS_AS bf16x8*)(lds + (slot) + aoff + m * 2048 + k * 1024); } while (0)
; #define D_LDB(dst, slot) do { _Pragma("unroll") for (int n = 0; n < 2; ++n) _Pragma("unroll") for (int k = 0; k < 2; ++k) \
;     dst[n][k] = *(const LDS_AS bf16x8*)(lds + (slot) + boff + n * 2048 + k * 1024); } while (0)
; #define D_MMA(ai, bj, At, Bf) do { __builtin_amdgcn_s_setprio(1); _Pragma("unroll") for (int m = 0; m < 4; ++m) _Pragma("unroll") for (int n = 0; n < 2; ++n) _Pragma("unroll") for (int k = 0; k < 2; ++k) \
;     acc[ai][bj][m][n] = __builtin_amdgcn_mfma_f32_16x16x32_bf16(Bf[n][k], At[m][k], acc[ai][bj][m][n], 0, 0, 0); __builtin_amdgcn_s_setprio(0); } while (0)
; #define D_WAIT_L(n) asm volatile("s_waitcnt lgkmcnt(" #n ")" ::: "memory")
; #define D_STAGE_A(slot, half, kt) D_STAGE(rsA, voffA, slot, half, kt)
; #define D_WAIT_L(n) asm volatile("s_waitcnt lgkmcnt(" #n ")" ::: "memory")
;     ...
;   for (int t = 0; t < (F8_PEEL ? nt - 2 : nt); t += 2) {
;     const int t1 = t + 1;
;     const int t2 = (F8_PEEL || t + 2 < nt) ? t + 2 : t;
;     const int t3 = (F8_PEEL || t + 2 < nt) ? t + 3 : t + 1;
;     D_LDB(B0, G_SB(0, 0)); G_SCHED(); D_LDA(At, G_SA(0, 0)); D_STAGE_A(G_SA(1, 1), 1, t1);
;     D_WAIT_L(8); G_BAR(); D_WAIT_L(0); G_SCHED(); D_MMA(0, 0, At, B0); G_BAR(); G_SCHED();
;     D_LDB(B1, G_SB(0, 1)); D_STAGE_B(G_SB(0, 0), 0, t2);
;     G_BAR(); D_WAIT_L(0); G_SCHED(); D_MMA(0, 1, At, B1); G_BAR(); G_SCHED();
;     D_LDA(At, G_SA(0, 1)); D_STAGE_A(G_SA(0, 0), 0, t2);
;     G_BAR(); D_WAIT_L(0); G_SCHED(); D_MMA(1, 0, At, B0); G_BAR(); G_SCHED();
;     D_STAGE_B(G_SB(0, 1), 1, t2);
;     G_WAIT_V(6); G_BAR(); G_SCHED(); D_MMA(1, 1, At, B1); G_BAR(); G_SCHED();
.LBB0_1606:
	s_add_i32 s74, 0, 0x10010
	v_add_u32_e32 v68, s74, v133
	v_add_u32_e32 v69, s74, v134
	ds_read_b128 v[146:149], v68
	ds_read_b128 v[154:157], v68 offset:2048
	ds_read_b128 v[150:153], v69
	ds_read_b128 v[158:161], v69 offset:2048
	s_add_i32 s38, s71, 1
	s_add_i32 s72, s71, 3
	s_add_i32 s70, s71, 2
	s_add_i32 s82, 0, 0x14010
	s_cmp_lt_u32 s71, 14
	s_cselect_b32 s73, s70, s71
	s_cselect_b32 s38, s72, s38
	s_lshl_b32 s78, s73, 7
	s_lshl_b32 s73, s38, 7
	s_add_i32 s83, s78, 0x20000
	s_add_i32 s81, s78, 0x40000
	s_add_i32 s80, s78, 0x60000
	s_add_i32 s79, 0, 0x18010
	s_add_i32 s77, 0, 0x1c010
	s_add_i32 s76, s73, 0x20000
	s_add_i32 s75, s73, 0x40000
	s_add_i32 s74, s73, 0x60000
	s_add_i32 s72, s69, 0x100
	s_cmp_gt_u32 s71, 13
	ds_read_b128 v[168:171], v135 offset:16
	ds_read_b128 v[176:179], v135 offset:2064
	ds_read_b128 v[172:175], v136 offset:16
	ds_read_b128 v[180:183], v136 offset:2064
	ds_read_b128 v[192:195], v135 offset:4112
	ds_read_b128 v[200:203], v135 offset:6160
	ds_read_b128 v[196:199], v136 offset:4112
	ds_read_b128 v[204:207], v136 offset:6160
	s_mov_b32 m0, s67
	s_nop 0
	buffer_load_dwordx4 v129, s[8:11], s69 offen lds
	s_nop 0
	s_mov_b32 m0, s68
	s_nop 0
	buffer_load_dwordx4 v132, s[8:11], s69 offen lds
	s_waitcnt lgkmcnt(8)
	s_barrier
	s_waitcnt lgkmcnt(0)
	s_setprio 1
	s_waitcnt lgkmcnt(0)
	v_mfma_scale_f32_16x16x128_f8f6f4 v[216:219], v[146:153], v[200:207], v[216:219], v165, v164 op_sel_hi:[0,0,0]
	v_mfma_scale_f32_16x16x128_f8f6f4 v[48:51], v[154:161], v[200:207], v[48:51], v165, v164 op_sel_hi:[0,0,0]
	v_mfma_scale_f32_16x16x128_f8f6f4 v[138:141], v[146:153], v[168:175], v[124:127], v165, v164 op_sel_hi:[0,0,0]
	v_mfma_scale_f32_16x16x128_f8f6f4 v[142:145], v[154:161], v[168:175], v[120:123], v165, v164 op_sel_hi:[0,0,0]
	v_mfma_scale_f32_16x16x128_f8f6f4 v[184:187], v[146:153], v[176:183], v[108:111], v165, v164 op_sel_hi:[0,0,0]
	v_mfma_scale_f32_16x16x128_f8f6f4 v[188:191], v[154:161], v[176:183], v[100:103], v165, v164 op_sel_hi:[0,0,0]
	v_mfma_scale_f32_16x16x128_f8f6f4 v[208:211], v[146:153], v[192:199], v[84:87], v165, v164 op_sel_hi:[0,0,0]
	v_mfma_scale_f32_16x16x128_f8f6f4 v[212:215], v[154:161], v[192:199], v[80:83], v165, v164 op_sel_hi:[0,0,0]
	s_setprio 0
	s_barrier
	v_add_u32_e32 v68, s82, v133
	v_add_u32_e32 v69, s82, v134
	s_nop 2
	ds_read_b128 v[80:83], v68
	ds_read_b128 v[120:123], v68 offset:2048
	ds_read_b128 v[84:87], v69
	ds_read_b128 v[124:127], v69 offset:2048
	s_mov_b32 m0, s39
	s_nop 0
	buffer_load_dwordx4 v130, s[4:7], s78 offen lds
	s_nop 0
	s_mov_b32 m0, s50
	s_nop 0
	buffer_load_dwordx4 v130, s[4:7], s83 offen lds
	s_barrier
	s_waitcnt lgkmcnt(0)
	s_setprio 1
	s_waitcnt lgkmcnt(1)
	v_mfma_scale_f32_16x16x128_f8f6f4 v[116:119], v[80:87], v[168:175], v[116:119], v165, v164 op_sel_hi:[0,0,0]
	s_waitcnt lgkmcnt(0)
	v_mfma_scale_f32_16x16x128_f8f6f4 v[112:115], v[120:127], v[168:175], v[112:115], v165, v164 op_sel_hi:[0,0,0]
	v_mfma_scale_f32_16x16x128_f8f6f4 v[76:79], v[80:87], v[200:207], v[76:79], v165, v164 op_sel_hi:[0,0,0]
	v_mfma_scale_f32_16x16x128_f8f6f4 v[166:169], v[80:87], v[176:183], v[104:107], v165, v164 op_sel_hi:[0,0,0]
	v_mfma_scale_f32_16x16x128_f8f6f4 v[170:173], v[120:127], v[176:183], v[96:99], v165, v164 op_sel_hi:[0,0,0]
	v_mfma_scale_f32_16x16x128_f8f6f4 v[174:177], v[80:87], v[192:199], v[92:95], v165, v164 op_sel_hi:[0,0,0]
	v_mfma_scale_f32_16x16x128_f8f6f4 v[178:181], v[120:127], v[192:199], v[88:91], v165, v164 op_sel_hi:[0,0,0]
	v_mfma_scale_f32_16x16x128_f8f6f4 v[192:195], v[120:127], v[200:207], v[16:19], v165, v164 op_sel_hi:[0,0,0]
	s_setprio 0
	s_barrier
	ds_read_b128 v[68:71], v135 offset:16400
	s_nop 2
	ds_read_b128 v[88:91], v135 offset:18448
	ds_read_b128 v[72:75], v136 offset:16400
	ds_read_b128 v[92:95], v136 offset:18448
	ds_read_b128 v[96:99], v135 offset:20496
	ds_read_b128 v[104:107], v135 offset:22544
	ds_read_b128 v[100:103], v136 offset:20496
	ds_read_b128 v[108:111], v136 offset:22544
	s_mov_b32 m0, s51
	s_nop 0
	buffer_load_dwordx4 v128, s[8:11], s78 offen lds
	s_nop 0
	s_mov_b32 m0, s54
	s_nop 0
	buffer_load_dwordx4 v131, s[8:11], s78 offen lds
	s_barrier
	s_waitcnt lgkmcnt(0)
	s_setprio 1
	s_waitcnt lgkmcnt(5)
	v_mfma_scale_f32_16x16x128_f8f6f4 v[56:59], v[146:153], v[68:75], v[56:59], v165, v164 op_sel_hi:[0,0,0]
	v_mfma_scale_f32_16x16x128_f8f6f4 v[52:55], v[154:161], v[68:75], v[52:55], v165, v164 op_sel_hi:[0,0,0]
	s_waitcnt lgkmcnt(1)
	v_mfma_scale_f32_16x16x128_f8f6f4 v[224:227], v[154:161], v[96:103], v[224:227], v165, v164 op_sel_hi:[0,0,0]
	v_mfma_scale_f32_16x16x128_f8f6f4 v[200:203], v[146:153], v[88:95], v[36:39], v165, v164 op_sel_hi:[0,0,0]
	v_mfma_scale_f32_16x16x128_f8f6f4 v[204:207], v[154:161], v[88:95], v[32:35], v165, v164 op_sel_hi:[0,0,0]
	v_mfma_scale_f32_16x16x128_f8f6f4 v[220:223], v[146:153], v[96:103], v[20:23], v165, v164 op_sel_hi:[0,0,0]
	s_waitcnt lgkmcnt(0)
	v_mfma_scale_f32_16x16x128_f8f6f4 v[228:231], v[146:153], v[104:111], v[4:7], v165, v164 op_sel_hi:[0,0,0]
	v_mfma_scale_f32_16x16x128_f8f6f4 v[232:235], v[154:161], v[104:111], v[0:3], v165, v164 op_sel_hi:[0,0,0]
	s_setprio 0
	s_barrier
	s_mov_b32 m0, s55
	s_nop 0
	buffer_load_dwordx4 v130, s[4:7], s81 offen lds
	s_nop 0
	s_mov_b32 m0, s58
	s_nop 0
	buffer_load_dwordx4 v130, s[4:7], s80 offen lds
	s_waitcnt vmcnt(6)
	s_barrier
; #define G_WAIT_V(n) asm volatile("s_waitcnt vmcnt(" #n ")" ::: "memory")
; #define G_BAR() __builtin_amdgcn_s_barrier()
; #define G_SCHED() __builtin_amdgcn_sched_barrier(0)
; #define D_STAGE_A(slot, half, kt) D_STAGE(rsA, voffA, slot, half, kt)
; #define D_STAGE_B(slot, half, kt) D_STAGE(rsB, voffB, slot, half, kt)
; #define D_LDA(dst, slot) do { _Pragma("unroll") for (int m = 0; m < 4; ++m) _Pragma("unroll") for (int k = 0; k < 2; ++k) \
;     dst[m][k] = *(const LDS_AS bf16x8*)(lds + (slot) + aoff + m * 2048 + k * 1024); } while (0)
; #define D_LDB(dst, slot) do { _Pragma("unroll") for (int n = 0; n < 2; ++n) _Pragma("unroll") for (int k = 0; k < 2; ++k) \
;     dst[n][k] = *(const LDS_AS bf16x8*)(lds + (slot) + boff + n * 2048 + k * 1024); } while (0)
; #define D_MMA(ai, bj, At, Bf) do { __builtin_amdgcn_s_setprio(1); _Pragma("unroll") for (int m = 0; m < 4; ++m) _Pragma("unroll") for (int n = 0; n < 2; ++n) _Pragma("unroll") for (int k = 0; k < 2; ++k) \
;     acc[ai][bj][m][n] = __builtin_amdgcn_mfma_f32_16x16x32_bf16(Bf[n][k], At[m][k], acc[ai][bj][m][n], 0, 0, 0); __builtin_amdgcn_s_setprio(0); } while (0)
; #define D_WAIT_L(n) asm volatile("s_waitcnt lgkmcnt(" #n ")" ::: "memory")
; #define D_STAGE_A(slot, half, kt) D_STAGE(rsA, voffA, slot, half, kt)
; #define D_STAGE_B(slot, half, kt) do { _Pragma("unroll") for (int _i = 0; _i < 2; ++_i) { const unsigned _m0 = ldsw + (unsigned)((slot) + _i * 8192); const unsigned _so = (unsigned)(kt) * 128u + (half) * bt_half + _i * bt_piece; \
;     asm volatile("s_mov_b32 m0, %0\n\ts_nop 4\n\tbuffer_load_dwordx4 %1, %2, %3 offen lds" :: "s"(_m0), "v"(voffB0), "s"(rsB), "s"(_so) : "m0", "memory"); } } while (0)
;     ...
;     G_WAIT_V(6); G_BAR(); G_SCHED(); D_MMA(1, 1, At, B1); G_BAR(); G_SCHED();
;     D_LDB(B0, G_SB(1, 0)); G_SCHED(); D_LDA(At, G_SA(1, 0)); D_STAGE_A(G_SA(0, 1), 1, t2);
;     D_WAIT_L(8); G_BAR(); D_WAIT_L(0); G_SCHED(); D_MMA(0, 0, At, B0); G_BAR(); G_SCHED();
;     D_LDB(B1, G_SB(1, 1)); D_STAGE_B(G_SB(1, 0), 0, t3);
;     G_BAR(); D_WAIT_L(0); G_SCHED(); D_MMA(0, 1, At, B1); G_BAR(); G_SCHED();
;     D_LDA(At, G_SA(1, 1)); D_STAGE_A(G_SA(1, 0), 0, t3);
;     G_BAR(); D_WAIT_L(0); G_SCHED(); D_MMA(1, 0, At, B0); G_BAR(); G_SCHED();
;     D_STAGE_B(G_SB(1, 1), 1, t3);
;     G_WAIT_V(6); G_BAR(); G_SCHED(); D_MMA(1, 1, At, B1); G_BAR(); G_SCHED();
;   }
;   if (!F8_PEEL) G_WAIT_V(0);
	s_setprio 1
	v_mfma_scale_f32_16x16x128_f8f6f4 v[64:67], v[80:87], v[68:75], v[64:67], v165, v164 op_sel_hi:[0,0,0]
	v_mfma_scale_f32_16x16x128_f8f6f4 v[60:63], v[120:127], v[68:75], v[60:63], v165, v164 op_sel_hi:[0,0,0]
	v_mfma_scale_f32_16x16x128_f8f6f4 v[236:239], v[80:87], v[88:95], v[44:47], v165, v164 op_sel_hi:[0,0,0]
	v_mfma_scale_f32_16x16x128_f8f6f4 v[240:243], v[120:127], v[88:95], v[40:43], v165, v164 op_sel_hi:[0,0,0]
	v_mfma_scale_f32_16x16x128_f8f6f4 v[244:247], v[80:87], v[96:103], v[28:31], v165, v164 op_sel_hi:[0,0,0]
	v_mfma_scale_f32_16x16x128_f8f6f4 v[248:251], v[120:127], v[96:103], v[24:27], v165, v164 op_sel_hi:[0,0,0]
	v_mfma_scale_f32_16x16x128_f8f6f4 v[68:71], v[80:87], v[104:111], v[12:15], v165, v164 op_sel_hi:[0,0,0]
	v_mfma_scale_f32_16x16x128_f8f6f4 v[72:75], v[120:127], v[104:111], v[8:11], v165, v164 op_sel_hi:[0,0,0]
	s_setprio 0
	s_barrier
	v_add_u32_e32 v4, s79, v133
	s_nop 2
	v_add_u32_e32 v12, s79, v134
	ds_read_b128 v[0:3], v4
	ds_read_b128 v[8:11], v4 offset:2048
	ds_read_b128 v[4:7], v12
	ds_read_b128 v[12:15], v12 offset:2048
	ds_read_b128 v[16:19], v135 offset:32784
	ds_read_b128 v[24:27], v135 offset:34832
	ds_read_b128 v[20:23], v136 offset:32784
	ds_read_b128 v[28:31], v136 offset:34832
	ds_read_b128 v[32:35], v135 offset:36880
	ds_read_b128 v[40:43], v135 offset:38928
	ds_read_b128 v[36:39], v136 offset:36880
	ds_read_b128 v[44:47], v136 offset:38928
	s_mov_b32 m0, s59
	s_nop 0
	buffer_load_dwordx4 v129, s[8:11], s78 offen lds
	s_nop 0
	s_mov_b32 m0, s60
	s_nop 0
	buffer_load_dwordx4 v132, s[8:11], s78 offen lds
	s_waitcnt lgkmcnt(8)
	s_barrier
	s_waitcnt lgkmcnt(0)
	s_setprio 1
	s_waitcnt lgkmcnt(5)
	v_mfma_scale_f32_16x16x128_f8f6f4 v[124:127], v[0:7], v[16:23], v[138:141], v165, v164 op_sel_hi:[0,0,0]
	v_mfma_scale_f32_16x16x128_f8f6f4 v[120:123], v[8:15], v[16:23], v[142:145], v165, v164 op_sel_hi:[0,0,0]
	s_waitcnt lgkmcnt(4)
	v_mfma_scale_f32_16x16x128_f8f6f4 v[108:111], v[0:7], v[24:31], v[184:187], v165, v164 op_sel_hi:[0,0,0]
	v_mfma_scale_f32_16x16x128_f8f6f4 v[100:103], v[8:15], v[24:31], v[188:191], v165, v164 op_sel_hi:[0,0,0]
	s_waitcnt lgkmcnt(1)
	v_mfma_scale_f32_16x16x128_f8f6f4 v[84:87], v[0:7], v[32:39], v[208:211], v165, v164 op_sel_hi:[0,0,0]
	v_mfma_scale_f32_16x16x128_f8f6f4 v[80:83], v[8:15], v[32:39], v[212:215], v165, v164 op_sel_hi:[0,0,0]
	s_waitcnt lgkmcnt(0)
	v_mfma_scale_f32_16x16x128_f8f6f4 v[216:219], v[0:7], v[40:47], v[216:219], v165, v164 op_sel_hi:[0,0,0]
	v_mfma_scale_f32_16x16x128_f8f6f4 v[48:51], v[8:15], v[40:47], v[48:51], v165, v164 op_sel_hi:[0,0,0]
	s_setprio 0
	s_barrier
	v_add_u32_e32 v88, s77, v133
	v_add_u32_e32 v89, s77, v134
	ds_read_b128 v[146:149], v88
	ds_read_b128 v[154:157], v88 offset:2048
	ds_read_b128 v[150:153], v89
	ds_read_b128 v[158:161], v89 offset:2048
	s_mov_b32 m0, s61
	s_nop 0
	buffer_load_dwordx4 v130, s[4:7], s73 offen lds
	s_nop 0
	s_mov_b32 m0, s62
	s_nop 0
	buffer_load_dwordx4 v130, s[4:7], s76 offen lds
	s_barrier
	s_waitcnt lgkmcnt(0)
	s_setprio 1
	s_waitcnt lgkmcnt(1)
	v_mfma_scale_f32_16x16x128_f8f6f4 v[116:119], v[146:153], v[16:23], v[116:119], v165, v164 op_sel_hi:[0,0,0]
	s_waitcnt lgkmcnt(0)
	v_mfma_scale_f32_16x16x128_f8f6f4 v[112:115], v[154:161], v[16:23], v[112:115], v165, v164 op_sel_hi:[0,0,0]
	v_mfma_scale_f32_16x16x128_f8f6f4 v[104:107], v[146:153], v[24:31], v[166:169], v165, v164 op_sel_hi:[0,0,0]
	v_mfma_scale_f32_16x16x128_f8f6f4 v[96:99], v[154:161], v[24:31], v[170:173], v165, v164 op_sel_hi:[0,0,0]
	v_mfma_scale_f32_16x16x128_f8f6f4 v[92:95], v[146:153], v[32:39], v[174:177], v165, v164 op_sel_hi:[0,0,0]
	v_mfma_scale_f32_16x16x128_f8f6f4 v[88:91], v[154:161], v[32:39], v[178:181], v165, v164 op_sel_hi:[0,0,0]
	v_mfma_scale_f32_16x16x128_f8f6f4 v[76:79], v[146:153], v[40:47], v[76:79], v165, v164 op_sel_hi:[0,0,0]
	v_mfma_scale_f32_16x16x128_f8f6f4 v[16:19], v[154:161], v[40:47], v[192:195], v165, v164 op_sel_hi:[0,0,0]
	s_setprio 0
	s_barrier
	ds_read_b128 v[24:27], v135 offset:49168
	ds_read_b128 v[168:171], v135 offset:51216
	ds_read_b128 v[28:31], v136 offset:49168
	ds_read_b128 v[172:175], v136 offset:51216
	ds_read_b128 v[176:179], v135 offset:53264
	ds_read_b128 v[192:195], v135 offset:55312
	ds_read_b128 v[180:183], v136 offset:53264
	ds_read_b128 v[196:199], v136 offset:55312
	s_mov_b32 m0, s63
	s_nop 0
	buffer_load_dwordx4 v128, s[8:11], s73 offen lds
	s_nop 0
	s_mov_b32 m0, s64
	s_nop 0
	buffer_load_dwordx4 v131, s[8:11], s73 offen lds
	s_barrier
	s_waitcnt lgkmcnt(0)
	s_setprio 1
	s_waitcnt lgkmcnt(5)
	v_mfma_scale_f32_16x16x128_f8f6f4 v[56:59], v[0:7], v[24:31], v[56:59], v165, v164 op_sel_hi:[0,0,0]
	v_mfma_scale_f32_16x16x128_f8f6f4 v[52:55], v[8:15], v[24:31], v[52:55], v165, v164 op_sel_hi:[0,0,0]
	s_waitcnt lgkmcnt(4)
	v_mfma_scale_f32_16x16x128_f8f6f4 v[36:39], v[0:7], v[168:175], v[200:203], v165, v164 op_sel_hi:[0,0,0]
	v_mfma_scale_f32_16x16x128_f8f6f4 v[32:35], v[8:15], v[168:175], v[204:207], v165, v164 op_sel_hi:[0,0,0]
	s_waitcnt lgkmcnt(1)
	v_mfma_scale_f32_16x16x128_f8f6f4 v[20:23], v[0:7], v[176:183], v[220:223], v165, v164 op_sel_hi:[0,0,0]
	v_mfma_scale_f32_16x16x128_f8f6f4 v[224:227], v[8:15], v[176:183], v[224:227], v165, v164 op_sel_hi:[0,0,0]
	s_waitcnt lgkmcnt(0)
	v_mfma_scale_f32_16x16x128_f8f6f4 v[4:7], v[0:7], v[192:199], v[228:231], v165, v164 op_sel_hi:[0,0,0]
	v_mfma_scale_f32_16x16x128_f8f6f4 v[0:3], v[8:15], v[192:199], v[232:235], v165, v164 op_sel_hi:[0,0,0]
	s_setprio 0
	s_barrier
	s_mov_b32 m0, s65
	s_nop 0
	buffer_load_dwordx4 v130, s[4:7], s75 offen lds
	s_nop 0
	s_mov_b32 m0, s66
	s_nop 0
	buffer_load_dwordx4 v130, s[4:7], s74 offen lds
	s_waitcnt vmcnt(6)
	s_barrier
	s_setprio 1
	v_mfma_scale_f32_16x16x128_f8f6f4 v[64:67], v[146:153], v[24:31], v[64:67], v165, v164 op_sel_hi:[0,0,0]
	v_mfma_scale_f32_16x16x128_f8f6f4 v[60:63], v[154:161], v[24:31], v[60:63], v165, v164 op_sel_hi:[0,0,0]
	v_mfma_scale_f32_16x16x128_f8f6f4 v[44:47], v[146:153], v[168:175], v[236:239], v165, v164 op_sel_hi:[0,0,0]
	v_mfma_scale_f32_16x16x128_f8f6f4 v[40:43], v[154:161], v[168:175], v[240:243], v165, v164 op_sel_hi:[0,0,0]
	v_mfma_scale_f32_16x16x128_f8f6f4 v[28:31], v[146:153], v[176:183], v[244:247], v165, v164 op_sel_hi:[0,0,0]
	v_mfma_scale_f32_16x16x128_f8f6f4 v[24:27], v[154:161], v[176:183], v[248:251], v165, v164 op_sel_hi:[0,0,0]
	v_mfma_scale_f32_16x16x128_f8f6f4 v[12:15], v[146:153], v[192:199], v[68:71], v165, v164 op_sel_hi:[0,0,0]
	v_mfma_scale_f32_16x16x128_f8f6f4 v[8:11], v[154:161], v[192:199], v[72:75], v165, v164 op_sel_hi:[0,0,0]
	s_setprio 0
	s_barrier
	s_mov_b32 s69, s72
	s_mov_b32 s71, s70
	s_cbranch_scc0 .LBB0_1606
	s_waitcnt vmcnt(0)
	s_cmpk_lt_u32 s13, 0x100
	s_cbranch_scc0 .LBB0_1609
	s_barrier
; #define LDS_AS __attribute__((address_space(3)))
; #define OPAQUE_TID(P) (((P).wid0 << 6) | lane_id_now())
; #define P_STAGE_A(slot, half, kt) do { _Pragma("unroll") for (int _i = 0; _i < 2; ++_i) { const unsigned _m0 = ldsw + (unsigned)((slot) + _i * 8192); const unsigned _so = (unsigned)(kt) * 128u; \
;     asm volatile("s_mov_b32 m0, %0\n\ts_nop 4\n\tbuffer_load_dwordx4 %1, %2, %3 offen lds" :: "s"(_m0), "v"(voffA[half][_i]), "s"(rsA), "s"(_so) : "m0", "memory"); } } while (0)
; #define P_STAGE_B(slot, half, kt) do { _Pragma("unroll") for (int _i = 0; _i < 2; ++_i) { const unsigned _m0 = ldsw + (unsigned)((slot) + _i * 8192); const unsigned _so = (unsigned)(kt) * 128u + (half) * bt_half + _i * bt_piece; \
;     asm volatile("s_mov_b32 m0, %0\n\ts_nop 4\n\tbuffer_load_dwordx4 %1, %2, %3 offen lds" :: "s"(_m0), "v"(voffB0), "s"(rsB), "s"(_so) : "m0", "memory"); } } while (0)
;   DI unsigned bt_rowoff(int h, int R) const { return (unsigned)(pn * 256 + 128 * h + (pn < 15 ? tcol_adj(R) : tcol_p64(R))) * 4096u; }
; template <class Cfg>
; DI void f8dma_issue_prologue_st(LDS_AS unsigned char* lds, const Cfg& cfg) {
;   const int tid = OPAQUE_TID(cfg.p), wid = __builtin_amdgcn_readfirstlane(tid >> 6), lane = tid & 63;
;   const LDS_AS unsigned* stash = (const LDS_AS unsigned*)(lds + F8_STASH);
;   unsigned voffA[2][2], voffB0;
;   voffA[0][0] = stash[tid]; voffA[0][1] = stash[512 + tid]; voffA[1][0] = stash[1024 + tid]; voffA[1][1] = stash[1536 + tid];
;   {
;     const int r = 8 * wid + (lane >> 3);
;     const unsigned cofs = 16u * (((unsigned)lane & 7u) ^ (((unsigned)lane >> 3) & 7u));
;     voffB0 = cfg.bt_rowoff(0, r) + cofs;
;   }
;   const unsigned bt_half = cfg.bt_rowoff(1, 0) - cfg.bt_rowoff(0, 0), bt_piece = cfg.bt_rowoff(0, 64) - cfg.bt_rowoff(0, 0);
;   const __amdgpu_buffer_rsrc_t rsA = __builtin_amdgcn_make_buffer_rsrc((void*)cfg.a_base(), 0, cfg.a_bytes(), 0x00020000);
;   const __amdgpu_buffer_rsrc_t rsB = __builtin_amdgcn_make_buffer_rsrc((void*)cfg.bt_base(), 0, cfg.bt_bytes(), 0x00020000);
;   const unsigned ldsw = (unsigned)__builtin_amdgcn_readfirstlane((int)(unsigned)(size_t)lds) + (unsigned)wid * 1024u;
;     ...
;   P_STAGE_B(G_SB(0, 0), 0, 0); P_STAGE_A(G_SA(0, 0), 0, 0); P_STAGE_B(G_SB(0, 1), 1, 0); P_STAGE_A(G_SA(0, 1), 1, 0);
;   P_STAGE_B(G_SB(1, 0), 0, 1); P_STAGE_A(G_SA(1, 0), 0, 1); P_STAGE_B(G_SB(1, 1), 1, 1);
.LBB0_1609:
	s_and_b64 vcc, exec, s[2:3]
	s_cbranch_vccnz .LBB0_1611
	v_mbcnt_lo_u32_b32 v72, -1, 0
	v_mbcnt_hi_u32_b32 v72, -1, v72
	s_ashr_i32 s13, s12, 31
	v_or_b32_e32 v68, s87, v72
	v_bfe_u32 v74, v72, 3, 3
	v_readfirstlane_b32 s2, v68
	s_ashr_i32 s38, s2, 6
	s_lshl_b32 s2, s38, 3
	v_lshrrev_b32_e32 v73, 3, v72
	v_or_b32_e32 v75, s2, v74
	v_xor_b32_e32 v72, v73, v72
	s_lshl_b32 s3, s38, 1
	v_lshlrev_b32_e32 v73, 1, v75
	v_mov_b32_e32 v75, 0x63
	s_and_b32 s3, s3, 4
	v_and_b32_e32 v73, 24, v73
	v_bitop3_b32 v74, s2, v75, v74 bitop3:0xc8
	v_lshlrev_b32_e32 v72, 4, v72
	v_or3_b32 v73, s3, v74, v73
	v_and_b32_e32 v72, 0x70, v72
	s_lshl_b32 s2, s44, 19
	v_lshlrev_b32_e32 v73, 11, v73
	v_or3_b32 v72, v73, s2, v72
	s_lshl_b64 s[2:3], s[12:13], 22
	v_lshl_add_u32 v68, v68, 2, 0
	s_add_u32 s4, s52, s2
	v_add_u32_e32 v70, 0x22410, v68
	s_addc_u32 s2, s53, s3
	ds_read2st64_b32 v[68:69], v70 offset1:8
	ds_read2st64_b32 v[70:71], v70 offset0:16 offset1:24
	s_and_b32 s5, s2, 0xffff
	s_lshl_b32 s2, s38, 10
	s_add_i32 s2, s2, 0
	s_add_i32 s3, s2, 0x10010
	s_mov_b32 m0, s3
	s_nop 0
	buffer_load_dwordx4 v72, s[4:7], s31 offen lds
	s_add_i32 s3, s2, 0x12010
	s_mov_b32 m0, s3
	s_nop 0
	buffer_load_dwordx4 v72, s[4:7], s7 offen lds
	s_add_i32 s3, s2, 16
	s_waitcnt lgkmcnt(1)
	s_mov_b32 m0, s3
	s_nop 0
	buffer_load_dwordx4 v68, s[8:11], s31 offen lds
	s_add_i32 s3, s2, 0x2010
	s_mov_b32 m0, s3
	s_nop 0
	buffer_load_dwordx4 v69, s[8:11], s31 offen lds
	s_add_i32 s3, s2, 0x14010
	s_mov_b32 m0, s3
	s_nop 0
	buffer_load_dwordx4 v72, s[4:7], s34 offen lds
	s_add_i32 s3, s2, 0x16010
	s_mov_b32 m0, s3
	s_nop 0
	buffer_load_dwordx4 v72, s[4:7], s35 offen lds
	s_add_i32 s3, s2, 0x4010
	s_waitcnt lgkmcnt(0)
	s_mov_b32 m0, s3
	s_nop 0
	buffer_load_dwordx4 v70, s[8:11], s31 offen lds
	s_add_i32 s3, s2, 0x6010
	s_mov_b32 m0, s3
	s_nop 0
	buffer_load_dwordx4 v71, s[8:11], s31 offen lds
	s_add_i32 s3, s2, 0x18010
	s_mov_b32 m0, s3
	s_nop 0
	buffer_load_dwordx4 v72, s[4:7], s33 offen lds
	s_add_i32 s3, s2, 0x1a010
	s_mov_b32 m0, s3
	s_nop 0
	buffer_load_dwordx4 v72, s[4:7], s36 offen lds
	s_add_i32 s3, s2, 0x8010
	s_mov_b32 m0, s3
	s_nop 0
	buffer_load_dwordx4 v68, s[8:11], s33 offen lds
	s_add_i32 s3, s2, 0xa010
	s_mov_b32 m0, s3
	s_nop 0
	buffer_load_dwordx4 v69, s[8:11], s33 offen lds
	s_add_i32 s3, s2, 0x1c010
	s_mov_b32 m0, s3
	s_nop 0
	buffer_load_dwordx4 v72, s[4:7], s37 offen lds
	s_add_i32 s2, s2, 0x1e010
	s_mov_b32 m0, s2
	s_nop 0
	buffer_load_dwordx4 v72, s[4:7], s42 offen lds

; #define G_WAIT_V(n) asm volatile("s_waitcnt vmcnt(" #n ")" ::: "memory")
; #define G_BAR() __builtin_amdgcn_s_barrier()
; #define D_STAGE_A(slot, half, kt) D_STAGE(rsA, voffA, slot, half, kt)
; #define D_STAGE_B(slot, half, kt) D_STAGE(rsB, voffB, slot, half, kt)
; #define D_STAGE_A(slot, half, kt) D_STAGE(rsA, voffA, slot, half, kt)
; #define D_STAGE_B(slot, half, kt) do { _Pragma("unroll") for (int _i = 0; _i < 2; ++_i) { const unsigned _m0 = ldsw + (unsigned)((slot) + _i * 8192); const unsigned _so = (unsigned)(kt) * 128u + (half) * bt_half + _i * bt_piece; \
;     asm volatile("s_mov_b32 m0, %0\n\ts_nop 4\n\tbuffer_load_dwordx4 %1, %2, %3 offen lds" :: "s"(_m0), "v"(voffB0), "s"(rsB), "s"(_so) : "m0", "memory"); } } while (0)
;   DI unsigned bt_rowoff(int h, int R) const { return (unsigned)(pn * 256 + 128 * h + (pn < 15 ? tcol_adj(R) : tcol_p64(R))) * 4096u; }
;   DI unsigned a_bytes() const { return (unsigned)NTOK * 4096u; }
;     ...
;   const unsigned bt_half = cfg.bt_rowoff(1, 0) - cfg.bt_rowoff(0, 0), bt_piece = cfg.bt_rowoff(0, 64) - cfg.bt_rowoff(0, 0);
;   const __amdgpu_buffer_rsrc_t rsA = __builtin_amdgcn_make_buffer_rsrc((void*)cfg.a_base(), 0, cfg.a_bytes(), 0x00020000);
;   const __amdgpu_buffer_rsrc_t rsB = __builtin_amdgcn_make_buffer_rsrc((void*)cfg.bt_base(), 0, cfg.bt_bytes(), 0x00020000);
;   const unsigned ldsw = (unsigned)__builtin_amdgcn_readfirstlane((int)(unsigned)(size_t)lds) + (unsigned)wid * 1024u;
;     ...
;   unsigned aoff[2], boff[2];
; #pragma unroll
;   for (int j = 0; j < 2; ++j) {
;     aoff[j] = (unsigned)(64 * wr + fr) * 128u + 16u * ((2u * fq + j) ^ ((unsigned)fr & 7u));
;     boff[j] = (unsigned)(32 * wc + fr) * 128u + 16u * ((2u * fq + j) ^ ((unsigned)fr & 7u));
;   }
;     ...
;   const int scw = cfg.scale_w(), scx = cfg.scale_x();
;     ...
;   f32x4 acc[2][2][4][2];
; #pragma unroll
;   for (int a = 0; a < 2; ++a)
; #pragma unroll
;     for (int b = 0; b < 2; ++b)
; #pragma unroll
;       for (int m = 0; m < 4; ++m)
; #pragma unroll
;         for (int n = 0; n < 2; ++n) acc[a][b][m][n] = (f32x4){0.f, 0.f, 0.f, 0.f};
;   i32x8 At[4], B0[2], B1[2];
;   if (!PRE) {
;     D_STAGE_B(G_SB(0, 0), 0, 0); D_STAGE_A(G_SA(0, 0), 0, 0); D_STAGE_B(G_SB(0, 1), 1, 0); D_STAGE_A(G_SA(0, 1), 1, 0);
;     D_STAGE_B(G_SB(1, 0), 0, 1); D_STAGE_A(G_SA(1, 0), 0, 1); D_STAGE_B(G_SB(1, 1), 1, 1);
;   }
;   G_WAIT_V(0); G_BAR();
.LBB0_1631:
	s_lshr_b32 s4, s4, 2
	v_lshlrev_b32_e32 v3, 1, v2
	v_and_b32_e32 v2, 0x63, v2
	s_ashr_i32 s15, s14, 31
	s_ashr_i32 s19, s13, 8
	s_lshl_b32 s18, s26, 8
	v_and_or_b32 v2, s4, 4, v2
	s_lshl_b64 s[4:5], s[14:15], 22
	s_add_u32 s4, s52, s4
	v_and_b32_e32 v3, 24, v3
	s_addc_u32 s5, s53, s5
	s_lshl_b32 s15, s66, 10
	v_or3_b32 v2, v2, v3, s18
	s_add_i32 s67, s15, 0
	v_lshl_or_b32 v66, v2, 11, v6
	s_and_b32 s5, s5, 0xffff
	s_add_i32 s39, s67, 0x10010
	s_mov_b32 m0, s39
	s_nop 0
	buffer_load_dwordx4 v66, s[4:7], s31 offen lds
	s_add_i32 s49, s67, 0x12010
	s_mov_b32 m0, s49
	s_nop 0
	buffer_load_dwordx4 v66, s[4:7], s7 offen lds
	s_waitcnt vmcnt(3)
	v_lshl_or_b32 v64, v7, 11, v6
	s_add_i32 s50, s67, 16
	s_mov_b32 m0, s50
	s_nop 0
	buffer_load_dwordx4 v64, s[8:11], s31 offen lds
	s_waitcnt vmcnt(1)
	v_lshl_or_b32 v67, v4, 11, v6
	s_add_i32 s51, s67, 0x2010
	s_mov_b32 m0, s51
	s_nop 0
	buffer_load_dwordx4 v67, s[8:11], s31 offen lds
	s_add_i32 s54, s67, 0x14010
	s_mov_b32 m0, s54
	s_nop 0
	buffer_load_dwordx4 v66, s[4:7], s34 offen lds
	s_add_i32 s55, s67, 0x16010
	s_mov_b32 m0, s55
	s_nop 0
	buffer_load_dwordx4 v66, s[4:7], s35 offen lds
	v_lshl_or_b32 v65, v8, 11, v6
	s_add_i32 s58, s67, 0x4010
	s_mov_b32 m0, s58
	s_nop 0
	buffer_load_dwordx4 v65, s[8:11], s31 offen lds
	s_waitcnt vmcnt(0)
	v_lshl_or_b32 v68, v5, 11, v6
	s_add_i32 s59, s67, 0x6010
	s_mov_b32 m0, s59
	s_nop 0
	buffer_load_dwordx4 v68, s[8:11], s31 offen lds
	s_add_i32 s60, s67, 0x18010
	s_mov_b32 m0, s60
	s_nop 0
	buffer_load_dwordx4 v66, s[4:7], s33 offen lds
	s_add_i32 s61, s67, 0x1a010
	s_mov_b32 m0, s61
	s_nop 0
	buffer_load_dwordx4 v66, s[4:7], s36 offen lds
	s_add_i32 s62, s67, 0x8010
	s_mov_b32 m0, s62
	s_nop 0
	buffer_load_dwordx4 v64, s[8:11], s33 offen lds
	s_add_i32 s63, s67, 0xa010
	s_mov_b32 m0, s63
	s_nop 0
	buffer_load_dwordx4 v67, s[8:11], s33 offen lds
	s_add_i32 s64, s67, 0x1c010
	s_mov_b32 m0, s64
	s_nop 0
	buffer_load_dwordx4 v66, s[4:7], s37 offen lds
	s_add_i32 s65, s67, 0x1e010
	s_mov_b32 m0, s65
	s_nop 0
	buffer_load_dwordx4 v66, s[4:7], s42 offen lds
	s_waitcnt vmcnt(0)
	s_cmp_lg_u32 s19, 1
	s_barrier
	s_cbranch_scc1 .LBB0_1633
	s_barrier

; #define G_WAIT_V(n) asm volatile("s_waitcnt vmcnt(" #n ")" ::: "memory")
; #define G_BAR() __builtin_amdgcn_s_barrier()
; #define G_SCHED() __builtin_amdgcn_sched_barrier(0)
; #define D_STAGE_A(slot, half, kt) D_STAGE(rsA, voffA, slot, half, kt)
; #define D_STAGE_B(slot, half, kt) D_STAGE(rsB, voffB, slot, half, kt)
; #define D_LDA(dst, slot) do { _Pragma("unroll") for (int m = 0; m < 4; ++m) _Pragma("unroll") for (int k = 0; k < 2; ++k) \
;     dst[m][k] = *(const LDS_AS bf16x8*)(lds + (slot) + aoff + m * 2048 + k * 1024); } while (0)
; #define D_LDB(dst, slot) do { _Pragma("unroll") for (int n = 0; n < 2; ++n) _Pragma("unroll") for (int k = 0; k < 2; ++k) \
;     dst[n][k] = *(const LDS_AS bf16x8*)(lds + (slot) + boff + n * 2048 + k * 1024); } while (0)
; #define D_MMA(ai, bj, At, Bf) do { __builtin_amdgcn_s_setprio(1); _Pragma("unroll") for (int m = 0; m < 4; ++m) _Pragma("unroll") for (int n = 0; n < 2; ++n) _Pragma("unroll") for (int k = 0; k < 2; ++k) \
;     acc[ai][bj][m][n] = __builtin_amdgcn_mfma_f32_16x16x32_bf16(Bf[n][k], At[m][k], acc[ai][bj][m][n], 0, 0, 0); __builtin_amdgcn_s_setprio(0); } while (0)
; #define D_WAIT_L(n) asm volatile("s_waitcnt lgkmcnt(" #n ")" ::: "memory")
; #define D_STAGE_A(slot, half, kt) D_STAGE(rsA, voffA, slot, half, kt)
; #define D_WAIT_L(n) asm volatile("s_waitcnt lgkmcnt(" #n ")" ::: "memory")
;     ...
;     D_LDB(B0, G_SB(0, 0)); G_SCHED(); D_LDA(At, G_SA(0, 0)); D_STAGE_A(G_SA(1, 1), 1, t1);
;     D_WAIT_L(8); G_BAR(); D_WAIT_L(0); G_SCHED(); D_MMA(0, 0, At, B0); G_BAR(); G_SCHED();
;     D_LDB(B1, G_SB(0, 1)); D_STAGE_B(G_SB(0, 0), 0, t2);
;     G_BAR(); D_WAIT_L(0); G_SCHED(); D_MMA(0, 1, At, B1); G_BAR(); G_SCHED();
;     D_LDA(At, G_SA(0, 1)); D_STAGE_A(G_SA(0, 0), 0, t2);
;     G_BAR(); D_WAIT_L(0); G_SCHED(); D_MMA(1, 0, At, B0); G_BAR(); G_SCHED();
;     D_STAGE_B(G_SB(0, 1), 1, t2);
;     G_WAIT_V(6); G_BAR(); G_SCHED(); D_MMA(1, 1, At, B1); G_BAR(); G_SCHED();
;     D_LDB(B0, G_SB(1, 0)); G_SCHED(); D_LDA(At, G_SA(1, 0)); D_STAGE_A(G_SA(0, 1), 1, t2);
;     D_WAIT_L(8); G_BAR(); D_WAIT_L(0); G_SCHED(); D_MMA(0, 0, At, B0); G_BAR(); G_SCHED();
;     D_LDB(B1, G_SB(1, 1)); D_STAGE_B(G_SB(1, 0), 0, t3);
.LBB0_1634:
	s_add_i32 s73, 0, 0x10010
	v_add_u32_e32 v73, s73, v69
	v_add_u32_e32 v86, s73, v70
	ds_read_b128 v[74:77], v73
	ds_read_b128 v[82:85], v73 offset:2048
	ds_read_b128 v[78:81], v86
	ds_read_b128 v[86:89], v86 offset:2048
	s_add_i32 s38, s71, 1
	s_add_i32 s70, s71, 3
	s_add_i32 s68, s71, 2
	s_add_i32 s78, 0, 0x14010
	s_cmp_lt_u32 s71, 14
	s_cselect_b32 s72, s68, s71
	s_cselect_b32 s38, s70, s38
	s_lshl_b32 s77, s72, 7
	s_lshl_b32 s72, s38, 7
	s_add_i32 s79, s77, 0x20000
	s_add_i32 s80, s77, 0x40000
	s_add_i32 s81, s77, 0x60000
	s_add_i32 s82, 0, 0x18010
	s_add_i32 s76, 0, 0x1c010
	s_add_i32 s75, s72, 0x20000
	s_add_i32 s74, s72, 0x40000
	s_add_i32 s73, s72, 0x60000
	s_add_i32 s70, s69, 0x100
	s_cmp_gt_u32 s71, 13
	ds_read_b128 v[90:93], v71 offset:16
	ds_read_b128 v[98:101], v71 offset:2064
	ds_read_b128 v[94:97], v72 offset:16
	ds_read_b128 v[102:105], v72 offset:2064
	ds_read_b128 v[106:109], v71 offset:4112
	ds_read_b128 v[114:117], v71 offset:6160
	ds_read_b128 v[110:113], v72 offset:4112
	ds_read_b128 v[118:121], v72 offset:6160
	s_mov_b32 m0, s66
	s_nop 0
	buffer_load_dwordx4 v65, s[8:11], s69 offen lds
	s_nop 0
	s_mov_b32 m0, s67
	s_nop 0
	buffer_load_dwordx4 v68, s[8:11], s69 offen lds
	s_waitcnt lgkmcnt(8)
	s_barrier
	s_waitcnt lgkmcnt(0)
	s_setprio 1
	s_waitcnt lgkmcnt(4)
	v_mfma_scale_f32_16x16x128_f8f6f4 v[40:43], v[74:81], v[98:105], v[40:43], v165, v164 op_sel_hi:[0,0,0]
	v_mfma_scale_f32_16x16x128_f8f6f4 v[32:35], v[82:89], v[98:105], v[32:35], v165, v164 op_sel_hi:[0,0,0]
	s_waitcnt lgkmcnt(1)
	v_mfma_scale_f32_16x16x128_f8f6f4 v[24:27], v[74:81], v[106:113], v[24:27], v165, v164 op_sel_hi:[0,0,0]
	v_mfma_scale_f32_16x16x128_f8f6f4 v[16:19], v[82:89], v[106:113], v[16:19], v165, v164 op_sel_hi:[0,0,0]
	s_waitcnt lgkmcnt(0)
	v_mfma_scale_f32_16x16x128_f8f6f4 v[8:11], v[74:81], v[114:121], v[8:11], v165, v164 op_sel_hi:[0,0,0]
	v_mfma_scale_f32_16x16x128_f8f6f4 v[122:125], v[74:81], v[90:97], v[48:51], v165, v164 op_sel_hi:[0,0,0]
	v_mfma_scale_f32_16x16x128_f8f6f4 v[126:129], v[82:89], v[90:97], v[52:55], v165, v164 op_sel_hi:[0,0,0]
	v_mfma_scale_f32_16x16x128_f8f6f4 v[130:133], v[82:89], v[114:121], v[0:3], v165, v164 op_sel_hi:[0,0,0]
	s_setprio 0
	s_barrier
	s_nop 4
	v_add_u32_e32 v0, s78, v69
	v_add_u32_e32 v1, s78, v70
	ds_read_b128 v[48:51], v0
	ds_read_b128 v[74:77], v0 offset:2048
	ds_read_b128 v[52:55], v1
	ds_read_b128 v[78:81], v1 offset:2048
	s_mov_b32 m0, s39
	s_nop 0
	buffer_load_dwordx4 v66, s[4:7], s77 offen lds
	s_nop 0
	s_mov_b32 m0, s49
	s_nop 0
	buffer_load_dwordx4 v66, s[4:7], s79 offen lds
	s_barrier
	s_waitcnt lgkmcnt(0)
	s_setprio 1
	s_waitcnt lgkmcnt(1)
	v_mfma_scale_f32_16x16x128_f8f6f4 v[44:47], v[48:55], v[98:105], v[44:47], v165, v164 op_sel_hi:[0,0,0]
	s_waitcnt lgkmcnt(0)
	v_mfma_scale_f32_16x16x128_f8f6f4 v[36:39], v[74:81], v[98:105], v[36:39], v165, v164 op_sel_hi:[0,0,0]
	v_mfma_scale_f32_16x16x128_f8f6f4 v[28:31], v[48:55], v[106:113], v[28:31], v165, v164 op_sel_hi:[0,0,0]
	v_mfma_scale_f32_16x16x128_f8f6f4 v[20:23], v[74:81], v[106:113], v[20:23], v165, v164 op_sel_hi:[0,0,0]
	v_mfma_scale_f32_16x16x128_f8f6f4 v[12:15], v[48:55], v[114:121], v[12:15], v165, v164 op_sel_hi:[0,0,0]
	v_mfma_scale_f32_16x16x128_f8f6f4 v[134:137], v[48:55], v[90:97], v[60:63], v165, v164 op_sel_hi:[0,0,0]
	v_mfma_scale_f32_16x16x128_f8f6f4 v[138:141], v[74:81], v[90:97], v[56:59], v165, v164 op_sel_hi:[0,0,0]
	v_mfma_scale_f32_16x16x128_f8f6f4 v[142:145], v[74:81], v[114:121], v[4:7], v165, v164 op_sel_hi:[0,0,0]
	s_setprio 0
	s_barrier
	s_mov_b32 m0, s50
	s_nop 0
	buffer_load_dwordx4 v64, s[8:11], s77 offen lds
	s_nop 0
	s_mov_b32 m0, s51
	s_nop 0
	buffer_load_dwordx4 v67, s[8:11], s77 offen lds
	s_barrier
	s_waitcnt lgkmcnt(0)
	s_barrier
	s_mov_b32 m0, s54
	s_nop 0
	buffer_load_dwordx4 v66, s[4:7], s80 offen lds
	s_nop 0
	s_mov_b32 m0, s55
	s_nop 0
	buffer_load_dwordx4 v66, s[4:7], s81 offen lds
	s_waitcnt vmcnt(6)
	s_barrier
	s_barrier
	v_add_u32_e32 v4, s82, v69
	v_add_u32_e32 v48, s82, v70
	ds_read_b128 v[0:3], v4
	ds_read_b128 v[56:59], v4 offset:2048
	ds_read_b128 v[4:7], v48
	ds_read_b128 v[60:63], v48 offset:2048
	ds_read_b128 v[74:77], v71 offset:32784
	ds_read_b128 v[82:85], v71 offset:34832
	ds_read_b128 v[78:81], v72 offset:32784
	ds_read_b128 v[86:89], v72 offset:34832
	ds_read_b128 v[90:93], v71 offset:36880
	ds_read_b128 v[98:101], v71 offset:38928
	ds_read_b128 v[94:97], v72 offset:36880
	ds_read_b128 v[102:105], v72 offset:38928
	s_mov_b32 m0, s58
	s_nop 0
	buffer_load_dwordx4 v65, s[8:11], s77 offen lds
	s_nop 0
	s_mov_b32 m0, s59
	s_nop 0
	buffer_load_dwordx4 v68, s[8:11], s77 offen lds
	s_waitcnt lgkmcnt(8)
	s_barrier
; #define G_WAIT_V(n) asm volatile("s_waitcnt vmcnt(" #n ")" ::: "memory")
; #define G_BAR() __builtin_amdgcn_s_barrier()
; #define G_SCHED() __builtin_amdgcn_sched_barrier(0)
; #define D_STAGE_A(slot, half, kt) D_STAGE(rsA, voffA, slot, half, kt)
; #define D_STAGE_B(slot, half, kt) D_STAGE(rsB, voffB, slot, half, kt)
; #define D_LDA(dst, slot) do { _Pragma("unroll") for (int m = 0; m < 4; ++m) _Pragma("unroll") for (int k = 0; k < 2; ++k) \
;     dst[m][k] = *(const LDS_AS bf16x8*)(lds + (slot) + aoff + m * 2048 + k * 1024); } while (0)
; #define D_LDB(dst, slot) do { _Pragma("unroll") for (int n = 0; n < 2; ++n) _Pragma("unroll") for (int k = 0; k < 2; ++k) \
;     dst[n][k] = *(const LDS_AS bf16x8*)(lds + (slot) + boff + n * 2048 + k * 1024); } while (0)
; #define D_MMA(ai, bj, At, Bf) do { __builtin_amdgcn_s_setprio(1); _Pragma("unroll") for (int m = 0; m < 4; ++m) _Pragma("unroll") for (int n = 0; n < 2; ++n) _Pragma("unroll") for (int k = 0; k < 2; ++k) \
;     acc[ai][bj][m][n] = __builtin_amdgcn_mfma_f32_16x16x32_bf16(Bf[n][k], At[m][k], acc[ai][bj][m][n], 0, 0, 0); __builtin_amdgcn_s_setprio(0); } while (0)
; #define D_WAIT_L(n) asm volatile("s_waitcnt lgkmcnt(" #n ")" ::: "memory")
; #define P_STAGE_A(slot, half, kt) do { _Pragma("unroll") for (int _i = 0; _i < 2; ++_i) { const unsigned _m0 = ldsw + (unsigned)((slot) + _i * 8192); const unsigned _so = (unsigned)(kt) * 128u; \
;     asm volatile("s_mov_b32 m0, %0\n\ts_nop 4\n\tbuffer_load_dwordx4 %1, %2, %3 offen lds" :: "s"(_m0), "v"(voffA[half][_i]), "s"(rsA), "s"(_so) : "m0", "memory"); } } while (0)
; template <class Cfg>
; DI void f8dma_issue_prologue_st(LDS_AS unsigned char* lds, const Cfg& cfg) {
;     ...
;   P_STAGE_B(G_SB(0, 0), 0, 0); P_STAGE_A(G_SA(0, 0), 0, 0); P_STAGE_B(G_SB(0, 1), 1, 0); P_STAGE_A(G_SA(0, 1), 1, 0);
;   P_STAGE_B(G_SB(1, 0), 0, 1); P_STAGE_A(G_SA(1, 0), 0, 1); P_STAGE_B(G_SB(1, 1), 1, 1);
;     ...
;     D_LDB(B1, G_SB(1, 1)); D_STAGE_B(G_SB(1, 0), 0, t3);
;     G_BAR(); D_WAIT_L(0); G_SCHED(); D_MMA(0, 1, At, B1); G_BAR(); G_SCHED();
;     D_LDA(At, G_SA(1, 1)); D_STAGE_A(G_SA(1, 0), 0, t3);
;     G_BAR(); D_WAIT_L(0); G_SCHED(); D_MMA(1, 0, At, B0); G_BAR(); G_SCHED();
;     D_STAGE_B(G_SB(1, 1), 1, t3);
;     G_WAIT_V(6); G_BAR(); G_SCHED(); D_MMA(1, 1, At, B1); G_BAR(); G_SCHED();
;   }
;   if (!F8_PEEL) G_WAIT_V(0);
	s_waitcnt lgkmcnt(0)
	s_setprio 1
	s_waitcnt lgkmcnt(5)
	v_mfma_scale_f32_16x16x128_f8f6f4 v[48:51], v[0:7], v[74:81], v[122:125], v165, v164 op_sel_hi:[0,0,0]
	v_mfma_scale_f32_16x16x128_f8f6f4 v[52:55], v[56:63], v[74:81], v[126:129], v165, v164 op_sel_hi:[0,0,0]
	s_waitcnt lgkmcnt(4)
	v_mfma_scale_f32_16x16x128_f8f6f4 v[40:43], v[0:7], v[82:89], v[40:43], v165, v164 op_sel_hi:[0,0,0]
	v_mfma_scale_f32_16x16x128_f8f6f4 v[32:35], v[56:63], v[82:89], v[32:35], v165, v164 op_sel_hi:[0,0,0]
	s_waitcnt lgkmcnt(1)
	v_mfma_scale_f32_16x16x128_f8f6f4 v[24:27], v[0:7], v[90:97], v[24:27], v165, v164 op_sel_hi:[0,0,0]
	v_mfma_scale_f32_16x16x128_f8f6f4 v[16:19], v[56:63], v[90:97], v[16:19], v165, v164 op_sel_hi:[0,0,0]
	s_waitcnt lgkmcnt(0)
	v_mfma_scale_f32_16x16x128_f8f6f4 v[8:11], v[0:7], v[98:105], v[8:11], v165, v164 op_sel_hi:[0,0,0]
	v_mfma_scale_f32_16x16x128_f8f6f4 v[0:3], v[56:63], v[98:105], v[130:133], v165, v164 op_sel_hi:[0,0,0]
	s_setprio 0
	s_barrier
	v_add_u32_e32 v4, s76, v69
	v_add_u32_e32 v5, s76, v70
	ds_read_b128 v[106:109], v4
	ds_read_b128 v[114:117], v4 offset:2048
	ds_read_b128 v[110:113], v5
	ds_read_b128 v[118:121], v5 offset:2048
	s_mov_b32 m0, s60
	s_nop 0
	buffer_load_dwordx4 v66, s[4:7], s72 offen lds
	s_nop 0
	s_mov_b32 m0, s61
	s_nop 0
	buffer_load_dwordx4 v66, s[4:7], s75 offen lds
	s_barrier
	s_waitcnt lgkmcnt(0)
	s_setprio 1
	s_waitcnt lgkmcnt(1)
	v_mfma_scale_f32_16x16x128_f8f6f4 v[60:63], v[106:113], v[74:81], v[134:137], v165, v164 op_sel_hi:[0,0,0]
	s_waitcnt lgkmcnt(0)
	v_mfma_scale_f32_16x16x128_f8f6f4 v[56:59], v[114:121], v[74:81], v[138:141], v165, v164 op_sel_hi:[0,0,0]
	v_mfma_scale_f32_16x16x128_f8f6f4 v[44:47], v[106:113], v[82:89], v[44:47], v165, v164 op_sel_hi:[0,0,0]
	v_mfma_scale_f32_16x16x128_f8f6f4 v[36:39], v[114:121], v[82:89], v[36:39], v165, v164 op_sel_hi:[0,0,0]
	v_mfma_scale_f32_16x16x128_f8f6f4 v[28:31], v[106:113], v[90:97], v[28:31], v165, v164 op_sel_hi:[0,0,0]
	v_mfma_scale_f32_16x16x128_f8f6f4 v[20:23], v[114:121], v[90:97], v[20:23], v165, v164 op_sel_hi:[0,0,0]
	v_mfma_scale_f32_16x16x128_f8f6f4 v[12:15], v[106:113], v[98:105], v[12:15], v165, v164 op_sel_hi:[0,0,0]
	v_mfma_scale_f32_16x16x128_f8f6f4 v[4:7], v[114:121], v[98:105], v[142:145], v165, v164 op_sel_hi:[0,0,0]
	s_setprio 0
	s_barrier
	s_mov_b32 m0, s62
	s_nop 0
	buffer_load_dwordx4 v64, s[8:11], s72 offen lds
	s_nop 0
	s_mov_b32 m0, s63
	s_nop 0
	buffer_load_dwordx4 v67, s[8:11], s72 offen lds
	s_barrier
	s_waitcnt lgkmcnt(0)
	s_barrier
	s_mov_b32 m0, s64
	s_nop 0
	buffer_load_dwordx4 v66, s[4:7], s74 offen lds
	s_nop 0
	s_mov_b32 m0, s65
	s_nop 0
	buffer_load_dwordx4 v66, s[4:7], s73 offen lds
	s_waitcnt vmcnt(6)
	s_barrier
	s_barrier
	s_mov_b32 s69, s70
	s_mov_b32 s71, s68
	s_cbranch_scc0 .LBB0_1634
	s_waitcnt vmcnt(0)
	s_cmpk_lt_u32 s13, 0x100
	s_cbranch_scc0 .LBB0_1637
	s_barrier
.LBB0_1637:
	s_and_b64 vcc, exec, s[2:3]
	s_cbranch_vccnz .LBB0_1639
	v_mbcnt_lo_u32_b32 v68, -1, 0
	v_mbcnt_hi_u32_b32 v68, -1, v68
	s_ashr_i32 s13, s12, 31
	v_or_b32_e32 v64, s87, v68
	v_bfe_u32 v70, v68, 3, 3
	v_readfirstlane_b32 s2, v64
	s_ashr_i32 s38, s2, 6
	s_lshl_b32 s2, s38, 3
	v_lshrrev_b32_e32 v69, 3, v68
	v_or_b32_e32 v71, s2, v70
	v_xor_b32_e32 v68, v69, v68
	s_lshl_b32 s3, s38, 1
	v_lshlrev_b32_e32 v69, 1, v71
	v_mov_b32_e32 v71, 0x63
	s_and_b32 s3, s3, 4
	v_and_b32_e32 v69, 24, v69
	v_bitop3_b32 v70, s2, v71, v70 bitop3:0xc8
	v_lshlrev_b32_e32 v68, 4, v68
	v_or3_b32 v69, s3, v70, v69
	v_and_b32_e32 v68, 0x70, v68
	s_lshl_b32 s2, s44, 19
	v_lshlrev_b32_e32 v69, 11, v69
	v_or3_b32 v68, v69, s2, v68
	s_lshl_b64 s[2:3], s[12:13], 22
	v_lshl_add_u32 v64, v64, 2, 0
	s_add_u32 s4, s52, s2
	v_add_u32_e32 v66, 0x22410, v64
	s_addc_u32 s2, s53, s3
	ds_read2st64_b32 v[64:65], v66 offset1:8
	ds_read2st64_b32 v[66:67], v66 offset0:16 offset1:24
	s_and_b32 s5, s2, 0xffff
	s_lshl_b32 s2, s38, 10
	s_add_i32 s2, s2, 0
	s_add_i32 s3, s2, 0x10010
	s_mov_b32 m0, s3
	s_nop 0
	buffer_load_dwordx4 v68, s[4:7], s31 offen lds
	s_add_i32 s3, s2, 0x12010
	s_mov_b32 m0, s3
	s_nop 0
	buffer_load_dwordx4 v68, s[4:7], s7 offen lds
	s_add_i32 s3, s2, 16
	s_waitcnt lgkmcnt(1)
	s_mov_b32 m0, s3
	s_nop 0
	buffer_load_dwordx4 v64, s[8:11], s31 offen lds
	s_add_i32 s3, s2, 0x2010
	s_mov_b32 m0, s3
	s_nop 0
	buffer_load_dwordx4 v65, s[8:11], s31 offen lds
	s_add_i32 s3, s2, 0x14010
	s_mov_b32 m0, s3
	s_nop 0
	buffer_load_dwordx4 v68, s[4:7], s34 offen lds
	s_add_i32 s3, s2, 0x16010
	s_mov_b32 m0, s3
	s_nop 0
	buffer_load_dwordx4 v68, s[4:7], s35 offen lds
	s_add_i32 s3, s2, 0x4010
	s_waitcnt lgkmcnt(0)
	s_mov_b32 m0, s3
	s_nop 0
	buffer_load_dwordx4 v66, s[8:11], s31 offen lds
	s_add_i32 s3, s2, 0x6010
	s_mov_b32 m0, s3
	s_nop 0
	buffer_load_dwordx4 v67, s[8:11], s31 offen lds
	s_add_i32 s3, s2, 0x18010
	s_mov_b32 m0, s3
	s_nop 0
	buffer_load_dwordx4 v68, s[4:7], s33 offen lds
	s_add_i32 s3, s2, 0x1a010
	s_mov_b32 m0, s3
	s_nop 0
	buffer_load_dwordx4 v68, s[4:7], s36 offen lds
	s_add_i32 s3, s2, 0x8010
	s_mov_b32 m0, s3
	s_nop 0
	buffer_load_dwordx4 v64, s[8:11], s33 offen lds
	s_add_i32 s3, s2, 0xa010
	s_mov_b32 m0, s3
	s_nop 0
	buffer_load_dwordx4 v65, s[8:11], s33 offen lds
	s_add_i32 s3, s2, 0x1c010
	s_mov_b32 m0, s3
	s_nop 0
	buffer_load_dwordx4 v68, s[4:7], s37 offen lds
	s_add_i32 s2, s2, 0x1e010
	s_mov_b32 m0, s2
	s_nop 0
	buffer_load_dwordx4 v68, s[4:7], s42 offen lds

; #define G_WAIT_V(n) asm volatile("s_waitcnt vmcnt(" #n ")" ::: "memory")
; #define G_BAR() __builtin_amdgcn_s_barrier()
; #define G_SCHED() __builtin_amdgcn_sched_barrier(0)
; #define D_STAGE_A(slot, half, kt) D_STAGE(rsA, voffA, slot, half, kt)
; #define D_STAGE_B(slot, half, kt) D_STAGE(rsB, voffB, slot, half, kt)
; #define D_LDA(dst, slot) do { _Pragma("unroll") for (int m = 0; m < 4; ++m) _Pragma("unroll") for (int k = 0; k < 2; ++k) \
;     dst[m][k] = *(const LDS_AS bf16x8*)(lds + (slot) + aoff + m * 2048 + k * 1024); } while (0)
; #define D_LDB(dst, slot) do { _Pragma("unroll") for (int n = 0; n < 2; ++n) _Pragma("unroll") for (int k = 0; k < 2; ++k) \
;     dst[n][k] = *(const LDS_AS bf16x8*)(lds + (slot) + boff + n * 2048 + k * 1024); } while (0)
; #define D_MMA(ai, bj, At, Bf) do { __builtin_amdgcn_s_setprio(1); _Pragma("unroll") for (int m = 0; m < 4; ++m) _Pragma("unroll") for (int n = 0; n < 2; ++n) _Pragma("unroll") for (int k = 0; k < 2; ++k) \
;     acc[ai][bj][m][n] = __builtin_amdgcn_mfma_f32_16x16x32_bf16(Bf[n][k], At[m][k], acc[ai][bj][m][n], 0, 0, 0); __builtin_amdgcn_s_setprio(0); } while (0)
; #define D_WAIT_L(n) asm volatile("s_waitcnt lgkmcnt(" #n ")" ::: "memory")
; #define D_STAGE_A(slot, half, kt) D_STAGE(rsA, voffA, slot, half, kt)
; #define D_STAGE_B(slot, half, kt) do { _Pragma("unroll") for (int _i = 0; _i < 2; ++_i) { const unsigned _m0 = ldsw + (unsigned)((slot) + _i * 8192); const unsigned _so = (unsigned)(kt) * 128u + (half) * bt_half + _i * bt_piece; \
;     asm volatile("s_mov_b32 m0, %0\n\ts_nop 4\n\tbuffer_load_dwordx4 %1, %2, %3 offen lds" :: "s"(_m0), "v"(voffB0), "s"(rsB), "s"(_so) : "m0", "memory"); } } while (0)
; #define D_WAIT_L(n) asm volatile("s_waitcnt lgkmcnt(" #n ")" ::: "memory")
;     ...
;     D_LDB(B0, G_SB(0, 0)); G_SCHED(); D_LDA(At, G_SA(0, 0)); D_STAGE_A(G_SA(1, 1), 1, t1);
;     D_WAIT_L(8); G_BAR(); D_WAIT_L(0); G_SCHED(); D_MMA(0, 0, At, B0); G_BAR(); G_SCHED();
;     D_LDB(B1, G_SB(0, 1)); D_STAGE_B(G_SB(0, 0), 0, t2);
;     G_BAR(); D_WAIT_L(0); G_SCHED(); D_MMA(0, 1, At, B1); G_BAR(); G_SCHED();
;     D_LDA(At, G_SA(0, 1)); D_STAGE_A(G_SA(0, 0), 0, t2);
;     G_BAR(); D_WAIT_L(0); G_SCHED(); D_MMA(1, 0, At, B0); G_BAR(); G_SCHED();
;     D_STAGE_B(G_SB(0, 1), 1, t2);
;     G_WAIT_V(6); G_BAR(); G_SCHED(); D_MMA(1, 1, At, B1); G_BAR(); G_SCHED();
.LBB0_1674:
	s_add_i32 s68, 0, 0x10010
	s_nop 0
	v_add_u32_e32 v68, s68, v132
	v_add_u32_e32 v69, s68, v133
	ds_read_b128 v[146:149], v68
	ds_read_b128 v[154:157], v68 offset:2048
	ds_read_b128 v[150:153], v69
	ds_read_b128 v[158:161], v69 offset:2048
	s_add_i32 s38, s64, 1
	s_add_i32 s66, s64, 3
	s_add_i32 s65, s64, 2
	s_add_i32 s76, 0, 0x14010
	s_cmp_lt_u32 s64, 14
	s_cselect_b32 s67, s65, s64
	s_cselect_b32 s38, s66, s38
	s_lshl_b32 s72, s67, 7
	s_lshl_b32 s67, s38, 7
	s_add_i32 s77, s72, 0x20000
	s_add_i32 s74, s72, 0x40000
	s_add_i32 s75, s72, 0x60000
	s_add_i32 s73, 0, 0x18010
	s_add_i32 s71, 0, 0x1c010
	s_add_i32 s70, s67, 0x20000
	s_add_i32 s68, s67, 0x40000
	s_add_i32 s69, s67, 0x60000
	s_add_i32 s66, s63, 0x100
	s_cmp_gt_u32 s64, 13
	ds_read_b128 v[168:171], v135 offset:16
	ds_read_b128 v[176:179], v135 offset:2064
	ds_read_b128 v[172:175], v136 offset:16
	ds_read_b128 v[180:183], v136 offset:2064
	ds_read_b128 v[192:195], v135 offset:4112
	ds_read_b128 v[200:203], v135 offset:6160
	ds_read_b128 v[196:199], v136 offset:4112
	ds_read_b128 v[204:207], v136 offset:6160
	s_waitcnt lgkmcnt(12)
	s_mov_b32 m0, s24
	s_nop 0
	buffer_load_dwordx4 v166, s[8:11], s63 offen lds
	s_nop 0
	s_mov_b32 m0, s51
	s_nop 0
	buffer_load_dwordx4 v167, s[8:11], s63 offen lds
	s_waitcnt lgkmcnt(8)
	s_barrier
	s_waitcnt lgkmcnt(0)
	s_setprio 1
	s_waitcnt lgkmcnt(0)
	v_mfma_scale_f32_16x16x128_f8f6f4 v[220:223], v[146:153], v[200:207], v[220:223], v165, v164 op_sel_hi:[0,0,0]
	v_mfma_scale_f32_16x16x128_f8f6f4 v[48:51], v[154:161], v[200:207], v[48:51], v165, v164 op_sel_hi:[0,0,0]
	v_mfma_scale_f32_16x16x128_f8f6f4 v[138:141], v[146:153], v[168:175], v[124:127], v165, v164 op_sel_hi:[0,0,0]
	v_mfma_scale_f32_16x16x128_f8f6f4 v[184:187], v[154:161], v[168:175], v[120:123], v165, v164 op_sel_hi:[0,0,0]
	v_mfma_scale_f32_16x16x128_f8f6f4 v[188:191], v[146:153], v[176:183], v[108:111], v165, v164 op_sel_hi:[0,0,0]
	v_mfma_scale_f32_16x16x128_f8f6f4 v[208:211], v[154:161], v[176:183], v[100:103], v165, v164 op_sel_hi:[0,0,0]
	v_mfma_scale_f32_16x16x128_f8f6f4 v[212:215], v[146:153], v[192:199], v[84:87], v165, v164 op_sel_hi:[0,0,0]
	v_mfma_scale_f32_16x16x128_f8f6f4 v[216:219], v[154:161], v[192:199], v[80:83], v165, v164 op_sel_hi:[0,0,0]
	s_setprio 0
	s_barrier
	v_add_u32_e32 v68, s76, v132
	v_add_u32_e32 v69, s76, v133
	s_nop 2
	ds_read_b128 v[80:83], v68
	ds_read_b128 v[120:123], v68 offset:2048
	ds_read_b128 v[84:87], v69
	ds_read_b128 v[124:127], v69 offset:2048
	s_mov_b32 m0, s25
	s_nop 0
	buffer_load_dwordx4 v134, s[4:7], s72 offen lds
	s_nop 0
	s_mov_b32 m0, s54
	s_nop 0
	buffer_load_dwordx4 v134, s[4:7], s77 offen lds
	s_barrier
	s_waitcnt lgkmcnt(0)
	s_setprio 1
	s_waitcnt lgkmcnt(1)
	v_mfma_scale_f32_16x16x128_f8f6f4 v[116:119], v[80:87], v[168:175], v[116:119], v165, v164 op_sel_hi:[0,0,0]
	s_waitcnt lgkmcnt(0)
	v_mfma_scale_f32_16x16x128_f8f6f4 v[112:115], v[120:127], v[168:175], v[112:115], v165, v164 op_sel_hi:[0,0,0]
	v_mfma_scale_f32_16x16x128_f8f6f4 v[76:79], v[80:87], v[200:207], v[76:79], v165, v164 op_sel_hi:[0,0,0]
	v_mfma_scale_f32_16x16x128_f8f6f4 v[168:171], v[80:87], v[176:183], v[104:107], v165, v164 op_sel_hi:[0,0,0]
	v_mfma_scale_f32_16x16x128_f8f6f4 v[172:175], v[120:127], v[176:183], v[96:99], v165, v164 op_sel_hi:[0,0,0]
	v_mfma_scale_f32_16x16x128_f8f6f4 v[176:179], v[80:87], v[192:199], v[92:95], v165, v164 op_sel_hi:[0,0,0]
	v_mfma_scale_f32_16x16x128_f8f6f4 v[180:183], v[120:127], v[192:199], v[88:91], v165, v164 op_sel_hi:[0,0,0]
	v_mfma_scale_f32_16x16x128_f8f6f4 v[192:195], v[120:127], v[200:207], v[72:75], v165, v164 op_sel_hi:[0,0,0]
	s_setprio 0
	s_barrier
	ds_read_b128 v[68:71], v135 offset:16400
	s_nop 2
	ds_read_b128 v[88:91], v135 offset:18448
	ds_read_b128 v[72:75], v136 offset:16400
	ds_read_b128 v[92:95], v136 offset:18448
	ds_read_b128 v[96:99], v135 offset:20496
	ds_read_b128 v[104:107], v135 offset:22544
	ds_read_b128 v[100:103], v136 offset:20496
	ds_read_b128 v[108:111], v136 offset:22544
	s_mov_b32 m0, s15
	s_nop 0
	buffer_load_dwordx4 v162, s[8:11], s72 offen lds
	s_nop 0
	s_mov_b32 m0, s55
	s_nop 0
	buffer_load_dwordx4 v163, s[8:11], s72 offen lds
	s_barrier
	s_waitcnt lgkmcnt(0)
	s_setprio 1
	s_waitcnt lgkmcnt(5)
	v_mfma_scale_f32_16x16x128_f8f6f4 v[56:59], v[146:153], v[68:75], v[56:59], v165, v164 op_sel_hi:[0,0,0]
	v_mfma_scale_f32_16x16x128_f8f6f4 v[52:55], v[154:161], v[68:75], v[52:55], v165, v164 op_sel_hi:[0,0,0]
	s_waitcnt lgkmcnt(4)
	v_mfma_scale_f32_16x16x128_f8f6f4 v[200:203], v[146:153], v[88:95], v[36:39], v165, v164 op_sel_hi:[0,0,0]
	v_mfma_scale_f32_16x16x128_f8f6f4 v[204:207], v[154:161], v[88:95], v[32:35], v165, v164 op_sel_hi:[0,0,0]
	s_waitcnt lgkmcnt(1)
	v_mfma_scale_f32_16x16x128_f8f6f4 v[224:227], v[146:153], v[96:103], v[20:23], v165, v164 op_sel_hi:[0,0,0]
	v_mfma_scale_f32_16x16x128_f8f6f4 v[228:231], v[154:161], v[96:103], v[16:19], v165, v164 op_sel_hi:[0,0,0]
	s_waitcnt lgkmcnt(0)
	v_mfma_scale_f32_16x16x128_f8f6f4 v[232:235], v[146:153], v[104:111], v[4:7], v165, v164 op_sel_hi:[0,0,0]
	v_mfma_scale_f32_16x16x128_f8f6f4 v[236:239], v[154:161], v[104:111], v[0:3], v165, v164 op_sel_hi:[0,0,0]
	s_setprio 0
	s_barrier
	s_mov_b32 m0, s26
	s_nop 0
	buffer_load_dwordx4 v134, s[4:7], s74 offen lds
	s_nop 0
	s_mov_b32 m0, s58
	s_nop 0
	buffer_load_dwordx4 v134, s[4:7], s75 offen lds
	s_waitcnt vmcnt(6)
	s_barrier
; #define G_WAIT_V(n) asm volatile("s_waitcnt vmcnt(" #n ")" ::: "memory")
; #define G_BAR() __builtin_amdgcn_s_barrier()
; #define G_SCHED() __builtin_amdgcn_sched_barrier(0)
; #define D_STAGE_A(slot, half, kt) D_STAGE(rsA, voffA, slot, half, kt)
; #define D_STAGE_B(slot, half, kt) D_STAGE(rsB, voffB, slot, half, kt)
; #define D_LDA(dst, slot) do { _Pragma("unroll") for (int m = 0; m < 4; ++m) _Pragma("unroll") for (int k = 0; k < 2; ++k) \
;     dst[m][k] = *(const LDS_AS bf16x8*)(lds + (slot) + aoff + m * 2048 + k * 1024); } while (0)
; #define D_LDB(dst, slot) do { _Pragma("unroll") for (int n = 0; n < 2; ++n) _Pragma("unroll") for (int k = 0; k < 2; ++k) \
;     dst[n][k] = *(const LDS_AS bf16x8*)(lds + (slot) + boff + n * 2048 + k * 1024); } while (0)
; #define D_MMA(ai, bj, At, Bf) do { __builtin_amdgcn_s_setprio(1); _Pragma("unroll") for (int m = 0; m < 4; ++m) _Pragma("unroll") for (int n = 0; n < 2; ++n) _Pragma("unroll") for (int k = 0; k < 2; ++k) \
;     acc[ai][bj][m][n] = __builtin_amdgcn_mfma_f32_16x16x32_bf16(Bf[n][k], At[m][k], acc[ai][bj][m][n], 0, 0, 0); __builtin_amdgcn_s_setprio(0); } while (0)
; #define D_WAIT_L(n) asm volatile("s_waitcnt lgkmcnt(" #n ")" ::: "memory")
; #define D_STAGE_A(slot, half, kt) D_STAGE(rsA, voffA, slot, half, kt)
; #define D_STAGE_B(slot, half, kt) do { _Pragma("unroll") for (int _i = 0; _i < 2; ++_i) { const unsigned _m0 = ldsw + (unsigned)((slot) + _i * 8192); const unsigned _so = (unsigned)(kt) * 128u + (half) * bt_half + _i * bt_piece; \
;     asm volatile("s_mov_b32 m0, %0\n\ts_nop 4\n\tbuffer_load_dwordx4 %1, %2, %3 offen lds" :: "s"(_m0), "v"(voffB0), "s"(rsB), "s"(_so) : "m0", "memory"); } } while (0)
; #define D_WAIT_L(n) asm volatile("s_waitcnt lgkmcnt(" #n ")" ::: "memory")
;     ...
;     D_LDB(B0, G_SB(1, 0)); G_SCHED(); D_LDA(At, G_SA(1, 0)); D_STAGE_A(G_SA(0, 1), 1, t2);
;     D_WAIT_L(8); G_BAR(); D_WAIT_L(0); G_SCHED(); D_MMA(0, 0, At, B0); G_BAR(); G_SCHED();
;     D_LDB(B1, G_SB(1, 1)); D_STAGE_B(G_SB(1, 0), 0, t3);
;     G_BAR(); D_WAIT_L(0); G_SCHED(); D_MMA(0, 1, At, B1); G_BAR(); G_SCHED();
;     D_LDA(At, G_SA(1, 1)); D_STAGE_A(G_SA(1, 0), 0, t3);
;     G_BAR(); D_WAIT_L(0); G_SCHED(); D_MMA(1, 0, At, B0); G_BAR(); G_SCHED();
;     D_STAGE_B(G_SB(1, 1), 1, t3);
;     G_WAIT_V(6); G_BAR(); G_SCHED(); D_MMA(1, 1, At, B1); G_BAR(); G_SCHED();
;   }
;   if (!F8_PEEL) G_WAIT_V(0);
	s_setprio 1
	v_mfma_scale_f32_16x16x128_f8f6f4 v[64:67], v[80:87], v[68:75], v[64:67], v165, v164 op_sel_hi:[0,0,0]
	v_mfma_scale_f32_16x16x128_f8f6f4 v[60:63], v[120:127], v[68:75], v[60:63], v165, v164 op_sel_hi:[0,0,0]
	v_mfma_scale_f32_16x16x128_f8f6f4 v[240:243], v[80:87], v[88:95], v[44:47], v165, v164 op_sel_hi:[0,0,0]
	v_mfma_scale_f32_16x16x128_f8f6f4 v[244:247], v[120:127], v[88:95], v[40:43], v165, v164 op_sel_hi:[0,0,0]
	v_mfma_scale_f32_16x16x128_f8f6f4 v[248:251], v[80:87], v[96:103], v[28:31], v165, v164 op_sel_hi:[0,0,0]
	v_mfma_scale_f32_16x16x128_f8f6f4 v[142:145], v[120:127], v[96:103], v[24:27], v165, v164 op_sel_hi:[0,0,0]
	v_mfma_scale_f32_16x16x128_f8f6f4 v[128:131], v[80:87], v[104:111], v[12:15], v165, v164 op_sel_hi:[0,0,0]
	v_mfma_scale_f32_16x16x128_f8f6f4 v[68:71], v[120:127], v[104:111], v[8:11], v165, v164 op_sel_hi:[0,0,0]
	s_setprio 0
	s_barrier
	v_add_u32_e32 v4, s73, v132
	s_nop 2
	v_add_u32_e32 v12, s73, v133
	ds_read_b128 v[0:3], v4
	ds_read_b128 v[8:11], v4 offset:2048
	ds_read_b128 v[4:7], v12
	ds_read_b128 v[12:15], v12 offset:2048
	ds_read_b128 v[16:19], v135 offset:32784
	ds_read_b128 v[24:27], v135 offset:34832
	ds_read_b128 v[20:23], v136 offset:32784
	ds_read_b128 v[28:31], v136 offset:34832
	ds_read_b128 v[32:35], v135 offset:36880
	ds_read_b128 v[40:43], v135 offset:38928
	ds_read_b128 v[36:39], v136 offset:36880
	ds_read_b128 v[44:47], v136 offset:38928
	s_mov_b32 m0, s27
	s_nop 0
	buffer_load_dwordx4 v166, s[8:11], s72 offen lds
	s_nop 0
	s_mov_b32 m0, s59
	s_nop 0
	buffer_load_dwordx4 v167, s[8:11], s72 offen lds
	s_waitcnt lgkmcnt(8)
	s_barrier
	s_waitcnt lgkmcnt(0)
	s_setprio 1
	s_waitcnt lgkmcnt(5)
	v_mfma_scale_f32_16x16x128_f8f6f4 v[124:127], v[0:7], v[16:23], v[138:141], v165, v164 op_sel_hi:[0,0,0]
	v_mfma_scale_f32_16x16x128_f8f6f4 v[120:123], v[8:15], v[16:23], v[184:187], v165, v164 op_sel_hi:[0,0,0]
	s_waitcnt lgkmcnt(4)
	v_mfma_scale_f32_16x16x128_f8f6f4 v[108:111], v[0:7], v[24:31], v[188:191], v165, v164 op_sel_hi:[0,0,0]
	v_mfma_scale_f32_16x16x128_f8f6f4 v[100:103], v[8:15], v[24:31], v[208:211], v165, v164 op_sel_hi:[0,0,0]
	s_waitcnt lgkmcnt(1)
	v_mfma_scale_f32_16x16x128_f8f6f4 v[84:87], v[0:7], v[32:39], v[212:215], v165, v164 op_sel_hi:[0,0,0]
	v_mfma_scale_f32_16x16x128_f8f6f4 v[80:83], v[8:15], v[32:39], v[216:219], v165, v164 op_sel_hi:[0,0,0]
	s_waitcnt lgkmcnt(0)
	v_mfma_scale_f32_16x16x128_f8f6f4 v[220:223], v[0:7], v[40:47], v[220:223], v165, v164 op_sel_hi:[0,0,0]
	v_mfma_scale_f32_16x16x128_f8f6f4 v[48:51], v[8:15], v[40:47], v[48:51], v165, v164 op_sel_hi:[0,0,0]
	s_setprio 0
	s_barrier
	v_add_u32_e32 v72, s71, v132
	v_add_u32_e32 v73, s71, v133
	ds_read_b128 v[146:149], v72
	ds_read_b128 v[154:157], v72 offset:2048
	ds_read_b128 v[150:153], v73
	ds_read_b128 v[158:161], v73 offset:2048
	s_mov_b32 m0, s39
	s_nop 0
	buffer_load_dwordx4 v134, s[4:7], s67 offen lds
	s_nop 0
	s_mov_b32 m0, s60
	s_nop 0
	buffer_load_dwordx4 v134, s[4:7], s70 offen lds
	s_barrier
	s_waitcnt lgkmcnt(0)
	s_setprio 1
	s_waitcnt lgkmcnt(1)
	v_mfma_scale_f32_16x16x128_f8f6f4 v[116:119], v[146:153], v[16:23], v[116:119], v165, v164 op_sel_hi:[0,0,0]
	s_waitcnt lgkmcnt(0)
	v_mfma_scale_f32_16x16x128_f8f6f4 v[112:115], v[154:161], v[16:23], v[112:115], v165, v164 op_sel_hi:[0,0,0]
	v_mfma_scale_f32_16x16x128_f8f6f4 v[104:107], v[146:153], v[24:31], v[168:171], v165, v164 op_sel_hi:[0,0,0]
	v_mfma_scale_f32_16x16x128_f8f6f4 v[96:99], v[154:161], v[24:31], v[172:175], v165, v164 op_sel_hi:[0,0,0]
	v_mfma_scale_f32_16x16x128_f8f6f4 v[92:95], v[146:153], v[32:39], v[176:179], v165, v164 op_sel_hi:[0,0,0]
	v_mfma_scale_f32_16x16x128_f8f6f4 v[88:91], v[154:161], v[32:39], v[180:183], v165, v164 op_sel_hi:[0,0,0]
	v_mfma_scale_f32_16x16x128_f8f6f4 v[76:79], v[146:153], v[40:47], v[76:79], v165, v164 op_sel_hi:[0,0,0]
	v_mfma_scale_f32_16x16x128_f8f6f4 v[72:75], v[154:161], v[40:47], v[192:195], v165, v164 op_sel_hi:[0,0,0]
	s_setprio 0
	s_barrier
	ds_read_b128 v[24:27], v135 offset:49168
	ds_read_b128 v[168:171], v135 offset:51216
	ds_read_b128 v[28:31], v136 offset:49168
	ds_read_b128 v[172:175], v136 offset:51216
	ds_read_b128 v[176:179], v135 offset:53264
	ds_read_b128 v[192:195], v135 offset:55312
	ds_read_b128 v[180:183], v136 offset:53264
	ds_read_b128 v[196:199], v136 offset:55312
	s_mov_b32 m0, s49
	s_nop 0
	buffer_load_dwordx4 v162, s[8:11], s67 offen lds
	s_nop 0
	s_mov_b32 m0, s61
	s_nop 0
	buffer_load_dwordx4 v163, s[8:11], s67 offen lds
	s_barrier
	s_waitcnt lgkmcnt(0)
	s_setprio 1
	s_waitcnt lgkmcnt(5)
	v_mfma_scale_f32_16x16x128_f8f6f4 v[56:59], v[0:7], v[24:31], v[56:59], v165, v164 op_sel_hi:[0,0,0]
	v_mfma_scale_f32_16x16x128_f8f6f4 v[52:55], v[8:15], v[24:31], v[52:55], v165, v164 op_sel_hi:[0,0,0]
	s_waitcnt lgkmcnt(4)
	v_mfma_scale_f32_16x16x128_f8f6f4 v[36:39], v[0:7], v[168:175], v[200:203], v165, v164 op_sel_hi:[0,0,0]
	v_mfma_scale_f32_16x16x128_f8f6f4 v[32:35], v[8:15], v[168:175], v[204:207], v165, v164 op_sel_hi:[0,0,0]
	s_waitcnt lgkmcnt(1)
	v_mfma_scale_f32_16x16x128_f8f6f4 v[20:23], v[0:7], v[176:183], v[224:227], v165, v164 op_sel_hi:[0,0,0]
	v_mfma_scale_f32_16x16x128_f8f6f4 v[16:19], v[8:15], v[176:183], v[228:231], v165, v164 op_sel_hi:[0,0,0]
	s_waitcnt lgkmcnt(0)
	v_mfma_scale_f32_16x16x128_f8f6f4 v[4:7], v[0:7], v[192:199], v[232:235], v165, v164 op_sel_hi:[0,0,0]
	v_mfma_scale_f32_16x16x128_f8f6f4 v[0:3], v[8:15], v[192:199], v[236:239], v165, v164 op_sel_hi:[0,0,0]
	s_setprio 0
	s_barrier
	s_mov_b32 m0, s50
	s_nop 0
	buffer_load_dwordx4 v134, s[4:7], s68 offen lds
	s_nop 0
	s_mov_b32 m0, s62
	s_nop 0
	buffer_load_dwordx4 v134, s[4:7], s69 offen lds
	s_waitcnt vmcnt(6)
	s_barrier
	s_setprio 1
	v_mfma_scale_f32_16x16x128_f8f6f4 v[64:67], v[146:153], v[24:31], v[64:67], v165, v164 op_sel_hi:[0,0,0]
	v_mfma_scale_f32_16x16x128_f8f6f4 v[60:63], v[154:161], v[24:31], v[60:63], v165, v164 op_sel_hi:[0,0,0]
	v_mfma_scale_f32_16x16x128_f8f6f4 v[44:47], v[146:153], v[168:175], v[240:243], v165, v164 op_sel_hi:[0,0,0]
	v_mfma_scale_f32_16x16x128_f8f6f4 v[40:43], v[154:161], v[168:175], v[244:247], v165, v164 op_sel_hi:[0,0,0]
	v_mfma_scale_f32_16x16x128_f8f6f4 v[28:31], v[146:153], v[176:183], v[248:251], v165, v164 op_sel_hi:[0,0,0]
	v_mfma_scale_f32_16x16x128_f8f6f4 v[24:27], v[154:161], v[176:183], v[142:145], v165, v164 op_sel_hi:[0,0,0]
	v_mfma_scale_f32_16x16x128_f8f6f4 v[12:15], v[146:153], v[192:199], v[128:131], v165, v164 op_sel_hi:[0,0,0]
	v_mfma_scale_f32_16x16x128_f8f6f4 v[8:11], v[154:161], v[192:199], v[68:71], v165, v164 op_sel_hi:[0,0,0]
	s_setprio 0
	s_barrier
	s_mov_b32 s63, s66
	s_mov_b32 s64, s65
	s_cbranch_scc0 .LBB0_1674
	s_waitcnt vmcnt(0)
	s_cmpk_lt_u32 s13, 0x100
	s_cbranch_scc0 .LBB0_1677
	s_barrier
; #define LDS_AS __attribute__((address_space(3)))
; #define OPAQUE_TID(P) (((P).wid0 << 6) | lane_id_now())
; #define P_STAGE_A(slot, half, kt) do { _Pragma("unroll") for (int _i = 0; _i < 2; ++_i) { const unsigned _m0 = ldsw + (unsigned)((slot) + _i * 8192); const unsigned _so = (unsigned)(kt) * 128u; \
;     asm volatile("s_mov_b32 m0, %0\n\ts_nop 4\n\tbuffer_load_dwordx4 %1, %2, %3 offen lds" :: "s"(_m0), "v"(voffA[half][_i]), "s"(rsA), "s"(_so) : "m0", "memory"); } } while (0)
; #define P_STAGE_B(slot, half, kt) do { _Pragma("unroll") for (int _i = 0; _i < 2; ++_i) { const unsigned _m0 = ldsw + (unsigned)((slot) + _i * 8192); const unsigned _so = (unsigned)(kt) * 128u + (half) * bt_half + _i * bt_piece; \
;     asm volatile("s_mov_b32 m0, %0\n\ts_nop 4\n\tbuffer_load_dwordx4 %1, %2, %3 offen lds" :: "s"(_m0), "v"(voffB0), "s"(rsB), "s"(_so) : "m0", "memory"); } } while (0)
;   DI unsigned bt_rowoff(int h, int R) const { return (unsigned)(pn * 256 + 128 * h + (pn < 15 ? tcol_adj(R) : tcol_p64(R))) * 4096u; }
; template <class Cfg>
; DI void f8dma_issue_prologue_st(LDS_AS unsigned char* lds, const Cfg& cfg) {
;   const int tid = OPAQUE_TID(cfg.p), wid = __builtin_amdgcn_readfirstlane(tid >> 6), lane = tid & 63;
;   const LDS_AS unsigned* stash = (const LDS_AS unsigned*)(lds + F8_STASH);
;   unsigned voffA[2][2], voffB0;
;   voffA[0][0] = stash[tid]; voffA[0][1] = stash[512 + tid]; voffA[1][0] = stash[1024 + tid]; voffA[1][1] = stash[1536 + tid];
;   {
;     const int r = 8 * wid + (lane >> 3);
;     const unsigned cofs = 16u * (((unsigned)lane & 7u) ^ (((unsigned)lane >> 3) & 7u));
;     voffB0 = cfg.bt_rowoff(0, r) + cofs;
;   }
;   const unsigned bt_half = cfg.bt_rowoff(1, 0) - cfg.bt_rowoff(0, 0), bt_piece = cfg.bt_rowoff(0, 64) - cfg.bt_rowoff(0, 0);
;   const __amdgpu_buffer_rsrc_t rsA = __builtin_amdgcn_make_buffer_rsrc((void*)cfg.a_base(), 0, cfg.a_bytes(), 0x00020000);
;   const __amdgpu_buffer_rsrc_t rsB = __builtin_amdgcn_make_buffer_rsrc((void*)cfg.bt_base(), 0, cfg.bt_bytes(), 0x00020000);
;   const unsigned ldsw = (unsigned)__builtin_amdgcn_readfirstlane((int)(unsigned)(size_t)lds) + (unsigned)wid * 1024u;
;     ...
;   P_STAGE_B(G_SB(0, 0), 0, 0); P_STAGE_A(G_SA(0, 0), 0, 0); P_STAGE_B(G_SB(0, 1), 1, 0); P_STAGE_A(G_SA(0, 1), 1, 0);
;   P_STAGE_B(G_SB(1, 0), 0, 1); P_STAGE_A(G_SA(1, 0), 0, 1); P_STAGE_B(G_SB(1, 1), 1, 1);
.LBB0_1677:
	s_and_b64 vcc, exec, s[2:3]
	s_cbranch_vccnz .LBB0_1679
	v_mbcnt_lo_u32_b32 v128, -1, 0
	v_mbcnt_hi_u32_b32 v128, -1, v128
	s_ashr_i32 s13, s12, 31
	v_or_b32_e32 v68, s87, v128
	v_bfe_u32 v130, v128, 3, 3
	v_readfirstlane_b32 s4, v68
	s_ashr_i32 s15, s4, 6
	s_lshl_b32 s4, s15, 3
	v_lshrrev_b32_e32 v129, 3, v128
	v_or_b32_e32 v131, s4, v130
	v_xor_b32_e32 v128, v129, v128
	s_lshl_b32 s5, s15, 1
	v_lshlrev_b32_e32 v129, 1, v131
	v_mov_b32_e32 v131, 0x63
	s_and_b32 s5, s5, 4
	v_and_b32_e32 v129, 24, v129
	v_bitop3_b32 v130, s4, v131, v130 bitop3:0xc8
	v_lshlrev_b32_e32 v128, 4, v128
	v_or3_b32 v129, s5, v130, v129
	v_and_b32_e32 v128, 0x70, v128
	s_lshl_b32 s4, s44, 19
	v_lshlrev_b32_e32 v129, 11, v129
	v_lshl_add_u32 v68, v68, 2, 0
	v_or3_b32 v128, v129, s4, v128
	s_lshl_b64 s[4:5], s[12:13], 22
	v_add_u32_e32 v70, 0x22410, v68
	s_add_u32 s4, s52, s4
	ds_read2st64_b32 v[68:69], v70 offset1:8
	ds_read2st64_b32 v[70:71], v70 offset0:16 offset1:24
	s_addc_u32 s5, s53, s5
	s_lshl_b32 s13, s15, 10
	s_add_i32 s13, s13, 0
	s_and_b32 s5, s5, 0xffff
	s_add_i32 s15, s13, 0x10010
	s_mov_b32 m0, s15
	s_nop 0
	buffer_load_dwordx4 v128, s[4:7], s31 offen lds
	s_add_i32 s15, s13, 0x12010
	s_mov_b32 m0, s15
	s_nop 0
	buffer_load_dwordx4 v128, s[4:7], s7 offen lds
	s_add_i32 s15, s13, 16
	s_waitcnt lgkmcnt(1)
	s_mov_b32 m0, s15
	s_nop 0
	buffer_load_dwordx4 v68, s[8:11], s31 offen lds
	s_add_i32 s15, s13, 0x2010
	s_mov_b32 m0, s15
	s_nop 0
	buffer_load_dwordx4 v69, s[8:11], s31 offen lds
	s_add_i32 s15, s13, 0x14010
	s_mov_b32 m0, s15
	s_nop 0
	buffer_load_dwordx4 v128, s[4:7], s34 offen lds
	s_add_i32 s15, s13, 0x16010
	s_mov_b32 m0, s15
	s_nop 0
	buffer_load_dwordx4 v128, s[4:7], s35 offen lds
	s_add_i32 s15, s13, 0x4010
	s_waitcnt lgkmcnt(0)
	s_mov_b32 m0, s15
	s_nop 0
	buffer_load_dwordx4 v70, s[8:11], s31 offen lds
	s_add_i32 s15, s13, 0x6010
	s_mov_b32 m0, s15
	s_nop 0
	buffer_load_dwordx4 v71, s[8:11], s31 offen lds
	s_add_i32 s15, s13, 0x18010
	s_mov_b32 m0, s15
	s_nop 0
	buffer_load_dwordx4 v128, s[4:7], s33 offen lds
	s_add_i32 s15, s13, 0x1a010
	s_mov_b32 m0, s15
	s_nop 0
	buffer_load_dwordx4 v128, s[4:7], s36 offen lds
	s_add_i32 s15, s13, 0x8010
	s_mov_b32 m0, s15
	s_nop 0
	buffer_load_dwordx4 v68, s[8:11], s33 offen lds
	s_add_i32 s15, s13, 0xa010
	s_mov_b32 m0, s15
	s_nop 0
	buffer_load_dwordx4 v69, s[8:11], s33 offen lds
	s_add_i32 s15, s13, 0x1c010
	s_mov_b32 m0, s15
	s_nop 0
	buffer_load_dwordx4 v128, s[4:7], s37 offen lds
	s_add_i32 s13, s13, 0x1e010
	s_mov_b32 m0, s13
	s_nop 0
	buffer_load_dwordx4 v128, s[4:7], s42 offen lds

; #define G_WAIT_V(n) asm volatile("s_waitcnt vmcnt(" #n ")" ::: "memory")
; #define G_BAR() __builtin_amdgcn_s_barrier()
; #define G_SCHED() __builtin_amdgcn_sched_barrier(0)
; #define D_STAGE_A(slot, half, kt) D_STAGE(rsA, voffA, slot, half, kt)
; #define D_STAGE_B(slot, half, kt) D_STAGE(rsB, voffB, slot, half, kt)
; #define D_LDA(dst, slot) do { _Pragma("unroll") for (int m = 0; m < 4; ++m) _Pragma("unroll") for (int k = 0; k < 2; ++k) \
;     dst[m][k] = *(const LDS_AS bf16x8*)(lds + (slot) + aoff + m * 2048 + k * 1024); } while (0)
; #define D_LDB(dst, slot) do { _Pragma("unroll") for (int n = 0; n < 2; ++n) _Pragma("unroll") for (int k = 0; k < 2; ++k) \
;     dst[n][k] = *(const LDS_AS bf16x8*)(lds + (slot) + boff + n * 2048 + k * 1024); } while (0)
; #define D_MMA(ai, bj, At, Bf) do { __builtin_amdgcn_s_setprio(1); _Pragma("unroll") for (int m = 0; m < 4; ++m) _Pragma("unroll") for (int n = 0; n < 2; ++n) _Pragma("unroll") for (int k = 0; k < 2; ++k) \
;     acc[ai][bj][m][n] = __builtin_amdgcn_mfma_f32_16x16x32_bf16(Bf[n][k], At[m][k], acc[ai][bj][m][n], 0, 0, 0); __builtin_amdgcn_s_setprio(0); } while (0)
; #define D_WAIT_L(n) asm volatile("s_waitcnt lgkmcnt(" #n ")" ::: "memory")
; #define D_STAGE_A(slot, half, kt) D_STAGE(rsA, voffA, slot, half, kt)
; #define D_WAIT_L(n) asm volatile("s_waitcnt lgkmcnt(" #n ")" ::: "memory")
;     ...
;     D_LDB(B0, G_SB(0, 0)); G_SCHED(); D_LDA(At, G_SA(0, 0)); D_STAGE_A(G_SA(1, 1), 1, t1);
;     D_WAIT_L(8); G_BAR(); D_WAIT_L(0); G_SCHED(); D_MMA(0, 0, At, B0); G_BAR(); G_SCHED();
;     D_LDB(B1, G_SB(0, 1)); D_STAGE_B(G_SB(0, 0), 0, t2);
;     G_BAR(); D_WAIT_L(0); G_SCHED(); D_MMA(0, 1, At, B1); G_BAR(); G_SCHED();
;     D_LDA(At, G_SA(0, 1)); D_STAGE_A(G_SA(0, 0), 0, t2);
;     G_BAR(); D_WAIT_L(0); G_SCHED(); D_MMA(1, 0, At, B0); G_BAR(); G_SCHED();
;     D_STAGE_B(G_SB(0, 1), 1, t2);
;     G_WAIT_V(6); G_BAR(); G_SCHED(); D_MMA(1, 1, At, B1); G_BAR(); G_SCHED();
;     D_LDB(B0, G_SB(1, 0)); G_SCHED(); D_LDA(At, G_SA(1, 0)); D_STAGE_A(G_SA(0, 1), 1, t2);
;     D_WAIT_L(8); G_BAR(); D_WAIT_L(0); G_SCHED(); D_MMA(0, 0, At, B0); G_BAR(); G_SCHED();
;     D_LDB(B1, G_SB(1, 1)); D_STAGE_B(G_SB(1, 0), 0, t3);
.LBB0_1701:
	s_add_i32 s68, 0, 0x10010
	s_waitcnt vmcnt(62)
	v_add_u32_e32 v73, s68, v68
	s_waitcnt vmcnt(49)
	v_add_u32_e32 v86, s68, v69
	ds_read_b128 v[74:77], v73
	ds_read_b128 v[82:85], v73 offset:2048
	ds_read_b128 v[78:81], v86
	s_waitcnt vmcnt(46)
	ds_read_b128 v[86:89], v86 offset:2048
	s_add_i32 s38, s66, 1
	s_add_i32 s65, s66, 3
	s_add_i32 s64, s66, 2
	s_add_i32 s73, 0, 0x14010
	s_cmp_lt_u32 s66, 14
	s_cselect_b32 s67, s64, s66
	s_cselect_b32 s38, s65, s38
	s_lshl_b32 s72, s67, 7
	s_lshl_b32 s67, s38, 7
	s_add_i32 s74, s72, 0x20000
	s_add_i32 s75, s72, 0x40000
	s_add_i32 s76, s72, 0x60000
	s_add_i32 s77, 0, 0x18010
	s_add_i32 s71, 0, 0x1c010
	s_add_i32 s70, s67, 0x20000
	s_add_i32 s68, s67, 0x40000
	s_add_i32 s69, s67, 0x60000
	s_add_i32 s65, s63, 0x100
	s_cmp_gt_u32 s66, 13
	s_waitcnt vmcnt(42)
	ds_read_b128 v[90:93], v71 offset:16
	s_waitcnt vmcnt(34)
	ds_read_b128 v[98:101], v71 offset:2064
	ds_read_b128 v[94:97], v72 offset:16
	s_waitcnt vmcnt(30)
	ds_read_b128 v[102:105], v72 offset:2064
	s_waitcnt vmcnt(26)
	ds_read_b128 v[106:109], v71 offset:4112
	s_waitcnt vmcnt(18)
	ds_read_b128 v[114:117], v71 offset:6160
	ds_read_b128 v[110:113], v72 offset:4112
	s_waitcnt vmcnt(2)
	ds_read_b128 v[118:121], v72 offset:6160
	s_waitcnt lgkmcnt(12)
	s_mov_b32 m0, s24
	s_nop 0
	buffer_load_dwordx4 v66, s[8:11], s63 offen lds
	s_nop 0
	s_mov_b32 m0, s51
	s_nop 0
	buffer_load_dwordx4 v67, s[8:11], s63 offen lds
	s_waitcnt lgkmcnt(8)
	s_barrier
	s_waitcnt lgkmcnt(0)
	s_setprio 1
	s_waitcnt lgkmcnt(4)
	v_mfma_scale_f32_16x16x128_f8f6f4 v[40:43], v[74:81], v[98:105], v[40:43], v165, v164 op_sel_hi:[0,0,0]
	v_mfma_scale_f32_16x16x128_f8f6f4 v[32:35], v[82:89], v[98:105], v[32:35], v165, v164 op_sel_hi:[0,0,0]
	s_waitcnt lgkmcnt(1)
	v_mfma_scale_f32_16x16x128_f8f6f4 v[24:27], v[74:81], v[106:113], v[24:27], v165, v164 op_sel_hi:[0,0,0]
	v_mfma_scale_f32_16x16x128_f8f6f4 v[16:19], v[82:89], v[106:113], v[16:19], v165, v164 op_sel_hi:[0,0,0]
	s_waitcnt lgkmcnt(0)
	v_mfma_scale_f32_16x16x128_f8f6f4 v[8:11], v[74:81], v[114:121], v[8:11], v165, v164 op_sel_hi:[0,0,0]
	s_waitcnt vmcnt(0)
	v_mfma_scale_f32_16x16x128_f8f6f4 v[122:125], v[74:81], v[90:97], v[48:51], v165, v164 op_sel_hi:[0,0,0]
	v_mfma_scale_f32_16x16x128_f8f6f4 v[126:129], v[82:89], v[90:97], v[52:55], v165, v164 op_sel_hi:[0,0,0]
	v_mfma_scale_f32_16x16x128_f8f6f4 v[130:133], v[82:89], v[114:121], v[0:3], v165, v164 op_sel_hi:[0,0,0]
	s_setprio 0
	s_barrier
	s_nop 4
	v_add_u32_e32 v0, s73, v68
	v_add_u32_e32 v1, s73, v69
	ds_read_b128 v[48:51], v0
	ds_read_b128 v[74:77], v0 offset:2048
	ds_read_b128 v[52:55], v1
	ds_read_b128 v[78:81], v1 offset:2048
	s_mov_b32 m0, s25
	s_nop 0
	buffer_load_dwordx4 v70, s[4:7], s72 offen lds
	s_nop 0
	s_mov_b32 m0, s54
	s_nop 0
	buffer_load_dwordx4 v70, s[4:7], s74 offen lds
	s_barrier
	s_waitcnt lgkmcnt(0)
	s_setprio 1
	s_waitcnt lgkmcnt(1)
	v_mfma_scale_f32_16x16x128_f8f6f4 v[44:47], v[48:55], v[98:105], v[44:47], v165, v164 op_sel_hi:[0,0,0]
	s_waitcnt lgkmcnt(0)
	v_mfma_scale_f32_16x16x128_f8f6f4 v[36:39], v[74:81], v[98:105], v[36:39], v165, v164 op_sel_hi:[0,0,0]
	v_mfma_scale_f32_16x16x128_f8f6f4 v[28:31], v[48:55], v[106:113], v[28:31], v165, v164 op_sel_hi:[0,0,0]
	v_mfma_scale_f32_16x16x128_f8f6f4 v[20:23], v[74:81], v[106:113], v[20:23], v165, v164 op_sel_hi:[0,0,0]
	v_mfma_scale_f32_16x16x128_f8f6f4 v[12:15], v[48:55], v[114:121], v[12:15], v165, v164 op_sel_hi:[0,0,0]
	v_mfma_scale_f32_16x16x128_f8f6f4 v[134:137], v[48:55], v[90:97], v[60:63], v165, v164 op_sel_hi:[0,0,0]
	v_mfma_scale_f32_16x16x128_f8f6f4 v[138:141], v[74:81], v[90:97], v[56:59], v165, v164 op_sel_hi:[0,0,0]
	v_mfma_scale_f32_16x16x128_f8f6f4 v[146:149], v[74:81], v[114:121], v[4:7], v165, v164 op_sel_hi:[0,0,0]
	s_setprio 0
	s_barrier
	s_mov_b32 m0, s15
	s_nop 0
	buffer_load_dwordx4 v64, s[8:11], s72 offen lds
	s_nop 0
	s_mov_b32 m0, s55
	s_nop 0
	buffer_load_dwordx4 v65, s[8:11], s72 offen lds
	s_barrier
	s_waitcnt lgkmcnt(0)
	s_barrier
	s_mov_b32 m0, s26
	s_nop 0
	buffer_load_dwordx4 v70, s[4:7], s75 offen lds
	s_nop 0
	s_mov_b32 m0, s58
	s_nop 0
	buffer_load_dwordx4 v70, s[4:7], s76 offen lds
	s_waitcnt vmcnt(6)
	s_barrier
	s_barrier
	v_add_u32_e32 v4, s77, v68
	v_add_u32_e32 v48, s77, v69
	ds_read_b128 v[0:3], v4
	ds_read_b128 v[56:59], v4 offset:2048
	ds_read_b128 v[4:7], v48
	ds_read_b128 v[60:63], v48 offset:2048
	ds_read_b128 v[74:77], v71 offset:32784
	ds_read_b128 v[82:85], v71 offset:34832
	ds_read_b128 v[78:81], v72 offset:32784
	ds_read_b128 v[86:89], v72 offset:34832
	ds_read_b128 v[90:93], v71 offset:36880
	ds_read_b128 v[98:101], v71 offset:38928
	ds_read_b128 v[94:97], v72 offset:36880
	ds_read_b128 v[102:105], v72 offset:38928
	s_mov_b32 m0, s27
	s_nop 0
	buffer_load_dwordx4 v66, s[8:11], s72 offen lds
	s_nop 0
	s_mov_b32 m0, s59
	s_nop 0
	buffer_load_dwordx4 v67, s[8:11], s72 offen lds
	s_waitcnt lgkmcnt(8)
	s_barrier
; #define G_WAIT_V(n) asm volatile("s_waitcnt vmcnt(" #n ")" ::: "memory")
; #define G_BAR() __builtin_amdgcn_s_barrier()
; #define G_SCHED() __builtin_amdgcn_sched_barrier(0)
; #define D_STAGE_A(slot, half, kt) D_STAGE(rsA, voffA, slot, half, kt)
; #define D_STAGE_B(slot, half, kt) D_STAGE(rsB, voffB, slot, half, kt)
; #define D_LDA(dst, slot) do { _Pragma("unroll") for (int m = 0; m < 4; ++m) _Pragma("unroll") for (int k = 0; k < 2; ++k) \
;     dst[m][k] = *(const LDS_AS bf16x8*)(lds + (slot) + aoff + m * 2048 + k * 1024); } while (0)
; #define D_LDB(dst, slot) do { _Pragma("unroll") for (int n = 0; n < 2; ++n) _Pragma("unroll") for (int k = 0; k < 2; ++k) \
;     dst[n][k] = *(const LDS_AS bf16x8*)(lds + (slot) + boff + n * 2048 + k * 1024); } while (0)
; #define D_MMA(ai, bj, At, Bf) do { __builtin_amdgcn_s_setprio(1); _Pragma("unroll") for (int m = 0; m < 4; ++m) _Pragma("unroll") for (int n = 0; n < 2; ++n) _Pragma("unroll") for (int k = 0; k < 2; ++k) \
;     acc[ai][bj][m][n] = __builtin_amdgcn_mfma_f32_16x16x32_bf16(Bf[n][k], At[m][k], acc[ai][bj][m][n], 0, 0, 0); __builtin_amdgcn_s_setprio(0); } while (0)
; #define D_WAIT_L(n) asm volatile("s_waitcnt lgkmcnt(" #n ")" ::: "memory")
; #define P_STAGE_A(slot, half, kt) do { _Pragma("unroll") for (int _i = 0; _i < 2; ++_i) { const unsigned _m0 = ldsw + (unsigned)((slot) + _i * 8192); const unsigned _so = (unsigned)(kt) * 128u; \
;     asm volatile("s_mov_b32 m0, %0\n\ts_nop 4\n\tbuffer_load_dwordx4 %1, %2, %3 offen lds" :: "s"(_m0), "v"(voffA[half][_i]), "s"(rsA), "s"(_so) : "m0", "memory"); } } while (0)
; template <class Cfg>
; DI void f8dma_issue_prologue_st(LDS_AS unsigned char* lds, const Cfg& cfg) {
;     ...
;   P_STAGE_B(G_SB(0, 0), 0, 0); P_STAGE_A(G_SA(0, 0), 0, 0); P_STAGE_B(G_SB(0, 1), 1, 0); P_STAGE_A(G_SA(0, 1), 1, 0);
;   P_STAGE_B(G_SB(1, 0), 0, 1); P_STAGE_A(G_SA(1, 0), 0, 1); P_STAGE_B(G_SB(1, 1), 1, 1);
;     ...
;     D_LDB(B1, G_SB(1, 1)); D_STAGE_B(G_SB(1, 0), 0, t3);
;     G_BAR(); D_WAIT_L(0); G_SCHED(); D_MMA(0, 1, At, B1); G_BAR(); G_SCHED();
;     D_LDA(At, G_SA(1, 1)); D_STAGE_A(G_SA(1, 0), 0, t3);
;     G_BAR(); D_WAIT_L(0); G_SCHED(); D_MMA(1, 0, At, B0); G_BAR(); G_SCHED();
;     D_STAGE_B(G_SB(1, 1), 1, t3);
;     G_WAIT_V(6); G_BAR(); G_SCHED(); D_MMA(1, 1, At, B1); G_BAR(); G_SCHED();
;   }
;   if (!F8_PEEL) G_WAIT_V(0);
	s_waitcnt lgkmcnt(0)
	s_setprio 1
	s_waitcnt lgkmcnt(5)
	v_mfma_scale_f32_16x16x128_f8f6f4 v[48:51], v[0:7], v[74:81], v[122:125], v165, v164 op_sel_hi:[0,0,0]
	v_mfma_scale_f32_16x16x128_f8f6f4 v[52:55], v[56:63], v[74:81], v[126:129], v165, v164 op_sel_hi:[0,0,0]
	s_waitcnt lgkmcnt(4)
	v_mfma_scale_f32_16x16x128_f8f6f4 v[40:43], v[0:7], v[82:89], v[40:43], v165, v164 op_sel_hi:[0,0,0]
	v_mfma_scale_f32_16x16x128_f8f6f4 v[32:35], v[56:63], v[82:89], v[32:35], v165, v164 op_sel_hi:[0,0,0]
	s_waitcnt lgkmcnt(1)
	v_mfma_scale_f32_16x16x128_f8f6f4 v[24:27], v[0:7], v[90:97], v[24:27], v165, v164 op_sel_hi:[0,0,0]
	v_mfma_scale_f32_16x16x128_f8f6f4 v[16:19], v[56:63], v[90:97], v[16:19], v165, v164 op_sel_hi:[0,0,0]
	s_waitcnt lgkmcnt(0)
	v_mfma_scale_f32_16x16x128_f8f6f4 v[8:11], v[0:7], v[98:105], v[8:11], v165, v164 op_sel_hi:[0,0,0]
	v_mfma_scale_f32_16x16x128_f8f6f4 v[0:3], v[56:63], v[98:105], v[130:133], v165, v164 op_sel_hi:[0,0,0]
	s_setprio 0
	s_barrier
	v_add_u32_e32 v4, s71, v68
	v_add_u32_e32 v5, s71, v69
	ds_read_b128 v[106:109], v4
	ds_read_b128 v[114:117], v4 offset:2048
	ds_read_b128 v[110:113], v5
	ds_read_b128 v[118:121], v5 offset:2048
	s_mov_b32 m0, s39
	s_nop 0
	buffer_load_dwordx4 v70, s[4:7], s67 offen lds
	s_nop 0
	s_mov_b32 m0, s60
	s_nop 0
	buffer_load_dwordx4 v70, s[4:7], s70 offen lds
	s_barrier
	s_waitcnt lgkmcnt(0)
	s_setprio 1
	s_waitcnt lgkmcnt(1)
	v_mfma_scale_f32_16x16x128_f8f6f4 v[60:63], v[106:113], v[74:81], v[134:137], v165, v164 op_sel_hi:[0,0,0]
	s_waitcnt lgkmcnt(0)
	v_mfma_scale_f32_16x16x128_f8f6f4 v[56:59], v[114:121], v[74:81], v[138:141], v165, v164 op_sel_hi:[0,0,0]
	v_mfma_scale_f32_16x16x128_f8f6f4 v[44:47], v[106:113], v[82:89], v[44:47], v165, v164 op_sel_hi:[0,0,0]
	v_mfma_scale_f32_16x16x128_f8f6f4 v[36:39], v[114:121], v[82:89], v[36:39], v165, v164 op_sel_hi:[0,0,0]
	v_mfma_scale_f32_16x16x128_f8f6f4 v[28:31], v[106:113], v[90:97], v[28:31], v165, v164 op_sel_hi:[0,0,0]
	v_mfma_scale_f32_16x16x128_f8f6f4 v[20:23], v[114:121], v[90:97], v[20:23], v165, v164 op_sel_hi:[0,0,0]
	v_mfma_scale_f32_16x16x128_f8f6f4 v[12:15], v[106:113], v[98:105], v[12:15], v165, v164 op_sel_hi:[0,0,0]
	v_mfma_scale_f32_16x16x128_f8f6f4 v[4:7], v[114:121], v[98:105], v[146:149], v165, v164 op_sel_hi:[0,0,0]
	s_setprio 0
	s_barrier
	s_mov_b32 m0, s49
	s_nop 0
	buffer_load_dwordx4 v64, s[8:11], s67 offen lds
	s_nop 0
	s_mov_b32 m0, s61
	s_nop 0
	buffer_load_dwordx4 v65, s[8:11], s67 offen lds
	s_barrier
	s_waitcnt lgkmcnt(0)
	s_barrier
	s_mov_b32 m0, s50
	s_nop 0
	buffer_load_dwordx4 v70, s[4:7], s68 offen lds
	s_nop 0
	s_mov_b32 m0, s62
	s_nop 0
	buffer_load_dwordx4 v70, s[4:7], s69 offen lds
	s_waitcnt vmcnt(6)
	s_barrier
	s_barrier
	s_mov_b32 s63, s65
	s_mov_b32 s66, s64
	s_cbranch_scc0 .LBB0_1701
	s_waitcnt vmcnt(0)
	s_cmpk_lt_u32 s13, 0x100
	s_cbranch_scc0 .LBB0_1704
	s_barrier
.LBB0_1704:
	s_and_b64 vcc, exec, s[2:3]
	s_cbranch_vccnz .LBB0_1706
	v_mbcnt_lo_u32_b32 v68, -1, 0
	v_mbcnt_hi_u32_b32 v68, -1, v68
	s_ashr_i32 s13, s12, 31
	v_or_b32_e32 v64, s87, v68
	v_bfe_u32 v70, v68, 3, 3
	v_readfirstlane_b32 s2, v64
	s_ashr_i32 s15, s2, 6
	s_lshl_b32 s2, s15, 3
	v_lshrrev_b32_e32 v69, 3, v68
	v_or_b32_e32 v71, s2, v70
	v_xor_b32_e32 v68, v69, v68
	s_lshl_b32 s3, s15, 1
	v_lshlrev_b32_e32 v69, 1, v71
	v_mov_b32_e32 v71, 0x63
	s_and_b32 s3, s3, 4
	v_and_b32_e32 v69, 24, v69
	v_bitop3_b32 v70, s2, v71, v70 bitop3:0xc8
	v_lshlrev_b32_e32 v68, 4, v68
	v_or3_b32 v69, s3, v70, v69
	v_and_b32_e32 v68, 0x70, v68
	s_lshl_b32 s2, s44, 19
	v_lshlrev_b32_e32 v69, 11, v69
	v_or3_b32 v68, v69, s2, v68
	s_lshl_b64 s[2:3], s[12:13], 22
	v_lshl_add_u32 v64, v64, 2, 0
	s_add_u32 s4, s52, s2
	v_add_u32_e32 v66, 0x22410, v64
	s_addc_u32 s2, s53, s3
	ds_read2st64_b32 v[64:65], v66 offset1:8
	ds_read2st64_b32 v[66:67], v66 offset0:16 offset1:24
	s_and_b32 s5, s2, 0xffff
	s_lshl_b32 s2, s15, 10
	s_add_i32 s2, s2, 0
	s_add_i32 s3, s2, 0x10010
	s_mov_b32 m0, s3
	s_nop 0
	buffer_load_dwordx4 v68, s[4:7], s31 offen lds
	s_add_i32 s3, s2, 0x12010
	s_mov_b32 m0, s3
	s_nop 0
	buffer_load_dwordx4 v68, s[4:7], s7 offen lds
	s_add_i32 s3, s2, 16
	s_waitcnt lgkmcnt(1)
	s_mov_b32 m0, s3
	s_nop 0
	buffer_load_dwordx4 v64, s[8:11], s31 offen lds
	s_add_i32 s3, s2, 0x2010
	s_mov_b32 m0, s3
	s_nop 0
	buffer_load_dwordx4 v65, s[8:11], s31 offen lds
	s_add_i32 s3, s2, 0x14010
	s_mov_b32 m0, s3
	s_nop 0
	buffer_load_dwordx4 v68, s[4:7], s34 offen lds
	s_add_i32 s3, s2, 0x16010
	s_mov_b32 m0, s3
	s_nop 0
	buffer_load_dwordx4 v68, s[4:7], s35 offen lds
	s_add_i32 s3, s2, 0x4010
	s_waitcnt lgkmcnt(0)
	s_mov_b32 m0, s3
	s_nop 0
	buffer_load_dwordx4 v66, s[8:11], s31 offen lds
	s_add_i32 s3, s2, 0x6010
	s_mov_b32 m0, s3
	s_nop 0
	buffer_load_dwordx4 v67, s[8:11], s31 offen lds
	s_add_i32 s3, s2, 0x18010
	s_mov_b32 m0, s3
	s_nop 0
	buffer_load_dwordx4 v68, s[4:7], s33 offen lds
	s_add_i32 s3, s2, 0x1a010
	s_mov_b32 m0, s3
	s_nop 0
	buffer_load_dwordx4 v68, s[4:7], s36 offen lds
	s_add_i32 s3, s2, 0x8010
	s_mov_b32 m0, s3
	s_nop 0
	buffer_load_dwordx4 v64, s[8:11], s33 offen lds
	s_add_i32 s3, s2, 0xa010
	s_mov_b32 m0, s3
	s_nop 0
	buffer_load_dwordx4 v65, s[8:11], s33 offen lds
	s_add_i32 s3, s2, 0x1c010
	s_mov_b32 m0, s3
	s_nop 0
	buffer_load_dwordx4 v68, s[4:7], s37 offen lds
	s_add_i32 s2, s2, 0x1e010
	s_mov_b32 m0, s2
	s_nop 0
	buffer_load_dwordx4 v68, s[4:7], s42 offen lds
